# batched tok/pool/router loads, flat->global, counted waits in branch epilogue, 64-bit acc zeroing
# speedup vs baseline: 1.0183x; 1.0183x over previous
.LBB0_362:
	s_andn2_b64 vcc, exec, s[0:1]
	s_cbranch_vccnz .LBB0_580
	s_mov_b32 s0, s84
	s_cmp_gt_i32 s0, 63
	s_cbranch_scc1 .LBB0_377
	v_readlane_b32 s40, v253, 6
	v_readlane_b32 s41, v253, 7
	v_readlane_b32 s42, v253, 8
	v_readlane_b32 s43, v253, 9
	v_readlane_b32 s44, v253, 10
	v_readlane_b32 s45, v253, 11
	s_mov_b64 s[12:13], s[40:41]
	s_mov_b64 s[14:15], s[42:43]
	s_mov_b64 s[2:3], s[14:15]
	s_mov_b64 s[0:1], s[14:15]
	s_mov_b32 s38, s84
	s_ashr_i32 s39, s38, 31
	s_waitcnt vmcnt(0)
	v_mov_b32_e32 v1, v0
	s_lshl_b64 s[12:13], s[38:39], 14
	s_add_u32 s2, s2, s12
	v_lshlrev_b32_e32 v6, 3, v1
	s_addc_u32 s3, s3, s13
	v_ashrrev_i32_e32 v7, 31, v6
	v_lshl_add_u64 v[2:3], v[6:7], 2, s[2:3]
	s_mov_b64 s[2:3], 0x6d800000
	v_lshl_add_u64 v[8:9], v[2:3], 0, s[2:3]
	s_mov_b32 s2, 0x6d800000
	v_add_co_u32_e32 v2, vcc, s2, v2
	v_and_b32_e32 v12, 63, v1
	s_nop 0
	v_addc_co_u32_e32 v3, vcc, 0, v3, vcc
	global_load_dwordx4 v[2:5], v[2:3], off
	s_nop 0
	global_load_dwordx4 v[14:17], v[8:9], off offset:16
	v_cmp_lt_i32_e32 vcc, v229, v228
	v_readlane_b32 s46, v253, 12
	v_readlane_b32 s47, v253, 13
	v_cndmask_b32_e32 v13, v229, v227, vcc
	v_lshlrev_b32_e32 v13, 2, v13
	v_cmp_eq_u32_e32 vcc, 0, v12
	s_mov_b64 s[16:17], s[44:45]
	s_waitcnt vmcnt(0) lgkmcnt(0)
	v_add_f32_e32 v3, v2, v3
	v_add_f32_e32 v10, v4, v3
	v_add_f32_e32 v11, v5, v10
	v_add_f32_e32 v4, v14, v11
	v_add_f32_e32 v5, v15, v4
	v_add_f32_e32 v8, v16, v5
	v_add_f32_e32 v9, v17, v8
	ds_bpermute_b32 v13, v13, v9
	s_waitcnt lgkmcnt(0)
	v_add_f32_e32 v13, v9, v13
	v_cndmask_b32_e32 v13, v13, v9, vcc
	v_cmp_lt_i32_e32 vcc, v252, v228
	s_nop 1
	v_cndmask_b32_e32 v14, v252, v227, vcc
	v_lshlrev_b32_e32 v14, 2, v14
	ds_bpermute_b32 v14, v14, v13
	v_cmp_gt_u32_e32 vcc, 2, v12
	s_waitcnt lgkmcnt(0)
	v_add_f32_e32 v14, v13, v14
	v_cndmask_b32_e32 v13, v14, v13, vcc
	v_cmp_lt_i32_e32 vcc, v239, v228
	s_nop 1
	v_cndmask_b32_e32 v14, v239, v227, vcc
	v_lshlrev_b32_e32 v14, 2, v14
	ds_bpermute_b32 v14, v14, v13
	v_cmp_gt_u32_e32 vcc, 4, v12
	s_waitcnt lgkmcnt(0)
	v_add_f32_e32 v14, v13, v14
	v_cndmask_b32_e32 v13, v14, v13, vcc
	v_cmp_lt_i32_e32 vcc, v232, v228
	s_nop 1
	v_cndmask_b32_e32 v14, v232, v227, vcc
	v_lshlrev_b32_e32 v14, 2, v14
	ds_bpermute_b32 v14, v14, v13
	v_cmp_gt_u32_e32 vcc, 8, v12
	s_waitcnt lgkmcnt(0)
	v_add_f32_e32 v14, v13, v14
	v_cndmask_b32_e32 v13, v14, v13, vcc
	v_cmp_lt_i32_e32 vcc, v233, v228
	s_nop 1
	v_cndmask_b32_e32 v14, v233, v227, vcc
	v_lshlrev_b32_e32 v14, 2, v14
	ds_bpermute_b32 v14, v14, v13
	v_cmp_gt_u32_e32 vcc, 16, v12
	s_waitcnt lgkmcnt(0)
	v_add_f32_e32 v14, v13, v14
	v_cndmask_b32_e32 v13, v14, v13, vcc
	v_cmp_lt_i32_e32 vcc, v234, v228
	s_nop 1
	v_cndmask_b32_e32 v14, v234, v227, vcc
	v_lshlrev_b32_e32 v14, 2, v14
	ds_bpermute_b32 v14, v14, v13
	v_cmp_eq_u32_e32 vcc, 63, v12
	s_waitcnt lgkmcnt(0)
	v_add_f32_e32 v15, v13, v14
	v_ashrrev_i32_e32 v14, 6, v1
	s_and_saveexec_b64 s[14:15], vcc
	v_lshl_add_u32 v16, v14, 2, 0
	ds_write_b32 v16, v15 offset:4096
	s_or_b64 exec, exec, s[14:15]
	v_cmp_gt_u32_e32 vcc, 32, v12
	s_waitcnt lgkmcnt(0)
	s_barrier
	v_cndmask_b32_e32 v12, v15, v13, vcc
	v_sub_f32_e32 v12, v12, v9
	v_cmp_lt_i32_e32 vcc, 0, v14
	s_and_saveexec_b64 s[14:15], vcc
	s_cbranch_execz .LBB0_376
	v_cmp_lt_u32_e32 vcc, 7, v14
	v_mov_b32_e32 v13, 0
	s_and_saveexec_b64 s[24:25], vcc
	s_cbranch_execz .LBB0_371
	v_and_b32_e32 v13, 0x7ffffff8, v14
	s_mov_b32 s2, 0
	s_mov_b64 s[40:41], 0
	v_readlane_b32 s3, v254, 39

.LBB0_376:
	s_or_b64 exec, exec, s[14:15]
	s_lshl_b64 s[14:15], s[38:39], 12
	s_lshl_b64 s[2:3], s[14:15], 2
	s_add_u32 s0, s0, s2
	s_addc_u32 s1, s1, s3
	v_lshl_add_u64 v[18:19], v[6:7], 2, s[0:1]
	v_pk_add_f32 v[14:15], v[2:3], v[12:13] op_sel_hi:[1,0]
	v_add_co_u32_e32 v2, vcc, 0x6d900000, v18
	s_mov_b64 s[0:1], 0x6d900000
	v_pk_add_f32 v[16:17], v[10:11], v[12:13] op_sel_hi:[1,0]
	v_addc_co_u32_e32 v3, vcc, 0, v19, vcc
	v_lshl_add_u64 v[20:21], v[18:19], 0, s[0:1]
	v_pk_add_f32 v[6:7], v[8:9], v[12:13] op_sel_hi:[1,0]
	v_pk_add_f32 v[4:5], v[4:5], v[12:13] op_sel_hi:[1,0]
	global_store_dwordx4 v[2:3], v[14:17], off
	global_store_dwordx4 v[20:21], v[4:7], off offset:16
	s_waitcnt lgkmcnt(0)
	s_barrier

.LBB0_390:
	s_add_u32 s1, s42, 0x100
	v_mov_b32_e32 v2, 0
	v_lshl_add_u64 v[142:143], s[40:41], 0, v[130:131]
	s_addc_u32 s24, s43, 0
	s_mov_b32 s25, -2
	s_mov_b64 s[42:43], 0
	v_mov_b32_e32 v3, 0
	v_mov_b64_e32 v[4:5], 0
	v_mov_b64_e32 v[6:7], 0
	v_mov_b64_e32 v[8:9], 0
	v_mov_b64_e32 v[18:19], 0
	v_mov_b64_e32 v[20:21], 0
	v_mov_b64_e32 v[22:23], 0
	v_mov_b64_e32 v[24:25], 0
	v_mov_b64_e32 v[34:35], 0
	v_mov_b64_e32 v[36:37], 0
	v_mov_b64_e32 v[38:39], 0
	v_mov_b64_e32 v[40:41], 0
	v_mov_b64_e32 v[50:51], 0
	v_mov_b64_e32 v[52:53], 0
	v_mov_b64_e32 v[54:55], 0
	v_mov_b64_e32 v[56:57], 0
	v_mov_b64_e32 v[10:11], 0
	v_mov_b64_e32 v[12:13], 0
	v_mov_b64_e32 v[14:15], 0
	v_mov_b64_e32 v[16:17], 0
	v_mov_b64_e32 v[26:27], 0
	v_mov_b64_e32 v[28:29], 0
	v_mov_b64_e32 v[30:31], 0
	v_mov_b64_e32 v[32:33], 0
	v_mov_b64_e32 v[42:43], 0
	v_mov_b64_e32 v[44:45], 0
	v_mov_b64_e32 v[46:47], 0
	v_mov_b64_e32 v[48:49], 0
	v_mov_b64_e32 v[58:59], 0
	v_mov_b64_e32 v[60:61], 0
	v_mov_b64_e32 v[62:63], 0
	v_mov_b64_e32 v[64:65], 0
	v_mov_b64_e32 v[66:67], 0
	v_mov_b64_e32 v[68:69], 0
	v_mov_b64_e32 v[70:71], 0
	v_mov_b64_e32 v[72:73], 0
	v_mov_b64_e32 v[82:83], 0
	v_mov_b64_e32 v[84:85], 0
	v_mov_b64_e32 v[86:87], 0
	v_mov_b64_e32 v[88:89], 0
	v_mov_b64_e32 v[98:99], 0
	v_mov_b64_e32 v[100:101], 0
	v_mov_b64_e32 v[102:103], 0
	v_mov_b64_e32 v[104:105], 0
	v_mov_b64_e32 v[114:115], 0
	v_mov_b64_e32 v[116:117], 0
	v_mov_b64_e32 v[118:119], 0
	v_mov_b64_e32 v[120:121], 0
	v_mov_b64_e32 v[74:75], 0
	v_mov_b64_e32 v[76:77], 0
	v_mov_b64_e32 v[78:79], 0
	v_mov_b64_e32 v[80:81], 0
	v_mov_b64_e32 v[90:91], 0
	v_mov_b64_e32 v[92:93], 0
	v_mov_b64_e32 v[94:95], 0
	v_mov_b64_e32 v[96:97], 0
	v_mov_b64_e32 v[106:107], 0
	v_mov_b64_e32 v[108:109], 0
	v_mov_b64_e32 v[110:111], 0
	v_mov_b64_e32 v[112:113], 0
	v_mov_b64_e32 v[122:123], 0
	v_mov_b64_e32 v[124:125], 0
	v_mov_b64_e32 v[126:127], 0
	v_mov_b64_e32 v[128:129], 0

.LBB0_394:
	s_cmp_lt_i32 s2, 2
	s_cselect_b64 s[40:41], -1, 0
	s_cmp_lt_i32 s2, 8
	s_cselect_b64 s[42:43], -1, 0
	s_cmp_lg_u32 s2, 7
	v_pk_mul_f32 v[140:141], v[122:123], s[10:11] op_sel_hi:[1,0]
	s_cselect_b64 s[58:59], -1, 0
	s_lshl_b32 s56, s2, 8
	v_pk_mul_f32 v[142:143], v[128:129], s[10:11] op_sel_hi:[1,0]
	v_pk_mul_f32 v[146:147], v[126:127], s[10:11] op_sel_hi:[1,0]
	v_pk_mul_f32 v[148:149], v[124:125], s[10:11] op_sel_hi:[1,0]
	s_ashr_i32 s57, s56, 31
	v_cndmask_b32_e64 v131, v123, v141, s[40:41]
	v_cndmask_b32_e64 v140, v122, v140, s[40:41]
	v_cndmask_b32_e64 v122, v125, v149, s[40:41]
	v_cndmask_b32_e64 v123, v124, v148, s[40:41]
	v_cndmask_b32_e64 v127, v127, v147, s[40:41]
	v_cndmask_b32_e64 v126, v126, v146, s[40:41]
	v_cndmask_b32_e64 v124, v129, v143, s[40:41]
	v_cndmask_b32_e64 v125, v128, v142, s[40:41]
	s_mov_b64 s[14:15], -1
	s_and_b64 vcc, exec, s[42:43]
	s_cbranch_vccz .LBB0_400
	s_and_b64 vcc, exec, s[58:59]
	s_cbranch_vccz .LBB0_397
	s_lshl_b32 s1, s46, 8
	s_add_i32 s1, s1, s74
	s_mul_hi_i32 s2, s1, 0x2800
	s_mulk_i32 s1, 0x2800
	s_add_u32 s1, s70, s1
	s_addc_u32 s2, s71, s2
	s_lshl_b64 s[14:15], s[56:57], 1
	s_add_u32 s1, s1, s14
	s_addc_u32 s2, s2, s15
	s_lshl_b32 s14, s75, 1
	s_add_u32 s14, s1, s14
	s_addc_u32 s15, s2, 0
	v_lshl_add_u64 v[128:129], s[14:15], 0, v[134:135]
	v_cvt_pk_bf16_f32 v146, v126, v127
	v_cvt_pk_bf16_f32 v147, v125, v124
	v_cvt_pk_bf16_f32 v148, v140, v131
	v_cvt_pk_bf16_f32 v149, v123, v122
	global_store_dwordx4 v[128:129], v[146:149], off
	s_mov_b64 s[14:15], 0
.LBB0_397:
	s_andn2_b64 vcc, exec, s[14:15]
	s_cbranch_vccnz .LBB0_399
	s_lshl_b32 s1, s46, 4
	s_ashr_i32 s2, s1, 31
	s_add_u32 s1, s88, s1
	v_readlane_b32 s14, v253, 34
	s_addc_u32 s2, s14, s2
	s_mulk_i32 s2, 0x300
	v_mad_u64_u32 v[128:129], s[14:15], s1, v235, v[138:139]
	v_add_u32_e32 v129, s2, v129
	v_cvt_pk_bf16_f32 v146, v126, v127
	v_cvt_pk_bf16_f32 v147, v125, v124
	v_cvt_pk_bf16_f32 v148, v140, v131
	v_cvt_pk_bf16_f32 v149, v123, v122
	global_store_dwordx4 v[128:129], v[146:149], off

.LBB0_400:
	s_andn2_b64 vcc, exec, s[14:15]
	s_add_i32 s1, s56, 0xfffff800
	s_cbranch_vccnz .LBB0_402
	v_exp_f32_e32 v126, v126
	v_exp_f32_e32 v127, v127
	v_exp_f32_e32 v128, v140
	v_exp_f32_e32 v129, v131
	s_mov_b32 s2, 0x437f0000
	v_pk_add_f32 v[126:127], v[126:127], 1.0 op_sel_hi:[1,0]
	v_pk_add_f32 v[128:129], v[128:129], 1.0 op_sel_hi:[1,0]
	v_rcp_f32_e32 v126, v126
	v_rcp_f32_e32 v127, v127
	v_rcp_f32_e32 v128, v128
	v_rcp_f32_e32 v129, v129
	v_pk_fma_f32 v[126:127], v[126:127], s[2:3], 0.5 op_sel_hi:[1,0,0]
	s_nop 0
	v_max_f32_e32 v126, 1.0, v126
	v_pk_fma_f32 v[128:129], v[128:129], s[2:3], 0.5 op_sel_hi:[1,0,0]
	v_cvt_u32_f32_e32 v131, v126
	v_max_f32_e32 v126, 1.0, v127
	v_cvt_u32_f32_e32 v140, v126
	v_max_f32_e32 v126, 1.0, v128
	v_cvt_u32_f32_e32 v128, v126
	v_max_f32_e32 v126, 1.0, v129
	v_cvt_u32_f32_e32 v129, v126
	v_exp_f32_e32 v126, v125
	v_exp_f32_e32 v127, v124
	s_nop 0
	v_pk_add_f32 v[124:125], v[126:127], 1.0 op_sel_hi:[1,0]
	v_exp_f32_e32 v126, v123
	v_exp_f32_e32 v127, v122
	v_rcp_f32_e32 v124, v124
	v_rcp_f32_e32 v125, v125
	v_pk_add_f32 v[122:123], v[126:127], 1.0 op_sel_hi:[1,0]
	s_nop 0
	v_rcp_f32_e32 v122, v122
	v_rcp_f32_e32 v123, v123
	v_pk_fma_f32 v[124:125], v[124:125], s[2:3], 0.5 op_sel_hi:[1,0,0]
	v_pk_fma_f32 v[122:123], v[122:123], s[2:3], 0.5 op_sel_hi:[1,0,0]
	s_lshl_b32 s2, s46, 8
	s_add_i32 s2, s2, s74
	s_mul_hi_i32 s14, s2, 0xc00
	s_mulk_i32 s2, 0xc00
	v_max_f32_e32 v124, 1.0, v124
	v_max_f32_e32 v125, 1.0, v125
	v_max_f32_e32 v122, 1.0, v122
	s_add_u32 s2, s72, s2
	v_cvt_u32_f32_sdwa v124, v124 dst_sel:WORD_1 dst_unused:UNUSED_PAD src0_sel:DWORD
	v_cvt_u32_f32_sdwa v125, v125 dst_sel:BYTE_3 dst_unused:UNUSED_PAD src0_sel:DWORD
	v_cvt_u32_f32_sdwa v126, v122 dst_sel:WORD_1 dst_unused:UNUSED_PAD src0_sel:DWORD
	v_max_f32_e32 v122, 1.0, v123
	s_addc_u32 s14, s73, s14
	v_cvt_u32_f32_sdwa v123, v122 dst_sel:BYTE_3 dst_unused:UNUSED_PAD src0_sel:DWORD
	s_add_u32 s2, s2, s1
	s_addc_u32 s15, s14, 0
	v_lshl_or_b32 v122, v140, 8, v131
	s_add_u32 s14, s2, s75
	v_or3_b32 v122, v122, v124, v125
	v_lshl_or_b32 v124, v129, 8, v128
	s_addc_u32 s15, s15, 0
	v_or3_b32 v123, v124, v126, v123
	v_lshl_add_u64 v[124:125], s[14:15], 0, v[136:137]
	global_store_dwordx2 v[124:125], v[122:123], off
.LBB0_402:
	v_pk_mul_f32 v[124:125], v[120:121], s[10:11] op_sel_hi:[1,0]
	v_pk_mul_f32 v[122:123], v[116:117], s[10:11] op_sel_hi:[1,0]
	v_pk_mul_f32 v[128:129], v[114:115], s[10:11] op_sel_hi:[1,0]
	v_cndmask_b32_e64 v116, v116, v122, s[40:41]
	v_cndmask_b32_e64 v122, v115, v129, s[40:41]
	v_cndmask_b32_e64 v115, v120, v124, s[40:41]
	v_cndmask_b32_e64 v120, 0, 1, s[42:43]
	v_pk_mul_f32 v[126:127], v[118:119], s[10:11] op_sel_hi:[1,0]
	v_cmp_ne_u32_e64 s[44:45], 1, v120
	v_cndmask_b32_e64 v120, 0, 1, s[58:59]
	v_cndmask_b32_e64 v117, v117, v123, s[40:41]
	v_cndmask_b32_e64 v123, v114, v128, s[40:41]
	v_cndmask_b32_e64 v114, v121, v125, s[40:41]
	v_cndmask_b32_e64 v119, v119, v127, s[40:41]
	v_cndmask_b32_e64 v118, v118, v126, s[40:41]
	s_mov_b64 s[14:15], -1
	s_andn2_b64 vcc, exec, s[42:43]
	v_cmp_ne_u32_e64 s[42:43], 1, v120
	s_cbranch_vccnz .LBB0_408
	s_and_b64 vcc, exec, s[42:43]
	s_cbranch_vccnz .LBB0_405
	s_lshl_b32 s2, s46, 8
	s_add_i32 s2, s2, s74
	s_mul_hi_i32 s14, s2, 0x2800
	s_mulk_i32 s2, 0x2800
	s_add_u32 s2, s70, s2
	s_addc_u32 s24, s71, s14
	s_lshl_b64 s[14:15], s[56:57], 1
	s_add_u32 s2, s2, s14
	s_addc_u32 s15, s24, s15
	s_lshl_b32 s14, s75, 1
	s_add_u32 s14, s2, s14
	s_addc_u32 s15, s15, 0
	v_lshl_add_u64 v[120:121], s[14:15], 0, v[134:135]
	s_mov_b64 s[14:15], 0
	v_cvt_pk_bf16_f32 v124, v118, v119
	v_cvt_pk_bf16_f32 v125, v115, v114
	v_cvt_pk_bf16_f32 v126, v123, v122
	v_cvt_pk_bf16_f32 v127, v116, v117
	global_store_dwordx4 v[120:121], v[124:127], off offset:256
.LBB0_405:
	s_andn2_b64 vcc, exec, s[14:15]
	s_cbranch_vccnz .LBB0_407
	s_lshl_b32 s2, s46, 4
	s_ashr_i32 s14, s2, 31
	v_readlane_b32 s15, v254, 46
	s_add_u32 s2, s15, s2
	v_readlane_b32 s15, v254, 48
	s_addc_u32 s14, s15, s14
	s_mul_i32 s24, s14, 0x300
	v_mad_u64_u32 v[120:121], s[14:15], s2, v235, v[138:139]
	v_add_u32_e32 v121, s24, v121
	v_cvt_pk_bf16_f32 v124, v118, v119
	v_cvt_pk_bf16_f32 v125, v115, v114
	v_cvt_pk_bf16_f32 v126, v123, v122
	v_cvt_pk_bf16_f32 v127, v116, v117
	global_store_dwordx4 v[120:121], v[124:127], off

.LBB0_408:
	s_andn2_b64 vcc, exec, s[14:15]
	s_cbranch_vccnz .LBB0_410
	v_exp_f32_e32 v118, v118
	v_exp_f32_e32 v119, v119
	v_exp_f32_e32 v120, v123
	v_exp_f32_e32 v121, v122
	s_mov_b32 s2, 0x437f0000
	v_pk_add_f32 v[118:119], v[118:119], 1.0 op_sel_hi:[1,0]
	v_exp_f32_e32 v116, v116
	v_rcp_f32_e32 v118, v118
	v_rcp_f32_e32 v119, v119
	v_pk_add_f32 v[120:121], v[120:121], 1.0 op_sel_hi:[1,0]
	v_exp_f32_e32 v117, v117
	v_rcp_f32_e32 v120, v120
	v_rcp_f32_e32 v121, v121
	v_pk_fma_f32 v[118:119], v[118:119], s[2:3], 0.5 op_sel_hi:[1,0,0]
	v_pk_add_f32 v[116:117], v[116:117], 1.0 op_sel_hi:[1,0]
	v_max_f32_e32 v118, 1.0, v118
	v_pk_fma_f32 v[120:121], v[120:121], s[2:3], 0.5 op_sel_hi:[1,0,0]
	v_cvt_u32_f32_e32 v122, v118
	v_max_f32_e32 v118, 1.0, v119
	v_cvt_u32_f32_e32 v123, v118
	v_max_f32_e32 v118, 1.0, v120
	v_cvt_u32_f32_e32 v120, v118
	v_max_f32_e32 v118, 1.0, v121
	v_cvt_u32_f32_e32 v121, v118
	v_exp_f32_e32 v118, v115
	v_exp_f32_e32 v119, v114
	v_rcp_f32_e32 v116, v116
	v_rcp_f32_e32 v117, v117
	v_pk_add_f32 v[114:115], v[118:119], 1.0 op_sel_hi:[1,0]
	s_nop 0
	v_rcp_f32_e32 v114, v114
	v_rcp_f32_e32 v115, v115
	v_pk_fma_f32 v[116:117], v[116:117], s[2:3], 0.5 op_sel_hi:[1,0,0]
	v_lshl_or_b32 v118, v123, 8, v122
	v_max_f32_e32 v116, 1.0, v116
	v_pk_fma_f32 v[114:115], v[114:115], s[2:3], 0.5 op_sel_hi:[1,0,0]
	s_lshl_b32 s2, s46, 8
	s_add_i32 s2, s2, s74
	s_mul_hi_i32 s14, s2, 0xc00
	s_mulk_i32 s2, 0xc00
	v_max_f32_e32 v114, 1.0, v114
	v_max_f32_e32 v115, 1.0, v115
	s_add_u32 s2, s72, s2
	v_cvt_u32_f32_sdwa v114, v114 dst_sel:WORD_1 dst_unused:UNUSED_PAD src0_sel:DWORD
	v_cvt_u32_f32_sdwa v115, v115 dst_sel:BYTE_3 dst_unused:UNUSED_PAD src0_sel:DWORD
	v_max_f32_e32 v117, 1.0, v117
	s_addc_u32 s14, s73, s14
	v_cvt_u32_f32_sdwa v116, v116 dst_sel:WORD_1 dst_unused:UNUSED_PAD src0_sel:DWORD
	v_cvt_u32_f32_sdwa v117, v117 dst_sel:BYTE_3 dst_unused:UNUSED_PAD src0_sel:DWORD
	s_add_u32 s2, s2, s1
	s_addc_u32 s15, s14, 0
	s_add_u32 s14, s2, s75
	v_or3_b32 v114, v118, v114, v115
	v_lshl_or_b32 v115, v121, 8, v120
	s_addc_u32 s15, s15, 0
	v_or3_b32 v115, v115, v116, v117
	v_lshl_add_u64 v[116:117], s[14:15], 0, v[136:137]
	global_store_dwordx2 v[116:117], v[114:115], off offset:128
.LBB0_410:
	v_pk_mul_f32 v[116:117], v[112:113], s[10:11] op_sel_hi:[1,0]
	v_pk_mul_f32 v[118:119], v[110:111], s[10:11] op_sel_hi:[1,0]
	v_pk_mul_f32 v[114:115], v[108:109], s[10:11] op_sel_hi:[1,0]
	v_pk_mul_f32 v[120:121], v[106:107], s[10:11] op_sel_hi:[1,0]
	v_cndmask_b32_e64 v109, v109, v115, s[40:41]
	v_cndmask_b32_e64 v108, v108, v114, s[40:41]
	v_cndmask_b32_e64 v114, v107, v121, s[40:41]
	v_cndmask_b32_e64 v115, v106, v120, s[40:41]
	v_cndmask_b32_e64 v106, v113, v117, s[40:41]
	v_cndmask_b32_e64 v107, v112, v116, s[40:41]
	v_cndmask_b32_e64 v111, v111, v119, s[40:41]
	v_cndmask_b32_e64 v110, v110, v118, s[40:41]
	s_and_b64 vcc, exec, s[44:45]
	s_mov_b64 s[14:15], -1
	s_cbranch_vccnz .LBB0_416
	s_and_b64 vcc, exec, s[42:43]
	s_cbranch_vccnz .LBB0_413
	s_lshl_b32 s2, s46, 8
	s_add_i32 s2, s2, s84
	s_mul_hi_i32 s14, s2, 0x2800
	s_mulk_i32 s2, 0x2800
	s_add_u32 s2, s70, s2
	s_addc_u32 s24, s71, s14
	s_lshl_b64 s[14:15], s[56:57], 1
	s_add_u32 s2, s2, s14
	s_addc_u32 s15, s24, s15
	s_lshl_b32 s14, s75, 1
	s_add_u32 s14, s2, s14
	s_addc_u32 s15, s15, 0
	v_lshl_add_u64 v[112:113], s[14:15], 0, v[134:135]
	s_mov_b64 s[14:15], 0
	v_cvt_pk_bf16_f32 v116, v110, v111
	v_cvt_pk_bf16_f32 v117, v107, v106
	v_cvt_pk_bf16_f32 v118, v115, v114
	v_cvt_pk_bf16_f32 v119, v108, v109
	global_store_dwordx4 v[112:113], v[116:119], off
.LBB0_413:
	s_andn2_b64 vcc, exec, s[14:15]
	s_cbranch_vccnz .LBB0_415
	s_lshl_b32 s2, s46, 4
	s_ashr_i32 s14, s2, 31
	v_readlane_b32 s15, v254, 50
	s_add_u32 s2, s15, s2
	v_readlane_b32 s15, v254, 52
	s_addc_u32 s14, s15, s14
	s_mul_i32 s24, s14, 0x300
	v_mad_u64_u32 v[112:113], s[14:15], s2, v235, v[138:139]
	v_add_u32_e32 v113, s24, v113
	v_cvt_pk_bf16_f32 v116, v110, v111
	v_cvt_pk_bf16_f32 v117, v107, v106
	v_cvt_pk_bf16_f32 v118, v115, v114
	v_cvt_pk_bf16_f32 v119, v108, v109
	global_store_dwordx4 v[112:113], v[116:119], off

.LBB0_416:
	s_andn2_b64 vcc, exec, s[14:15]
	s_cbranch_vccnz .LBB0_418
	v_exp_f32_e32 v110, v110
	v_exp_f32_e32 v111, v111
	v_exp_f32_e32 v112, v115
	v_exp_f32_e32 v113, v114
	s_mov_b32 s2, 0x437f0000
	v_pk_add_f32 v[110:111], v[110:111], 1.0 op_sel_hi:[1,0]
	v_exp_f32_e32 v108, v108
	v_rcp_f32_e32 v110, v110
	v_rcp_f32_e32 v111, v111
	v_pk_add_f32 v[112:113], v[112:113], 1.0 op_sel_hi:[1,0]
	v_exp_f32_e32 v109, v109
	v_rcp_f32_e32 v112, v112
	v_rcp_f32_e32 v113, v113
	v_pk_fma_f32 v[110:111], v[110:111], s[2:3], 0.5 op_sel_hi:[1,0,0]
	v_pk_add_f32 v[108:109], v[108:109], 1.0 op_sel_hi:[1,0]
	v_max_f32_e32 v110, 1.0, v110
	v_pk_fma_f32 v[112:113], v[112:113], s[2:3], 0.5 op_sel_hi:[1,0,0]
	v_cvt_u32_f32_e32 v114, v110
	v_max_f32_e32 v110, 1.0, v111
	v_cvt_u32_f32_e32 v115, v110
	v_max_f32_e32 v110, 1.0, v112
	v_cvt_u32_f32_e32 v112, v110
	v_max_f32_e32 v110, 1.0, v113
	v_cvt_u32_f32_e32 v113, v110
	v_exp_f32_e32 v110, v107
	v_exp_f32_e32 v111, v106
	v_rcp_f32_e32 v108, v108
	v_rcp_f32_e32 v109, v109
	v_pk_add_f32 v[106:107], v[110:111], 1.0 op_sel_hi:[1,0]
	s_nop 0
	v_rcp_f32_e32 v106, v106
	v_rcp_f32_e32 v107, v107
	v_pk_fma_f32 v[108:109], v[108:109], s[2:3], 0.5 op_sel_hi:[1,0,0]
	v_lshl_or_b32 v110, v115, 8, v114
	v_max_f32_e32 v108, 1.0, v108
	v_pk_fma_f32 v[106:107], v[106:107], s[2:3], 0.5 op_sel_hi:[1,0,0]
	s_lshl_b32 s2, s46, 8
	s_add_i32 s2, s2, s84
	s_mul_hi_i32 s14, s2, 0xc00
	s_mulk_i32 s2, 0xc00
	v_max_f32_e32 v106, 1.0, v106
	v_max_f32_e32 v107, 1.0, v107
	s_add_u32 s2, s72, s2
	v_cvt_u32_f32_sdwa v106, v106 dst_sel:WORD_1 dst_unused:UNUSED_PAD src0_sel:DWORD
	v_cvt_u32_f32_sdwa v107, v107 dst_sel:BYTE_3 dst_unused:UNUSED_PAD src0_sel:DWORD
	v_max_f32_e32 v109, 1.0, v109
	s_addc_u32 s14, s73, s14
	v_cvt_u32_f32_sdwa v108, v108 dst_sel:WORD_1 dst_unused:UNUSED_PAD src0_sel:DWORD
	v_cvt_u32_f32_sdwa v109, v109 dst_sel:BYTE_3 dst_unused:UNUSED_PAD src0_sel:DWORD
	s_add_u32 s2, s2, s1
	s_addc_u32 s15, s14, 0
	s_add_u32 s14, s2, s75
	v_or3_b32 v106, v110, v106, v107
	v_lshl_or_b32 v107, v113, 8, v112
	s_addc_u32 s15, s15, 0
	v_or3_b32 v107, v107, v108, v109
	v_lshl_add_u64 v[108:109], s[14:15], 0, v[136:137]
	global_store_dwordx2 v[108:109], v[106:107], off
.LBB0_418:
	v_pk_mul_f32 v[108:109], v[104:105], s[10:11] op_sel_hi:[1,0]
	v_pk_mul_f32 v[110:111], v[102:103], s[10:11] op_sel_hi:[1,0]
	v_pk_mul_f32 v[106:107], v[100:101], s[10:11] op_sel_hi:[1,0]
	v_pk_mul_f32 v[112:113], v[98:99], s[10:11] op_sel_hi:[1,0]
	v_cndmask_b32_e64 v101, v101, v107, s[40:41]
	v_cndmask_b32_e64 v100, v100, v106, s[40:41]
	v_cndmask_b32_e64 v106, v99, v113, s[40:41]
	v_cndmask_b32_e64 v107, v98, v112, s[40:41]
	v_cndmask_b32_e64 v98, v105, v109, s[40:41]
	v_cndmask_b32_e64 v99, v104, v108, s[40:41]
	v_cndmask_b32_e64 v103, v103, v111, s[40:41]
	v_cndmask_b32_e64 v102, v102, v110, s[40:41]
	s_and_b64 vcc, exec, s[44:45]
	s_mov_b64 s[14:15], -1
	s_cbranch_vccnz .LBB0_424
	s_and_b64 vcc, exec, s[42:43]
	s_cbranch_vccnz .LBB0_421
	s_lshl_b32 s2, s46, 8
	s_add_i32 s2, s2, s84
	s_mul_hi_i32 s14, s2, 0x2800
	s_mulk_i32 s2, 0x2800
	s_add_u32 s2, s70, s2
	s_addc_u32 s24, s71, s14
	s_lshl_b64 s[14:15], s[56:57], 1
	s_add_u32 s2, s2, s14
	s_addc_u32 s15, s24, s15
	s_lshl_b32 s14, s75, 1
	s_add_u32 s14, s2, s14
	s_addc_u32 s15, s15, 0
	v_lshl_add_u64 v[104:105], s[14:15], 0, v[134:135]
	s_mov_b64 s[14:15], 0
	v_cvt_pk_bf16_f32 v108, v102, v103
	v_cvt_pk_bf16_f32 v109, v99, v98
	v_cvt_pk_bf16_f32 v110, v107, v106
	v_cvt_pk_bf16_f32 v111, v100, v101
	global_store_dwordx4 v[104:105], v[108:111], off offset:256
.LBB0_421:
	s_andn2_b64 vcc, exec, s[14:15]
	s_cbranch_vccnz .LBB0_423
	s_lshl_b32 s2, s46, 4
	s_ashr_i32 s14, s2, 31
	v_readlane_b32 s15, v254, 54
	s_add_u32 s2, s15, s2
	v_readlane_b32 s15, v254, 55
	s_addc_u32 s14, s15, s14
	s_mul_i32 s24, s14, 0x300
	v_mad_u64_u32 v[104:105], s[14:15], s2, v235, v[138:139]
	v_add_u32_e32 v105, s24, v105
	v_cvt_pk_bf16_f32 v108, v102, v103
	v_cvt_pk_bf16_f32 v109, v99, v98
	v_cvt_pk_bf16_f32 v110, v107, v106
	v_cvt_pk_bf16_f32 v111, v100, v101
	global_store_dwordx4 v[104:105], v[108:111], off

.LBB0_424:
	s_andn2_b64 vcc, exec, s[14:15]
	s_cbranch_vccnz .LBB0_426
	v_exp_f32_e32 v102, v102
	v_exp_f32_e32 v103, v103
	v_exp_f32_e32 v104, v107
	v_exp_f32_e32 v105, v106
	s_mov_b32 s2, 0x437f0000
	v_pk_add_f32 v[102:103], v[102:103], 1.0 op_sel_hi:[1,0]
	v_exp_f32_e32 v100, v100
	v_rcp_f32_e32 v102, v102
	v_rcp_f32_e32 v103, v103
	v_pk_add_f32 v[104:105], v[104:105], 1.0 op_sel_hi:[1,0]
	v_exp_f32_e32 v101, v101
	v_rcp_f32_e32 v104, v104
	v_rcp_f32_e32 v105, v105
	v_pk_fma_f32 v[102:103], v[102:103], s[2:3], 0.5 op_sel_hi:[1,0,0]
	v_pk_add_f32 v[100:101], v[100:101], 1.0 op_sel_hi:[1,0]
	v_max_f32_e32 v102, 1.0, v102
	v_pk_fma_f32 v[104:105], v[104:105], s[2:3], 0.5 op_sel_hi:[1,0,0]
	v_cvt_u32_f32_e32 v106, v102
	v_max_f32_e32 v102, 1.0, v103
	v_cvt_u32_f32_e32 v107, v102
	v_max_f32_e32 v102, 1.0, v104
	v_cvt_u32_f32_e32 v104, v102
	v_max_f32_e32 v102, 1.0, v105
	v_cvt_u32_f32_e32 v105, v102
	v_exp_f32_e32 v102, v99
	v_exp_f32_e32 v103, v98
	v_rcp_f32_e32 v100, v100
	v_rcp_f32_e32 v101, v101
	v_pk_add_f32 v[98:99], v[102:103], 1.0 op_sel_hi:[1,0]
	s_nop 0
	v_rcp_f32_e32 v98, v98
	v_rcp_f32_e32 v99, v99
	v_pk_fma_f32 v[100:101], v[100:101], s[2:3], 0.5 op_sel_hi:[1,0,0]
	v_lshl_or_b32 v102, v107, 8, v106
	v_max_f32_e32 v100, 1.0, v100
	v_pk_fma_f32 v[98:99], v[98:99], s[2:3], 0.5 op_sel_hi:[1,0,0]
	s_lshl_b32 s2, s46, 8
	s_add_i32 s2, s2, s84
	s_mul_hi_i32 s14, s2, 0xc00
	s_mulk_i32 s2, 0xc00
	v_max_f32_e32 v98, 1.0, v98
	v_max_f32_e32 v99, 1.0, v99
	s_add_u32 s2, s72, s2
	v_cvt_u32_f32_sdwa v98, v98 dst_sel:WORD_1 dst_unused:UNUSED_PAD src0_sel:DWORD
	v_cvt_u32_f32_sdwa v99, v99 dst_sel:BYTE_3 dst_unused:UNUSED_PAD src0_sel:DWORD
	v_max_f32_e32 v101, 1.0, v101
	s_addc_u32 s14, s73, s14
	v_cvt_u32_f32_sdwa v100, v100 dst_sel:WORD_1 dst_unused:UNUSED_PAD src0_sel:DWORD
	v_cvt_u32_f32_sdwa v101, v101 dst_sel:BYTE_3 dst_unused:UNUSED_PAD src0_sel:DWORD
	s_add_u32 s2, s2, s1
	s_addc_u32 s15, s14, 0
	s_add_u32 s14, s2, s75
	v_or3_b32 v98, v102, v98, v99
	v_lshl_or_b32 v99, v105, 8, v104
	s_addc_u32 s15, s15, 0
	v_or3_b32 v99, v99, v100, v101
	v_lshl_add_u64 v[100:101], s[14:15], 0, v[136:137]
	global_store_dwordx2 v[100:101], v[98:99], off offset:128
.LBB0_426:
	v_pk_mul_f32 v[100:101], v[96:97], s[10:11] op_sel_hi:[1,0]
	v_pk_mul_f32 v[102:103], v[94:95], s[10:11] op_sel_hi:[1,0]
	v_pk_mul_f32 v[98:99], v[92:93], s[10:11] op_sel_hi:[1,0]
	v_pk_mul_f32 v[104:105], v[90:91], s[10:11] op_sel_hi:[1,0]
	v_cndmask_b32_e64 v93, v93, v99, s[40:41]
	v_cndmask_b32_e64 v92, v92, v98, s[40:41]
	v_cndmask_b32_e64 v98, v91, v105, s[40:41]
	v_cndmask_b32_e64 v99, v90, v104, s[40:41]
	v_cndmask_b32_e64 v90, v97, v101, s[40:41]
	v_cndmask_b32_e64 v91, v96, v100, s[40:41]
	v_cndmask_b32_e64 v95, v95, v103, s[40:41]
	v_cndmask_b32_e64 v94, v94, v102, s[40:41]
	s_and_b64 vcc, exec, s[44:45]
	s_mov_b64 s[14:15], -1
	s_cbranch_vccnz .LBB0_432
	s_and_b64 vcc, exec, s[42:43]
	s_cbranch_vccnz .LBB0_429
	s_lshl_b32 s2, s46, 8
	s_add_i32 s2, s2, s78
	s_mul_hi_i32 s14, s2, 0x2800
	s_mulk_i32 s2, 0x2800
	s_add_u32 s2, s70, s2
	s_addc_u32 s24, s71, s14
	s_lshl_b64 s[14:15], s[56:57], 1
	s_add_u32 s2, s2, s14
	s_addc_u32 s15, s24, s15
	s_lshl_b32 s14, s75, 1
	s_add_u32 s14, s2, s14
	s_addc_u32 s15, s15, 0
	v_lshl_add_u64 v[96:97], s[14:15], 0, v[134:135]
	s_mov_b64 s[14:15], 0
	v_cvt_pk_bf16_f32 v100, v94, v95
	v_cvt_pk_bf16_f32 v101, v91, v90
	v_cvt_pk_bf16_f32 v102, v99, v98
	v_cvt_pk_bf16_f32 v103, v92, v93
	global_store_dwordx4 v[96:97], v[100:103], off
.LBB0_429:
	s_andn2_b64 vcc, exec, s[14:15]
	s_cbranch_vccnz .LBB0_431
	s_lshl_b32 s2, s46, 4
	s_ashr_i32 s14, s2, 31
	v_readlane_b32 s15, v254, 56
	s_add_u32 s2, s15, s2
	v_readlane_b32 s15, v254, 58
	s_addc_u32 s14, s15, s14
	s_mul_i32 s24, s14, 0x300
	v_mad_u64_u32 v[96:97], s[14:15], s2, v235, v[138:139]
	v_add_u32_e32 v97, s24, v97
	v_cvt_pk_bf16_f32 v100, v94, v95
	v_cvt_pk_bf16_f32 v101, v91, v90
	v_cvt_pk_bf16_f32 v102, v99, v98
	v_cvt_pk_bf16_f32 v103, v92, v93
	global_store_dwordx4 v[96:97], v[100:103], off

.LBB0_432:
	s_andn2_b64 vcc, exec, s[14:15]
	s_cbranch_vccnz .LBB0_434
	v_exp_f32_e32 v94, v94
	v_exp_f32_e32 v95, v95
	v_exp_f32_e32 v96, v99
	v_exp_f32_e32 v97, v98
	s_mov_b32 s2, 0x437f0000
	v_pk_add_f32 v[94:95], v[94:95], 1.0 op_sel_hi:[1,0]
	v_exp_f32_e32 v92, v92
	v_rcp_f32_e32 v94, v94
	v_rcp_f32_e32 v95, v95
	v_pk_add_f32 v[96:97], v[96:97], 1.0 op_sel_hi:[1,0]
	v_exp_f32_e32 v93, v93
	v_rcp_f32_e32 v96, v96
	v_rcp_f32_e32 v97, v97
	v_pk_fma_f32 v[94:95], v[94:95], s[2:3], 0.5 op_sel_hi:[1,0,0]
	v_pk_add_f32 v[92:93], v[92:93], 1.0 op_sel_hi:[1,0]
	v_max_f32_e32 v94, 1.0, v94
	v_pk_fma_f32 v[96:97], v[96:97], s[2:3], 0.5 op_sel_hi:[1,0,0]
	v_cvt_u32_f32_e32 v98, v94
	v_max_f32_e32 v94, 1.0, v95
	v_cvt_u32_f32_e32 v99, v94
	v_max_f32_e32 v94, 1.0, v96
	v_cvt_u32_f32_e32 v96, v94
	v_max_f32_e32 v94, 1.0, v97
	v_cvt_u32_f32_e32 v97, v94
	v_exp_f32_e32 v94, v91
	v_exp_f32_e32 v95, v90
	v_rcp_f32_e32 v92, v92
	v_rcp_f32_e32 v93, v93
	v_pk_add_f32 v[90:91], v[94:95], 1.0 op_sel_hi:[1,0]
	s_nop 0
	v_rcp_f32_e32 v90, v90
	v_rcp_f32_e32 v91, v91
	v_pk_fma_f32 v[92:93], v[92:93], s[2:3], 0.5 op_sel_hi:[1,0,0]
	v_lshl_or_b32 v94, v99, 8, v98
	v_max_f32_e32 v92, 1.0, v92
	v_pk_fma_f32 v[90:91], v[90:91], s[2:3], 0.5 op_sel_hi:[1,0,0]
	s_lshl_b32 s2, s46, 8
	s_add_i32 s2, s2, s78
	s_mul_hi_i32 s14, s2, 0xc00
	s_mulk_i32 s2, 0xc00
	v_max_f32_e32 v90, 1.0, v90
	v_max_f32_e32 v91, 1.0, v91
	s_add_u32 s2, s72, s2
	v_cvt_u32_f32_sdwa v90, v90 dst_sel:WORD_1 dst_unused:UNUSED_PAD src0_sel:DWORD
	v_cvt_u32_f32_sdwa v91, v91 dst_sel:BYTE_3 dst_unused:UNUSED_PAD src0_sel:DWORD
	v_max_f32_e32 v93, 1.0, v93
	s_addc_u32 s14, s73, s14
	v_cvt_u32_f32_sdwa v92, v92 dst_sel:WORD_1 dst_unused:UNUSED_PAD src0_sel:DWORD
	v_cvt_u32_f32_sdwa v93, v93 dst_sel:BYTE_3 dst_unused:UNUSED_PAD src0_sel:DWORD
	s_add_u32 s2, s2, s1
	s_addc_u32 s15, s14, 0
	s_add_u32 s14, s2, s75
	v_or3_b32 v90, v94, v90, v91
	v_lshl_or_b32 v91, v97, 8, v96
	s_addc_u32 s15, s15, 0
	v_or3_b32 v91, v91, v92, v93
	v_lshl_add_u64 v[92:93], s[14:15], 0, v[136:137]
	global_store_dwordx2 v[92:93], v[90:91], off
.LBB0_434:
	v_pk_mul_f32 v[92:93], v[88:89], s[10:11] op_sel_hi:[1,0]
	v_pk_mul_f32 v[94:95], v[86:87], s[10:11] op_sel_hi:[1,0]
	v_pk_mul_f32 v[90:91], v[84:85], s[10:11] op_sel_hi:[1,0]
	v_pk_mul_f32 v[96:97], v[82:83], s[10:11] op_sel_hi:[1,0]
	v_cndmask_b32_e64 v85, v85, v91, s[40:41]
	v_cndmask_b32_e64 v84, v84, v90, s[40:41]
	v_cndmask_b32_e64 v90, v83, v97, s[40:41]
	v_cndmask_b32_e64 v91, v82, v96, s[40:41]
	v_cndmask_b32_e64 v82, v89, v93, s[40:41]
	v_cndmask_b32_e64 v83, v88, v92, s[40:41]
	v_cndmask_b32_e64 v87, v87, v95, s[40:41]
	v_cndmask_b32_e64 v86, v86, v94, s[40:41]
	s_and_b64 vcc, exec, s[44:45]
	s_mov_b64 s[14:15], -1
	s_cbranch_vccnz .LBB0_440
	s_and_b64 vcc, exec, s[42:43]
	s_cbranch_vccnz .LBB0_437
	s_lshl_b32 s2, s46, 8
	s_add_i32 s2, s2, s78
	s_mul_hi_i32 s14, s2, 0x2800
	s_mulk_i32 s2, 0x2800
	s_add_u32 s2, s70, s2
	s_addc_u32 s24, s71, s14
	s_lshl_b64 s[14:15], s[56:57], 1
	s_add_u32 s2, s2, s14
	s_addc_u32 s15, s24, s15
	s_lshl_b32 s14, s75, 1
	s_add_u32 s14, s2, s14
	s_addc_u32 s15, s15, 0
	v_lshl_add_u64 v[88:89], s[14:15], 0, v[134:135]
	s_mov_b64 s[14:15], 0
	v_cvt_pk_bf16_f32 v92, v86, v87
	v_cvt_pk_bf16_f32 v93, v83, v82
	v_cvt_pk_bf16_f32 v94, v91, v90
	v_cvt_pk_bf16_f32 v95, v84, v85
	global_store_dwordx4 v[88:89], v[92:95], off offset:256
.LBB0_437:
	s_andn2_b64 vcc, exec, s[14:15]
	s_cbranch_vccnz .LBB0_439
	s_lshl_b32 s2, s46, 4
	s_ashr_i32 s14, s2, 31
	v_readlane_b32 s15, v254, 59
	s_add_u32 s2, s15, s2
	v_readlane_b32 s15, v254, 60
	s_addc_u32 s14, s15, s14
	s_mul_i32 s24, s14, 0x300
	v_mad_u64_u32 v[88:89], s[14:15], s2, v235, v[138:139]
	v_add_u32_e32 v89, s24, v89
	v_cvt_pk_bf16_f32 v92, v86, v87
	v_cvt_pk_bf16_f32 v93, v83, v82
	v_cvt_pk_bf16_f32 v94, v91, v90
	v_cvt_pk_bf16_f32 v95, v84, v85
	global_store_dwordx4 v[88:89], v[92:95], off

.LBB0_440:
	s_andn2_b64 vcc, exec, s[14:15]
	s_cbranch_vccnz .LBB0_442
	v_exp_f32_e32 v86, v86
	v_exp_f32_e32 v87, v87
	v_exp_f32_e32 v88, v91
	v_exp_f32_e32 v89, v90
	s_mov_b32 s2, 0x437f0000
	v_pk_add_f32 v[86:87], v[86:87], 1.0 op_sel_hi:[1,0]
	v_exp_f32_e32 v84, v84
	v_rcp_f32_e32 v86, v86
	v_rcp_f32_e32 v87, v87
	v_pk_add_f32 v[88:89], v[88:89], 1.0 op_sel_hi:[1,0]
	v_exp_f32_e32 v85, v85
	v_rcp_f32_e32 v88, v88
	v_rcp_f32_e32 v89, v89
	v_pk_fma_f32 v[86:87], v[86:87], s[2:3], 0.5 op_sel_hi:[1,0,0]
	v_pk_add_f32 v[84:85], v[84:85], 1.0 op_sel_hi:[1,0]
	v_max_f32_e32 v86, 1.0, v86
	v_pk_fma_f32 v[88:89], v[88:89], s[2:3], 0.5 op_sel_hi:[1,0,0]
	v_cvt_u32_f32_e32 v90, v86
	v_max_f32_e32 v86, 1.0, v87
	v_cvt_u32_f32_e32 v91, v86
	v_max_f32_e32 v86, 1.0, v88
	v_cvt_u32_f32_e32 v88, v86
	v_max_f32_e32 v86, 1.0, v89
	v_cvt_u32_f32_e32 v89, v86
	v_exp_f32_e32 v86, v83
	v_exp_f32_e32 v87, v82
	v_rcp_f32_e32 v84, v84
	v_rcp_f32_e32 v85, v85
	v_pk_add_f32 v[82:83], v[86:87], 1.0 op_sel_hi:[1,0]
	s_nop 0
	v_rcp_f32_e32 v82, v82
	v_rcp_f32_e32 v83, v83
	v_pk_fma_f32 v[84:85], v[84:85], s[2:3], 0.5 op_sel_hi:[1,0,0]
	v_lshl_or_b32 v86, v91, 8, v90
	v_max_f32_e32 v84, 1.0, v84
	v_pk_fma_f32 v[82:83], v[82:83], s[2:3], 0.5 op_sel_hi:[1,0,0]
	s_lshl_b32 s2, s46, 8
	s_add_i32 s2, s2, s78
	s_mul_hi_i32 s14, s2, 0xc00
	s_mulk_i32 s2, 0xc00
	v_max_f32_e32 v82, 1.0, v82
	v_max_f32_e32 v83, 1.0, v83
	s_add_u32 s2, s72, s2
	v_cvt_u32_f32_sdwa v82, v82 dst_sel:WORD_1 dst_unused:UNUSED_PAD src0_sel:DWORD
	v_cvt_u32_f32_sdwa v83, v83 dst_sel:BYTE_3 dst_unused:UNUSED_PAD src0_sel:DWORD
	v_max_f32_e32 v85, 1.0, v85
	s_addc_u32 s14, s73, s14
	v_cvt_u32_f32_sdwa v84, v84 dst_sel:WORD_1 dst_unused:UNUSED_PAD src0_sel:DWORD
	v_cvt_u32_f32_sdwa v85, v85 dst_sel:BYTE_3 dst_unused:UNUSED_PAD src0_sel:DWORD
	s_add_u32 s2, s2, s1
	s_addc_u32 s15, s14, 0
	s_add_u32 s14, s2, s75
	v_or3_b32 v82, v86, v82, v83
	v_lshl_or_b32 v83, v89, 8, v88
	s_addc_u32 s15, s15, 0
	v_or3_b32 v83, v83, v84, v85
	v_lshl_add_u64 v[84:85], s[14:15], 0, v[136:137]
	global_store_dwordx2 v[84:85], v[82:83], off offset:128
.LBB0_442:
	v_pk_mul_f32 v[84:85], v[80:81], s[10:11] op_sel_hi:[1,0]
	v_pk_mul_f32 v[86:87], v[78:79], s[10:11] op_sel_hi:[1,0]
	v_pk_mul_f32 v[82:83], v[76:77], s[10:11] op_sel_hi:[1,0]
	v_pk_mul_f32 v[88:89], v[74:75], s[10:11] op_sel_hi:[1,0]
	v_cndmask_b32_e64 v77, v77, v83, s[40:41]
	v_cndmask_b32_e64 v76, v76, v82, s[40:41]
	v_cndmask_b32_e64 v82, v75, v89, s[40:41]
	v_cndmask_b32_e64 v83, v74, v88, s[40:41]
	v_cndmask_b32_e64 v74, v81, v85, s[40:41]
	v_cndmask_b32_e64 v75, v80, v84, s[40:41]
	v_cndmask_b32_e64 v79, v79, v87, s[40:41]
	v_cndmask_b32_e64 v78, v78, v86, s[40:41]
	s_and_b64 vcc, exec, s[44:45]
	s_mov_b64 s[14:15], -1
	s_cbranch_vccnz .LBB0_448
	s_and_b64 vcc, exec, s[42:43]
	s_cbranch_vccnz .LBB0_445
	s_lshl_b32 s2, s46, 8
	s_add_i32 s2, s2, s90
	s_mul_hi_i32 s14, s2, 0x2800
	s_mulk_i32 s2, 0x2800
	s_add_u32 s2, s70, s2
	s_addc_u32 s24, s71, s14
	s_lshl_b64 s[14:15], s[56:57], 1
	s_add_u32 s2, s2, s14
	s_addc_u32 s15, s24, s15
	s_lshl_b32 s14, s75, 1
	s_add_u32 s14, s2, s14
	s_addc_u32 s15, s15, 0
	v_lshl_add_u64 v[80:81], s[14:15], 0, v[134:135]
	s_mov_b64 s[14:15], 0
	v_cvt_pk_bf16_f32 v84, v78, v79
	v_cvt_pk_bf16_f32 v85, v75, v74
	v_cvt_pk_bf16_f32 v86, v83, v82
	v_cvt_pk_bf16_f32 v87, v76, v77
	global_store_dwordx4 v[80:81], v[84:87], off
.LBB0_445:
	s_andn2_b64 vcc, exec, s[14:15]
	s_cbranch_vccnz .LBB0_447
	s_lshl_b32 s2, s46, 4
	s_ashr_i32 s14, s2, 31
	v_readlane_b32 s15, v254, 62
	s_add_u32 s2, s15, s2
	v_readlane_b32 s15, v255, 0
	s_addc_u32 s14, s15, s14
	s_mul_i32 s24, s14, 0x300
	v_mad_u64_u32 v[80:81], s[14:15], s2, v235, v[138:139]
	v_add_u32_e32 v81, s24, v81
	v_cvt_pk_bf16_f32 v84, v78, v79
	v_cvt_pk_bf16_f32 v85, v75, v74
	v_cvt_pk_bf16_f32 v86, v83, v82
	v_cvt_pk_bf16_f32 v87, v76, v77
	global_store_dwordx4 v[80:81], v[84:87], off

.LBB0_448:
	s_andn2_b64 vcc, exec, s[14:15]
	s_cbranch_vccnz .LBB0_450
	v_exp_f32_e32 v78, v78
	v_exp_f32_e32 v79, v79
	v_exp_f32_e32 v80, v83
	v_exp_f32_e32 v81, v82
	s_mov_b32 s2, 0x437f0000
	v_pk_add_f32 v[78:79], v[78:79], 1.0 op_sel_hi:[1,0]
	v_exp_f32_e32 v76, v76
	v_rcp_f32_e32 v78, v78
	v_rcp_f32_e32 v79, v79
	v_pk_add_f32 v[80:81], v[80:81], 1.0 op_sel_hi:[1,0]
	v_exp_f32_e32 v77, v77
	v_rcp_f32_e32 v80, v80
	v_rcp_f32_e32 v81, v81
	v_pk_fma_f32 v[78:79], v[78:79], s[2:3], 0.5 op_sel_hi:[1,0,0]
	v_pk_add_f32 v[76:77], v[76:77], 1.0 op_sel_hi:[1,0]
	v_max_f32_e32 v78, 1.0, v78
	v_pk_fma_f32 v[80:81], v[80:81], s[2:3], 0.5 op_sel_hi:[1,0,0]
	v_cvt_u32_f32_e32 v82, v78
	v_max_f32_e32 v78, 1.0, v79
	v_cvt_u32_f32_e32 v83, v78
	v_max_f32_e32 v78, 1.0, v80
	v_cvt_u32_f32_e32 v80, v78
	v_max_f32_e32 v78, 1.0, v81
	v_cvt_u32_f32_e32 v81, v78
	v_exp_f32_e32 v78, v75
	v_exp_f32_e32 v79, v74
	v_rcp_f32_e32 v76, v76
	v_rcp_f32_e32 v77, v77
	v_pk_add_f32 v[74:75], v[78:79], 1.0 op_sel_hi:[1,0]
	s_nop 0
	v_rcp_f32_e32 v74, v74
	v_rcp_f32_e32 v75, v75
	v_pk_fma_f32 v[76:77], v[76:77], s[2:3], 0.5 op_sel_hi:[1,0,0]
	v_lshl_or_b32 v78, v83, 8, v82
	v_max_f32_e32 v76, 1.0, v76
	v_pk_fma_f32 v[74:75], v[74:75], s[2:3], 0.5 op_sel_hi:[1,0,0]
	s_lshl_b32 s2, s46, 8
	s_add_i32 s2, s2, s90
	s_mul_hi_i32 s14, s2, 0xc00
	s_mulk_i32 s2, 0xc00
	v_max_f32_e32 v74, 1.0, v74
	v_max_f32_e32 v75, 1.0, v75
	s_add_u32 s2, s72, s2
	v_cvt_u32_f32_sdwa v74, v74 dst_sel:WORD_1 dst_unused:UNUSED_PAD src0_sel:DWORD
	v_cvt_u32_f32_sdwa v75, v75 dst_sel:BYTE_3 dst_unused:UNUSED_PAD src0_sel:DWORD
	v_max_f32_e32 v77, 1.0, v77
	s_addc_u32 s14, s73, s14
	v_cvt_u32_f32_sdwa v76, v76 dst_sel:WORD_1 dst_unused:UNUSED_PAD src0_sel:DWORD
	v_cvt_u32_f32_sdwa v77, v77 dst_sel:BYTE_3 dst_unused:UNUSED_PAD src0_sel:DWORD
	s_add_u32 s2, s2, s1
	s_addc_u32 s15, s14, 0
	s_add_u32 s14, s2, s75
	v_or3_b32 v74, v78, v74, v75
	v_lshl_or_b32 v75, v81, 8, v80
	s_addc_u32 s15, s15, 0
	v_or3_b32 v75, v75, v76, v77
	v_lshl_add_u64 v[76:77], s[14:15], 0, v[136:137]
	global_store_dwordx2 v[76:77], v[74:75], off
.LBB0_450:
	v_pk_mul_f32 v[76:77], v[72:73], s[10:11] op_sel_hi:[1,0]
	v_pk_mul_f32 v[78:79], v[70:71], s[10:11] op_sel_hi:[1,0]
	v_pk_mul_f32 v[74:75], v[68:69], s[10:11] op_sel_hi:[1,0]
	v_pk_mul_f32 v[80:81], v[66:67], s[10:11] op_sel_hi:[1,0]
	v_cndmask_b32_e64 v69, v69, v75, s[40:41]
	v_cndmask_b32_e64 v68, v68, v74, s[40:41]
	v_cndmask_b32_e64 v74, v67, v81, s[40:41]
	v_cndmask_b32_e64 v75, v66, v80, s[40:41]
	v_cndmask_b32_e64 v66, v73, v77, s[40:41]
	v_cndmask_b32_e64 v67, v72, v76, s[40:41]
	v_cndmask_b32_e64 v71, v71, v79, s[40:41]
	v_cndmask_b32_e64 v70, v70, v78, s[40:41]
	s_and_b64 vcc, exec, s[44:45]
	s_mov_b64 s[14:15], -1
	s_cbranch_vccnz .LBB0_456
	s_and_b64 vcc, exec, s[42:43]
	s_cbranch_vccnz .LBB0_453
	s_lshl_b32 s2, s46, 8
	s_add_i32 s2, s2, s90
	s_mul_hi_i32 s14, s2, 0x2800
	s_mulk_i32 s2, 0x2800
	s_add_u32 s2, s70, s2
	s_addc_u32 s24, s71, s14
	s_lshl_b64 s[14:15], s[56:57], 1
	s_add_u32 s2, s2, s14
	s_addc_u32 s15, s24, s15
	s_lshl_b32 s14, s75, 1
	s_add_u32 s14, s2, s14
	s_addc_u32 s15, s15, 0
	v_lshl_add_u64 v[72:73], s[14:15], 0, v[134:135]
	s_mov_b64 s[14:15], 0
	v_cvt_pk_bf16_f32 v76, v70, v71
	v_cvt_pk_bf16_f32 v77, v67, v66
	v_cvt_pk_bf16_f32 v78, v75, v74
	v_cvt_pk_bf16_f32 v79, v68, v69
	global_store_dwordx4 v[72:73], v[76:79], off offset:256
.LBB0_453:
	s_andn2_b64 vcc, exec, s[14:15]
	s_cbranch_vccnz .LBB0_455
	s_lshl_b32 s2, s46, 4
	s_ashr_i32 s14, s2, 31
	v_readlane_b32 s15, v255, 2
	s_add_u32 s2, s15, s2
	v_readlane_b32 s15, v255, 4
	s_addc_u32 s14, s15, s14
	s_mul_i32 s24, s14, 0x300
	v_mad_u64_u32 v[72:73], s[14:15], s2, v235, v[138:139]
	v_add_u32_e32 v73, s24, v73
	v_cvt_pk_bf16_f32 v76, v70, v71
	v_cvt_pk_bf16_f32 v77, v67, v66
	v_cvt_pk_bf16_f32 v78, v75, v74
	v_cvt_pk_bf16_f32 v79, v68, v69
	global_store_dwordx4 v[72:73], v[76:79], off

.LBB0_456:
	s_andn2_b64 vcc, exec, s[14:15]
	s_cbranch_vccnz .LBB0_458
	v_exp_f32_e32 v70, v70
	v_exp_f32_e32 v71, v71
	v_exp_f32_e32 v72, v75
	v_exp_f32_e32 v73, v74
	s_mov_b32 s2, 0x437f0000
	v_pk_add_f32 v[70:71], v[70:71], 1.0 op_sel_hi:[1,0]
	v_exp_f32_e32 v68, v68
	v_rcp_f32_e32 v70, v70
	v_rcp_f32_e32 v71, v71
	v_pk_add_f32 v[72:73], v[72:73], 1.0 op_sel_hi:[1,0]
	v_exp_f32_e32 v69, v69
	v_rcp_f32_e32 v72, v72
	v_rcp_f32_e32 v73, v73
	v_pk_fma_f32 v[70:71], v[70:71], s[2:3], 0.5 op_sel_hi:[1,0,0]
	v_pk_add_f32 v[68:69], v[68:69], 1.0 op_sel_hi:[1,0]
	v_max_f32_e32 v70, 1.0, v70
	v_pk_fma_f32 v[72:73], v[72:73], s[2:3], 0.5 op_sel_hi:[1,0,0]
	v_cvt_u32_f32_e32 v74, v70
	v_max_f32_e32 v70, 1.0, v71
	v_cvt_u32_f32_e32 v75, v70
	v_max_f32_e32 v70, 1.0, v72
	v_cvt_u32_f32_e32 v72, v70
	v_max_f32_e32 v70, 1.0, v73
	v_cvt_u32_f32_e32 v73, v70
	v_exp_f32_e32 v70, v67
	v_exp_f32_e32 v71, v66
	v_rcp_f32_e32 v68, v68
	v_rcp_f32_e32 v69, v69
	v_pk_add_f32 v[66:67], v[70:71], 1.0 op_sel_hi:[1,0]
	s_nop 0
	v_rcp_f32_e32 v66, v66
	v_rcp_f32_e32 v67, v67
	v_pk_fma_f32 v[68:69], v[68:69], s[2:3], 0.5 op_sel_hi:[1,0,0]
	v_lshl_or_b32 v70, v75, 8, v74
	v_max_f32_e32 v68, 1.0, v68
	v_pk_fma_f32 v[66:67], v[66:67], s[2:3], 0.5 op_sel_hi:[1,0,0]
	s_lshl_b32 s2, s46, 8
	s_add_i32 s2, s2, s90
	s_mul_hi_i32 s14, s2, 0xc00
	s_mulk_i32 s2, 0xc00
	v_max_f32_e32 v66, 1.0, v66
	v_max_f32_e32 v67, 1.0, v67
	s_add_u32 s2, s72, s2
	v_cvt_u32_f32_sdwa v66, v66 dst_sel:WORD_1 dst_unused:UNUSED_PAD src0_sel:DWORD
	v_cvt_u32_f32_sdwa v67, v67 dst_sel:BYTE_3 dst_unused:UNUSED_PAD src0_sel:DWORD
	v_max_f32_e32 v69, 1.0, v69
	s_addc_u32 s14, s73, s14
	v_cvt_u32_f32_sdwa v68, v68 dst_sel:WORD_1 dst_unused:UNUSED_PAD src0_sel:DWORD
	v_cvt_u32_f32_sdwa v69, v69 dst_sel:BYTE_3 dst_unused:UNUSED_PAD src0_sel:DWORD
	s_add_u32 s2, s2, s1
	s_addc_u32 s15, s14, 0
	s_add_u32 s14, s2, s75
	v_or3_b32 v66, v70, v66, v67
	v_lshl_or_b32 v67, v73, 8, v72
	s_addc_u32 s15, s15, 0
	v_or3_b32 v67, v67, v68, v69
	v_lshl_add_u64 v[68:69], s[14:15], 0, v[136:137]
	global_store_dwordx2 v[68:69], v[66:67], off offset:128
.LBB0_458:
	v_pk_mul_f32 v[68:69], v[64:65], s[10:11] op_sel_hi:[1,0]
	v_pk_mul_f32 v[70:71], v[62:63], s[10:11] op_sel_hi:[1,0]
	v_pk_mul_f32 v[66:67], v[60:61], s[10:11] op_sel_hi:[1,0]
	v_pk_mul_f32 v[72:73], v[58:59], s[10:11] op_sel_hi:[1,0]
	v_cndmask_b32_e64 v61, v61, v67, s[40:41]
	v_cndmask_b32_e64 v60, v60, v66, s[40:41]
	v_cndmask_b32_e64 v66, v59, v73, s[40:41]
	v_cndmask_b32_e64 v67, v58, v72, s[40:41]
	v_cndmask_b32_e64 v58, v65, v69, s[40:41]
	v_cndmask_b32_e64 v59, v64, v68, s[40:41]
	v_cndmask_b32_e64 v63, v63, v71, s[40:41]
	v_cndmask_b32_e64 v62, v62, v70, s[40:41]
	s_and_b64 vcc, exec, s[44:45]
	s_mov_b64 s[14:15], -1
	s_cbranch_vccnz .LBB0_464
	s_and_b64 vcc, exec, s[42:43]
	s_cbranch_vccnz .LBB0_461
	s_lshl_b32 s2, s46, 8
	s_add_i32 s2, s2, s81
	s_mul_hi_i32 s14, s2, 0x2800
	s_mulk_i32 s2, 0x2800
	s_add_u32 s2, s70, s2
	s_addc_u32 s24, s71, s14
	s_lshl_b64 s[14:15], s[56:57], 1
	s_add_u32 s2, s2, s14
	s_addc_u32 s15, s24, s15
	s_lshl_b32 s14, s75, 1
	s_add_u32 s14, s2, s14
	s_addc_u32 s15, s15, 0
	v_lshl_add_u64 v[64:65], s[14:15], 0, v[134:135]
	s_mov_b64 s[14:15], 0
	v_cvt_pk_bf16_f32 v68, v62, v63
	v_cvt_pk_bf16_f32 v69, v59, v58
	v_cvt_pk_bf16_f32 v70, v67, v66
	v_cvt_pk_bf16_f32 v71, v60, v61
	global_store_dwordx4 v[64:65], v[68:71], off
.LBB0_461:
	s_andn2_b64 vcc, exec, s[14:15]
	s_cbranch_vccnz .LBB0_463
	s_lshl_b32 s2, s46, 4
	s_ashr_i32 s14, s2, 31
	v_readlane_b32 s15, v255, 6
	s_add_u32 s2, s15, s2
	v_readlane_b32 s15, v255, 8
	s_addc_u32 s14, s15, s14
	s_mul_i32 s24, s14, 0x300
	v_mad_u64_u32 v[64:65], s[14:15], s2, v235, v[138:139]
	v_add_u32_e32 v65, s24, v65
	v_cvt_pk_bf16_f32 v68, v62, v63
	v_cvt_pk_bf16_f32 v69, v59, v58
	v_cvt_pk_bf16_f32 v70, v67, v66
	v_cvt_pk_bf16_f32 v71, v60, v61
	global_store_dwordx4 v[64:65], v[68:71], off

.LBB0_464:
	s_andn2_b64 vcc, exec, s[14:15]
	s_cbranch_vccnz .LBB0_466
	v_exp_f32_e32 v62, v62
	v_exp_f32_e32 v63, v63
	v_exp_f32_e32 v64, v67
	v_exp_f32_e32 v65, v66
	s_mov_b32 s2, 0x437f0000
	v_pk_add_f32 v[62:63], v[62:63], 1.0 op_sel_hi:[1,0]
	v_exp_f32_e32 v60, v60
	v_rcp_f32_e32 v62, v62
	v_rcp_f32_e32 v63, v63
	v_pk_add_f32 v[64:65], v[64:65], 1.0 op_sel_hi:[1,0]
	v_exp_f32_e32 v61, v61
	v_rcp_f32_e32 v64, v64
	v_rcp_f32_e32 v65, v65
	v_pk_fma_f32 v[62:63], v[62:63], s[2:3], 0.5 op_sel_hi:[1,0,0]
	v_pk_add_f32 v[60:61], v[60:61], 1.0 op_sel_hi:[1,0]
	v_max_f32_e32 v62, 1.0, v62
	v_pk_fma_f32 v[64:65], v[64:65], s[2:3], 0.5 op_sel_hi:[1,0,0]
	v_cvt_u32_f32_e32 v66, v62
	v_max_f32_e32 v62, 1.0, v63
	v_cvt_u32_f32_e32 v67, v62
	v_max_f32_e32 v62, 1.0, v64
	v_cvt_u32_f32_e32 v64, v62
	v_max_f32_e32 v62, 1.0, v65
	v_cvt_u32_f32_e32 v65, v62
	v_exp_f32_e32 v62, v59
	v_exp_f32_e32 v63, v58
	v_rcp_f32_e32 v60, v60
	v_rcp_f32_e32 v61, v61
	v_pk_add_f32 v[58:59], v[62:63], 1.0 op_sel_hi:[1,0]
	s_nop 0
	v_rcp_f32_e32 v58, v58
	v_rcp_f32_e32 v59, v59
	v_pk_fma_f32 v[60:61], v[60:61], s[2:3], 0.5 op_sel_hi:[1,0,0]
	v_lshl_or_b32 v62, v67, 8, v66
	v_max_f32_e32 v60, 1.0, v60
	v_pk_fma_f32 v[58:59], v[58:59], s[2:3], 0.5 op_sel_hi:[1,0,0]
	s_lshl_b32 s2, s46, 8
	s_add_i32 s2, s2, s81
	s_mul_hi_i32 s14, s2, 0xc00
	s_mulk_i32 s2, 0xc00
	v_max_f32_e32 v58, 1.0, v58
	v_max_f32_e32 v59, 1.0, v59
	s_add_u32 s2, s72, s2
	v_cvt_u32_f32_sdwa v58, v58 dst_sel:WORD_1 dst_unused:UNUSED_PAD src0_sel:DWORD
	v_cvt_u32_f32_sdwa v59, v59 dst_sel:BYTE_3 dst_unused:UNUSED_PAD src0_sel:DWORD
	v_max_f32_e32 v61, 1.0, v61
	s_addc_u32 s14, s73, s14
	v_cvt_u32_f32_sdwa v60, v60 dst_sel:WORD_1 dst_unused:UNUSED_PAD src0_sel:DWORD
	v_cvt_u32_f32_sdwa v61, v61 dst_sel:BYTE_3 dst_unused:UNUSED_PAD src0_sel:DWORD
	s_add_u32 s2, s2, s1
	s_addc_u32 s15, s14, 0
	s_add_u32 s14, s2, s75
	v_or3_b32 v58, v62, v58, v59
	v_lshl_or_b32 v59, v65, 8, v64
	s_addc_u32 s15, s15, 0
	v_or3_b32 v59, v59, v60, v61
	v_lshl_add_u64 v[60:61], s[14:15], 0, v[136:137]
	global_store_dwordx2 v[60:61], v[58:59], off
.LBB0_466:
	v_pk_mul_f32 v[60:61], v[56:57], s[10:11] op_sel_hi:[1,0]
	v_pk_mul_f32 v[62:63], v[54:55], s[10:11] op_sel_hi:[1,0]
	v_pk_mul_f32 v[58:59], v[52:53], s[10:11] op_sel_hi:[1,0]
	v_pk_mul_f32 v[64:65], v[50:51], s[10:11] op_sel_hi:[1,0]
	v_cndmask_b32_e64 v53, v53, v59, s[40:41]
	v_cndmask_b32_e64 v52, v52, v58, s[40:41]
	v_cndmask_b32_e64 v58, v51, v65, s[40:41]
	v_cndmask_b32_e64 v59, v50, v64, s[40:41]
	v_cndmask_b32_e64 v50, v57, v61, s[40:41]
	v_cndmask_b32_e64 v51, v56, v60, s[40:41]
	v_cndmask_b32_e64 v55, v55, v63, s[40:41]
	v_cndmask_b32_e64 v54, v54, v62, s[40:41]
	s_and_b64 vcc, exec, s[44:45]
	s_mov_b64 s[14:15], -1
	s_cbranch_vccnz .LBB0_472
	s_and_b64 vcc, exec, s[42:43]
	s_cbranch_vccnz .LBB0_469
	s_lshl_b32 s2, s46, 8
	s_add_i32 s2, s2, s81
	s_mul_hi_i32 s14, s2, 0x2800
	s_mulk_i32 s2, 0x2800
	s_add_u32 s2, s70, s2
	s_addc_u32 s24, s71, s14
	s_lshl_b64 s[14:15], s[56:57], 1
	s_add_u32 s2, s2, s14
	s_addc_u32 s15, s24, s15
	s_lshl_b32 s14, s75, 1
	s_add_u32 s14, s2, s14
	s_addc_u32 s15, s15, 0
	v_lshl_add_u64 v[56:57], s[14:15], 0, v[134:135]
	s_mov_b64 s[14:15], 0
	v_cvt_pk_bf16_f32 v60, v54, v55
	v_cvt_pk_bf16_f32 v61, v51, v50
	v_cvt_pk_bf16_f32 v62, v59, v58
	v_cvt_pk_bf16_f32 v63, v52, v53
	global_store_dwordx4 v[56:57], v[60:63], off offset:256
.LBB0_469:
	s_andn2_b64 vcc, exec, s[14:15]
	s_cbranch_vccnz .LBB0_471
	s_lshl_b32 s2, s46, 4
	s_ashr_i32 s14, s2, 31
	v_readlane_b32 s15, v255, 10
	s_add_u32 s2, s15, s2
	v_readlane_b32 s15, v255, 11
	s_addc_u32 s14, s15, s14
	s_mul_i32 s24, s14, 0x300
	v_mad_u64_u32 v[56:57], s[14:15], s2, v235, v[138:139]
	v_add_u32_e32 v57, s24, v57
	v_cvt_pk_bf16_f32 v60, v54, v55
	v_cvt_pk_bf16_f32 v61, v51, v50
	v_cvt_pk_bf16_f32 v62, v59, v58
	v_cvt_pk_bf16_f32 v63, v52, v53
	global_store_dwordx4 v[56:57], v[60:63], off

.LBB0_472:
	s_andn2_b64 vcc, exec, s[14:15]
	s_cbranch_vccnz .LBB0_474
	v_exp_f32_e32 v54, v54
	v_exp_f32_e32 v55, v55
	v_exp_f32_e32 v56, v59
	v_exp_f32_e32 v57, v58
	s_mov_b32 s2, 0x437f0000
	v_pk_add_f32 v[54:55], v[54:55], 1.0 op_sel_hi:[1,0]
	v_exp_f32_e32 v52, v52
	v_rcp_f32_e32 v54, v54
	v_rcp_f32_e32 v55, v55
	v_pk_add_f32 v[56:57], v[56:57], 1.0 op_sel_hi:[1,0]
	v_exp_f32_e32 v53, v53
	v_rcp_f32_e32 v56, v56
	v_rcp_f32_e32 v57, v57
	v_pk_fma_f32 v[54:55], v[54:55], s[2:3], 0.5 op_sel_hi:[1,0,0]
	v_pk_add_f32 v[52:53], v[52:53], 1.0 op_sel_hi:[1,0]
	v_max_f32_e32 v54, 1.0, v54
	v_pk_fma_f32 v[56:57], v[56:57], s[2:3], 0.5 op_sel_hi:[1,0,0]
	v_cvt_u32_f32_e32 v58, v54
	v_max_f32_e32 v54, 1.0, v55
	v_cvt_u32_f32_e32 v59, v54
	v_max_f32_e32 v54, 1.0, v56
	v_cvt_u32_f32_e32 v56, v54
	v_max_f32_e32 v54, 1.0, v57
	v_cvt_u32_f32_e32 v57, v54
	v_exp_f32_e32 v54, v51
	v_exp_f32_e32 v55, v50
	v_rcp_f32_e32 v52, v52
	v_rcp_f32_e32 v53, v53
	v_pk_add_f32 v[50:51], v[54:55], 1.0 op_sel_hi:[1,0]
	s_nop 0
	v_rcp_f32_e32 v50, v50
	v_rcp_f32_e32 v51, v51
	v_pk_fma_f32 v[52:53], v[52:53], s[2:3], 0.5 op_sel_hi:[1,0,0]
	v_lshl_or_b32 v54, v59, 8, v58
	v_max_f32_e32 v52, 1.0, v52
	v_pk_fma_f32 v[50:51], v[50:51], s[2:3], 0.5 op_sel_hi:[1,0,0]
	s_lshl_b32 s2, s46, 8
	s_add_i32 s2, s2, s81
	s_mul_hi_i32 s14, s2, 0xc00
	s_mulk_i32 s2, 0xc00
	v_max_f32_e32 v50, 1.0, v50
	v_max_f32_e32 v51, 1.0, v51
	s_add_u32 s2, s72, s2
	v_cvt_u32_f32_sdwa v50, v50 dst_sel:WORD_1 dst_unused:UNUSED_PAD src0_sel:DWORD
	v_cvt_u32_f32_sdwa v51, v51 dst_sel:BYTE_3 dst_unused:UNUSED_PAD src0_sel:DWORD
	v_max_f32_e32 v53, 1.0, v53
	s_addc_u32 s14, s73, s14
	v_cvt_u32_f32_sdwa v52, v52 dst_sel:WORD_1 dst_unused:UNUSED_PAD src0_sel:DWORD
	v_cvt_u32_f32_sdwa v53, v53 dst_sel:BYTE_3 dst_unused:UNUSED_PAD src0_sel:DWORD
	s_add_u32 s2, s2, s1
	s_addc_u32 s15, s14, 0
	s_add_u32 s14, s2, s75
	v_or3_b32 v50, v54, v50, v51
	v_lshl_or_b32 v51, v57, 8, v56
	s_addc_u32 s15, s15, 0
	v_or3_b32 v51, v51, v52, v53
	v_lshl_add_u64 v[52:53], s[14:15], 0, v[136:137]
	global_store_dwordx2 v[52:53], v[50:51], off offset:128
.LBB0_474:
	v_pk_mul_f32 v[52:53], v[48:49], s[10:11] op_sel_hi:[1,0]
	v_pk_mul_f32 v[54:55], v[46:47], s[10:11] op_sel_hi:[1,0]
	v_pk_mul_f32 v[50:51], v[44:45], s[10:11] op_sel_hi:[1,0]
	v_pk_mul_f32 v[56:57], v[42:43], s[10:11] op_sel_hi:[1,0]
	v_cndmask_b32_e64 v45, v45, v51, s[40:41]
	v_cndmask_b32_e64 v44, v44, v50, s[40:41]
	v_cndmask_b32_e64 v50, v43, v57, s[40:41]
	v_cndmask_b32_e64 v51, v42, v56, s[40:41]
	v_cndmask_b32_e64 v42, v49, v53, s[40:41]
	v_cndmask_b32_e64 v43, v48, v52, s[40:41]
	v_cndmask_b32_e64 v47, v47, v55, s[40:41]
	v_cndmask_b32_e64 v46, v46, v54, s[40:41]
	s_and_b64 vcc, exec, s[44:45]
	s_mov_b64 s[14:15], -1
	s_cbranch_vccnz .LBB0_480
	s_and_b64 vcc, exec, s[42:43]
	s_cbranch_vccnz .LBB0_477
	s_lshl_b32 s2, s46, 8
	s_add_i32 s2, s2, s80
	s_mul_hi_i32 s14, s2, 0x2800
	s_mulk_i32 s2, 0x2800
	s_add_u32 s2, s70, s2
	s_addc_u32 s24, s71, s14
	s_lshl_b64 s[14:15], s[56:57], 1
	s_add_u32 s2, s2, s14
	s_addc_u32 s15, s24, s15
	s_lshl_b32 s14, s75, 1
	s_add_u32 s14, s2, s14
	s_addc_u32 s15, s15, 0
	v_lshl_add_u64 v[48:49], s[14:15], 0, v[134:135]
	s_mov_b64 s[14:15], 0
	v_cvt_pk_bf16_f32 v52, v46, v47
	v_cvt_pk_bf16_f32 v53, v43, v42
	v_cvt_pk_bf16_f32 v54, v51, v50
	v_cvt_pk_bf16_f32 v55, v44, v45
	global_store_dwordx4 v[48:49], v[52:55], off
.LBB0_477:
	s_andn2_b64 vcc, exec, s[14:15]
	s_cbranch_vccnz .LBB0_479
	s_lshl_b32 s2, s46, 4
	s_ashr_i32 s14, s2, 31
	v_readlane_b32 s15, v255, 12
	s_add_u32 s2, s15, s2
	v_readlane_b32 s15, v255, 13
	s_addc_u32 s14, s15, s14
	s_mul_i32 s24, s14, 0x300
	v_mad_u64_u32 v[48:49], s[14:15], s2, v235, v[138:139]
	v_add_u32_e32 v49, s24, v49
	v_cvt_pk_bf16_f32 v52, v46, v47
	v_cvt_pk_bf16_f32 v53, v43, v42
	v_cvt_pk_bf16_f32 v54, v51, v50
	v_cvt_pk_bf16_f32 v55, v44, v45
	global_store_dwordx4 v[48:49], v[52:55], off

.LBB0_480:
	s_andn2_b64 vcc, exec, s[14:15]
	s_cbranch_vccnz .LBB0_482
	v_exp_f32_e32 v46, v46
	v_exp_f32_e32 v47, v47
	v_exp_f32_e32 v48, v51
	v_exp_f32_e32 v49, v50
	s_mov_b32 s2, 0x437f0000
	v_pk_add_f32 v[46:47], v[46:47], 1.0 op_sel_hi:[1,0]
	v_exp_f32_e32 v44, v44
	v_rcp_f32_e32 v46, v46
	v_rcp_f32_e32 v47, v47
	v_pk_add_f32 v[48:49], v[48:49], 1.0 op_sel_hi:[1,0]
	v_exp_f32_e32 v45, v45
	v_rcp_f32_e32 v48, v48
	v_rcp_f32_e32 v49, v49
	v_pk_fma_f32 v[46:47], v[46:47], s[2:3], 0.5 op_sel_hi:[1,0,0]
	v_pk_add_f32 v[44:45], v[44:45], 1.0 op_sel_hi:[1,0]
	v_max_f32_e32 v46, 1.0, v46
	v_pk_fma_f32 v[48:49], v[48:49], s[2:3], 0.5 op_sel_hi:[1,0,0]
	v_cvt_u32_f32_e32 v50, v46
	v_max_f32_e32 v46, 1.0, v47
	v_cvt_u32_f32_e32 v51, v46
	v_max_f32_e32 v46, 1.0, v48
	v_cvt_u32_f32_e32 v48, v46
	v_max_f32_e32 v46, 1.0, v49
	v_cvt_u32_f32_e32 v49, v46
	v_exp_f32_e32 v46, v43
	v_exp_f32_e32 v47, v42
	v_rcp_f32_e32 v44, v44
	v_rcp_f32_e32 v45, v45
	v_pk_add_f32 v[42:43], v[46:47], 1.0 op_sel_hi:[1,0]
	s_nop 0
	v_rcp_f32_e32 v42, v42
	v_rcp_f32_e32 v43, v43
	v_pk_fma_f32 v[44:45], v[44:45], s[2:3], 0.5 op_sel_hi:[1,0,0]
	v_lshl_or_b32 v46, v51, 8, v50
	v_max_f32_e32 v44, 1.0, v44
	v_pk_fma_f32 v[42:43], v[42:43], s[2:3], 0.5 op_sel_hi:[1,0,0]
	s_lshl_b32 s2, s46, 8
	s_add_i32 s2, s2, s80
	s_mul_hi_i32 s14, s2, 0xc00
	s_mulk_i32 s2, 0xc00
	v_max_f32_e32 v42, 1.0, v42
	v_max_f32_e32 v43, 1.0, v43
	s_add_u32 s2, s72, s2
	v_cvt_u32_f32_sdwa v42, v42 dst_sel:WORD_1 dst_unused:UNUSED_PAD src0_sel:DWORD
	v_cvt_u32_f32_sdwa v43, v43 dst_sel:BYTE_3 dst_unused:UNUSED_PAD src0_sel:DWORD
	v_max_f32_e32 v45, 1.0, v45
	s_addc_u32 s14, s73, s14
	v_cvt_u32_f32_sdwa v44, v44 dst_sel:WORD_1 dst_unused:UNUSED_PAD src0_sel:DWORD
	v_cvt_u32_f32_sdwa v45, v45 dst_sel:BYTE_3 dst_unused:UNUSED_PAD src0_sel:DWORD
	s_add_u32 s2, s2, s1
	s_addc_u32 s15, s14, 0
	s_add_u32 s14, s2, s75
	v_or3_b32 v42, v46, v42, v43
	v_lshl_or_b32 v43, v49, 8, v48
	s_addc_u32 s15, s15, 0
	v_or3_b32 v43, v43, v44, v45
	v_lshl_add_u64 v[44:45], s[14:15], 0, v[136:137]
	global_store_dwordx2 v[44:45], v[42:43], off
.LBB0_482:
	v_pk_mul_f32 v[44:45], v[40:41], s[10:11] op_sel_hi:[1,0]
	v_pk_mul_f32 v[46:47], v[38:39], s[10:11] op_sel_hi:[1,0]
	v_pk_mul_f32 v[42:43], v[36:37], s[10:11] op_sel_hi:[1,0]
	v_pk_mul_f32 v[48:49], v[34:35], s[10:11] op_sel_hi:[1,0]
	v_cndmask_b32_e64 v37, v37, v43, s[40:41]
	v_cndmask_b32_e64 v36, v36, v42, s[40:41]
	v_cndmask_b32_e64 v42, v35, v49, s[40:41]
	v_cndmask_b32_e64 v43, v34, v48, s[40:41]
	v_cndmask_b32_e64 v34, v41, v45, s[40:41]
	v_cndmask_b32_e64 v35, v40, v44, s[40:41]
	v_cndmask_b32_e64 v39, v39, v47, s[40:41]
	v_cndmask_b32_e64 v38, v38, v46, s[40:41]
	s_and_b64 vcc, exec, s[44:45]
	s_mov_b64 s[14:15], -1
	s_cbranch_vccnz .LBB0_488
	s_and_b64 vcc, exec, s[42:43]
	s_cbranch_vccnz .LBB0_485
	s_lshl_b32 s2, s46, 8
	s_add_i32 s2, s2, s80
	s_mul_hi_i32 s14, s2, 0x2800
	s_mulk_i32 s2, 0x2800
	s_add_u32 s2, s70, s2
	s_addc_u32 s24, s71, s14
	s_lshl_b64 s[14:15], s[56:57], 1
	s_add_u32 s2, s2, s14
	s_addc_u32 s15, s24, s15
	s_lshl_b32 s14, s75, 1
	s_add_u32 s14, s2, s14
	s_addc_u32 s15, s15, 0
	v_lshl_add_u64 v[40:41], s[14:15], 0, v[134:135]
	s_mov_b64 s[14:15], 0
	v_cvt_pk_bf16_f32 v44, v38, v39
	v_cvt_pk_bf16_f32 v45, v35, v34
	v_cvt_pk_bf16_f32 v46, v43, v42
	v_cvt_pk_bf16_f32 v47, v36, v37
	global_store_dwordx4 v[40:41], v[44:47], off offset:256
.LBB0_485:
	s_andn2_b64 vcc, exec, s[14:15]
	s_cbranch_vccnz .LBB0_487
	s_lshl_b32 s2, s46, 4
	s_ashr_i32 s14, s2, 31
	v_readlane_b32 s15, v255, 14
	s_add_u32 s2, s15, s2
	v_readlane_b32 s15, v255, 15
	s_addc_u32 s14, s15, s14
	s_mul_i32 s24, s14, 0x300
	v_mad_u64_u32 v[40:41], s[14:15], s2, v235, v[138:139]
	v_add_u32_e32 v41, s24, v41
	v_cvt_pk_bf16_f32 v44, v38, v39
	v_cvt_pk_bf16_f32 v45, v35, v34
	v_cvt_pk_bf16_f32 v46, v43, v42
	v_cvt_pk_bf16_f32 v47, v36, v37
	global_store_dwordx4 v[40:41], v[44:47], off

.LBB0_488:
	s_andn2_b64 vcc, exec, s[14:15]
	s_cbranch_vccnz .LBB0_490
	v_exp_f32_e32 v38, v38
	v_exp_f32_e32 v39, v39
	v_exp_f32_e32 v40, v43
	v_exp_f32_e32 v41, v42
	s_mov_b32 s2, 0x437f0000
	v_pk_add_f32 v[38:39], v[38:39], 1.0 op_sel_hi:[1,0]
	v_exp_f32_e32 v36, v36
	v_rcp_f32_e32 v38, v38
	v_rcp_f32_e32 v39, v39
	v_pk_add_f32 v[40:41], v[40:41], 1.0 op_sel_hi:[1,0]
	v_exp_f32_e32 v37, v37
	v_rcp_f32_e32 v40, v40
	v_rcp_f32_e32 v41, v41
	v_pk_fma_f32 v[38:39], v[38:39], s[2:3], 0.5 op_sel_hi:[1,0,0]
	v_pk_add_f32 v[36:37], v[36:37], 1.0 op_sel_hi:[1,0]
	v_max_f32_e32 v38, 1.0, v38
	v_pk_fma_f32 v[40:41], v[40:41], s[2:3], 0.5 op_sel_hi:[1,0,0]
	v_cvt_u32_f32_e32 v42, v38
	v_max_f32_e32 v38, 1.0, v39
	v_cvt_u32_f32_e32 v43, v38
	v_max_f32_e32 v38, 1.0, v40
	v_cvt_u32_f32_e32 v40, v38
	v_max_f32_e32 v38, 1.0, v41
	v_cvt_u32_f32_e32 v41, v38
	v_exp_f32_e32 v38, v35
	v_exp_f32_e32 v39, v34
	v_rcp_f32_e32 v36, v36
	v_rcp_f32_e32 v37, v37
	v_pk_add_f32 v[34:35], v[38:39], 1.0 op_sel_hi:[1,0]
	s_nop 0
	v_rcp_f32_e32 v34, v34
	v_rcp_f32_e32 v35, v35
	v_pk_fma_f32 v[36:37], v[36:37], s[2:3], 0.5 op_sel_hi:[1,0,0]
	v_lshl_or_b32 v38, v43, 8, v42
	v_max_f32_e32 v36, 1.0, v36
	v_pk_fma_f32 v[34:35], v[34:35], s[2:3], 0.5 op_sel_hi:[1,0,0]
	s_lshl_b32 s2, s46, 8
	s_add_i32 s2, s2, s80
	s_mul_hi_i32 s14, s2, 0xc00
	s_mulk_i32 s2, 0xc00
	v_max_f32_e32 v34, 1.0, v34
	v_max_f32_e32 v35, 1.0, v35
	s_add_u32 s2, s72, s2
	v_cvt_u32_f32_sdwa v34, v34 dst_sel:WORD_1 dst_unused:UNUSED_PAD src0_sel:DWORD
	v_cvt_u32_f32_sdwa v35, v35 dst_sel:BYTE_3 dst_unused:UNUSED_PAD src0_sel:DWORD
	v_max_f32_e32 v37, 1.0, v37
	s_addc_u32 s14, s73, s14
	v_cvt_u32_f32_sdwa v36, v36 dst_sel:WORD_1 dst_unused:UNUSED_PAD src0_sel:DWORD
	v_cvt_u32_f32_sdwa v37, v37 dst_sel:BYTE_3 dst_unused:UNUSED_PAD src0_sel:DWORD
	s_add_u32 s2, s2, s1
	s_addc_u32 s15, s14, 0
	s_add_u32 s14, s2, s75
	v_or3_b32 v34, v38, v34, v35
	v_lshl_or_b32 v35, v41, 8, v40
	s_addc_u32 s15, s15, 0
	v_or3_b32 v35, v35, v36, v37
	v_lshl_add_u64 v[36:37], s[14:15], 0, v[136:137]
	global_store_dwordx2 v[36:37], v[34:35], off offset:128
.LBB0_490:
	v_pk_mul_f32 v[36:37], v[32:33], s[10:11] op_sel_hi:[1,0]
	v_pk_mul_f32 v[38:39], v[30:31], s[10:11] op_sel_hi:[1,0]
	v_pk_mul_f32 v[34:35], v[28:29], s[10:11] op_sel_hi:[1,0]
	v_pk_mul_f32 v[40:41], v[26:27], s[10:11] op_sel_hi:[1,0]
	v_cndmask_b32_e64 v29, v29, v35, s[40:41]
	v_cndmask_b32_e64 v28, v28, v34, s[40:41]
	v_cndmask_b32_e64 v34, v27, v41, s[40:41]
	v_cndmask_b32_e64 v35, v26, v40, s[40:41]
	v_cndmask_b32_e64 v26, v33, v37, s[40:41]
	v_cndmask_b32_e64 v27, v32, v36, s[40:41]
	v_cndmask_b32_e64 v31, v31, v39, s[40:41]
	v_cndmask_b32_e64 v30, v30, v38, s[40:41]
	s_and_b64 vcc, exec, s[44:45]
	s_mov_b64 s[14:15], -1
	s_cbranch_vccnz .LBB0_496
	s_and_b64 vcc, exec, s[42:43]
	s_cbranch_vccnz .LBB0_493
	s_lshl_b32 s2, s46, 8
	s_add_i32 s2, s2, s85
	s_mul_hi_i32 s14, s2, 0x2800
	s_mulk_i32 s2, 0x2800
	s_add_u32 s2, s70, s2
	s_addc_u32 s24, s71, s14
	s_lshl_b64 s[14:15], s[56:57], 1
	s_add_u32 s2, s2, s14
	s_addc_u32 s15, s24, s15
	s_lshl_b32 s14, s75, 1
	s_add_u32 s14, s2, s14
	s_addc_u32 s15, s15, 0
	v_lshl_add_u64 v[32:33], s[14:15], 0, v[134:135]
	s_mov_b64 s[14:15], 0
	v_cvt_pk_bf16_f32 v36, v30, v31
	v_cvt_pk_bf16_f32 v37, v27, v26
	v_cvt_pk_bf16_f32 v38, v35, v34
	v_cvt_pk_bf16_f32 v39, v28, v29
	global_store_dwordx4 v[32:33], v[36:39], off
.LBB0_493:
	s_andn2_b64 vcc, exec, s[14:15]
	s_cbranch_vccnz .LBB0_495
	s_lshl_b32 s2, s46, 4
	s_ashr_i32 s14, s2, 31
	v_readlane_b32 s15, v255, 16
	s_add_u32 s2, s15, s2
	v_readlane_b32 s15, v255, 17
	s_addc_u32 s14, s15, s14
	s_mul_i32 s24, s14, 0x300
	v_mad_u64_u32 v[32:33], s[14:15], s2, v235, v[138:139]
	v_add_u32_e32 v33, s24, v33
	v_cvt_pk_bf16_f32 v36, v30, v31
	v_cvt_pk_bf16_f32 v37, v27, v26
	v_cvt_pk_bf16_f32 v38, v35, v34
	v_cvt_pk_bf16_f32 v39, v28, v29
	global_store_dwordx4 v[32:33], v[36:39], off

.LBB0_496:
	s_andn2_b64 vcc, exec, s[14:15]
	s_cbranch_vccnz .LBB0_498
	v_exp_f32_e32 v30, v30
	v_exp_f32_e32 v31, v31
	v_exp_f32_e32 v32, v35
	v_exp_f32_e32 v33, v34
	s_mov_b32 s2, 0x437f0000
	v_pk_add_f32 v[30:31], v[30:31], 1.0 op_sel_hi:[1,0]
	v_exp_f32_e32 v28, v28
	v_rcp_f32_e32 v30, v30
	v_rcp_f32_e32 v31, v31
	v_pk_add_f32 v[32:33], v[32:33], 1.0 op_sel_hi:[1,0]
	v_exp_f32_e32 v29, v29
	v_rcp_f32_e32 v32, v32
	v_rcp_f32_e32 v33, v33
	v_pk_fma_f32 v[30:31], v[30:31], s[2:3], 0.5 op_sel_hi:[1,0,0]
	v_pk_add_f32 v[28:29], v[28:29], 1.0 op_sel_hi:[1,0]
	v_max_f32_e32 v30, 1.0, v30
	v_pk_fma_f32 v[32:33], v[32:33], s[2:3], 0.5 op_sel_hi:[1,0,0]
	v_cvt_u32_f32_e32 v34, v30
	v_max_f32_e32 v30, 1.0, v31
	v_cvt_u32_f32_e32 v35, v30
	v_max_f32_e32 v30, 1.0, v32
	v_cvt_u32_f32_e32 v32, v30
	v_max_f32_e32 v30, 1.0, v33
	v_cvt_u32_f32_e32 v33, v30
	v_exp_f32_e32 v30, v27
	v_exp_f32_e32 v31, v26
	v_rcp_f32_e32 v28, v28
	v_rcp_f32_e32 v29, v29
	v_pk_add_f32 v[26:27], v[30:31], 1.0 op_sel_hi:[1,0]
	s_nop 0
	v_rcp_f32_e32 v26, v26
	v_rcp_f32_e32 v27, v27
	v_pk_fma_f32 v[28:29], v[28:29], s[2:3], 0.5 op_sel_hi:[1,0,0]
	v_lshl_or_b32 v30, v35, 8, v34
	v_max_f32_e32 v28, 1.0, v28
	v_pk_fma_f32 v[26:27], v[26:27], s[2:3], 0.5 op_sel_hi:[1,0,0]
	s_lshl_b32 s2, s46, 8
	s_add_i32 s2, s2, s85
	s_mul_hi_i32 s14, s2, 0xc00
	s_mulk_i32 s2, 0xc00
	v_max_f32_e32 v26, 1.0, v26
	v_max_f32_e32 v27, 1.0, v27
	s_add_u32 s2, s72, s2
	v_cvt_u32_f32_sdwa v26, v26 dst_sel:WORD_1 dst_unused:UNUSED_PAD src0_sel:DWORD
	v_cvt_u32_f32_sdwa v27, v27 dst_sel:BYTE_3 dst_unused:UNUSED_PAD src0_sel:DWORD
	v_max_f32_e32 v29, 1.0, v29
	s_addc_u32 s14, s73, s14
	v_cvt_u32_f32_sdwa v28, v28 dst_sel:WORD_1 dst_unused:UNUSED_PAD src0_sel:DWORD
	v_cvt_u32_f32_sdwa v29, v29 dst_sel:BYTE_3 dst_unused:UNUSED_PAD src0_sel:DWORD
	s_add_u32 s2, s2, s1
	s_addc_u32 s15, s14, 0
	s_add_u32 s14, s2, s75
	v_or3_b32 v26, v30, v26, v27
	v_lshl_or_b32 v27, v33, 8, v32
	s_addc_u32 s15, s15, 0
	v_or3_b32 v27, v27, v28, v29
	v_lshl_add_u64 v[28:29], s[14:15], 0, v[136:137]
	global_store_dwordx2 v[28:29], v[26:27], off
.LBB0_498:
	v_pk_mul_f32 v[28:29], v[24:25], s[10:11] op_sel_hi:[1,0]
	v_pk_mul_f32 v[30:31], v[22:23], s[10:11] op_sel_hi:[1,0]
	v_pk_mul_f32 v[26:27], v[20:21], s[10:11] op_sel_hi:[1,0]
	v_pk_mul_f32 v[32:33], v[18:19], s[10:11] op_sel_hi:[1,0]
	v_cndmask_b32_e64 v21, v21, v27, s[40:41]
	v_cndmask_b32_e64 v20, v20, v26, s[40:41]
	v_cndmask_b32_e64 v26, v19, v33, s[40:41]
	v_cndmask_b32_e64 v27, v18, v32, s[40:41]
	v_cndmask_b32_e64 v18, v25, v29, s[40:41]
	v_cndmask_b32_e64 v19, v24, v28, s[40:41]
	v_cndmask_b32_e64 v23, v23, v31, s[40:41]
	v_cndmask_b32_e64 v22, v22, v30, s[40:41]
	s_and_b64 vcc, exec, s[44:45]
	s_mov_b64 s[14:15], -1
	s_cbranch_vccnz .LBB0_504
	s_and_b64 vcc, exec, s[42:43]
	s_cbranch_vccnz .LBB0_501
	s_lshl_b32 s2, s46, 8
	s_add_i32 s2, s2, s85
	s_mul_hi_i32 s14, s2, 0x2800
	s_mulk_i32 s2, 0x2800
	s_add_u32 s2, s70, s2
	s_addc_u32 s24, s71, s14
	s_lshl_b64 s[14:15], s[56:57], 1
	s_add_u32 s2, s2, s14
	s_addc_u32 s15, s24, s15
	s_lshl_b32 s14, s75, 1
	s_add_u32 s14, s2, s14
	s_addc_u32 s15, s15, 0
	v_lshl_add_u64 v[24:25], s[14:15], 0, v[134:135]
	s_mov_b64 s[14:15], 0
	v_cvt_pk_bf16_f32 v28, v22, v23
	v_cvt_pk_bf16_f32 v29, v19, v18
	v_cvt_pk_bf16_f32 v30, v27, v26
	v_cvt_pk_bf16_f32 v31, v20, v21
	global_store_dwordx4 v[24:25], v[28:31], off offset:256
.LBB0_501:
	s_andn2_b64 vcc, exec, s[14:15]
	s_cbranch_vccnz .LBB0_503
	s_lshl_b32 s2, s46, 4
	s_ashr_i32 s14, s2, 31
	v_readlane_b32 s15, v255, 18
	s_add_u32 s2, s15, s2
	v_readlane_b32 s15, v255, 19
	s_addc_u32 s14, s15, s14
	s_mul_i32 s24, s14, 0x300
	v_mad_u64_u32 v[24:25], s[14:15], s2, v235, v[138:139]
	v_add_u32_e32 v25, s24, v25
	v_cvt_pk_bf16_f32 v28, v22, v23
	v_cvt_pk_bf16_f32 v29, v19, v18
	v_cvt_pk_bf16_f32 v30, v27, v26
	v_cvt_pk_bf16_f32 v31, v20, v21
	global_store_dwordx4 v[24:25], v[28:31], off

.LBB0_504:
	s_andn2_b64 vcc, exec, s[14:15]
	s_cbranch_vccnz .LBB0_506
	v_exp_f32_e32 v22, v22
	v_exp_f32_e32 v23, v23
	v_exp_f32_e32 v24, v27
	v_exp_f32_e32 v25, v26
	s_mov_b32 s2, 0x437f0000
	v_pk_add_f32 v[22:23], v[22:23], 1.0 op_sel_hi:[1,0]
	v_exp_f32_e32 v20, v20
	v_rcp_f32_e32 v22, v22
	v_rcp_f32_e32 v23, v23
	v_pk_add_f32 v[24:25], v[24:25], 1.0 op_sel_hi:[1,0]
	v_exp_f32_e32 v21, v21
	v_rcp_f32_e32 v24, v24
	v_rcp_f32_e32 v25, v25
	v_pk_fma_f32 v[22:23], v[22:23], s[2:3], 0.5 op_sel_hi:[1,0,0]
	v_pk_add_f32 v[20:21], v[20:21], 1.0 op_sel_hi:[1,0]
	v_max_f32_e32 v22, 1.0, v22
	v_pk_fma_f32 v[24:25], v[24:25], s[2:3], 0.5 op_sel_hi:[1,0,0]
	v_cvt_u32_f32_e32 v26, v22
	v_max_f32_e32 v22, 1.0, v23
	v_cvt_u32_f32_e32 v27, v22
	v_max_f32_e32 v22, 1.0, v24
	v_cvt_u32_f32_e32 v24, v22
	v_max_f32_e32 v22, 1.0, v25
	v_cvt_u32_f32_e32 v25, v22
	v_exp_f32_e32 v22, v19
	v_exp_f32_e32 v23, v18
	v_rcp_f32_e32 v20, v20
	v_rcp_f32_e32 v21, v21
	v_pk_add_f32 v[18:19], v[22:23], 1.0 op_sel_hi:[1,0]
	s_nop 0
	v_rcp_f32_e32 v18, v18
	v_rcp_f32_e32 v19, v19
	v_pk_fma_f32 v[20:21], v[20:21], s[2:3], 0.5 op_sel_hi:[1,0,0]
	v_lshl_or_b32 v22, v27, 8, v26
	v_max_f32_e32 v20, 1.0, v20
	v_pk_fma_f32 v[18:19], v[18:19], s[2:3], 0.5 op_sel_hi:[1,0,0]
	s_lshl_b32 s2, s46, 8
	s_add_i32 s2, s2, s85
	s_mul_hi_i32 s14, s2, 0xc00
	s_mulk_i32 s2, 0xc00
	v_max_f32_e32 v18, 1.0, v18
	v_max_f32_e32 v19, 1.0, v19
	s_add_u32 s2, s72, s2
	v_cvt_u32_f32_sdwa v18, v18 dst_sel:WORD_1 dst_unused:UNUSED_PAD src0_sel:DWORD
	v_cvt_u32_f32_sdwa v19, v19 dst_sel:BYTE_3 dst_unused:UNUSED_PAD src0_sel:DWORD
	v_max_f32_e32 v21, 1.0, v21
	s_addc_u32 s14, s73, s14
	v_cvt_u32_f32_sdwa v20, v20 dst_sel:WORD_1 dst_unused:UNUSED_PAD src0_sel:DWORD
	v_cvt_u32_f32_sdwa v21, v21 dst_sel:BYTE_3 dst_unused:UNUSED_PAD src0_sel:DWORD
	s_add_u32 s2, s2, s1
	s_addc_u32 s15, s14, 0
	s_add_u32 s14, s2, s75
	v_or3_b32 v18, v22, v18, v19
	v_lshl_or_b32 v19, v25, 8, v24
	s_addc_u32 s15, s15, 0
	v_or3_b32 v19, v19, v20, v21
	v_lshl_add_u64 v[20:21], s[14:15], 0, v[136:137]
	global_store_dwordx2 v[20:21], v[18:19], off offset:128
.LBB0_506:
	v_pk_mul_f32 v[20:21], v[16:17], s[10:11] op_sel_hi:[1,0]
	v_pk_mul_f32 v[22:23], v[14:15], s[10:11] op_sel_hi:[1,0]
	v_pk_mul_f32 v[18:19], v[12:13], s[10:11] op_sel_hi:[1,0]
	v_pk_mul_f32 v[24:25], v[10:11], s[10:11] op_sel_hi:[1,0]
	v_cndmask_b32_e64 v13, v13, v19, s[40:41]
	v_cndmask_b32_e64 v12, v12, v18, s[40:41]
	v_cndmask_b32_e64 v18, v11, v25, s[40:41]
	v_cndmask_b32_e64 v19, v10, v24, s[40:41]
	v_cndmask_b32_e64 v10, v17, v21, s[40:41]
	v_cndmask_b32_e64 v11, v16, v20, s[40:41]
	v_cndmask_b32_e64 v15, v15, v23, s[40:41]
	v_cndmask_b32_e64 v14, v14, v22, s[40:41]
	s_and_b64 vcc, exec, s[44:45]
	s_mov_b64 s[14:15], -1
	s_cbranch_vccnz .LBB0_512
	s_and_b64 vcc, exec, s[42:43]
	s_cbranch_vccnz .LBB0_509
	s_lshl_b32 s2, s46, 8
	s_add_i32 s2, s2, s96
	s_mul_hi_i32 s14, s2, 0x2800
	s_mulk_i32 s2, 0x2800
	s_add_u32 s2, s70, s2
	s_addc_u32 s24, s71, s14
	s_lshl_b64 s[14:15], s[56:57], 1
	s_add_u32 s2, s2, s14
	s_addc_u32 s15, s24, s15
	s_lshl_b32 s14, s75, 1
	s_add_u32 s14, s2, s14
	s_addc_u32 s15, s15, 0
	v_lshl_add_u64 v[16:17], s[14:15], 0, v[134:135]
	s_mov_b64 s[14:15], 0
	v_cvt_pk_bf16_f32 v20, v14, v15
	v_cvt_pk_bf16_f32 v21, v11, v10
	v_cvt_pk_bf16_f32 v22, v19, v18
	v_cvt_pk_bf16_f32 v23, v12, v13
	global_store_dwordx4 v[16:17], v[20:23], off
.LBB0_509:
	s_andn2_b64 vcc, exec, s[14:15]
	s_cbranch_vccnz .LBB0_511
	s_lshl_b32 s2, s46, 4
	s_ashr_i32 s14, s2, 31
	v_readlane_b32 s15, v255, 20
	s_add_u32 s2, s15, s2
	v_readlane_b32 s15, v255, 21
	s_addc_u32 s14, s15, s14
	s_mul_i32 s24, s14, 0x300
	v_mad_u64_u32 v[16:17], s[14:15], s2, v235, v[138:139]
	v_add_u32_e32 v17, s24, v17
	v_cvt_pk_bf16_f32 v20, v14, v15
	v_cvt_pk_bf16_f32 v21, v11, v10
	v_cvt_pk_bf16_f32 v22, v19, v18
	v_cvt_pk_bf16_f32 v23, v12, v13
	global_store_dwordx4 v[16:17], v[20:23], off

.LBB0_512:
	s_andn2_b64 vcc, exec, s[14:15]
	s_cbranch_vccnz .LBB0_514
	v_exp_f32_e32 v14, v14
	v_exp_f32_e32 v15, v15
	v_exp_f32_e32 v16, v19
	v_exp_f32_e32 v17, v18
	s_mov_b32 s2, 0x437f0000
	v_pk_add_f32 v[14:15], v[14:15], 1.0 op_sel_hi:[1,0]
	v_exp_f32_e32 v12, v12
	v_rcp_f32_e32 v14, v14
	v_rcp_f32_e32 v15, v15
	v_pk_add_f32 v[16:17], v[16:17], 1.0 op_sel_hi:[1,0]
	v_exp_f32_e32 v13, v13
	v_rcp_f32_e32 v16, v16
	v_rcp_f32_e32 v17, v17
	v_pk_fma_f32 v[14:15], v[14:15], s[2:3], 0.5 op_sel_hi:[1,0,0]
	v_pk_add_f32 v[12:13], v[12:13], 1.0 op_sel_hi:[1,0]
	v_max_f32_e32 v14, 1.0, v14
	v_pk_fma_f32 v[16:17], v[16:17], s[2:3], 0.5 op_sel_hi:[1,0,0]
	v_cvt_u32_f32_e32 v18, v14
	v_max_f32_e32 v14, 1.0, v15
	v_cvt_u32_f32_e32 v19, v14
	v_max_f32_e32 v14, 1.0, v16
	v_cvt_u32_f32_e32 v16, v14
	v_max_f32_e32 v14, 1.0, v17
	v_cvt_u32_f32_e32 v17, v14
	v_exp_f32_e32 v14, v11
	v_exp_f32_e32 v15, v10
	v_rcp_f32_e32 v12, v12
	v_rcp_f32_e32 v13, v13
	v_pk_add_f32 v[10:11], v[14:15], 1.0 op_sel_hi:[1,0]
	s_nop 0
	v_rcp_f32_e32 v10, v10
	v_rcp_f32_e32 v11, v11
	v_pk_fma_f32 v[12:13], v[12:13], s[2:3], 0.5 op_sel_hi:[1,0,0]
	v_lshl_or_b32 v14, v19, 8, v18
	v_max_f32_e32 v12, 1.0, v12
	v_pk_fma_f32 v[10:11], v[10:11], s[2:3], 0.5 op_sel_hi:[1,0,0]
	s_lshl_b32 s2, s46, 8
	s_add_i32 s2, s2, s96
	s_mul_hi_i32 s14, s2, 0xc00
	s_mulk_i32 s2, 0xc00
	v_max_f32_e32 v10, 1.0, v10
	v_max_f32_e32 v11, 1.0, v11
	s_add_u32 s2, s72, s2
	v_cvt_u32_f32_sdwa v10, v10 dst_sel:WORD_1 dst_unused:UNUSED_PAD src0_sel:DWORD
	v_cvt_u32_f32_sdwa v11, v11 dst_sel:BYTE_3 dst_unused:UNUSED_PAD src0_sel:DWORD
	v_max_f32_e32 v13, 1.0, v13
	s_addc_u32 s14, s73, s14
	v_cvt_u32_f32_sdwa v12, v12 dst_sel:WORD_1 dst_unused:UNUSED_PAD src0_sel:DWORD
	v_cvt_u32_f32_sdwa v13, v13 dst_sel:BYTE_3 dst_unused:UNUSED_PAD src0_sel:DWORD
	s_add_u32 s2, s2, s1
	s_addc_u32 s15, s14, 0
	s_add_u32 s14, s2, s75
	v_or3_b32 v10, v14, v10, v11
	v_lshl_or_b32 v11, v17, 8, v16
	s_addc_u32 s15, s15, 0
	v_or3_b32 v11, v11, v12, v13
	v_lshl_add_u64 v[12:13], s[14:15], 0, v[136:137]
	global_store_dwordx2 v[12:13], v[10:11], off
.LBB0_514:
	v_pk_mul_f32 v[12:13], v[8:9], s[10:11] op_sel_hi:[1,0]
	v_pk_mul_f32 v[14:15], v[6:7], s[10:11] op_sel_hi:[1,0]
	v_pk_mul_f32 v[10:11], v[4:5], s[10:11] op_sel_hi:[1,0]
	v_pk_mul_f32 v[16:17], v[2:3], s[10:11] op_sel_hi:[1,0]
	v_cndmask_b32_e64 v5, v5, v11, s[40:41]
	v_cndmask_b32_e64 v4, v4, v10, s[40:41]
	v_cndmask_b32_e64 v10, v3, v17, s[40:41]
	v_cndmask_b32_e64 v11, v2, v16, s[40:41]
	v_cndmask_b32_e64 v2, v9, v13, s[40:41]
	v_cndmask_b32_e64 v3, v8, v12, s[40:41]
	v_cndmask_b32_e64 v7, v7, v15, s[40:41]
	v_cndmask_b32_e64 v6, v6, v14, s[40:41]
	s_and_b64 vcc, exec, s[44:45]
	s_mov_b64 s[14:15], -1
	s_cbranch_vccnz .LBB0_521
	s_and_b64 vcc, exec, s[42:43]
	s_cbranch_vccnz .LBB0_517
	s_lshl_b32 s2, s46, 8
	s_add_i32 s2, s2, s96
	s_mul_hi_i32 s14, s2, 0x2800
	s_mulk_i32 s2, 0x2800
	s_add_u32 s2, s70, s2
	s_addc_u32 s24, s71, s14
	s_lshl_b64 s[14:15], s[56:57], 1
	s_add_u32 s2, s2, s14
	s_addc_u32 s15, s24, s15
	s_lshl_b32 s14, s75, 1
	s_add_u32 s14, s2, s14
	s_addc_u32 s15, s15, 0
	v_lshl_add_u64 v[8:9], s[14:15], 0, v[134:135]
	s_mov_b64 s[14:15], 0
	v_cvt_pk_bf16_f32 v12, v6, v7
	v_cvt_pk_bf16_f32 v13, v3, v2
	v_cvt_pk_bf16_f32 v14, v11, v10
	v_cvt_pk_bf16_f32 v15, v4, v5
	global_store_dwordx4 v[8:9], v[12:15], off offset:256
.LBB0_517:
	s_andn2_b64 vcc, exec, s[14:15]
	s_cbranch_vccnz .LBB0_519
	s_lshl_b32 s2, s46, 4
	s_ashr_i32 s14, s2, 31
	v_readlane_b32 s15, v255, 22
	s_add_u32 s2, s15, s2
	v_readlane_b32 s15, v255, 23
	s_addc_u32 s14, s15, s14
	s_mul_i32 s24, s14, 0x300
	v_mad_u64_u32 v[8:9], s[14:15], s2, v235, v[138:139]
	v_add_u32_e32 v9, s24, v9
	v_cvt_pk_bf16_f32 v12, v6, v7
	v_cvt_pk_bf16_f32 v13, v3, v2
	v_cvt_pk_bf16_f32 v14, v11, v10
	v_cvt_pk_bf16_f32 v15, v4, v5
	global_store_dwordx4 v[8:9], v[12:15], off

.LBB0_522:
	v_exp_f32_e32 v6, v6
	v_exp_f32_e32 v7, v7
	v_exp_f32_e32 v8, v11
	v_exp_f32_e32 v9, v10
	s_mov_b32 s2, 0x437f0000
	v_pk_add_f32 v[6:7], v[6:7], 1.0 op_sel_hi:[1,0]
	v_exp_f32_e32 v4, v4
	v_rcp_f32_e32 v6, v6
	v_rcp_f32_e32 v7, v7
	v_pk_add_f32 v[8:9], v[8:9], 1.0 op_sel_hi:[1,0]
	v_exp_f32_e32 v5, v5
	v_rcp_f32_e32 v8, v8
	v_rcp_f32_e32 v9, v9
	v_pk_fma_f32 v[6:7], v[6:7], s[2:3], 0.5 op_sel_hi:[1,0,0]
	v_pk_add_f32 v[4:5], v[4:5], 1.0 op_sel_hi:[1,0]
	v_max_f32_e32 v6, 1.0, v6
	v_pk_fma_f32 v[8:9], v[8:9], s[2:3], 0.5 op_sel_hi:[1,0,0]
	v_cvt_u32_f32_e32 v10, v6
	v_max_f32_e32 v6, 1.0, v7
	v_cvt_u32_f32_e32 v11, v6
	v_max_f32_e32 v6, 1.0, v8
	v_cvt_u32_f32_e32 v8, v6
	v_max_f32_e32 v6, 1.0, v9
	v_cvt_u32_f32_e32 v9, v6
	v_exp_f32_e32 v6, v3
	v_exp_f32_e32 v7, v2
	v_rcp_f32_e32 v4, v4
	v_rcp_f32_e32 v5, v5
	v_pk_add_f32 v[2:3], v[6:7], 1.0 op_sel_hi:[1,0]
	s_nop 0
	v_rcp_f32_e32 v2, v2
	v_rcp_f32_e32 v3, v3
	v_pk_fma_f32 v[4:5], v[4:5], s[2:3], 0.5 op_sel_hi:[1,0,0]
	v_lshl_or_b32 v6, v11, 8, v10
	v_max_f32_e32 v4, 1.0, v4
	v_pk_fma_f32 v[2:3], v[2:3], s[2:3], 0.5 op_sel_hi:[1,0,0]
	s_lshl_b32 s2, s46, 8
	s_add_i32 s2, s2, s96
	s_mul_hi_i32 s14, s2, 0xc00
	s_mulk_i32 s2, 0xc00
	v_max_f32_e32 v2, 1.0, v2
	v_max_f32_e32 v3, 1.0, v3
	s_add_u32 s2, s72, s2
	v_cvt_u32_f32_sdwa v2, v2 dst_sel:WORD_1 dst_unused:UNUSED_PAD src0_sel:DWORD
	v_cvt_u32_f32_sdwa v3, v3 dst_sel:BYTE_3 dst_unused:UNUSED_PAD src0_sel:DWORD
	v_max_f32_e32 v5, 1.0, v5
	s_addc_u32 s14, s73, s14
	v_cvt_u32_f32_sdwa v4, v4 dst_sel:WORD_1 dst_unused:UNUSED_PAD src0_sel:DWORD
	v_cvt_u32_f32_sdwa v5, v5 dst_sel:BYTE_3 dst_unused:UNUSED_PAD src0_sel:DWORD
	s_add_u32 s1, s2, s1
	s_addc_u32 s2, s14, 0
	s_add_u32 s14, s1, s75
	v_or3_b32 v2, v6, v2, v3
	v_lshl_or_b32 v3, v9, 8, v8
	s_addc_u32 s15, s2, 0
	v_or3_b32 v3, v3, v4, v5
	v_lshl_add_u64 v[4:5], s[14:15], 0, v[136:137]
	global_store_dwordx2 v[4:5], v[2:3], off offset:128
	s_andn2_b64 vcc, exec, s[38:39]
	s_mov_b64 s[14:15], -1
	s_cbranch_vccnz .LBB0_384

.LBB0_590:
	v_mov_b32_e32 v2, 0
	s_mov_b32 s41, 0
	s_mov_b64 s[56:57], -1
	s_mov_b64 s[14:15], 0
	v_mov_b32_e32 v3, 0
	v_mov_b64_e32 v[4:5], 0
	v_mov_b64_e32 v[6:7], 0
	v_mov_b64_e32 v[8:9], 0
	v_mov_b64_e32 v[10:11], 0
	v_mov_b64_e32 v[12:13], 0
	v_mov_b64_e32 v[14:15], 0
	v_mov_b64_e32 v[16:17], 0
	v_mov_b64_e32 v[18:19], 0
	v_mov_b64_e32 v[20:21], 0
	v_mov_b64_e32 v[22:23], 0
	v_mov_b64_e32 v[24:25], 0
	v_mov_b64_e32 v[26:27], 0
	v_mov_b64_e32 v[28:29], 0
	v_mov_b64_e32 v[30:31], 0
	v_mov_b64_e32 v[32:33], 0
	v_mov_b64_e32 v[34:35], 0
	v_mov_b64_e32 v[36:37], 0
	v_mov_b64_e32 v[38:39], 0
	v_mov_b64_e32 v[40:41], 0
	v_mov_b64_e32 v[42:43], 0
	v_mov_b64_e32 v[44:45], 0
	v_mov_b64_e32 v[46:47], 0
	v_mov_b64_e32 v[48:49], 0
	v_mov_b64_e32 v[50:51], 0
	v_mov_b64_e32 v[52:53], 0
	v_mov_b64_e32 v[54:55], 0
	v_mov_b64_e32 v[56:57], 0
	v_mov_b64_e32 v[58:59], 0
	v_mov_b64_e32 v[60:61], 0
	v_mov_b64_e32 v[62:63], 0
	v_mov_b64_e32 v[64:65], 0
	s_mov_b64 s[0:1], 0x8000
	s_mov_b64 s[2:3], 0x10000
	s_mov_b64 s[12:13], 0x8080
	s_mov_b64 s[38:39], 0x10080
	s_mov_b64 s[66:67], 0x24080
	s_mov_b64 s[26:27], 0x24000
	s_mov_b64 s[30:31], 0xc080
	s_mov_b64 s[94:95], 0x18080

.LBB0_594:
	s_ashr_i32 s41, s40, 31
	s_lshl_b32 s24, s69, 8
	s_lshl_b64 s[14:15], s[40:41], 11
	s_ashr_i32 s25, s24, 31
	s_add_u32 s24, s14, s24
	s_addc_u32 s25, s15, s25
	s_add_u32 s14, s24, s68
	s_addc_u32 s15, s25, s74
	s_lshl_b64 s[14:15], s[14:15], 9
	v_lshl_add_u64 v[72:73], v[68:69], 0, s[14:15]
	s_add_u32 s14, s75, s24
	s_addc_u32 s15, s76, s25
	s_lshl_b64 s[14:15], s[14:15], 9
	global_store_dwordx4 v[72:73], v[62:65], off
	global_store_dwordx4 v[72:73], v[58:61], off offset:16
	v_readlane_b32 s90, v253, 15
	v_readlane_b32 s85, v253, 14
	v_lshl_add_u64 v[58:59], v[68:69], 0, s[14:15]
	s_add_u32 s14, s77, s24
	s_addc_u32 s15, s78, s25
	s_lshl_b64 s[14:15], s[14:15], 9
	global_store_dwordx4 v[58:59], v[54:57], off
	global_store_dwordx4 v[58:59], v[50:53], off offset:16
	v_readlane_b32 s91, v253, 16
	s_mov_b64 s[66:67], s[22:23]
	v_lshl_add_u64 v[50:51], v[68:69], 0, s[14:15]
	s_add_u32 s14, s79, s24
	s_addc_u32 s15, s80, s25
	s_lshl_b64 s[14:15], s[14:15], 9
	global_store_dwordx4 v[50:51], v[46:49], off
	global_store_dwordx4 v[50:51], v[42:45], off offset:16
	s_mov_b64 s[26:27], 0xc080
	s_mov_b64 s[30:31], 0x18080
	v_lshl_add_u64 v[42:43], v[68:69], 0, s[14:15]
	s_mov_b32 s14, 0x10000
	global_store_dwordx4 v[42:43], v[38:41], off
	global_store_dwordx4 v[42:43], v[34:37], off offset:16
	s_mov_b64 s[94:95], 0x200
	s_mov_b32 s88, s96
	v_add_co_u32_e32 v36, vcc, s14, v72
	s_mov_b32 s14, 0x12000
	s_nop 0
	v_addc_co_u32_e32 v37, vcc, 0, v73, vcc
	v_lshl_add_u64 v[34:35], v[72:73], 0, s[0:1]
	global_store_dwordx4 v[36:37], v[30:33], off
	global_store_dwordx4 v[34:35], v[26:29], off offset:16
	s_mov_b64 s[0:1], 0x12000
	s_nop 0
	v_add_co_u32_e32 v28, vcc, s14, v72
	v_lshl_add_u64 v[26:27], v[72:73], 0, s[0:1]
	s_nop 0
	v_addc_co_u32_e32 v29, vcc, 0, v73, vcc
	global_store_dwordx4 v[28:29], v[22:25], off
	global_store_dwordx4 v[26:27], v[18:21], off offset:16
	s_mov_b64 s[14:15], 0x14000
	s_nop 0
	v_add_co_u32_e32 v20, vcc, 0x14000, v72
	v_lshl_add_u64 v[18:19], v[72:73], 0, s[14:15]
	s_nop 0
	v_addc_co_u32_e32 v21, vcc, 0, v73, vcc
	global_store_dwordx4 v[20:21], v[14:17], off
	global_store_dwordx4 v[18:19], v[10:13], off offset:16
	s_mov_b64 s[14:15], 0x16000
	s_nop 0
	v_add_co_u32_e32 v12, vcc, 0x16000, v72
	v_lshl_add_u64 v[10:11], v[72:73], 0, s[14:15]
	s_nop 0
	v_addc_co_u32_e32 v13, vcc, 0, v73, vcc
	s_andn2_b64 vcc, exec, s[54:55]
	s_mov_b64 s[14:15], -1
	global_store_dwordx4 v[12:13], v[6:9], off
	global_store_dwordx4 v[10:11], v[2:5], off offset:16
	s_cbranch_vccnz .LBB0_587
	v_readlane_b32 s0, v254, 50
	v_readlane_b32 s1, v254, 51
	s_andn2_b64 vcc, exec, s[0:1]
	s_cbranch_vccnz .LBB0_586
	s_barrier
	s_branch .LBB0_586

.LBB0_602:
	v_add_co_u32_e32 v8, vcc, 0xffff2000, v2
	v_add_u32_e32 v1, 0x1000, v1
	s_nop 0
	v_addc_co_u32_e32 v9, vcc, -1, v3, vcc
	v_add_co_u32_e32 v12, vcc, 0xffff4000, v2
	s_movk_i32 s2, 0xfff
	s_nop 0
	v_addc_co_u32_e32 v13, vcc, -1, v3, vcc
	v_add_co_u32_e32 v16, vcc, 0xffff6000, v2
	global_load_dwordx4 v[8:11], v[8:9], off
	s_nop 0
	global_load_dwordx4 v[12:15], v[12:13], off
	v_addc_co_u32_e32 v17, vcc, -1, v3, vcc
	v_add_co_u32_e32 v20, vcc, 0xffff8000, v2
	s_nop 1
	v_addc_co_u32_e32 v21, vcc, -1, v3, vcc
	v_add_co_u32_e32 v24, vcc, 0xffffa000, v2
	global_load_dwordx4 v[16:19], v[16:17], off
	s_nop 0
	global_load_dwordx4 v[20:23], v[20:21], off
	v_addc_co_u32_e32 v25, vcc, -1, v3, vcc
	v_add_co_u32_e32 v28, vcc, 0xffffc000, v2
	s_nop 1
	v_addc_co_u32_e32 v29, vcc, -1, v3, vcc
	v_add_co_u32_e32 v32, vcc, 0xffffe000, v2
	global_load_dwordx4 v[24:27], v[24:25], off
	s_nop 0
	global_load_dwordx4 v[28:31], v[28:29], off
	v_addc_co_u32_e32 v33, vcc, -1, v3, vcc
	global_load_dwordx4 v[32:35], v[32:33], off
	s_nop 0
	global_load_dwordx4 v[36:39], v[2:3], off
	v_cmp_lt_i32_e32 vcc, s2, v1
	s_or_b64 s[40:41], vcc, s[40:41]
	v_lshl_add_u64 v[2:3], v[2:3], 0, s[0:1]
	s_waitcnt vmcnt(0) lgkmcnt(0)
	ds_write_b128 v4, v[8:11]
	ds_write_b128 v4, v[12:15] offset:8192
	ds_write_b128 v4, v[16:19] offset:16384
	ds_write_b128 v4, v[20:23] offset:24576
	ds_write_b128 v4, v[24:27] offset:32768
	ds_write_b128 v4, v[28:31] offset:40960
	ds_write_b128 v4, v[32:35] offset:49152
	ds_write_b128 v4, v[36:39] offset:57344
	v_add_u32_e32 v4, 0x10000, v4
	s_andn2_b64 exec, exec, s[40:41]
	s_cbranch_execnz .LBB0_602
.LBB0_603:
	s_mov_b64 s[76:77], 0x10000
	s_or_b64 exec, exec, s[24:25]
	v_cmp_gt_i32_e32 vcc, 64, v6
	s_waitcnt lgkmcnt(0)
	s_barrier
	s_and_saveexec_b64 s[40:41], vcc
	s_cbranch_execz .LBB0_607
	v_readlane_b32 s0, v253, 32
	v_readlane_b32 s1, v253, 33
	s_lshl_b64 s[2:3], s[0:1], 13
	s_add_u32 s2, s14, s2
	s_addc_u32 s3, s15, s3
	s_lshl_b32 s12, s38, 7
	v_lshl_add_u32 v2, v6, 1, s12
	v_ashrrev_i32_e32 v3, 31, v2
	v_lshl_add_u64 v[2:3], v[2:3], 2, s[2:3]
	v_add_co_u32_e32 v2, vcc, 0x4e00000, v2
	s_and_b32 s12, s88, 7
	s_nop 0
	v_addc_co_u32_e32 v3, vcc, 0, v3, vcc
	global_load_dwordx2 v[2:3], v[2:3], off
	s_add_i32 s2, 0, 0x1000
	s_mul_i32 s3, s38, 0x180000
	s_mul_i32 s12, s12, 0x30000
	v_lshl_add_u32 v1, v6, 2, s2
	s_mul_hi_i32 s2, s38, 0x180000
	s_add_u32 s3, s3, s12
	s_addc_u32 s12, s2, 0
	s_add_u32 s2, s42, s3
	s_addc_u32 s3, s43, s12
	v_lshl_add_u64 v[6:7], v[6:7], 1, s[2:3]
	v_mov_b32_e32 v8, 0
	s_mov_b64 s[42:43], 0
	v_mov_b32_e32 v12, 0
	s_waitcnt vmcnt(0) lgkmcnt(0)
	v_pk_mov_b32 v[4:5], v[2:3], v[2:3] op_sel:[1,0]
.LBB0_605:
	v_lshl_add_u64 v[10:11], v[6:7], 0, s[42:43]
	v_bfe_u32 v9, v12, 16, 1
	v_add_co_u32_e32 v16, vcc, 0x61000000, v10
	ds_read2st64_b32 v[14:15], v1 offset1:1
	v_add3_u32 v9, v12, v9, s11
	v_addc_co_u32_e32 v17, vcc, 0, v11, vcc
	global_store_short_d16_hi v[16:17], v9, off offset:512
	v_bfe_u32 v9, v8, 16, 1
	v_add3_u32 v9, v8, v9, s11
	global_store_short_d16_hi v[16:17], v9, off offset:640
	v_pk_mul_f32 v[8:9], v[2:3], v[8:9] op_sel_hi:[1,0]
	s_mov_b32 s2, 0x61001000
	v_pk_fma_f32 v[18:19], v[4:5], v[12:13], v[8:9] op_sel_hi:[1,0,1]
	v_pk_fma_f32 v[8:9], v[4:5], v[12:13], v[8:9] op_sel_hi:[1,0,1] neg_lo:[0,0,1] neg_hi:[0,0,1]
	ds_read2st64_b32 v[12:13], v1 offset0:2 offset1:3
	v_mov_b32_e32 v19, v9
	s_waitcnt lgkmcnt(0)
	v_mov_b32_e32 v8, v15
	v_mov_b32_e32 v9, v14
	v_pk_add_f32 v[8:9], v[18:19], v[8:9]
	v_add_co_u32_e32 v10, vcc, s2, v10
	v_bfe_u32 v14, v9, 16, 1
	v_add3_u32 v14, v9, v14, s11
	global_store_short_d16_hi v[16:17], v14, off offset:1280
	v_bfe_u32 v14, v8, 16, 1
	v_add3_u32 v14, v8, v14, s11
	global_store_short_d16_hi v[16:17], v14, off offset:1408
	v_pk_mul_f32 v[14:15], v[2:3], v[8:9] op_sel_hi:[1,0]
	v_addc_co_u32_e32 v11, vcc, 0, v11, vcc
	v_pk_fma_f32 v[18:19], v[4:5], v[8:9], v[14:15] op_sel:[0,1,0]
	v_pk_fma_f32 v[8:9], v[4:5], v[8:9], v[14:15] op_sel:[0,1,0] neg_lo:[0,0,1] neg_hi:[0,0,1]
	s_add_u32 s42, s42, 0x1800
	v_mov_b32_e32 v19, v9
	v_mov_b32_e32 v8, v13
	v_mov_b32_e32 v9, v12
	v_pk_add_f32 v[8:9], v[18:19], v[8:9]
	ds_read2st64_b32 v[12:13], v1 offset0:4 offset1:5
	v_bfe_u32 v14, v9, 16, 1
	v_add3_u32 v14, v9, v14, s11
	global_store_short_d16_hi v[16:17], v14, off offset:2048
	v_bfe_u32 v14, v8, 16, 1
	v_add3_u32 v14, v8, v14, s11
	global_store_short_d16_hi v[16:17], v14, off offset:2176
	v_pk_mul_f32 v[14:15], v[2:3], v[8:9] op_sel_hi:[1,0]
	s_addc_u32 s43, s43, 0
	v_pk_fma_f32 v[18:19], v[4:5], v[8:9], v[14:15] op_sel:[0,1,0]
	v_pk_fma_f32 v[8:9], v[4:5], v[8:9], v[14:15] op_sel:[0,1,0] neg_lo:[0,0,1] neg_hi:[0,0,1]
	s_cmp_eq_u32 s42, 0x30000
	v_mov_b32_e32 v19, v9
	s_waitcnt lgkmcnt(0)
	v_mov_b32_e32 v8, v13
	v_mov_b32_e32 v9, v12
	v_pk_add_f32 v[8:9], v[18:19], v[8:9]
	ds_read2st64_b32 v[12:13], v1 offset0:6 offset1:7
	v_bfe_u32 v14, v9, 16, 1
	v_add3_u32 v14, v9, v14, s11
	global_store_short_d16_hi v[16:17], v14, off offset:2816
	v_bfe_u32 v14, v8, 16, 1
	v_add3_u32 v14, v8, v14, s11
	global_store_short_d16_hi v[16:17], v14, off offset:2944
	v_pk_mul_f32 v[14:15], v[2:3], v[8:9] op_sel_hi:[1,0]
	s_nop 0
	v_pk_fma_f32 v[18:19], v[4:5], v[8:9], v[14:15] op_sel:[0,1,0]
	v_pk_fma_f32 v[8:9], v[4:5], v[8:9], v[14:15] op_sel:[0,1,0] neg_lo:[0,0,1] neg_hi:[0,0,1]
	s_nop 0
	v_mov_b32_e32 v19, v9
	s_waitcnt lgkmcnt(0)
	v_mov_b32_e32 v8, v13
	v_mov_b32_e32 v9, v12
	v_pk_add_f32 v[8:9], v[18:19], v[8:9]
	ds_read2st64_b32 v[12:13], v1 offset0:8 offset1:9
	v_bfe_u32 v14, v9, 16, 1
	v_add3_u32 v14, v9, v14, s11
	global_store_short_d16_hi v[16:17], v14, off offset:3584
	v_bfe_u32 v14, v8, 16, 1
	v_add3_u32 v14, v8, v14, s11
	global_store_short_d16_hi v[16:17], v14, off offset:3712
	v_pk_mul_f32 v[14:15], v[2:3], v[8:9] op_sel_hi:[1,0]
	s_nop 0
	v_pk_fma_f32 v[16:17], v[4:5], v[8:9], v[14:15] op_sel:[0,1,0]
	v_pk_fma_f32 v[8:9], v[4:5], v[8:9], v[14:15] op_sel:[0,1,0] neg_lo:[0,0,1] neg_hi:[0,0,1]
	s_nop 0
	v_mov_b32_e32 v17, v9
	s_waitcnt lgkmcnt(0)
	v_mov_b32_e32 v8, v13
	v_mov_b32_e32 v9, v12
	v_pk_add_f32 v[8:9], v[16:17], v[8:9]
	ds_read2st64_b32 v[12:13], v1 offset0:10 offset1:11
	v_bfe_u32 v14, v9, 16, 1
	v_add3_u32 v14, v9, v14, s11
	global_store_short_d16_hi v[10:11], v14, off offset:256
	v_bfe_u32 v14, v8, 16, 1
	v_add3_u32 v14, v8, v14, s11
	global_store_short_d16_hi v[10:11], v14, off offset:384
	v_pk_mul_f32 v[14:15], v[2:3], v[8:9] op_sel_hi:[1,0]
	s_nop 0
	v_pk_fma_f32 v[16:17], v[4:5], v[8:9], v[14:15] op_sel:[0,1,0]
	v_pk_fma_f32 v[8:9], v[4:5], v[8:9], v[14:15] op_sel:[0,1,0] neg_lo:[0,0,1] neg_hi:[0,0,1]
	s_nop 0
	v_mov_b32_e32 v17, v9
	s_waitcnt lgkmcnt(0)
	v_mov_b32_e32 v8, v13
	v_mov_b32_e32 v9, v12
	v_pk_add_f32 v[8:9], v[16:17], v[8:9]
	ds_read2st64_b32 v[12:13], v1 offset0:12 offset1:13
	v_bfe_u32 v14, v9, 16, 1
	v_add3_u32 v14, v9, v14, s11
	global_store_short_d16_hi v[10:11], v14, off offset:1024
	v_bfe_u32 v14, v8, 16, 1
	v_add3_u32 v14, v8, v14, s11
	global_store_short_d16_hi v[10:11], v14, off offset:1152
	v_pk_mul_f32 v[14:15], v[2:3], v[8:9] op_sel_hi:[1,0]
	s_nop 0
	v_pk_fma_f32 v[16:17], v[4:5], v[8:9], v[14:15] op_sel:[0,1,0]
	v_pk_fma_f32 v[8:9], v[4:5], v[8:9], v[14:15] op_sel:[0,1,0] neg_lo:[0,0,1] neg_hi:[0,0,1]
	s_nop 0
	v_mov_b32_e32 v17, v9
	s_waitcnt lgkmcnt(0)
	v_mov_b32_e32 v8, v13
	v_mov_b32_e32 v9, v12
	v_pk_add_f32 v[8:9], v[16:17], v[8:9]
	ds_read2st64_b32 v[12:13], v1 offset0:14 offset1:15
	v_bfe_u32 v14, v9, 16, 1
	v_add3_u32 v14, v9, v14, s11
	global_store_short_d16_hi v[10:11], v14, off offset:1792
	v_bfe_u32 v14, v8, 16, 1
	v_add3_u32 v14, v8, v14, s11
	global_store_short_d16_hi v[10:11], v14, off offset:1920
	v_pk_mul_f32 v[10:11], v[2:3], v[8:9] op_sel_hi:[1,0]
	v_add_u32_e32 v1, 0x1000, v1
	v_pk_fma_f32 v[14:15], v[4:5], v[8:9], v[10:11] op_sel:[0,1,0]
	v_pk_fma_f32 v[8:9], v[4:5], v[8:9], v[10:11] op_sel:[0,1,0] neg_lo:[0,0,1] neg_hi:[0,0,1]
	s_nop 0
	v_mov_b32_e32 v15, v9
	s_waitcnt lgkmcnt(0)
	v_mov_b32_e32 v8, v13
	v_mov_b32_e32 v9, v12
	v_pk_add_f32 v[8:9], v[14:15], v[8:9]
	s_nop 0
	v_mov_b32_e32 v12, v9
	s_cbranch_scc0 .LBB0_605
	s_waitcnt vmcnt(0)
	s_waitcnt vmcnt(0)
	buffer_inv sc1
	s_waitcnt vmcnt(0)

.LBB0_615:
	s_add_u32 s35, s52, 0x100
	s_addc_u32 s43, s53, 0
	s_add_u32 s50, s50, 0x18080
	v_mov_b32_e32 v2, 0
	s_addc_u32 s51, s51, 0
	s_mov_b32 s52, -2
	v_mov_b32_e32 v3, 0
	v_mov_b64_e32 v[4:5], 0
	v_mov_b64_e32 v[6:7], 0
	v_mov_b64_e32 v[8:9], 0
	v_mov_b64_e32 v[18:19], 0
	v_mov_b64_e32 v[20:21], 0
	v_mov_b64_e32 v[22:23], 0
	v_mov_b64_e32 v[24:25], 0
	v_mov_b64_e32 v[34:35], 0
	v_mov_b64_e32 v[36:37], 0
	v_mov_b64_e32 v[38:39], 0
	v_mov_b64_e32 v[40:41], 0
	v_mov_b64_e32 v[50:51], 0
	v_mov_b64_e32 v[52:53], 0
	v_mov_b64_e32 v[54:55], 0
	v_mov_b64_e32 v[56:57], 0
	v_mov_b64_e32 v[10:11], 0
	v_mov_b64_e32 v[12:13], 0
	v_mov_b64_e32 v[14:15], 0
	v_mov_b64_e32 v[16:17], 0
	v_mov_b64_e32 v[26:27], 0
	v_mov_b64_e32 v[28:29], 0
	v_mov_b64_e32 v[30:31], 0
	v_mov_b64_e32 v[32:33], 0
	v_mov_b64_e32 v[42:43], 0
	v_mov_b64_e32 v[44:45], 0
	v_mov_b64_e32 v[46:47], 0
	v_mov_b64_e32 v[48:49], 0
	v_mov_b64_e32 v[58:59], 0
	v_mov_b64_e32 v[60:61], 0
	v_mov_b64_e32 v[62:63], 0
	v_mov_b64_e32 v[64:65], 0
	v_mov_b64_e32 v[66:67], 0
	v_mov_b64_e32 v[68:69], 0
	v_mov_b64_e32 v[70:71], 0
	v_mov_b64_e32 v[72:73], 0
	v_mov_b64_e32 v[82:83], 0
	v_mov_b64_e32 v[84:85], 0
	v_mov_b64_e32 v[86:87], 0
	v_mov_b64_e32 v[88:89], 0
	v_mov_b64_e32 v[98:99], 0
	v_mov_b64_e32 v[100:101], 0
	v_mov_b64_e32 v[102:103], 0
	v_mov_b64_e32 v[104:105], 0
	v_mov_b64_e32 v[114:115], 0
	v_mov_b64_e32 v[116:117], 0
	v_mov_b64_e32 v[118:119], 0
	v_mov_b64_e32 v[120:121], 0
	v_mov_b64_e32 v[74:75], 0
	v_mov_b64_e32 v[76:77], 0
	v_mov_b64_e32 v[78:79], 0
	v_mov_b64_e32 v[80:81], 0
	v_mov_b64_e32 v[90:91], 0
	v_mov_b64_e32 v[92:93], 0
	v_mov_b64_e32 v[94:95], 0
	v_mov_b64_e32 v[96:97], 0
	v_mov_b64_e32 v[106:107], 0
	v_mov_b64_e32 v[108:109], 0
	v_mov_b64_e32 v[110:111], 0
	v_mov_b64_e32 v[112:113], 0
	v_mov_b64_e32 v[122:123], 0
	v_mov_b64_e32 v[124:125], 0
	v_mov_b64_e32 v[126:127], 0
	v_mov_b64_e32 v[128:129], 0
	s_mov_b64 s[78:79], 0x24080

.LBB0_619:
	v_mul_f32_e32 v137, 0x3d372713, v126
	v_mul_f32_e32 v137, v126, v137
	v_fma_f32 v137, v126, v137, v126
	v_mul_f32_e32 v137, 0x3fcc422a, v137
	v_mul_f32_e32 v137, 0xbfb8aa3b, v137
	v_exp_f32_e32 v137, v137
	s_lshl_b32 s2, s2, 8
	s_add_i32 s50, s2, s54
	s_ashr_i32 s51, s50, 31
	v_add_f32_e32 v137, 1.0, v137
	v_rcp_f32_e32 v137, v137
	s_lshl_b64 s[14:15], s[50:51], 13
	s_add_u32 s35, s57, s14
	s_addc_u32 s43, s59, s15
	v_mul_f32_e32 v126, v126, v137
	v_mul_f32_e32 v137, 0x3d372713, v127
	v_mul_f32_e32 v137, v127, v137
	v_fma_f32 v137, v127, v137, v127
	v_mul_f32_e32 v137, 0x3fcc422a, v137
	v_mul_f32_e32 v137, 0xbfb8aa3b, v137
	v_exp_f32_e32 v137, v137
	s_lshl_b32 s14, s34, 4
	s_ashr_i32 s15, s14, 31
	s_lshl_b64 s[52:53], s[14:15], 1
	v_add_f32_e32 v137, 1.0, v137
	v_rcp_f32_e32 v137, v137
	s_add_u32 s14, s35, s52
	s_addc_u32 s15, s43, s53
	s_movk_i32 s34, 0x1000
	v_mul_f32_e32 v127, v127, v137
	v_mul_f32_e32 v137, 0x3d372713, v128
	v_mul_f32_e32 v137, v128, v137
	v_fma_f32 v137, v128, v137, v128
	v_mul_f32_e32 v137, 0x3fcc422a, v137
	v_mul_f32_e32 v137, 0xbfb8aa3b, v137
	v_exp_f32_e32 v137, v137
	s_nop 0
	v_add_f32_e32 v137, 1.0, v137
	v_rcp_f32_e32 v137, v137
	s_nop 0
	v_mul_f32_e32 v128, v128, v137
	v_mul_f32_e32 v137, 0x3d372713, v129
	v_mul_f32_e32 v137, v129, v137
	v_fma_f32 v137, v129, v137, v129
	v_mul_f32_e32 v137, 0x3fcc422a, v137
	v_mul_f32_e32 v137, 0xbfb8aa3b, v137
	v_exp_f32_e32 v137, v137
	s_nop 0
	v_add_f32_e32 v137, 1.0, v137
	v_rcp_f32_e32 v137, v137
	s_nop 0
	v_mul_f32_e32 v129, v129, v137
	v_mul_f32_e32 v137, 0x3d372713, v122
	v_mul_f32_e32 v137, v122, v137
	v_fma_f32 v137, v122, v137, v122
	v_mul_f32_e32 v137, 0x3fcc422a, v137
	v_mul_f32_e32 v137, 0xbfb8aa3b, v137
	v_exp_f32_e32 v137, v137
	s_nop 0
	v_add_f32_e32 v137, 1.0, v137
	v_rcp_f32_e32 v137, v137
	s_nop 0
	v_mul_f32_e32 v137, v122, v137
	v_mul_f32_e32 v122, 0x3d372713, v123
	v_mul_f32_e32 v122, v123, v122
	v_fma_f32 v122, v123, v122, v123
	v_mul_f32_e32 v122, 0x3fcc422a, v122
	v_mul_f32_e32 v122, 0xbfb8aa3b, v122
	v_exp_f32_e32 v122, v122
	s_nop 0
	v_add_f32_e32 v122, 1.0, v122
	v_rcp_f32_e32 v122, v122
	s_nop 0
	v_mul_f32_e32 v138, v123, v122
	v_mul_f32_e32 v122, 0x3d372713, v124
	v_mul_f32_e32 v122, v124, v122
	v_fma_f32 v122, v124, v122, v124
	v_mul_f32_e32 v122, 0x3fcc422a, v122
	v_mul_f32_e32 v122, 0xbfb8aa3b, v122
	v_exp_f32_e32 v122, v122
	s_nop 0
	v_add_f32_e32 v122, 1.0, v122
	v_rcp_f32_e32 v122, v122
	s_nop 0
	v_mul_f32_e32 v139, v124, v122
	v_mul_f32_e32 v122, 0x3d372713, v125
	v_mul_f32_e32 v122, v125, v122
	v_fma_f32 v122, v125, v122, v125
	v_mul_f32_e32 v122, 0x3fcc422a, v122
	v_mul_f32_e32 v122, 0xbfb8aa3b, v122
	v_exp_f32_e32 v122, v122
	s_nop 0
	v_add_f32_e32 v122, 1.0, v122
	v_rcp_f32_e32 v122, v122
	s_nop 0
	v_mul_f32_e32 v125, v125, v122
	v_cvt_pk_bf16_f32 v122, v126, v127
	v_lshl_add_u64 v[126:127], s[14:15], 0, v[132:133]
	v_cvt_pk_bf16_f32 v123, v128, v129
	v_cvt_pk_bf16_f32 v124, v137, v138
	v_cvt_pk_bf16_f32 v125, v139, v125
	global_store_dwordx4 v[126:127], v[122:125], off
	s_add_i32 s14, s60, s2
	s_ashr_i32 s15, s14, 31
	v_mul_f32_e32 v122, 0x3d372713, v118
	v_mul_f32_e32 v122, v118, v122
	v_fma_f32 v122, v118, v122, v118
	v_mul_f32_e32 v122, 0x3fcc422a, v122
	v_mul_f32_e32 v122, 0xbfb8aa3b, v122
	v_exp_f32_e32 v122, v122
	s_lshl_b64 s[14:15], s[14:15], 13
	s_add_u32 s14, s57, s14
	s_addc_u32 s15, s59, s15
	v_add_f32_e32 v122, 1.0, v122
	v_rcp_f32_e32 v122, v122
	s_add_u32 s14, s14, s52
	s_addc_u32 s15, s15, s53
	v_mul_f32_e32 v118, v118, v122
	v_mul_f32_e32 v122, 0x3d372713, v119
	v_mul_f32_e32 v122, v119, v122
	v_fma_f32 v122, v119, v122, v119
	v_mul_f32_e32 v122, 0x3fcc422a, v122
	v_mul_f32_e32 v122, 0xbfb8aa3b, v122
	v_exp_f32_e32 v122, v122
	s_nop 0
	v_add_f32_e32 v122, 1.0, v122
	v_rcp_f32_e32 v122, v122
	s_nop 0
	v_mul_f32_e32 v119, v119, v122
	v_mul_f32_e32 v122, 0x3d372713, v120
	v_mul_f32_e32 v122, v120, v122
	v_fma_f32 v122, v120, v122, v120
	v_mul_f32_e32 v122, 0x3fcc422a, v122
	v_mul_f32_e32 v122, 0xbfb8aa3b, v122
	v_exp_f32_e32 v122, v122
	s_nop 0
	v_add_f32_e32 v122, 1.0, v122
	v_rcp_f32_e32 v122, v122
	s_nop 0
	v_mul_f32_e32 v120, v120, v122
	v_mul_f32_e32 v122, 0x3d372713, v121
	v_mul_f32_e32 v122, v121, v122
	v_fma_f32 v122, v121, v122, v121
	v_mul_f32_e32 v122, 0x3fcc422a, v122
	v_mul_f32_e32 v122, 0xbfb8aa3b, v122
	v_exp_f32_e32 v122, v122
	s_nop 0
	v_add_f32_e32 v122, 1.0, v122
	v_rcp_f32_e32 v122, v122
	s_nop 0
	v_mul_f32_e32 v121, v121, v122
	v_mul_f32_e32 v122, 0x3d372713, v114
	v_mul_f32_e32 v122, v114, v122
	v_fma_f32 v122, v114, v122, v114
	v_mul_f32_e32 v122, 0x3fcc422a, v122
	v_mul_f32_e32 v122, 0xbfb8aa3b, v122
	v_exp_f32_e32 v122, v122
	s_nop 0
	v_add_f32_e32 v122, 1.0, v122
	v_rcp_f32_e32 v122, v122
	s_nop 0
	v_mul_f32_e32 v122, v114, v122
	v_mul_f32_e32 v114, 0x3d372713, v115
	v_mul_f32_e32 v114, v115, v114
	v_fma_f32 v114, v115, v114, v115
	v_mul_f32_e32 v114, 0x3fcc422a, v114
	v_mul_f32_e32 v114, 0xbfb8aa3b, v114
	v_exp_f32_e32 v114, v114
	s_nop 0
	v_add_f32_e32 v114, 1.0, v114
	v_rcp_f32_e32 v114, v114
	s_nop 0
	v_mul_f32_e32 v123, v115, v114
	v_mul_f32_e32 v114, 0x3d372713, v116
	v_mul_f32_e32 v114, v116, v114
	v_fma_f32 v114, v116, v114, v116
	v_mul_f32_e32 v114, 0x3fcc422a, v114
	v_mul_f32_e32 v114, 0xbfb8aa3b, v114
	v_exp_f32_e32 v114, v114
	s_nop 0
	v_add_f32_e32 v114, 1.0, v114
	v_rcp_f32_e32 v114, v114
	s_nop 0
	v_mul_f32_e32 v124, v116, v114
	v_mul_f32_e32 v114, 0x3d372713, v117
	v_mul_f32_e32 v114, v117, v114
	v_fma_f32 v114, v117, v114, v117
	v_mul_f32_e32 v114, 0x3fcc422a, v114
	v_mul_f32_e32 v114, 0xbfb8aa3b, v114
	v_exp_f32_e32 v114, v114
	s_nop 0
	v_add_f32_e32 v114, 1.0, v114
	v_rcp_f32_e32 v114, v114
	s_nop 0
	v_mul_f32_e32 v117, v117, v114
	v_cvt_pk_bf16_f32 v114, v118, v119
	v_add_co_u32_e32 v118, vcc, s34, v126
	v_cvt_pk_bf16_f32 v115, v120, v121
	v_cvt_pk_bf16_f32 v116, v122, v123
	v_cvt_pk_bf16_f32 v117, v124, v117
	s_nop 1
	v_addc_co_u32_e32 v119, vcc, 0, v127, vcc
	global_store_dwordx4 v[118:119], v[114:117], off
	s_nop 1
	v_mul_f32_e32 v114, 0x3d372713, v110
	v_mul_f32_e32 v114, v110, v114
	v_fma_f32 v114, v110, v114, v110
	v_mul_f32_e32 v114, 0x3fcc422a, v114
	v_mul_f32_e32 v114, 0xbfb8aa3b, v114
	v_exp_f32_e32 v114, v114
	s_nop 0
	v_add_f32_e32 v114, 1.0, v114
	v_rcp_f32_e32 v114, v114
	s_nop 0
	v_mul_f32_e32 v110, v110, v114
	v_mul_f32_e32 v114, 0x3d372713, v111
	v_mul_f32_e32 v114, v111, v114
	v_fma_f32 v114, v111, v114, v111
	v_mul_f32_e32 v114, 0x3fcc422a, v114
	v_mul_f32_e32 v114, 0xbfb8aa3b, v114
	v_exp_f32_e32 v114, v114
	s_nop 0
	v_add_f32_e32 v114, 1.0, v114
	v_rcp_f32_e32 v114, v114
	s_nop 0
	v_mul_f32_e32 v111, v111, v114
	v_mul_f32_e32 v114, 0x3d372713, v112
	v_mul_f32_e32 v114, v112, v114
	v_fma_f32 v114, v112, v114, v112
	v_mul_f32_e32 v114, 0x3fcc422a, v114
	v_mul_f32_e32 v114, 0xbfb8aa3b, v114
	v_exp_f32_e32 v114, v114
	s_nop 0
	v_add_f32_e32 v114, 1.0, v114
	v_rcp_f32_e32 v114, v114
	s_nop 0
	v_mul_f32_e32 v112, v112, v114
	v_mul_f32_e32 v114, 0x3d372713, v113
	v_mul_f32_e32 v114, v113, v114
	v_fma_f32 v114, v113, v114, v113
	v_mul_f32_e32 v114, 0x3fcc422a, v114
	v_mul_f32_e32 v114, 0xbfb8aa3b, v114
	v_exp_f32_e32 v114, v114
	s_nop 0
	v_add_f32_e32 v114, 1.0, v114
	v_rcp_f32_e32 v114, v114
	s_nop 0
	v_mul_f32_e32 v113, v113, v114
	v_mul_f32_e32 v114, 0x3d372713, v106
	v_mul_f32_e32 v114, v106, v114
	v_fma_f32 v114, v106, v114, v106
	v_mul_f32_e32 v114, 0x3fcc422a, v114
	v_mul_f32_e32 v114, 0xbfb8aa3b, v114
	v_exp_f32_e32 v114, v114
	s_nop 0
	v_add_f32_e32 v114, 1.0, v114
	v_rcp_f32_e32 v114, v114
	s_nop 0
	v_mul_f32_e32 v114, v106, v114
	v_mul_f32_e32 v106, 0x3d372713, v107
	v_mul_f32_e32 v106, v107, v106
	v_fma_f32 v106, v107, v106, v107
	v_mul_f32_e32 v106, 0x3fcc422a, v106
	v_mul_f32_e32 v106, 0xbfb8aa3b, v106
	v_exp_f32_e32 v106, v106
	s_nop 0
	v_add_f32_e32 v106, 1.0, v106
	v_rcp_f32_e32 v106, v106
	s_nop 0
	v_mul_f32_e32 v115, v107, v106
	v_mul_f32_e32 v106, 0x3d372713, v108
	v_mul_f32_e32 v106, v108, v106
	v_fma_f32 v106, v108, v106, v108
	v_mul_f32_e32 v106, 0x3fcc422a, v106
	v_mul_f32_e32 v106, 0xbfb8aa3b, v106
	v_exp_f32_e32 v106, v106
	s_nop 0
	v_add_f32_e32 v106, 1.0, v106
	v_rcp_f32_e32 v106, v106
	s_nop 0
	v_mul_f32_e32 v116, v108, v106
	v_mul_f32_e32 v106, 0x3d372713, v109
	v_mul_f32_e32 v106, v109, v106
	v_fma_f32 v106, v109, v106, v109
	v_mul_f32_e32 v106, 0x3fcc422a, v106
	v_mul_f32_e32 v106, 0xbfb8aa3b, v106
	v_exp_f32_e32 v106, v106
	s_nop 0
	v_add_f32_e32 v106, 1.0, v106
	v_rcp_f32_e32 v106, v106
	s_nop 0
	v_mul_f32_e32 v109, v109, v106
	v_cvt_pk_bf16_f32 v106, v110, v111
	v_lshl_add_u64 v[110:111], s[14:15], 0, v[132:133]
	v_cvt_pk_bf16_f32 v107, v112, v113
	v_cvt_pk_bf16_f32 v108, v114, v115
	v_cvt_pk_bf16_f32 v109, v116, v109
	global_store_dwordx4 v[110:111], v[106:109], off
	s_add_i32 s14, s61, s2
	s_ashr_i32 s15, s14, 31
	v_mul_f32_e32 v106, 0x3d372713, v102
	v_mul_f32_e32 v106, v102, v106
	v_fma_f32 v106, v102, v106, v102
	v_mul_f32_e32 v106, 0x3fcc422a, v106
	v_mul_f32_e32 v106, 0xbfb8aa3b, v106
	v_exp_f32_e32 v106, v106
	s_lshl_b64 s[14:15], s[14:15], 13
	s_add_u32 s14, s57, s14
	s_addc_u32 s15, s59, s15
	v_add_f32_e32 v106, 1.0, v106
	v_rcp_f32_e32 v106, v106
	s_add_u32 s14, s14, s52
	s_addc_u32 s15, s15, s53
	v_mul_f32_e32 v102, v102, v106
	v_mul_f32_e32 v106, 0x3d372713, v103
	v_mul_f32_e32 v106, v103, v106
	v_fma_f32 v106, v103, v106, v103
	v_mul_f32_e32 v106, 0x3fcc422a, v106
	v_mul_f32_e32 v106, 0xbfb8aa3b, v106
	v_exp_f32_e32 v106, v106
	s_nop 0
	v_add_f32_e32 v106, 1.0, v106
	v_rcp_f32_e32 v106, v106
	s_nop 0
	v_mul_f32_e32 v103, v103, v106
	v_mul_f32_e32 v106, 0x3d372713, v104
	v_mul_f32_e32 v106, v104, v106
	v_fma_f32 v106, v104, v106, v104
	v_mul_f32_e32 v106, 0x3fcc422a, v106
	v_mul_f32_e32 v106, 0xbfb8aa3b, v106
	v_exp_f32_e32 v106, v106
	s_nop 0
	v_add_f32_e32 v106, 1.0, v106
	v_rcp_f32_e32 v106, v106
	s_nop 0
	v_mul_f32_e32 v104, v104, v106
	v_mul_f32_e32 v106, 0x3d372713, v105
	v_mul_f32_e32 v106, v105, v106
	v_fma_f32 v106, v105, v106, v105
	v_mul_f32_e32 v106, 0x3fcc422a, v106
	v_mul_f32_e32 v106, 0xbfb8aa3b, v106
	v_exp_f32_e32 v106, v106
	s_nop 0
	v_add_f32_e32 v106, 1.0, v106
	v_rcp_f32_e32 v106, v106
	s_nop 0
	v_mul_f32_e32 v105, v105, v106
	v_mul_f32_e32 v106, 0x3d372713, v98
	v_mul_f32_e32 v106, v98, v106
	v_fma_f32 v106, v98, v106, v98
	v_mul_f32_e32 v106, 0x3fcc422a, v106
	v_mul_f32_e32 v106, 0xbfb8aa3b, v106
	v_exp_f32_e32 v106, v106
	s_nop 0
	v_add_f32_e32 v106, 1.0, v106
	v_rcp_f32_e32 v106, v106
	s_nop 0
	v_mul_f32_e32 v106, v98, v106
	v_mul_f32_e32 v98, 0x3d372713, v99
	v_mul_f32_e32 v98, v99, v98
	v_fma_f32 v98, v99, v98, v99
	v_mul_f32_e32 v98, 0x3fcc422a, v98
	v_mul_f32_e32 v98, 0xbfb8aa3b, v98
	v_exp_f32_e32 v98, v98
	s_nop 0
	v_add_f32_e32 v98, 1.0, v98
	v_rcp_f32_e32 v98, v98
	s_nop 0
	v_mul_f32_e32 v107, v99, v98
	v_mul_f32_e32 v98, 0x3d372713, v100
	v_mul_f32_e32 v98, v100, v98
	v_fma_f32 v98, v100, v98, v100
	v_mul_f32_e32 v98, 0x3fcc422a, v98
	v_mul_f32_e32 v98, 0xbfb8aa3b, v98
	v_exp_f32_e32 v98, v98
	s_nop 0
	v_add_f32_e32 v98, 1.0, v98
	v_rcp_f32_e32 v98, v98
	s_nop 0
	v_mul_f32_e32 v108, v100, v98
	v_mul_f32_e32 v98, 0x3d372713, v101
	v_mul_f32_e32 v98, v101, v98
	v_fma_f32 v98, v101, v98, v101
	v_mul_f32_e32 v98, 0x3fcc422a, v98
	v_mul_f32_e32 v98, 0xbfb8aa3b, v98
	v_exp_f32_e32 v98, v98
	s_nop 0
	v_add_f32_e32 v98, 1.0, v98
	v_rcp_f32_e32 v98, v98
	s_nop 0
	v_mul_f32_e32 v101, v101, v98
	v_cvt_pk_bf16_f32 v98, v102, v103
	v_add_co_u32_e32 v102, vcc, s34, v110
	v_cvt_pk_bf16_f32 v99, v104, v105
	v_cvt_pk_bf16_f32 v100, v106, v107
	v_cvt_pk_bf16_f32 v101, v108, v101
	s_nop 1
	v_addc_co_u32_e32 v103, vcc, 0, v111, vcc
	global_store_dwordx4 v[102:103], v[98:101], off
	s_nop 1
	v_mul_f32_e32 v98, 0x3d372713, v94
	v_mul_f32_e32 v98, v94, v98
	v_fma_f32 v98, v94, v98, v94
	v_mul_f32_e32 v98, 0x3fcc422a, v98
	v_mul_f32_e32 v98, 0xbfb8aa3b, v98
	v_exp_f32_e32 v98, v98
	s_nop 0
	v_add_f32_e32 v98, 1.0, v98
	v_rcp_f32_e32 v98, v98
	s_nop 0
	v_mul_f32_e32 v94, v94, v98
	v_mul_f32_e32 v98, 0x3d372713, v95
	v_mul_f32_e32 v98, v95, v98
	v_fma_f32 v98, v95, v98, v95
	v_mul_f32_e32 v98, 0x3fcc422a, v98
	v_mul_f32_e32 v98, 0xbfb8aa3b, v98
	v_exp_f32_e32 v98, v98
	s_nop 0
	v_add_f32_e32 v98, 1.0, v98
	v_rcp_f32_e32 v98, v98
	s_nop 0
	v_mul_f32_e32 v95, v95, v98
	v_mul_f32_e32 v98, 0x3d372713, v96
	v_mul_f32_e32 v98, v96, v98
	v_fma_f32 v98, v96, v98, v96
	v_mul_f32_e32 v98, 0x3fcc422a, v98
	v_mul_f32_e32 v98, 0xbfb8aa3b, v98
	v_exp_f32_e32 v98, v98
	s_nop 0
	v_add_f32_e32 v98, 1.0, v98
	v_rcp_f32_e32 v98, v98
	s_nop 0
	v_mul_f32_e32 v96, v96, v98
	v_mul_f32_e32 v98, 0x3d372713, v97
	v_mul_f32_e32 v98, v97, v98
	v_fma_f32 v98, v97, v98, v97
	v_mul_f32_e32 v98, 0x3fcc422a, v98
	v_mul_f32_e32 v98, 0xbfb8aa3b, v98
	v_exp_f32_e32 v98, v98
	s_nop 0
	v_add_f32_e32 v98, 1.0, v98
	v_rcp_f32_e32 v98, v98
	s_nop 0
	v_mul_f32_e32 v97, v97, v98
	v_mul_f32_e32 v98, 0x3d372713, v90
	v_mul_f32_e32 v98, v90, v98
	v_fma_f32 v98, v90, v98, v90
	v_mul_f32_e32 v98, 0x3fcc422a, v98
	v_mul_f32_e32 v98, 0xbfb8aa3b, v98
	v_exp_f32_e32 v98, v98
	s_nop 0
	v_add_f32_e32 v98, 1.0, v98
	v_rcp_f32_e32 v98, v98
	s_nop 0
	v_mul_f32_e32 v98, v90, v98
	v_mul_f32_e32 v90, 0x3d372713, v91
	v_mul_f32_e32 v90, v91, v90
	v_fma_f32 v90, v91, v90, v91
	v_mul_f32_e32 v90, 0x3fcc422a, v90
	v_mul_f32_e32 v90, 0xbfb8aa3b, v90
	v_exp_f32_e32 v90, v90
	s_nop 0
	v_add_f32_e32 v90, 1.0, v90
	v_rcp_f32_e32 v90, v90
	s_nop 0
	v_mul_f32_e32 v99, v91, v90
	v_mul_f32_e32 v90, 0x3d372713, v92
	v_mul_f32_e32 v90, v92, v90
	v_fma_f32 v90, v92, v90, v92
	v_mul_f32_e32 v90, 0x3fcc422a, v90
	v_mul_f32_e32 v90, 0xbfb8aa3b, v90
	v_exp_f32_e32 v90, v90
	s_nop 0
	v_add_f32_e32 v90, 1.0, v90
	v_rcp_f32_e32 v90, v90
	s_nop 0
	v_mul_f32_e32 v100, v92, v90
	v_mul_f32_e32 v90, 0x3d372713, v93
	v_mul_f32_e32 v90, v93, v90
	v_fma_f32 v90, v93, v90, v93
	v_mul_f32_e32 v90, 0x3fcc422a, v90
	v_mul_f32_e32 v90, 0xbfb8aa3b, v90
	v_exp_f32_e32 v90, v90
	s_nop 0
	v_add_f32_e32 v90, 1.0, v90
	v_rcp_f32_e32 v90, v90
	s_nop 0
	v_mul_f32_e32 v93, v93, v90
	v_cvt_pk_bf16_f32 v90, v94, v95
	v_lshl_add_u64 v[94:95], s[14:15], 0, v[132:133]
	v_cvt_pk_bf16_f32 v91, v96, v97
	v_cvt_pk_bf16_f32 v92, v98, v99
	v_cvt_pk_bf16_f32 v93, v100, v93
	global_store_dwordx4 v[94:95], v[90:93], off
	s_add_i32 s14, s68, s2
	s_ashr_i32 s15, s14, 31
	v_mul_f32_e32 v90, 0x3d372713, v86
	v_mul_f32_e32 v90, v86, v90
	v_fma_f32 v90, v86, v90, v86
	v_mul_f32_e32 v90, 0x3fcc422a, v90
	v_mul_f32_e32 v90, 0xbfb8aa3b, v90
	v_exp_f32_e32 v90, v90
	s_lshl_b64 s[14:15], s[14:15], 13
	s_add_u32 s2, s57, s14
	s_addc_u32 s15, s59, s15
	v_add_f32_e32 v90, 1.0, v90
	v_rcp_f32_e32 v90, v90
	s_add_u32 s14, s2, s52
	s_addc_u32 s15, s15, s53
	v_mul_f32_e32 v86, v86, v90
	v_mul_f32_e32 v90, 0x3d372713, v87
	v_mul_f32_e32 v90, v87, v90
	v_fma_f32 v90, v87, v90, v87
	v_mul_f32_e32 v90, 0x3fcc422a, v90
	v_mul_f32_e32 v90, 0xbfb8aa3b, v90
	v_exp_f32_e32 v90, v90
	s_nop 0
	v_add_f32_e32 v90, 1.0, v90
	v_rcp_f32_e32 v90, v90
	s_nop 0
	v_mul_f32_e32 v87, v87, v90
	v_mul_f32_e32 v90, 0x3d372713, v88
	v_mul_f32_e32 v90, v88, v90
	v_fma_f32 v90, v88, v90, v88
	v_mul_f32_e32 v90, 0x3fcc422a, v90
	v_mul_f32_e32 v90, 0xbfb8aa3b, v90
	v_exp_f32_e32 v90, v90
	s_nop 0
	v_add_f32_e32 v90, 1.0, v90
	v_rcp_f32_e32 v90, v90
	s_nop 0
	v_mul_f32_e32 v88, v88, v90
	v_mul_f32_e32 v90, 0x3d372713, v89
	v_mul_f32_e32 v90, v89, v90
	v_fma_f32 v90, v89, v90, v89
	v_mul_f32_e32 v90, 0x3fcc422a, v90
	v_mul_f32_e32 v90, 0xbfb8aa3b, v90
	v_exp_f32_e32 v90, v90
	s_nop 0
	v_add_f32_e32 v90, 1.0, v90
	v_rcp_f32_e32 v90, v90
	s_nop 0
	v_mul_f32_e32 v89, v89, v90
	v_mul_f32_e32 v90, 0x3d372713, v82
	v_mul_f32_e32 v90, v82, v90
	v_fma_f32 v90, v82, v90, v82
	v_mul_f32_e32 v90, 0x3fcc422a, v90
	v_mul_f32_e32 v90, 0xbfb8aa3b, v90
	v_exp_f32_e32 v90, v90
	s_nop 0
	v_add_f32_e32 v90, 1.0, v90
	v_rcp_f32_e32 v90, v90
	s_nop 0
	v_mul_f32_e32 v90, v82, v90
	v_mul_f32_e32 v82, 0x3d372713, v83
	v_mul_f32_e32 v82, v83, v82
	v_fma_f32 v82, v83, v82, v83
	v_mul_f32_e32 v82, 0x3fcc422a, v82
	v_mul_f32_e32 v82, 0xbfb8aa3b, v82
	v_exp_f32_e32 v82, v82
	s_nop 0
	v_add_f32_e32 v82, 1.0, v82
	v_rcp_f32_e32 v82, v82
	s_nop 0
	v_mul_f32_e32 v91, v83, v82
	v_mul_f32_e32 v82, 0x3d372713, v84
	v_mul_f32_e32 v82, v84, v82
	v_fma_f32 v82, v84, v82, v84
	v_mul_f32_e32 v82, 0x3fcc422a, v82
	v_mul_f32_e32 v82, 0xbfb8aa3b, v82
	v_exp_f32_e32 v82, v82
	s_nop 0
	v_add_f32_e32 v82, 1.0, v82
	v_rcp_f32_e32 v82, v82
	s_nop 0
	v_mul_f32_e32 v92, v84, v82
	v_mul_f32_e32 v82, 0x3d372713, v85
	v_mul_f32_e32 v82, v85, v82
	v_fma_f32 v82, v85, v82, v85
	v_mul_f32_e32 v82, 0x3fcc422a, v82
	v_mul_f32_e32 v82, 0xbfb8aa3b, v82
	v_exp_f32_e32 v82, v82
	s_nop 0
	v_add_f32_e32 v82, 1.0, v82
	v_rcp_f32_e32 v82, v82
	s_nop 0
	v_mul_f32_e32 v85, v85, v82
	v_cvt_pk_bf16_f32 v82, v86, v87
	v_add_co_u32_e32 v86, vcc, s34, v94
	v_cvt_pk_bf16_f32 v83, v88, v89
	v_cvt_pk_bf16_f32 v84, v90, v91
	v_cvt_pk_bf16_f32 v85, v92, v85
	s_nop 1
	v_addc_co_u32_e32 v87, vcc, 0, v95, vcc
	global_store_dwordx4 v[86:87], v[82:85], off
	s_nop 1
	v_mul_f32_e32 v82, 0x3d372713, v78
	v_mul_f32_e32 v82, v78, v82
	v_fma_f32 v82, v78, v82, v78
	v_mul_f32_e32 v82, 0x3fcc422a, v82
	v_mul_f32_e32 v82, 0xbfb8aa3b, v82
	v_exp_f32_e32 v82, v82
	s_nop 0
	v_add_f32_e32 v82, 1.0, v82
	v_rcp_f32_e32 v82, v82
	s_nop 0
	v_mul_f32_e32 v78, v78, v82
	v_mul_f32_e32 v82, 0x3d372713, v79
	v_mul_f32_e32 v82, v79, v82
	v_fma_f32 v82, v79, v82, v79
	v_mul_f32_e32 v82, 0x3fcc422a, v82
	v_mul_f32_e32 v82, 0xbfb8aa3b, v82
	v_exp_f32_e32 v82, v82
	s_nop 0
	v_add_f32_e32 v82, 1.0, v82
	v_rcp_f32_e32 v82, v82
	s_nop 0
	v_mul_f32_e32 v79, v79, v82
	v_mul_f32_e32 v82, 0x3d372713, v80
	v_mul_f32_e32 v82, v80, v82
	v_fma_f32 v82, v80, v82, v80
	v_mul_f32_e32 v82, 0x3fcc422a, v82
	v_mul_f32_e32 v82, 0xbfb8aa3b, v82
	v_exp_f32_e32 v82, v82
	s_nop 0
	v_add_f32_e32 v82, 1.0, v82
	v_rcp_f32_e32 v82, v82
	s_nop 0
	v_mul_f32_e32 v80, v80, v82
	v_mul_f32_e32 v82, 0x3d372713, v81
	v_mul_f32_e32 v82, v81, v82
	v_fma_f32 v82, v81, v82, v81
	v_mul_f32_e32 v82, 0x3fcc422a, v82
	v_mul_f32_e32 v82, 0xbfb8aa3b, v82
	v_exp_f32_e32 v82, v82
	s_nop 0
	v_add_f32_e32 v82, 1.0, v82
	v_rcp_f32_e32 v82, v82
	s_nop 0
	v_mul_f32_e32 v81, v81, v82
	v_mul_f32_e32 v82, 0x3d372713, v74
	v_mul_f32_e32 v82, v74, v82
	v_fma_f32 v82, v74, v82, v74
	v_mul_f32_e32 v82, 0x3fcc422a, v82
	v_mul_f32_e32 v82, 0xbfb8aa3b, v82
	v_exp_f32_e32 v82, v82
	s_nop 0
	v_add_f32_e32 v82, 1.0, v82
	v_rcp_f32_e32 v82, v82
	s_nop 0
	v_mul_f32_e32 v82, v74, v82
	v_mul_f32_e32 v74, 0x3d372713, v75
	v_mul_f32_e32 v74, v75, v74
	v_fma_f32 v74, v75, v74, v75
	v_mul_f32_e32 v74, 0x3fcc422a, v74
	v_mul_f32_e32 v74, 0xbfb8aa3b, v74
	v_exp_f32_e32 v74, v74
	s_nop 0
	v_add_f32_e32 v74, 1.0, v74
	v_rcp_f32_e32 v74, v74
	s_nop 0
	v_mul_f32_e32 v83, v75, v74
	v_mul_f32_e32 v74, 0x3d372713, v76
	v_mul_f32_e32 v74, v76, v74
	v_fma_f32 v74, v76, v74, v76
	v_mul_f32_e32 v74, 0x3fcc422a, v74
	v_mul_f32_e32 v74, 0xbfb8aa3b, v74
	v_exp_f32_e32 v74, v74
	s_nop 0
	v_add_f32_e32 v74, 1.0, v74
	v_rcp_f32_e32 v74, v74
	s_nop 0
	v_mul_f32_e32 v84, v76, v74
	v_mul_f32_e32 v74, 0x3d372713, v77
	v_mul_f32_e32 v74, v77, v74
	v_fma_f32 v74, v77, v74, v77
	v_mul_f32_e32 v74, 0x3fcc422a, v74
	v_mul_f32_e32 v74, 0xbfb8aa3b, v74
	v_exp_f32_e32 v74, v74
	s_nop 0
	v_add_f32_e32 v74, 1.0, v74
	v_rcp_f32_e32 v74, v74
	s_nop 0
	v_mul_f32_e32 v77, v77, v74
	v_cvt_pk_bf16_f32 v74, v78, v79
	v_lshl_add_u64 v[78:79], s[14:15], 0, v[132:133]
	v_cvt_pk_bf16_f32 v75, v80, v81
	v_cvt_pk_bf16_f32 v76, v82, v83
	v_cvt_pk_bf16_f32 v77, v84, v77
	global_store_dwordx4 v[78:79], v[74:77], off
	s_add_i32 s14, s50, 0x80
	s_ashr_i32 s15, s14, 31
	v_mul_f32_e32 v74, 0x3d372713, v70
	v_mul_f32_e32 v74, v70, v74
	v_fma_f32 v74, v70, v74, v70
	v_mul_f32_e32 v74, 0x3fcc422a, v74
	v_mul_f32_e32 v74, 0xbfb8aa3b, v74
	v_exp_f32_e32 v74, v74
	s_lshl_b64 s[14:15], s[14:15], 13
	s_add_u32 s2, s57, s14
	s_addc_u32 s15, s59, s15
	v_add_f32_e32 v74, 1.0, v74
	v_rcp_f32_e32 v74, v74
	s_add_u32 s14, s2, s52
	s_addc_u32 s15, s15, s53
	v_mul_f32_e32 v70, v70, v74
	v_mul_f32_e32 v74, 0x3d372713, v71
	v_mul_f32_e32 v74, v71, v74
	v_fma_f32 v74, v71, v74, v71
	v_mul_f32_e32 v74, 0x3fcc422a, v74
	v_mul_f32_e32 v74, 0xbfb8aa3b, v74
	v_exp_f32_e32 v74, v74
	s_nop 0
	v_add_f32_e32 v74, 1.0, v74
	v_rcp_f32_e32 v74, v74
	s_nop 0
	v_mul_f32_e32 v71, v71, v74
	v_mul_f32_e32 v74, 0x3d372713, v72
	v_mul_f32_e32 v74, v72, v74
	v_fma_f32 v74, v72, v74, v72
	v_mul_f32_e32 v74, 0x3fcc422a, v74
	v_mul_f32_e32 v74, 0xbfb8aa3b, v74
	v_exp_f32_e32 v74, v74
	s_nop 0
	v_add_f32_e32 v74, 1.0, v74
	v_rcp_f32_e32 v74, v74
	s_nop 0
	v_mul_f32_e32 v72, v72, v74
	v_mul_f32_e32 v74, 0x3d372713, v73
	v_mul_f32_e32 v74, v73, v74
	v_fma_f32 v74, v73, v74, v73
	v_mul_f32_e32 v74, 0x3fcc422a, v74
	v_mul_f32_e32 v74, 0xbfb8aa3b, v74
	v_exp_f32_e32 v74, v74
	s_nop 0
	v_add_f32_e32 v74, 1.0, v74
	v_rcp_f32_e32 v74, v74
	s_nop 0
	v_mul_f32_e32 v73, v73, v74
	v_mul_f32_e32 v74, 0x3d372713, v66
	v_mul_f32_e32 v74, v66, v74
	v_fma_f32 v74, v66, v74, v66
	v_mul_f32_e32 v74, 0x3fcc422a, v74
	v_mul_f32_e32 v74, 0xbfb8aa3b, v74
	v_exp_f32_e32 v74, v74
	s_nop 0
	v_add_f32_e32 v74, 1.0, v74
	v_rcp_f32_e32 v74, v74
	s_nop 0
	v_mul_f32_e32 v74, v66, v74
	v_mul_f32_e32 v66, 0x3d372713, v67
	v_mul_f32_e32 v66, v67, v66
	v_fma_f32 v66, v67, v66, v67
	v_mul_f32_e32 v66, 0x3fcc422a, v66
	v_mul_f32_e32 v66, 0xbfb8aa3b, v66
	v_exp_f32_e32 v66, v66
	s_nop 0
	v_add_f32_e32 v66, 1.0, v66
	v_rcp_f32_e32 v66, v66
	s_nop 0
	v_mul_f32_e32 v75, v67, v66
	v_mul_f32_e32 v66, 0x3d372713, v68
	v_mul_f32_e32 v66, v68, v66
	v_fma_f32 v66, v68, v66, v68
	v_mul_f32_e32 v66, 0x3fcc422a, v66
	v_mul_f32_e32 v66, 0xbfb8aa3b, v66
	v_exp_f32_e32 v66, v66
	s_nop 0
	v_add_f32_e32 v66, 1.0, v66
	v_rcp_f32_e32 v66, v66
	s_nop 0
	v_mul_f32_e32 v76, v68, v66
	v_mul_f32_e32 v66, 0x3d372713, v69
	v_mul_f32_e32 v66, v69, v66
	v_fma_f32 v66, v69, v66, v69
	v_mul_f32_e32 v66, 0x3fcc422a, v66
	v_mul_f32_e32 v66, 0xbfb8aa3b, v66
	v_exp_f32_e32 v66, v66
	s_nop 0
	v_add_f32_e32 v66, 1.0, v66
	v_rcp_f32_e32 v66, v66
	s_nop 0
	v_mul_f32_e32 v69, v69, v66
	v_cvt_pk_bf16_f32 v66, v70, v71
	v_add_co_u32_e32 v70, vcc, s34, v78
	v_cvt_pk_bf16_f32 v67, v72, v73
	v_cvt_pk_bf16_f32 v68, v74, v75
	v_cvt_pk_bf16_f32 v69, v76, v69
	s_nop 1
	v_addc_co_u32_e32 v71, vcc, 0, v79, vcc
	global_store_dwordx4 v[70:71], v[66:69], off
	s_nop 1
	v_mul_f32_e32 v66, 0x3d372713, v62
	v_mul_f32_e32 v66, v62, v66
	v_fma_f32 v66, v62, v66, v62
	v_mul_f32_e32 v66, 0x3fcc422a, v66
	v_mul_f32_e32 v66, 0xbfb8aa3b, v66
	v_exp_f32_e32 v66, v66
	s_nop 0
	v_add_f32_e32 v66, 1.0, v66
	v_rcp_f32_e32 v66, v66
	s_nop 0
	v_mul_f32_e32 v62, v62, v66
	v_mul_f32_e32 v66, 0x3d372713, v63
	v_mul_f32_e32 v66, v63, v66
	v_fma_f32 v66, v63, v66, v63
	v_mul_f32_e32 v66, 0x3fcc422a, v66
	v_mul_f32_e32 v66, 0xbfb8aa3b, v66
	v_exp_f32_e32 v66, v66
	s_nop 0
	v_add_f32_e32 v66, 1.0, v66
	v_rcp_f32_e32 v66, v66
	s_nop 0
	v_mul_f32_e32 v63, v63, v66
	v_mul_f32_e32 v66, 0x3d372713, v64
	v_mul_f32_e32 v66, v64, v66
	v_fma_f32 v66, v64, v66, v64
	v_mul_f32_e32 v66, 0x3fcc422a, v66
	v_mul_f32_e32 v66, 0xbfb8aa3b, v66
	v_exp_f32_e32 v66, v66
	s_nop 0
	v_add_f32_e32 v66, 1.0, v66
	v_rcp_f32_e32 v66, v66
	s_nop 0
	v_mul_f32_e32 v64, v64, v66
	v_mul_f32_e32 v66, 0x3d372713, v65
	v_mul_f32_e32 v66, v65, v66
	v_fma_f32 v66, v65, v66, v65
	v_mul_f32_e32 v66, 0x3fcc422a, v66
	v_mul_f32_e32 v66, 0xbfb8aa3b, v66
	v_exp_f32_e32 v66, v66
	s_nop 0
	v_add_f32_e32 v66, 1.0, v66
	v_rcp_f32_e32 v66, v66
	s_nop 0
	v_mul_f32_e32 v65, v65, v66
	v_mul_f32_e32 v66, 0x3d372713, v58
	v_mul_f32_e32 v66, v58, v66
	v_fma_f32 v66, v58, v66, v58
	v_mul_f32_e32 v66, 0x3fcc422a, v66
	v_mul_f32_e32 v66, 0xbfb8aa3b, v66
	v_exp_f32_e32 v66, v66
	s_nop 0
	v_add_f32_e32 v66, 1.0, v66
	v_rcp_f32_e32 v66, v66
	s_nop 0
	v_mul_f32_e32 v66, v58, v66
	v_mul_f32_e32 v58, 0x3d372713, v59
	v_mul_f32_e32 v58, v59, v58
	v_fma_f32 v58, v59, v58, v59
	v_mul_f32_e32 v58, 0x3fcc422a, v58
	v_mul_f32_e32 v58, 0xbfb8aa3b, v58
	v_exp_f32_e32 v58, v58
	s_nop 0
	v_add_f32_e32 v58, 1.0, v58
	v_rcp_f32_e32 v58, v58
	s_nop 0
	v_mul_f32_e32 v67, v59, v58
	v_mul_f32_e32 v58, 0x3d372713, v60
	v_mul_f32_e32 v58, v60, v58
	v_fma_f32 v58, v60, v58, v60
	v_mul_f32_e32 v58, 0x3fcc422a, v58
	v_mul_f32_e32 v58, 0xbfb8aa3b, v58
	v_exp_f32_e32 v58, v58
	s_nop 0
	v_add_f32_e32 v58, 1.0, v58
	v_rcp_f32_e32 v58, v58
	s_nop 0
	v_mul_f32_e32 v68, v60, v58
	v_mul_f32_e32 v58, 0x3d372713, v61
	v_mul_f32_e32 v58, v61, v58
	v_fma_f32 v58, v61, v58, v61
	v_mul_f32_e32 v58, 0x3fcc422a, v58
	v_mul_f32_e32 v58, 0xbfb8aa3b, v58
	v_exp_f32_e32 v58, v58
	s_nop 0
	v_add_f32_e32 v58, 1.0, v58
	v_rcp_f32_e32 v58, v58
	s_nop 0
	v_mul_f32_e32 v61, v61, v58
	v_cvt_pk_bf16_f32 v58, v62, v63
	v_lshl_add_u64 v[62:63], s[14:15], 0, v[132:133]
	v_cvt_pk_bf16_f32 v59, v64, v65
	v_cvt_pk_bf16_f32 v60, v66, v67
	v_cvt_pk_bf16_f32 v61, v68, v61
	global_store_dwordx4 v[62:63], v[58:61], off
	s_add_i32 s14, s50, 0x90
	s_ashr_i32 s15, s14, 31
	v_mul_f32_e32 v58, 0x3d372713, v54
	v_mul_f32_e32 v58, v54, v58
	v_fma_f32 v58, v54, v58, v54
	v_mul_f32_e32 v58, 0x3fcc422a, v58
	v_mul_f32_e32 v58, 0xbfb8aa3b, v58
	v_exp_f32_e32 v58, v58
	s_lshl_b64 s[14:15], s[14:15], 13
	s_add_u32 s2, s57, s14
	s_addc_u32 s15, s59, s15
	v_add_f32_e32 v58, 1.0, v58
	v_rcp_f32_e32 v58, v58
	s_add_u32 s14, s2, s52
	s_addc_u32 s15, s15, s53
	v_mul_f32_e32 v54, v54, v58
	v_mul_f32_e32 v58, 0x3d372713, v55
	v_mul_f32_e32 v58, v55, v58
	v_fma_f32 v58, v55, v58, v55
	v_mul_f32_e32 v58, 0x3fcc422a, v58
	v_mul_f32_e32 v58, 0xbfb8aa3b, v58
	v_exp_f32_e32 v58, v58
	s_nop 0
	v_add_f32_e32 v58, 1.0, v58
	v_rcp_f32_e32 v58, v58
	s_nop 0
	v_mul_f32_e32 v55, v55, v58
	v_mul_f32_e32 v58, 0x3d372713, v56
	v_mul_f32_e32 v58, v56, v58
	v_fma_f32 v58, v56, v58, v56
	v_mul_f32_e32 v58, 0x3fcc422a, v58
	v_mul_f32_e32 v58, 0xbfb8aa3b, v58
	v_exp_f32_e32 v58, v58
	s_nop 0
	v_add_f32_e32 v58, 1.0, v58
	v_rcp_f32_e32 v58, v58
	s_nop 0
	v_mul_f32_e32 v56, v56, v58
	v_mul_f32_e32 v58, 0x3d372713, v57
	v_mul_f32_e32 v58, v57, v58
	v_fma_f32 v58, v57, v58, v57
	v_mul_f32_e32 v58, 0x3fcc422a, v58
	v_mul_f32_e32 v58, 0xbfb8aa3b, v58
	v_exp_f32_e32 v58, v58
	s_nop 0
	v_add_f32_e32 v58, 1.0, v58
	v_rcp_f32_e32 v58, v58
	s_nop 0
	v_mul_f32_e32 v57, v57, v58
	v_mul_f32_e32 v58, 0x3d372713, v50
	v_mul_f32_e32 v58, v50, v58
	v_fma_f32 v58, v50, v58, v50
	v_mul_f32_e32 v58, 0x3fcc422a, v58
	v_mul_f32_e32 v58, 0xbfb8aa3b, v58
	v_exp_f32_e32 v58, v58
	s_nop 0
	v_add_f32_e32 v58, 1.0, v58
	v_rcp_f32_e32 v58, v58
	s_nop 0
	v_mul_f32_e32 v58, v50, v58
	v_mul_f32_e32 v50, 0x3d372713, v51
	v_mul_f32_e32 v50, v51, v50
	v_fma_f32 v50, v51, v50, v51
	v_mul_f32_e32 v50, 0x3fcc422a, v50
	v_mul_f32_e32 v50, 0xbfb8aa3b, v50
	v_exp_f32_e32 v50, v50
	s_nop 0
	v_add_f32_e32 v50, 1.0, v50
	v_rcp_f32_e32 v50, v50
	s_nop 0
	v_mul_f32_e32 v59, v51, v50
	v_mul_f32_e32 v50, 0x3d372713, v52
	v_mul_f32_e32 v50, v52, v50
	v_fma_f32 v50, v52, v50, v52
	v_mul_f32_e32 v50, 0x3fcc422a, v50
	v_mul_f32_e32 v50, 0xbfb8aa3b, v50
	v_exp_f32_e32 v50, v50
	s_nop 0
	v_add_f32_e32 v50, 1.0, v50
	v_rcp_f32_e32 v50, v50
	s_nop 0
	v_mul_f32_e32 v60, v52, v50
	v_mul_f32_e32 v50, 0x3d372713, v53
	v_mul_f32_e32 v50, v53, v50
	v_fma_f32 v50, v53, v50, v53
	v_mul_f32_e32 v50, 0x3fcc422a, v50
	v_mul_f32_e32 v50, 0xbfb8aa3b, v50
	v_exp_f32_e32 v50, v50
	s_nop 0
	v_add_f32_e32 v50, 1.0, v50
	v_rcp_f32_e32 v50, v50
	s_nop 0
	v_mul_f32_e32 v53, v53, v50
	v_cvt_pk_bf16_f32 v50, v54, v55
	v_add_co_u32_e32 v54, vcc, s34, v62
	v_cvt_pk_bf16_f32 v51, v56, v57
	v_cvt_pk_bf16_f32 v52, v58, v59
	v_cvt_pk_bf16_f32 v53, v60, v53
	s_nop 1
	v_addc_co_u32_e32 v55, vcc, 0, v63, vcc
	global_store_dwordx4 v[54:55], v[50:53], off
	s_nop 1
	v_mul_f32_e32 v50, 0x3d372713, v46
	v_mul_f32_e32 v50, v46, v50
	v_fma_f32 v50, v46, v50, v46
	v_mul_f32_e32 v50, 0x3fcc422a, v50
	v_mul_f32_e32 v50, 0xbfb8aa3b, v50
	v_exp_f32_e32 v50, v50
	s_nop 0
	v_add_f32_e32 v50, 1.0, v50
	v_rcp_f32_e32 v50, v50
	s_nop 0
	v_mul_f32_e32 v46, v46, v50
	v_mul_f32_e32 v50, 0x3d372713, v47
	v_mul_f32_e32 v50, v47, v50
	v_fma_f32 v50, v47, v50, v47
	v_mul_f32_e32 v50, 0x3fcc422a, v50
	v_mul_f32_e32 v50, 0xbfb8aa3b, v50
	v_exp_f32_e32 v50, v50
	s_nop 0
	v_add_f32_e32 v50, 1.0, v50
	v_rcp_f32_e32 v50, v50
	s_nop 0
	v_mul_f32_e32 v47, v47, v50
	v_mul_f32_e32 v50, 0x3d372713, v48
	v_mul_f32_e32 v50, v48, v50
	v_fma_f32 v50, v48, v50, v48
	v_mul_f32_e32 v50, 0x3fcc422a, v50
	v_mul_f32_e32 v50, 0xbfb8aa3b, v50
	v_exp_f32_e32 v50, v50
	s_nop 0
	v_add_f32_e32 v50, 1.0, v50
	v_rcp_f32_e32 v50, v50
	s_nop 0
	v_mul_f32_e32 v48, v48, v50
	v_mul_f32_e32 v50, 0x3d372713, v49
	v_mul_f32_e32 v50, v49, v50
	v_fma_f32 v50, v49, v50, v49
	v_mul_f32_e32 v50, 0x3fcc422a, v50
	v_mul_f32_e32 v50, 0xbfb8aa3b, v50
	v_exp_f32_e32 v50, v50
	s_nop 0
	v_add_f32_e32 v50, 1.0, v50
	v_rcp_f32_e32 v50, v50
	s_nop 0
	v_mul_f32_e32 v49, v49, v50
	v_mul_f32_e32 v50, 0x3d372713, v42
	v_mul_f32_e32 v50, v42, v50
	v_fma_f32 v50, v42, v50, v42
	v_mul_f32_e32 v50, 0x3fcc422a, v50
	v_mul_f32_e32 v50, 0xbfb8aa3b, v50
	v_exp_f32_e32 v50, v50
	s_nop 0
	v_add_f32_e32 v50, 1.0, v50
	v_rcp_f32_e32 v50, v50
	s_nop 0
	v_mul_f32_e32 v50, v42, v50
	v_mul_f32_e32 v42, 0x3d372713, v43
	v_mul_f32_e32 v42, v43, v42
	v_fma_f32 v42, v43, v42, v43
	v_mul_f32_e32 v42, 0x3fcc422a, v42
	v_mul_f32_e32 v42, 0xbfb8aa3b, v42
	v_exp_f32_e32 v42, v42
	s_nop 0
	v_add_f32_e32 v42, 1.0, v42
	v_rcp_f32_e32 v42, v42
	s_nop 0
	v_mul_f32_e32 v51, v43, v42
	v_mul_f32_e32 v42, 0x3d372713, v44
	v_mul_f32_e32 v42, v44, v42
	v_fma_f32 v42, v44, v42, v44
	v_mul_f32_e32 v42, 0x3fcc422a, v42
	v_mul_f32_e32 v42, 0xbfb8aa3b, v42
	v_exp_f32_e32 v42, v42
	s_nop 0
	v_add_f32_e32 v42, 1.0, v42
	v_rcp_f32_e32 v42, v42
	s_nop 0
	v_mul_f32_e32 v52, v44, v42
	v_mul_f32_e32 v42, 0x3d372713, v45
	v_mul_f32_e32 v42, v45, v42
	v_fma_f32 v42, v45, v42, v45
	v_mul_f32_e32 v42, 0x3fcc422a, v42
	v_mul_f32_e32 v42, 0xbfb8aa3b, v42
	v_exp_f32_e32 v42, v42
	s_nop 0
	v_add_f32_e32 v42, 1.0, v42
	v_rcp_f32_e32 v42, v42
	s_nop 0
	v_mul_f32_e32 v45, v45, v42
	v_cvt_pk_bf16_f32 v42, v46, v47
	v_lshl_add_u64 v[46:47], s[14:15], 0, v[132:133]
	v_cvt_pk_bf16_f32 v43, v48, v49
	v_cvt_pk_bf16_f32 v44, v50, v51
	v_cvt_pk_bf16_f32 v45, v52, v45
	global_store_dwordx4 v[46:47], v[42:45], off
	s_add_i32 s14, s50, 0xa0
	s_ashr_i32 s15, s14, 31
	v_mul_f32_e32 v42, 0x3d372713, v38
	v_mul_f32_e32 v42, v38, v42
	v_fma_f32 v42, v38, v42, v38
	v_mul_f32_e32 v42, 0x3fcc422a, v42
	v_mul_f32_e32 v42, 0xbfb8aa3b, v42
	v_exp_f32_e32 v42, v42
	s_lshl_b64 s[14:15], s[14:15], 13
	s_add_u32 s2, s57, s14
	s_addc_u32 s15, s59, s15
	v_add_f32_e32 v42, 1.0, v42
	v_rcp_f32_e32 v42, v42
	s_add_u32 s14, s2, s52
	s_addc_u32 s15, s15, s53
	v_mul_f32_e32 v38, v38, v42
	v_mul_f32_e32 v42, 0x3d372713, v39
	v_mul_f32_e32 v42, v39, v42
	v_fma_f32 v42, v39, v42, v39
	v_mul_f32_e32 v42, 0x3fcc422a, v42
	v_mul_f32_e32 v42, 0xbfb8aa3b, v42
	v_exp_f32_e32 v42, v42
	s_nop 0
	v_add_f32_e32 v42, 1.0, v42
	v_rcp_f32_e32 v42, v42
	s_nop 0
	v_mul_f32_e32 v39, v39, v42
	v_mul_f32_e32 v42, 0x3d372713, v40
	v_mul_f32_e32 v42, v40, v42
	v_fma_f32 v42, v40, v42, v40
	v_mul_f32_e32 v42, 0x3fcc422a, v42
	v_mul_f32_e32 v42, 0xbfb8aa3b, v42
	v_exp_f32_e32 v42, v42
	s_nop 0
	v_add_f32_e32 v42, 1.0, v42
	v_rcp_f32_e32 v42, v42
	s_nop 0
	v_mul_f32_e32 v40, v40, v42
	v_mul_f32_e32 v42, 0x3d372713, v41
	v_mul_f32_e32 v42, v41, v42
	v_fma_f32 v42, v41, v42, v41
	v_mul_f32_e32 v42, 0x3fcc422a, v42
	v_mul_f32_e32 v42, 0xbfb8aa3b, v42
	v_exp_f32_e32 v42, v42
	s_nop 0
	v_add_f32_e32 v42, 1.0, v42
	v_rcp_f32_e32 v42, v42
	s_nop 0
	v_mul_f32_e32 v41, v41, v42
	v_mul_f32_e32 v42, 0x3d372713, v34
	v_mul_f32_e32 v42, v34, v42
	v_fma_f32 v42, v34, v42, v34
	v_mul_f32_e32 v42, 0x3fcc422a, v42
	v_mul_f32_e32 v42, 0xbfb8aa3b, v42
	v_exp_f32_e32 v42, v42
	s_nop 0
	v_add_f32_e32 v42, 1.0, v42
	v_rcp_f32_e32 v42, v42
	s_nop 0
	v_mul_f32_e32 v42, v34, v42
	v_mul_f32_e32 v34, 0x3d372713, v35
	v_mul_f32_e32 v34, v35, v34
	v_fma_f32 v34, v35, v34, v35
	v_mul_f32_e32 v34, 0x3fcc422a, v34
	v_mul_f32_e32 v34, 0xbfb8aa3b, v34
	v_exp_f32_e32 v34, v34
	s_nop 0
	v_add_f32_e32 v34, 1.0, v34
	v_rcp_f32_e32 v34, v34
	s_nop 0
	v_mul_f32_e32 v43, v35, v34
	v_mul_f32_e32 v34, 0x3d372713, v36
	v_mul_f32_e32 v34, v36, v34
	v_fma_f32 v34, v36, v34, v36
	v_mul_f32_e32 v34, 0x3fcc422a, v34
	v_mul_f32_e32 v34, 0xbfb8aa3b, v34
	v_exp_f32_e32 v34, v34
	s_nop 0
	v_add_f32_e32 v34, 1.0, v34
	v_rcp_f32_e32 v34, v34
	s_nop 0
	v_mul_f32_e32 v44, v36, v34
	v_mul_f32_e32 v34, 0x3d372713, v37
	v_mul_f32_e32 v34, v37, v34
	v_fma_f32 v34, v37, v34, v37
	v_mul_f32_e32 v34, 0x3fcc422a, v34
	v_mul_f32_e32 v34, 0xbfb8aa3b, v34
	v_exp_f32_e32 v34, v34
	s_nop 0
	v_add_f32_e32 v34, 1.0, v34
	v_rcp_f32_e32 v34, v34
	s_nop 0
	v_mul_f32_e32 v37, v37, v34
	v_cvt_pk_bf16_f32 v34, v38, v39
	v_add_co_u32_e32 v38, vcc, s34, v46
	v_cvt_pk_bf16_f32 v35, v40, v41
	v_cvt_pk_bf16_f32 v36, v42, v43
	v_cvt_pk_bf16_f32 v37, v44, v37
	s_nop 1
	v_addc_co_u32_e32 v39, vcc, 0, v47, vcc
	global_store_dwordx4 v[38:39], v[34:37], off
	s_nop 1
	v_mul_f32_e32 v34, 0x3d372713, v30
	v_mul_f32_e32 v34, v30, v34
	v_fma_f32 v34, v30, v34, v30
	v_mul_f32_e32 v34, 0x3fcc422a, v34
	v_mul_f32_e32 v34, 0xbfb8aa3b, v34
	v_exp_f32_e32 v34, v34
	s_nop 0
	v_add_f32_e32 v34, 1.0, v34
	v_rcp_f32_e32 v34, v34
	s_nop 0
	v_mul_f32_e32 v30, v30, v34
	v_mul_f32_e32 v34, 0x3d372713, v31
	v_mul_f32_e32 v34, v31, v34
	v_fma_f32 v34, v31, v34, v31
	v_mul_f32_e32 v34, 0x3fcc422a, v34
	v_mul_f32_e32 v34, 0xbfb8aa3b, v34
	v_exp_f32_e32 v34, v34
	s_nop 0
	v_add_f32_e32 v34, 1.0, v34
	v_rcp_f32_e32 v34, v34
	s_nop 0
	v_mul_f32_e32 v31, v31, v34
	v_mul_f32_e32 v34, 0x3d372713, v32
	v_mul_f32_e32 v34, v32, v34
	v_fma_f32 v34, v32, v34, v32
	v_mul_f32_e32 v34, 0x3fcc422a, v34
	v_mul_f32_e32 v34, 0xbfb8aa3b, v34
	v_exp_f32_e32 v34, v34
	s_nop 0
	v_add_f32_e32 v34, 1.0, v34
	v_rcp_f32_e32 v34, v34
	s_nop 0
	v_mul_f32_e32 v32, v32, v34
	v_mul_f32_e32 v34, 0x3d372713, v33
	v_mul_f32_e32 v34, v33, v34
	v_fma_f32 v34, v33, v34, v33
	v_mul_f32_e32 v34, 0x3fcc422a, v34
	v_mul_f32_e32 v34, 0xbfb8aa3b, v34
	v_exp_f32_e32 v34, v34
	s_nop 0
	v_add_f32_e32 v34, 1.0, v34
	v_rcp_f32_e32 v34, v34
	s_nop 0
	v_mul_f32_e32 v33, v33, v34
	v_mul_f32_e32 v34, 0x3d372713, v26
	v_mul_f32_e32 v34, v26, v34
	v_fma_f32 v34, v26, v34, v26
	v_mul_f32_e32 v34, 0x3fcc422a, v34
	v_mul_f32_e32 v34, 0xbfb8aa3b, v34
	v_exp_f32_e32 v34, v34
	s_nop 0
	v_add_f32_e32 v34, 1.0, v34
	v_rcp_f32_e32 v34, v34
	s_nop 0
	v_mul_f32_e32 v34, v26, v34
	v_mul_f32_e32 v26, 0x3d372713, v27
	v_mul_f32_e32 v26, v27, v26
	v_fma_f32 v26, v27, v26, v27
	v_mul_f32_e32 v26, 0x3fcc422a, v26
	v_mul_f32_e32 v26, 0xbfb8aa3b, v26
	v_exp_f32_e32 v26, v26
	s_nop 0
	v_add_f32_e32 v26, 1.0, v26
	v_rcp_f32_e32 v26, v26
	s_nop 0
	v_mul_f32_e32 v35, v27, v26
	v_mul_f32_e32 v26, 0x3d372713, v28
	v_mul_f32_e32 v26, v28, v26
	v_fma_f32 v26, v28, v26, v28
	v_mul_f32_e32 v26, 0x3fcc422a, v26
	v_mul_f32_e32 v26, 0xbfb8aa3b, v26
	v_exp_f32_e32 v26, v26
	s_nop 0
	v_add_f32_e32 v26, 1.0, v26
	v_rcp_f32_e32 v26, v26
	s_nop 0
	v_mul_f32_e32 v36, v28, v26
	v_mul_f32_e32 v26, 0x3d372713, v29
	v_mul_f32_e32 v26, v29, v26
	v_fma_f32 v26, v29, v26, v29
	v_mul_f32_e32 v26, 0x3fcc422a, v26
	v_mul_f32_e32 v26, 0xbfb8aa3b, v26
	v_exp_f32_e32 v26, v26
	s_nop 0
	v_add_f32_e32 v26, 1.0, v26
	v_rcp_f32_e32 v26, v26
	s_nop 0
	v_mul_f32_e32 v29, v29, v26
	v_cvt_pk_bf16_f32 v26, v30, v31
	v_lshl_add_u64 v[30:31], s[14:15], 0, v[132:133]
	v_cvt_pk_bf16_f32 v27, v32, v33
	v_cvt_pk_bf16_f32 v28, v34, v35
	v_cvt_pk_bf16_f32 v29, v36, v29
	global_store_dwordx4 v[30:31], v[26:29], off
	s_add_i32 s14, s50, 0xb0
	s_ashr_i32 s15, s14, 31
	v_mul_f32_e32 v26, 0x3d372713, v22
	v_mul_f32_e32 v26, v22, v26
	v_fma_f32 v26, v22, v26, v22
	v_mul_f32_e32 v26, 0x3fcc422a, v26
	v_mul_f32_e32 v26, 0xbfb8aa3b, v26
	v_exp_f32_e32 v26, v26
	s_lshl_b64 s[14:15], s[14:15], 13
	s_add_u32 s2, s57, s14
	s_addc_u32 s15, s59, s15
	v_add_f32_e32 v26, 1.0, v26
	v_rcp_f32_e32 v26, v26
	s_add_u32 s14, s2, s52
	s_addc_u32 s15, s15, s53
	v_mul_f32_e32 v22, v22, v26
	v_mul_f32_e32 v26, 0x3d372713, v23
	v_mul_f32_e32 v26, v23, v26
	v_fma_f32 v26, v23, v26, v23
	v_mul_f32_e32 v26, 0x3fcc422a, v26
	v_mul_f32_e32 v26, 0xbfb8aa3b, v26
	v_exp_f32_e32 v26, v26
	s_nop 0
	v_add_f32_e32 v26, 1.0, v26
	v_rcp_f32_e32 v26, v26
	s_nop 0
	v_mul_f32_e32 v23, v23, v26
	v_mul_f32_e32 v26, 0x3d372713, v24
	v_mul_f32_e32 v26, v24, v26
	v_fma_f32 v26, v24, v26, v24
	v_mul_f32_e32 v26, 0x3fcc422a, v26
	v_mul_f32_e32 v26, 0xbfb8aa3b, v26
	v_exp_f32_e32 v26, v26
	s_nop 0
	v_add_f32_e32 v26, 1.0, v26
	v_rcp_f32_e32 v26, v26
	s_nop 0
	v_mul_f32_e32 v24, v24, v26
	v_mul_f32_e32 v26, 0x3d372713, v25
	v_mul_f32_e32 v26, v25, v26
	v_fma_f32 v26, v25, v26, v25
	v_mul_f32_e32 v26, 0x3fcc422a, v26
	v_mul_f32_e32 v26, 0xbfb8aa3b, v26
	v_exp_f32_e32 v26, v26
	s_nop 0
	v_add_f32_e32 v26, 1.0, v26
	v_rcp_f32_e32 v26, v26
	s_nop 0
	v_mul_f32_e32 v25, v25, v26
	v_mul_f32_e32 v26, 0x3d372713, v18
	v_mul_f32_e32 v26, v18, v26
	v_fma_f32 v26, v18, v26, v18
	v_mul_f32_e32 v26, 0x3fcc422a, v26
	v_mul_f32_e32 v26, 0xbfb8aa3b, v26
	v_exp_f32_e32 v26, v26
	s_nop 0
	v_add_f32_e32 v26, 1.0, v26
	v_rcp_f32_e32 v26, v26
	s_nop 0
	v_mul_f32_e32 v26, v18, v26
	v_mul_f32_e32 v18, 0x3d372713, v19
	v_mul_f32_e32 v18, v19, v18
	v_fma_f32 v18, v19, v18, v19
	v_mul_f32_e32 v18, 0x3fcc422a, v18
	v_mul_f32_e32 v18, 0xbfb8aa3b, v18
	v_exp_f32_e32 v18, v18
	s_nop 0
	v_add_f32_e32 v18, 1.0, v18
	v_rcp_f32_e32 v18, v18
	s_nop 0
	v_mul_f32_e32 v27, v19, v18
	v_mul_f32_e32 v18, 0x3d372713, v20
	v_mul_f32_e32 v18, v20, v18
	v_fma_f32 v18, v20, v18, v20
	v_mul_f32_e32 v18, 0x3fcc422a, v18
	v_mul_f32_e32 v18, 0xbfb8aa3b, v18
	v_exp_f32_e32 v18, v18
	s_nop 0
	v_add_f32_e32 v18, 1.0, v18
	v_rcp_f32_e32 v18, v18
	s_nop 0
	v_mul_f32_e32 v28, v20, v18
	v_mul_f32_e32 v18, 0x3d372713, v21
	v_mul_f32_e32 v18, v21, v18
	v_fma_f32 v18, v21, v18, v21
	v_mul_f32_e32 v18, 0x3fcc422a, v18
	v_mul_f32_e32 v18, 0xbfb8aa3b, v18
	v_exp_f32_e32 v18, v18
	s_nop 0
	v_add_f32_e32 v18, 1.0, v18
	v_rcp_f32_e32 v18, v18
	s_nop 0
	v_mul_f32_e32 v21, v21, v18
	v_cvt_pk_bf16_f32 v18, v22, v23
	v_add_co_u32_e32 v22, vcc, s34, v30
	v_cvt_pk_bf16_f32 v19, v24, v25
	v_cvt_pk_bf16_f32 v20, v26, v27
	v_cvt_pk_bf16_f32 v21, v28, v21
	s_nop 1
	v_addc_co_u32_e32 v23, vcc, 0, v31, vcc
	global_store_dwordx4 v[22:23], v[18:21], off
	s_nop 1
	v_mul_f32_e32 v18, 0x3d372713, v14
	v_mul_f32_e32 v18, v14, v18
	v_fma_f32 v18, v14, v18, v14
	v_mul_f32_e32 v18, 0x3fcc422a, v18
	v_mul_f32_e32 v18, 0xbfb8aa3b, v18
	v_exp_f32_e32 v18, v18
	s_nop 0
	v_add_f32_e32 v18, 1.0, v18
	v_rcp_f32_e32 v18, v18
	s_nop 0
	v_mul_f32_e32 v14, v14, v18
	v_mul_f32_e32 v18, 0x3d372713, v15
	v_mul_f32_e32 v18, v15, v18
	v_fma_f32 v18, v15, v18, v15
	v_mul_f32_e32 v18, 0x3fcc422a, v18
	v_mul_f32_e32 v18, 0xbfb8aa3b, v18
	v_exp_f32_e32 v18, v18
	s_nop 0
	v_add_f32_e32 v18, 1.0, v18
	v_rcp_f32_e32 v18, v18
	s_nop 0
	v_mul_f32_e32 v15, v15, v18
	v_mul_f32_e32 v18, 0x3d372713, v16
	v_mul_f32_e32 v18, v16, v18
	v_fma_f32 v18, v16, v18, v16
	v_mul_f32_e32 v18, 0x3fcc422a, v18
	v_mul_f32_e32 v18, 0xbfb8aa3b, v18
	v_exp_f32_e32 v18, v18
	s_nop 0
	v_add_f32_e32 v18, 1.0, v18
	v_rcp_f32_e32 v18, v18
	s_nop 0
	v_mul_f32_e32 v16, v16, v18
	v_mul_f32_e32 v18, 0x3d372713, v17
	v_mul_f32_e32 v18, v17, v18
	v_fma_f32 v18, v17, v18, v17
	v_mul_f32_e32 v18, 0x3fcc422a, v18
	v_mul_f32_e32 v18, 0xbfb8aa3b, v18
	v_exp_f32_e32 v18, v18
	s_nop 0
	v_add_f32_e32 v18, 1.0, v18
	v_rcp_f32_e32 v18, v18
	s_nop 0
	v_mul_f32_e32 v17, v17, v18
	v_mul_f32_e32 v18, 0x3d372713, v10
	v_mul_f32_e32 v18, v10, v18
	v_fma_f32 v18, v10, v18, v10
	v_mul_f32_e32 v18, 0x3fcc422a, v18
	v_mul_f32_e32 v18, 0xbfb8aa3b, v18
	v_exp_f32_e32 v18, v18
	s_nop 0
	v_add_f32_e32 v18, 1.0, v18
	v_rcp_f32_e32 v18, v18
	s_nop 0
	v_mul_f32_e32 v18, v10, v18
	v_mul_f32_e32 v10, 0x3d372713, v11
	v_mul_f32_e32 v10, v11, v10
	v_fma_f32 v10, v11, v10, v11
	v_mul_f32_e32 v10, 0x3fcc422a, v10
	v_mul_f32_e32 v10, 0xbfb8aa3b, v10
	v_exp_f32_e32 v10, v10
	s_nop 0
	v_add_f32_e32 v10, 1.0, v10
	v_rcp_f32_e32 v10, v10
	s_nop 0
	v_mul_f32_e32 v19, v11, v10
	v_mul_f32_e32 v10, 0x3d372713, v12
	v_mul_f32_e32 v10, v12, v10
	v_fma_f32 v10, v12, v10, v12
	v_mul_f32_e32 v10, 0x3fcc422a, v10
	v_mul_f32_e32 v10, 0xbfb8aa3b, v10
	v_exp_f32_e32 v10, v10
	s_nop 0
	v_add_f32_e32 v10, 1.0, v10
	v_rcp_f32_e32 v10, v10
	s_nop 0
	v_mul_f32_e32 v20, v12, v10
	v_mul_f32_e32 v10, 0x3d372713, v13
	v_mul_f32_e32 v10, v13, v10
	v_fma_f32 v10, v13, v10, v13
	v_mul_f32_e32 v10, 0x3fcc422a, v10
	v_mul_f32_e32 v10, 0xbfb8aa3b, v10
	v_exp_f32_e32 v10, v10
	s_nop 0
	v_add_f32_e32 v10, 1.0, v10
	v_rcp_f32_e32 v10, v10
	s_nop 0
	v_mul_f32_e32 v13, v13, v10
	v_cvt_pk_bf16_f32 v10, v14, v15
	v_lshl_add_u64 v[14:15], s[14:15], 0, v[132:133]
	v_cvt_pk_bf16_f32 v11, v16, v17
	v_cvt_pk_bf16_f32 v12, v18, v19
	v_cvt_pk_bf16_f32 v13, v20, v13
	global_store_dwordx4 v[14:15], v[10:13], off
	s_mov_b64 s[14:15], -1
	s_nop 0
	v_mul_f32_e32 v10, 0x3d372713, v6
	v_mul_f32_e32 v10, v6, v10
	v_fma_f32 v10, v6, v10, v6
	v_mul_f32_e32 v10, 0x3fcc422a, v10
	v_mul_f32_e32 v10, 0xbfb8aa3b, v10
	v_exp_f32_e32 v10, v10
	s_nop 0
	v_add_f32_e32 v10, 1.0, v10
	v_rcp_f32_e32 v10, v10
	s_nop 0
	v_mul_f32_e32 v6, v6, v10
	v_mul_f32_e32 v10, 0x3d372713, v7
	v_mul_f32_e32 v10, v7, v10
	v_fma_f32 v10, v7, v10, v7
	v_mul_f32_e32 v10, 0x3fcc422a, v10
	v_mul_f32_e32 v10, 0xbfb8aa3b, v10
	v_exp_f32_e32 v10, v10
	s_nop 0
	v_add_f32_e32 v10, 1.0, v10
	v_rcp_f32_e32 v10, v10
	s_nop 0
	v_mul_f32_e32 v7, v7, v10
	v_mul_f32_e32 v10, 0x3d372713, v8
	v_mul_f32_e32 v10, v8, v10
	v_fma_f32 v10, v8, v10, v8
	v_mul_f32_e32 v10, 0x3fcc422a, v10
	v_mul_f32_e32 v10, 0xbfb8aa3b, v10
	v_exp_f32_e32 v10, v10
	s_nop 0
	v_add_f32_e32 v10, 1.0, v10
	v_rcp_f32_e32 v10, v10
	s_nop 0
	v_mul_f32_e32 v8, v8, v10
	v_mul_f32_e32 v10, 0x3d372713, v9
	v_mul_f32_e32 v10, v9, v10
	v_fma_f32 v10, v9, v10, v9
	v_mul_f32_e32 v10, 0x3fcc422a, v10
	v_mul_f32_e32 v10, 0xbfb8aa3b, v10
	v_exp_f32_e32 v10, v10
	s_nop 0
	v_add_f32_e32 v10, 1.0, v10
	v_rcp_f32_e32 v10, v10
	s_nop 0
	v_mul_f32_e32 v9, v9, v10
	v_mul_f32_e32 v10, 0x3d372713, v2
	v_mul_f32_e32 v10, v2, v10
	v_fma_f32 v10, v2, v10, v2
	v_mul_f32_e32 v10, 0x3fcc422a, v10
	v_mul_f32_e32 v10, 0xbfb8aa3b, v10
	v_exp_f32_e32 v10, v10
	s_nop 0
	v_add_f32_e32 v10, 1.0, v10
	v_rcp_f32_e32 v10, v10
	s_nop 0
	v_mul_f32_e32 v10, v2, v10
	v_mul_f32_e32 v2, 0x3d372713, v3
	v_mul_f32_e32 v2, v3, v2
	v_fma_f32 v2, v3, v2, v3
	v_mul_f32_e32 v2, 0x3fcc422a, v2
	v_mul_f32_e32 v2, 0xbfb8aa3b, v2
	v_exp_f32_e32 v2, v2
	s_nop 0
	v_add_f32_e32 v2, 1.0, v2
	v_rcp_f32_e32 v2, v2
	s_nop 0
	v_mul_f32_e32 v11, v3, v2
	v_mul_f32_e32 v2, 0x3d372713, v4
	v_mul_f32_e32 v2, v4, v2
	v_fma_f32 v2, v4, v2, v4
	v_mul_f32_e32 v2, 0x3fcc422a, v2
	v_mul_f32_e32 v2, 0xbfb8aa3b, v2
	v_exp_f32_e32 v2, v2
	s_nop 0
	v_add_f32_e32 v2, 1.0, v2
	v_rcp_f32_e32 v2, v2
	s_nop 0
	v_mul_f32_e32 v12, v4, v2
	v_mul_f32_e32 v2, 0x3d372713, v5
	v_mul_f32_e32 v2, v5, v2
	v_fma_f32 v2, v5, v2, v5
	v_mul_f32_e32 v2, 0x3fcc422a, v2
	v_mul_f32_e32 v2, 0xbfb8aa3b, v2
	v_exp_f32_e32 v2, v2
	s_nop 0
	v_add_f32_e32 v2, 1.0, v2
	v_rcp_f32_e32 v2, v2
	s_nop 0
	v_mul_f32_e32 v5, v5, v2
	v_cvt_pk_bf16_f32 v2, v6, v7
	v_add_co_u32_e32 v6, vcc, 0x1000, v14
	v_cvt_pk_bf16_f32 v3, v8, v9
	v_cvt_pk_bf16_f32 v4, v10, v11
	v_cvt_pk_bf16_f32 v5, v12, v5
	s_nop 1
	v_addc_co_u32_e32 v7, vcc, 0, v15, vcc
	s_andn2_b64 vcc, exec, s[48:49]
	global_store_dwordx4 v[6:7], v[2:5], off
	s_cbranch_vccnz .LBB0_612
	s_andn2_b64 vcc, exec, s[0:1]
	s_cbranch_vccnz .LBB0_611
	s_barrier
	s_branch .LBB0_611

.LBB0_642:
	v_bfe_u32 v1, v2, 4, 2
	s_lshl_b32 s15, s15, 5
	v_and_b32_e32 v38, 15, v2
	v_lshlrev_b32_e32 v39, 4, v1
	v_lshlrev_b32_e32 v2, 2, v2
	s_and_b32 s17, s15, 0x60
	s_lshl_b32 s16, s14, 6
	v_lshl_or_b32 v3, v38, 6, v39
	v_and_b32_e32 v2, 32, v2
	s_lshl_b32 s14, s14, 13
	s_lshl_b32 s15, s17, 7
	v_bitop3_b32 v40, v3, s15, v2 bitop3:0xde
	v_bitop3_b32 v4, v3, s14, v2 bitop3:0xde
	v_lshl_add_u64 v[2:3], v[34:35], 0, s[92:93]
	s_add_i32 m0, s3, 0x19000
	s_mov_b64 s[58:59], 0x8080
	s_waitcnt vmcnt(2)
	s_barrier
	global_load_lds_dwordx4 v[2:3], off
	v_lshl_add_u64 v[2:3], v[34:35], 0, s[58:59]
	s_add_i32 m0, s3, 0x1b000
	s_add_i32 s33, s3, 0x9000
	global_load_lds_dwordx4 v[2:3], off
	v_lshl_add_u64 v[2:3], v[36:37], 0, s[92:93]
	s_mov_b32 m0, s33
	s_add_i32 s34, s3, 0xb000
	global_load_lds_dwordx4 v[2:3], off
	v_lshl_add_u64 v[2:3], v[36:37], 0, s[58:59]
	s_mov_b32 m0, s34
	s_mov_b64 s[60:61], 0x10080
	global_load_lds_dwordx4 v[2:3], off
	s_add_i32 m0, s3, 0x1d000
	v_lshl_add_u64 v[2:3], v[34:35], 0, s[60:61]
	global_load_lds_dwordx4 v[2:3], off
	v_lshl_add_u64 v[2:3], v[34:35], 0, s[30:31]
	s_add_i32 m0, s3, 0x1f000
	s_mov_b32 s96, 0
	global_load_lds_dwordx4 v[2:3], off
	s_waitcnt vmcnt(6)
	v_mov_b32_e32 v2, 0
	s_mov_b64 s[42:43], -1
	s_mov_b64 s[44:45], 0
	v_add_u32_e32 v41, 0, v4
	v_mov_b32_e32 v3, 0
	v_mov_b64_e32 v[4:5], 0
	v_mov_b64_e32 v[6:7], 0
	v_mov_b64_e32 v[8:9], 0
	v_mov_b64_e32 v[18:19], 0
	v_mov_b64_e32 v[20:21], 0
	v_mov_b64_e32 v[22:23], 0
	v_mov_b64_e32 v[24:25], 0
	v_mov_b64_e32 v[50:51], 0
	v_mov_b64_e32 v[52:53], 0
	v_mov_b64_e32 v[54:55], 0
	v_mov_b64_e32 v[56:57], 0
	v_mov_b64_e32 v[66:67], 0
	v_mov_b64_e32 v[68:69], 0
	v_mov_b64_e32 v[70:71], 0
	v_mov_b64_e32 v[72:73], 0
	v_mov_b64_e32 v[10:11], 0
	v_mov_b64_e32 v[12:13], 0
	v_mov_b64_e32 v[14:15], 0
	v_mov_b64_e32 v[16:17], 0
	v_mov_b64_e32 v[26:27], 0
	v_mov_b64_e32 v[28:29], 0
	v_mov_b64_e32 v[30:31], 0
	v_mov_b64_e32 v[32:33], 0
	v_mov_b64_e32 v[58:59], 0
	v_mov_b64_e32 v[60:61], 0
	v_mov_b64_e32 v[62:63], 0
	v_mov_b64_e32 v[64:65], 0
	v_mov_b64_e32 v[74:75], 0
	v_mov_b64_e32 v[76:77], 0
	v_mov_b64_e32 v[78:79], 0
	v_mov_b64_e32 v[80:81], 0
	v_mov_b64_e32 v[82:83], 0
	v_mov_b64_e32 v[84:85], 0
	v_mov_b64_e32 v[86:87], 0
	v_mov_b64_e32 v[88:89], 0
	v_mov_b64_e32 v[98:99], 0
	v_mov_b64_e32 v[100:101], 0
	v_mov_b64_e32 v[102:103], 0
	v_mov_b64_e32 v[104:105], 0
	v_mov_b64_e32 v[114:115], 0
	v_mov_b64_e32 v[116:117], 0
	v_mov_b64_e32 v[118:119], 0
	v_mov_b64_e32 v[120:121], 0
	v_mov_b64_e32 v[130:131], 0
	v_mov_b64_e32 v[132:133], 0
	v_mov_b64_e32 v[134:135], 0
	v_mov_b64_e32 v[136:137], 0
	v_mov_b64_e32 v[90:91], 0
	v_mov_b64_e32 v[92:93], 0
	v_mov_b64_e32 v[94:95], 0
	v_mov_b64_e32 v[96:97], 0
	v_mov_b64_e32 v[106:107], 0
	v_mov_b64_e32 v[108:109], 0
	v_mov_b64_e32 v[110:111], 0
	v_mov_b64_e32 v[112:113], 0
	v_mov_b64_e32 v[122:123], 0
	v_mov_b64_e32 v[124:125], 0
	v_mov_b64_e32 v[126:127], 0
	v_mov_b64_e32 v[128:129], 0
	v_mov_b64_e32 v[138:139], 0
	v_mov_b64_e32 v[140:141], 0
	v_mov_b64_e32 v[142:143], 0
	v_mov_b64_e32 v[144:145], 0
	s_mov_b64 s[54:55], 0x8000
	s_mov_b64 s[56:57], 0x10000
	s_barrier

.LBB0_646:
	v_readlane_b32 s24, v253, 32
	s_add_u32 s3, s40, 0x6c800000
	v_readlane_b32 s25, v253, 33
	s_addc_u32 s14, s41, 0
	s_lshl_b64 s[24:25], s[24:25], 10
	s_add_u32 s1, s38, s24
	s_addc_u32 s2, s39, s25
	s_lshl_b32 s15, s17, 2
	s_add_u32 s24, s1, s15
	v_lshlrev_b32_e32 v1, 5, v1
	s_addc_u32 s25, s2, 0
	s_lshl_b32 s0, s0, 8
	v_lshl_or_b32 v186, v38, 9, v39
	global_load_dwordx4 v[42:45], v1, s[24:25] offset:16
	global_load_dwordx4 v[46:49], v1, s[24:25]
	global_load_dwordx4 v[34:37], v1, s[24:25] offset:528
	global_load_dwordx4 v[38:41], v1, s[24:25] offset:512
	s_add_i32 s0, s16, s0
	s_ashr_i32 s1, s0, 31
	s_lshl_b64 s[38:39], s[0:1], 9
	s_add_u32 s1, s12, s38
	s_addc_u32 s2, s13, s39
	s_lshl_b32 s15, s17, 1
	s_add_u32 s16, s1, s15
	s_addc_u32 s17, s2, 0
	v_lshl_add_u64 v[150:151], s[16:17], 0, v[186:187]
	global_load_dwordx4 v[146:149], v[150:151], off
	s_add_u32 s1, s3, s38
	s_addc_u32 s2, s14, s39
	s_add_u32 s16, s1, s15
	s_addc_u32 s17, s2, 0
	s_waitcnt vmcnt(0)
	v_pk_add_f32 v[140:141], v[140:141], v[44:45]
	v_pk_add_f32 v[142:143], v[142:143], v[46:47]
	v_mul_f32_e32 v140, 0xbfb8aa3b, v140
	v_mul_f32_e32 v142, 0xbfb8aa3b, v142
	v_exp_f32_e32 v142, v142
	v_exp_f32_e32 v140, v140
	v_pk_add_f32 v[144:145], v[144:145], v[48:49]
	v_pk_add_f32 v[138:139], v[138:139], v[42:43]
	v_add_f32_e32 v142, 1.0, v142
	v_add_f32_e32 v140, 1.0, v140
	v_rcp_f32_e32 v142, v142
	v_rcp_f32_e32 v140, v140
	v_mul_f32_e32 v138, 0xbfb8aa3b, v138
	s_waitcnt lgkmcnt(0)
	v_lshlrev_b32_e32 v1, 16, v146
	v_lshlrev_b32_e32 v157, 16, v149
	v_mul_f32_e32 v1, v142, v1
	v_mul_f32_e32 v142, 0xbfb8aa3b, v143
	v_mul_f32_e32 v143, 0xbfb8aa3b, v144
	v_mul_f32_e32 v144, v140, v157
	v_mul_f32_e32 v140, 0xbfb8aa3b, v145
	v_exp_f32_e32 v140, v140
	v_and_b32_e32 v154, 0xffff0000, v147
	v_mul_f32_e32 v139, 0xbfb8aa3b, v139
	v_exp_f32_e32 v138, v138
	v_add_f32_e32 v140, 1.0, v140
	v_rcp_f32_e32 v140, v140
	v_exp_f32_e32 v142, v142
	v_exp_f32_e32 v139, v139
	v_exp_f32_e32 v143, v143
	v_mul_f32_e32 v145, v140, v154
	v_mul_f32_e32 v140, 0xbfb8aa3b, v141
	v_exp_f32_e32 v140, v140
	v_add_f32_e32 v138, 1.0, v138
	v_add_f32_e32 v142, 1.0, v142
	v_add_f32_e32 v139, 1.0, v139
	v_rcp_f32_e32 v138, v138
	v_rcp_f32_e32 v142, v142
	v_rcp_f32_e32 v139, v139
	v_add_f32_e32 v143, 1.0, v143
	v_add_f32_e32 v140, 1.0, v140
	v_and_b32_e32 v152, 0xffff0000, v146
	v_lshlrev_b32_e32 v153, 16, v147
	v_lshlrev_b32_e32 v155, 16, v148
	v_and_b32_e32 v156, 0xffff0000, v148
	v_and_b32_e32 v158, 0xffff0000, v149
	global_load_dwordx4 v[146:149], v[150:151], off offset:256
	v_rcp_f32_e32 v143, v143
	v_rcp_f32_e32 v140, v140
	v_mul_f32_e32 v138, v138, v155
	v_mul_f32_e32 v142, v142, v152
	v_mul_f32_e32 v139, v139, v156
	v_mul_f32_e32 v143, v143, v153
	v_mul_f32_e32 v150, v140, v158
	v_cvt_pk_bf16_f32 v140, v1, v142
	v_cvt_pk_bf16_f32 v141, v143, v145
	v_cvt_pk_bf16_f32 v142, v138, v139
	v_lshl_add_u64 v[138:139], s[16:17], 0, v[186:187]
	s_add_i32 s16, s0, 16
	s_ashr_i32 s17, s16, 31
	s_lshl_b64 s[38:39], s[16:17], 9
	s_add_u32 s1, s12, s38
	s_addc_u32 s2, s13, s39
	s_add_u32 s16, s1, s15
	v_cvt_pk_bf16_f32 v143, v144, v150
	global_store_dwordx4 v[138:139], v[140:143], off
	s_addc_u32 s17, s2, 0
	v_pk_add_f32 v[134:135], v[134:135], v[38:39]
	v_lshl_add_u64 v[140:141], s[16:17], 0, v[186:187]
	global_load_dwordx4 v[142:145], v[140:141], off
	v_pk_add_f32 v[132:133], v[132:133], v[36:37]
	v_pk_add_f32 v[130:131], v[130:131], v[34:35]
	v_mul_f32_e32 v134, 0xbfb8aa3b, v134
	v_mul_f32_e32 v130, 0xbfb8aa3b, v130
	v_mul_f32_e32 v131, 0xbfb8aa3b, v131
	v_mul_f32_e32 v132, 0xbfb8aa3b, v132
	v_exp_f32_e32 v134, v134
	v_exp_f32_e32 v130, v130
	v_exp_f32_e32 v131, v131
	v_exp_f32_e32 v132, v132
	v_add_f32_e32 v134, 1.0, v134
	v_add_f32_e32 v130, 1.0, v130
	v_add_f32_e32 v131, 1.0, v131
	v_add_f32_e32 v132, 1.0, v132
	v_rcp_f32_e32 v134, v134
	v_rcp_f32_e32 v130, v130
	v_rcp_f32_e32 v131, v131
	v_rcp_f32_e32 v132, v132
	v_pk_add_f32 v[136:137], v[136:137], v[40:41]
	v_pk_add_f32 v[124:125], v[124:125], v[44:45]
	v_pk_add_f32 v[128:129], v[128:129], v[48:49]
	v_mul_f32_e32 v124, 0xbfb8aa3b, v124
	v_exp_f32_e32 v124, v124
	v_mul_f32_e32 v133, 0xbfb8aa3b, v133
	v_exp_f32_e32 v133, v133
	v_pk_add_f32 v[126:127], v[126:127], v[46:47]
	v_add_f32_e32 v124, 1.0, v124
	v_rcp_f32_e32 v124, v124
	v_add_f32_e32 v133, 1.0, v133
	v_pk_add_f32 v[122:123], v[122:123], v[42:43]
	v_rcp_f32_e32 v133, v133
	v_mul_f32_e32 v126, 0xbfb8aa3b, v126
	v_mul_f32_e32 v122, 0xbfb8aa3b, v122
	v_mul_f32_e32 v123, 0xbfb8aa3b, v123
	v_exp_f32_e32 v126, v126
	v_exp_f32_e32 v122, v122
	v_mul_f32_e32 v127, 0xbfb8aa3b, v127
	v_exp_f32_e32 v123, v123
	v_mul_f32_e32 v128, 0xbfb8aa3b, v128
	v_exp_f32_e32 v127, v127
	v_exp_f32_e32 v128, v128
	v_add_f32_e32 v126, 1.0, v126
	v_add_f32_e32 v122, 1.0, v122
	v_add_f32_e32 v123, 1.0, v123
	v_rcp_f32_e32 v126, v126
	v_rcp_f32_e32 v122, v122
	v_add_f32_e32 v127, 1.0, v127
	v_rcp_f32_e32 v123, v123
	v_add_f32_e32 v128, 1.0, v128
	v_rcp_f32_e32 v127, v127
	v_rcp_f32_e32 v128, v128
	s_add_u32 s1, s3, s38
	s_addc_u32 s2, s14, s39
	s_add_u32 s16, s1, s15
	s_addc_u32 s17, s2, 0
	s_waitcnt vmcnt(0) lgkmcnt(0)
	v_lshlrev_b32_e32 v1, 16, v146
	v_lshlrev_b32_e32 v151, 16, v148
	v_and_b32_e32 v148, 0xffff0000, v148
	v_lshlrev_b32_e32 v152, 16, v149
	v_mul_f32_e32 v1, v134, v1
	v_mul_f32_e32 v134, v130, v151
	v_mul_f32_e32 v130, 0xbfb8aa3b, v135
	v_mul_f32_e32 v135, v131, v148
	v_mul_f32_e32 v131, 0xbfb8aa3b, v136
	v_mul_f32_e32 v136, v132, v152
	v_mul_f32_e32 v132, 0xbfb8aa3b, v137
	v_exp_f32_e32 v130, v130
	v_exp_f32_e32 v131, v131
	v_exp_f32_e32 v132, v132
	v_and_b32_e32 v146, 0xffff0000, v146
	v_add_f32_e32 v130, 1.0, v130
	v_add_f32_e32 v131, 1.0, v131
	v_add_f32_e32 v132, 1.0, v132
	v_rcp_f32_e32 v130, v130
	v_rcp_f32_e32 v131, v131
	v_rcp_f32_e32 v132, v132
	v_lshlrev_b32_e32 v150, 16, v147
	v_and_b32_e32 v147, 0xffff0000, v147
	v_mul_f32_e32 v130, v130, v146
	v_mul_f32_e32 v131, v131, v150
	v_mul_f32_e32 v132, v132, v147
	v_cvt_pk_bf16_f32 v130, v1, v130
	v_cvt_pk_bf16_f32 v131, v131, v132
	v_cvt_pk_bf16_f32 v132, v134, v135
	v_lshlrev_b32_e32 v135, 16, v145
	v_mul_f32_e32 v135, v124, v135
	v_mul_f32_e32 v124, 0xbfb8aa3b, v129
	v_exp_f32_e32 v124, v124
	v_and_b32_e32 v134, 0xffff0000, v143
	v_and_b32_e32 v149, 0xffff0000, v149
	v_mul_f32_e32 v133, v133, v149
	v_add_f32_e32 v124, 1.0, v124
	v_rcp_f32_e32 v124, v124
	v_cvt_pk_bf16_f32 v133, v136, v133
	global_store_dwordx4 v[138:139], v[130:133], off offset:256
	v_mul_f32_e32 v129, v124, v134
	v_mul_f32_e32 v124, 0xbfb8aa3b, v125
	v_exp_f32_e32 v124, v124
	global_load_dwordx4 v[130:133], v[140:141], off offset:256
	v_lshlrev_b32_e32 v138, 16, v142
	v_and_b32_e32 v139, 0xffff0000, v142
	v_add_f32_e32 v124, 1.0, v124
	v_rcp_f32_e32 v124, v124
	v_lshlrev_b32_e32 v142, 16, v144
	v_and_b32_e32 v137, 0xffff0000, v144
	v_lshlrev_b32_e32 v136, 16, v143
	v_and_b32_e32 v1, 0xffff0000, v145
	v_mul_f32_e32 v126, v126, v138
	v_mul_f32_e32 v122, v122, v142
	v_mul_f32_e32 v123, v123, v137
	v_mul_f32_e32 v127, v127, v139
	v_mul_f32_e32 v128, v128, v136
	v_mul_f32_e32 v1, v124, v1
	v_cvt_pk_bf16_f32 v124, v126, v127
	v_cvt_pk_bf16_f32 v125, v128, v129
	v_cvt_pk_bf16_f32 v126, v122, v123
	v_lshl_add_u64 v[122:123], s[16:17], 0, v[186:187]
	s_add_i32 s16, s0, 32
	s_ashr_i32 s17, s16, 31
	s_lshl_b64 s[38:39], s[16:17], 9
	s_add_u32 s1, s12, s38
	s_addc_u32 s2, s13, s39
	s_add_u32 s16, s1, s15
	v_cvt_pk_bf16_f32 v127, v135, v1
	global_store_dwordx4 v[122:123], v[124:127], off
	s_addc_u32 s17, s2, 0
	v_lshl_add_u64 v[128:129], s[16:17], 0, v[186:187]
	global_load_dwordx4 v[124:127], v[128:129], off
	v_pk_add_f32 v[118:119], v[118:119], v[38:39]
	v_pk_add_f32 v[116:117], v[116:117], v[36:37]
	v_pk_add_f32 v[114:115], v[114:115], v[34:35]
	v_mul_f32_e32 v118, 0xbfb8aa3b, v118
	v_mul_f32_e32 v114, 0xbfb8aa3b, v114
	v_mul_f32_e32 v115, 0xbfb8aa3b, v115
	v_mul_f32_e32 v116, 0xbfb8aa3b, v116
	v_exp_f32_e32 v118, v118
	v_exp_f32_e32 v114, v114
	v_exp_f32_e32 v115, v115
	v_exp_f32_e32 v116, v116
	v_add_f32_e32 v118, 1.0, v118
	v_add_f32_e32 v114, 1.0, v114
	v_add_f32_e32 v115, 1.0, v115
	v_add_f32_e32 v116, 1.0, v116
	v_rcp_f32_e32 v118, v118
	v_rcp_f32_e32 v114, v114
	v_rcp_f32_e32 v115, v115
	v_rcp_f32_e32 v116, v116
	v_pk_add_f32 v[120:121], v[120:121], v[40:41]
	v_mul_f32_e32 v117, 0xbfb8aa3b, v117
	v_exp_f32_e32 v117, v117
	v_pk_add_f32 v[110:111], v[110:111], v[46:47]
	v_pk_add_f32 v[108:109], v[108:109], v[44:45]
	v_mul_f32_e32 v110, 0xbfb8aa3b, v110
	v_mul_f32_e32 v108, 0xbfb8aa3b, v108
	v_exp_f32_e32 v110, v110
	v_exp_f32_e32 v108, v108
	v_add_f32_e32 v117, 1.0, v117
	v_rcp_f32_e32 v117, v117
	v_add_f32_e32 v110, 1.0, v110
	v_add_f32_e32 v108, 1.0, v108
	v_rcp_f32_e32 v110, v110
	v_rcp_f32_e32 v108, v108
	v_pk_add_f32 v[112:113], v[112:113], v[48:49]
	v_pk_add_f32 v[106:107], v[106:107], v[42:43]
	s_add_u32 s1, s3, s38
	v_mul_f32_e32 v106, 0xbfb8aa3b, v106
	v_mul_f32_e32 v107, 0xbfb8aa3b, v107
	v_exp_f32_e32 v106, v106
	v_exp_f32_e32 v107, v107
	s_addc_u32 s2, s14, s39
	s_add_u32 s16, s1, s15
	v_add_f32_e32 v106, 1.0, v106
	v_add_f32_e32 v107, 1.0, v107
	v_rcp_f32_e32 v106, v106
	v_rcp_f32_e32 v107, v107
	s_addc_u32 s17, s2, 0
	v_pk_add_f32 v[102:103], v[102:103], v[38:39]
	s_waitcnt vmcnt(0) lgkmcnt(0)
	v_lshlrev_b32_e32 v1, 16, v130
	v_lshlrev_b32_e32 v135, 16, v132
	v_and_b32_e32 v132, 0xffff0000, v132
	v_lshlrev_b32_e32 v136, 16, v133
	v_mul_f32_e32 v1, v118, v1
	v_mul_f32_e32 v118, v114, v135
	v_mul_f32_e32 v114, 0xbfb8aa3b, v119
	v_mul_f32_e32 v119, v115, v132
	v_mul_f32_e32 v115, 0xbfb8aa3b, v120
	v_mul_f32_e32 v120, v116, v136
	v_mul_f32_e32 v116, 0xbfb8aa3b, v121
	v_exp_f32_e32 v114, v114
	v_exp_f32_e32 v115, v115
	v_exp_f32_e32 v116, v116
	v_and_b32_e32 v130, 0xffff0000, v130
	v_add_f32_e32 v114, 1.0, v114
	v_add_f32_e32 v115, 1.0, v115
	v_add_f32_e32 v116, 1.0, v116
	v_rcp_f32_e32 v114, v114
	v_rcp_f32_e32 v115, v115
	v_rcp_f32_e32 v116, v116
	v_lshlrev_b32_e32 v134, 16, v131
	v_and_b32_e32 v131, 0xffff0000, v131
	v_and_b32_e32 v133, 0xffff0000, v133
	v_mul_f32_e32 v114, v114, v130
	v_mul_f32_e32 v115, v115, v134
	v_mul_f32_e32 v116, v116, v131
	v_mul_f32_e32 v117, v117, v133
	v_cvt_pk_bf16_f32 v114, v1, v114
	v_cvt_pk_bf16_f32 v115, v115, v116
	v_cvt_pk_bf16_f32 v116, v118, v119
	v_cvt_pk_bf16_f32 v117, v120, v117
	global_store_dwordx4 v[122:123], v[114:117], off offset:256
	v_lshlrev_b32_e32 v1, 16, v124
	v_lshlrev_b32_e32 v123, 16, v127
	v_mul_f32_e32 v1, v110, v1
	v_mul_f32_e32 v110, 0xbfb8aa3b, v111
	v_mul_f32_e32 v111, 0xbfb8aa3b, v112
	v_mul_f32_e32 v112, v108, v123
	v_mul_f32_e32 v108, 0xbfb8aa3b, v113
	v_exp_f32_e32 v108, v108
	global_load_dwordx4 v[114:117], v[128:129], off offset:256
	v_and_b32_e32 v120, 0xffff0000, v125
	v_exp_f32_e32 v110, v110
	v_add_f32_e32 v108, 1.0, v108
	v_rcp_f32_e32 v108, v108
	v_exp_f32_e32 v111, v111
	v_add_f32_e32 v110, 1.0, v110
	v_rcp_f32_e32 v110, v110
	v_mul_f32_e32 v113, v108, v120
	v_mul_f32_e32 v108, 0xbfb8aa3b, v109
	v_exp_f32_e32 v108, v108
	v_add_f32_e32 v111, 1.0, v111
	v_rcp_f32_e32 v111, v111
	v_and_b32_e32 v118, 0xffff0000, v124
	v_add_f32_e32 v108, 1.0, v108
	v_rcp_f32_e32 v108, v108
	v_lshlrev_b32_e32 v121, 16, v126
	v_and_b32_e32 v122, 0xffff0000, v126
	v_lshlrev_b32_e32 v119, 16, v125
	v_and_b32_e32 v124, 0xffff0000, v127
	v_mul_f32_e32 v106, v106, v121
	v_mul_f32_e32 v110, v110, v118
	v_mul_f32_e32 v107, v107, v122
	v_mul_f32_e32 v111, v111, v119
	v_mul_f32_e32 v118, v108, v124
	v_cvt_pk_bf16_f32 v108, v1, v110
	v_cvt_pk_bf16_f32 v109, v111, v113
	v_cvt_pk_bf16_f32 v110, v106, v107
	v_lshl_add_u64 v[106:107], s[16:17], 0, v[186:187]
	s_add_i32 s16, s0, 48
	s_ashr_i32 s17, s16, 31
	s_lshl_b64 s[38:39], s[16:17], 9
	s_add_u32 s1, s12, s38
	s_addc_u32 s2, s13, s39
	s_add_u32 s16, s1, s15
	v_cvt_pk_bf16_f32 v111, v112, v118
	global_store_dwordx4 v[106:107], v[108:111], off
	s_addc_u32 s17, s2, 0
	v_lshl_add_u64 v[112:113], s[16:17], 0, v[186:187]
	global_load_dwordx4 v[108:111], v[112:113], off
	v_pk_add_f32 v[100:101], v[100:101], v[36:37]
	v_pk_add_f32 v[98:99], v[98:99], v[34:35]
	v_mul_f32_e32 v102, 0xbfb8aa3b, v102
	v_mul_f32_e32 v98, 0xbfb8aa3b, v98
	v_mul_f32_e32 v99, 0xbfb8aa3b, v99
	v_mul_f32_e32 v100, 0xbfb8aa3b, v100
	v_exp_f32_e32 v102, v102
	v_exp_f32_e32 v98, v98
	v_exp_f32_e32 v99, v99
	v_exp_f32_e32 v100, v100
	v_add_f32_e32 v102, 1.0, v102
	v_add_f32_e32 v98, 1.0, v98
	v_add_f32_e32 v99, 1.0, v99
	v_add_f32_e32 v100, 1.0, v100
	v_rcp_f32_e32 v102, v102
	v_rcp_f32_e32 v98, v98
	v_rcp_f32_e32 v99, v99
	v_rcp_f32_e32 v100, v100
	v_pk_add_f32 v[104:105], v[104:105], v[40:41]
	v_mul_f32_e32 v101, 0xbfb8aa3b, v101
	v_exp_f32_e32 v101, v101
	v_pk_add_f32 v[94:95], v[94:95], v[46:47]
	v_pk_add_f32 v[92:93], v[92:93], v[44:45]
	v_mul_f32_e32 v94, 0xbfb8aa3b, v94
	v_add_f32_e32 v101, 1.0, v101
	v_rcp_f32_e32 v101, v101
	v_mul_f32_e32 v92, 0xbfb8aa3b, v92
	v_exp_f32_e32 v94, v94
	v_exp_f32_e32 v92, v92
	v_pk_add_f32 v[96:97], v[96:97], v[48:49]
	v_pk_add_f32 v[90:91], v[90:91], v[42:43]
	v_add_f32_e32 v94, 1.0, v94
	v_add_f32_e32 v92, 1.0, v92
	v_rcp_f32_e32 v94, v94
	v_rcp_f32_e32 v92, v92
	v_mul_f32_e32 v90, 0xbfb8aa3b, v90
	v_mul_f32_e32 v91, 0xbfb8aa3b, v91
	v_exp_f32_e32 v90, v90
	v_exp_f32_e32 v91, v91
	s_waitcnt vmcnt(0) lgkmcnt(0)
	v_lshlrev_b32_e32 v1, 16, v114
	v_lshlrev_b32_e32 v119, 16, v116
	v_and_b32_e32 v116, 0xffff0000, v116
	v_lshlrev_b32_e32 v120, 16, v117
	v_mul_f32_e32 v1, v102, v1
	v_mul_f32_e32 v102, v98, v119
	v_mul_f32_e32 v98, 0xbfb8aa3b, v103
	v_mul_f32_e32 v103, v99, v116
	v_mul_f32_e32 v99, 0xbfb8aa3b, v104
	v_mul_f32_e32 v104, v100, v120
	v_mul_f32_e32 v100, 0xbfb8aa3b, v105
	v_exp_f32_e32 v98, v98
	v_exp_f32_e32 v99, v99
	v_exp_f32_e32 v100, v100
	v_and_b32_e32 v114, 0xffff0000, v114
	v_add_f32_e32 v98, 1.0, v98
	v_add_f32_e32 v99, 1.0, v99
	v_add_f32_e32 v100, 1.0, v100
	v_rcp_f32_e32 v98, v98
	v_rcp_f32_e32 v99, v99
	v_rcp_f32_e32 v100, v100
	v_lshlrev_b32_e32 v118, 16, v115
	v_and_b32_e32 v115, 0xffff0000, v115
	v_and_b32_e32 v117, 0xffff0000, v117
	v_mul_f32_e32 v98, v98, v114
	v_mul_f32_e32 v99, v99, v118
	v_mul_f32_e32 v100, v100, v115
	v_mul_f32_e32 v101, v101, v117
	v_cvt_pk_bf16_f32 v98, v1, v98
	v_cvt_pk_bf16_f32 v99, v99, v100
	v_cvt_pk_bf16_f32 v100, v102, v103
	v_cvt_pk_bf16_f32 v101, v104, v101
	global_store_dwordx4 v[106:107], v[98:101], off offset:256
	global_load_dwordx4 v[98:101], v[112:113], off offset:256
	v_add_f32_e32 v90, 1.0, v90
	v_add_f32_e32 v91, 1.0, v91
	v_rcp_f32_e32 v90, v90
	v_rcp_f32_e32 v91, v91
	s_add_u32 s1, s3, s38
	v_lshlrev_b32_e32 v1, 16, v108
	v_lshlrev_b32_e32 v107, 16, v111
	v_mul_f32_e32 v1, v94, v1
	v_mul_f32_e32 v94, 0xbfb8aa3b, v95
	v_mul_f32_e32 v95, 0xbfb8aa3b, v96
	v_mul_f32_e32 v96, v92, v107
	v_mul_f32_e32 v92, 0xbfb8aa3b, v97
	v_exp_f32_e32 v92, v92
	v_and_b32_e32 v104, 0xffff0000, v109
	v_exp_f32_e32 v94, v94
	v_exp_f32_e32 v95, v95
	v_add_f32_e32 v92, 1.0, v92
	v_rcp_f32_e32 v92, v92
	v_add_f32_e32 v94, 1.0, v94
	v_rcp_f32_e32 v94, v94
	v_add_f32_e32 v95, 1.0, v95
	v_mul_f32_e32 v97, v92, v104
	v_mul_f32_e32 v92, 0xbfb8aa3b, v93
	v_exp_f32_e32 v92, v92
	v_rcp_f32_e32 v95, v95
	s_addc_u32 s2, s14, s39
	v_and_b32_e32 v102, 0xffff0000, v108
	v_add_f32_e32 v92, 1.0, v92
	v_rcp_f32_e32 v92, v92
	v_lshlrev_b32_e32 v105, 16, v110
	v_and_b32_e32 v106, 0xffff0000, v110
	s_add_u32 s16, s1, s15
	v_lshlrev_b32_e32 v103, 16, v109
	v_and_b32_e32 v108, 0xffff0000, v111
	v_mul_f32_e32 v90, v90, v105
	v_mul_f32_e32 v94, v94, v102
	v_mul_f32_e32 v91, v91, v106
	s_addc_u32 s17, s2, 0
	v_mul_f32_e32 v95, v95, v103
	v_mul_f32_e32 v102, v92, v108
	v_cvt_pk_bf16_f32 v92, v1, v94
	v_cvt_pk_bf16_f32 v93, v95, v97
	v_cvt_pk_bf16_f32 v94, v90, v91
	v_lshl_add_u64 v[90:91], s[16:17], 0, v[186:187]
	s_add_i32 s16, s0, 0x80
	s_ashr_i32 s17, s16, 31
	s_lshl_b64 s[38:39], s[16:17], 9
	s_add_u32 s1, s12, s38
	s_addc_u32 s2, s13, s39
	s_add_u32 s16, s1, s15
	v_cvt_pk_bf16_f32 v95, v96, v102
	global_store_dwordx4 v[90:91], v[92:95], off
	s_addc_u32 s17, s2, 0
	v_lshl_add_u64 v[96:97], s[16:17], 0, v[186:187]
	global_load_dwordx4 v[92:95], v[96:97], off
	v_pk_add_f32 v[86:87], v[86:87], v[38:39]
	v_pk_add_f32 v[84:85], v[84:85], v[36:37]
	v_pk_add_f32 v[82:83], v[82:83], v[34:35]
	v_mul_f32_e32 v86, 0xbfb8aa3b, v86
	v_mul_f32_e32 v82, 0xbfb8aa3b, v82
	v_mul_f32_e32 v83, 0xbfb8aa3b, v83
	v_mul_f32_e32 v84, 0xbfb8aa3b, v84
	v_exp_f32_e32 v86, v86
	v_exp_f32_e32 v82, v82
	v_exp_f32_e32 v83, v83
	v_exp_f32_e32 v84, v84
	v_add_f32_e32 v86, 1.0, v86
	v_add_f32_e32 v82, 1.0, v82
	v_add_f32_e32 v83, 1.0, v83
	v_add_f32_e32 v84, 1.0, v84
	v_rcp_f32_e32 v86, v86
	v_rcp_f32_e32 v82, v82
	v_rcp_f32_e32 v83, v83
	v_rcp_f32_e32 v84, v84
	v_pk_add_f32 v[88:89], v[88:89], v[40:41]
	v_mul_f32_e32 v85, 0xbfb8aa3b, v85
	v_exp_f32_e32 v85, v85
	v_pk_add_f32 v[78:79], v[78:79], v[46:47]
	s_waitcnt vmcnt(0) lgkmcnt(0)
	v_lshlrev_b32_e32 v1, 16, v98
	v_lshlrev_b32_e32 v103, 16, v100
	v_and_b32_e32 v100, 0xffff0000, v100
	v_lshlrev_b32_e32 v104, 16, v101
	v_mul_f32_e32 v1, v86, v1
	v_mul_f32_e32 v86, v82, v103
	v_mul_f32_e32 v82, 0xbfb8aa3b, v87
	v_mul_f32_e32 v87, v83, v100
	v_mul_f32_e32 v83, 0xbfb8aa3b, v88
	v_mul_f32_e32 v88, v84, v104
	v_mul_f32_e32 v84, 0xbfb8aa3b, v89
	v_exp_f32_e32 v82, v82
	v_exp_f32_e32 v83, v83
	v_exp_f32_e32 v84, v84
	v_add_f32_e32 v85, 1.0, v85
	v_add_f32_e32 v82, 1.0, v82
	v_add_f32_e32 v83, 1.0, v83
	v_add_f32_e32 v84, 1.0, v84
	v_rcp_f32_e32 v82, v82
	v_rcp_f32_e32 v83, v83
	v_rcp_f32_e32 v84, v84
	v_rcp_f32_e32 v85, v85
	v_and_b32_e32 v98, 0xffff0000, v98
	v_lshlrev_b32_e32 v102, 16, v99
	v_and_b32_e32 v99, 0xffff0000, v99
	v_and_b32_e32 v101, 0xffff0000, v101
	v_mul_f32_e32 v82, v82, v98
	v_mul_f32_e32 v83, v83, v102
	v_mul_f32_e32 v84, v84, v99
	v_mul_f32_e32 v85, v85, v101
	v_cvt_pk_bf16_f32 v82, v1, v82
	v_cvt_pk_bf16_f32 v83, v83, v84
	v_cvt_pk_bf16_f32 v84, v86, v87
	v_cvt_pk_bf16_f32 v85, v88, v85
	global_store_dwordx4 v[90:91], v[82:85], off offset:256
	global_load_dwordx4 v[82:85], v[96:97], off offset:256
	v_pk_add_f32 v[76:77], v[76:77], v[44:45]
	v_mul_f32_e32 v78, 0xbfb8aa3b, v78
	v_mul_f32_e32 v76, 0xbfb8aa3b, v76
	v_exp_f32_e32 v78, v78
	v_exp_f32_e32 v76, v76
	v_pk_add_f32 v[80:81], v[80:81], v[48:49]
	v_pk_add_f32 v[74:75], v[74:75], v[42:43]
	v_add_f32_e32 v78, 1.0, v78
	v_add_f32_e32 v76, 1.0, v76
	v_rcp_f32_e32 v78, v78
	v_rcp_f32_e32 v76, v76
	v_mul_f32_e32 v74, 0xbfb8aa3b, v74
	v_mul_f32_e32 v75, 0xbfb8aa3b, v75
	v_exp_f32_e32 v74, v74
	v_exp_f32_e32 v75, v75
	s_add_u32 s1, s3, s38
	s_addc_u32 s2, s14, s39
	v_add_f32_e32 v74, 1.0, v74
	v_add_f32_e32 v75, 1.0, v75
	v_lshlrev_b32_e32 v1, 16, v92
	v_lshlrev_b32_e32 v91, 16, v95
	v_mul_f32_e32 v1, v78, v1
	v_mul_f32_e32 v78, 0xbfb8aa3b, v79
	v_mul_f32_e32 v79, 0xbfb8aa3b, v80
	v_mul_f32_e32 v80, v76, v91
	v_mul_f32_e32 v76, 0xbfb8aa3b, v81
	v_exp_f32_e32 v76, v76
	v_and_b32_e32 v88, 0xffff0000, v93
	v_exp_f32_e32 v78, v78
	v_exp_f32_e32 v79, v79
	v_add_f32_e32 v76, 1.0, v76
	v_rcp_f32_e32 v76, v76
	v_add_f32_e32 v78, 1.0, v78
	v_rcp_f32_e32 v74, v74
	v_rcp_f32_e32 v78, v78
	v_mul_f32_e32 v81, v76, v88
	v_mul_f32_e32 v76, 0xbfb8aa3b, v77
	v_exp_f32_e32 v76, v76
	v_rcp_f32_e32 v75, v75
	v_add_f32_e32 v79, 1.0, v79
	v_rcp_f32_e32 v79, v79
	v_add_f32_e32 v76, 1.0, v76
	v_rcp_f32_e32 v76, v76
	v_and_b32_e32 v86, 0xffff0000, v92
	v_lshlrev_b32_e32 v89, 16, v94
	v_and_b32_e32 v90, 0xffff0000, v94
	s_add_u32 s16, s1, s15
	v_lshlrev_b32_e32 v87, 16, v93
	v_and_b32_e32 v92, 0xffff0000, v95
	v_mul_f32_e32 v74, v74, v89
	v_mul_f32_e32 v78, v78, v86
	v_mul_f32_e32 v75, v75, v90
	s_addc_u32 s17, s2, 0
	v_mul_f32_e32 v79, v79, v87
	v_mul_f32_e32 v86, v76, v92
	v_cvt_pk_bf16_f32 v76, v1, v78
	v_cvt_pk_bf16_f32 v77, v79, v81
	v_cvt_pk_bf16_f32 v78, v74, v75
	v_lshl_add_u64 v[74:75], s[16:17], 0, v[186:187]
	s_add_i32 s16, s0, 0x90
	s_ashr_i32 s17, s16, 31
	s_lshl_b64 s[38:39], s[16:17], 9
	s_add_u32 s1, s12, s38
	s_addc_u32 s2, s13, s39
	s_add_u32 s16, s1, s15
	v_cvt_pk_bf16_f32 v79, v80, v86
	global_store_dwordx4 v[74:75], v[76:79], off
	s_addc_u32 s17, s2, 0
	v_lshl_add_u64 v[80:81], s[16:17], 0, v[186:187]
	global_load_dwordx4 v[76:79], v[80:81], off
	v_pk_add_f32 v[70:71], v[70:71], v[38:39]
	v_pk_add_f32 v[68:69], v[68:69], v[36:37]
	v_pk_add_f32 v[66:67], v[66:67], v[34:35]
	v_mul_f32_e32 v70, 0xbfb8aa3b, v70
	v_mul_f32_e32 v66, 0xbfb8aa3b, v66
	v_mul_f32_e32 v67, 0xbfb8aa3b, v67
	v_mul_f32_e32 v68, 0xbfb8aa3b, v68
	v_exp_f32_e32 v70, v70
	v_exp_f32_e32 v66, v66
	v_exp_f32_e32 v67, v67
	v_exp_f32_e32 v68, v68
	v_add_f32_e32 v70, 1.0, v70
	v_add_f32_e32 v66, 1.0, v66
	v_add_f32_e32 v67, 1.0, v67
	v_add_f32_e32 v68, 1.0, v68
	v_rcp_f32_e32 v70, v70
	v_rcp_f32_e32 v66, v66
	v_rcp_f32_e32 v67, v67
	v_rcp_f32_e32 v68, v68
	s_waitcnt vmcnt(0) lgkmcnt(0)
	v_lshlrev_b32_e32 v1, 16, v82
	v_lshlrev_b32_e32 v87, 16, v84
	v_and_b32_e32 v84, 0xffff0000, v84
	v_lshlrev_b32_e32 v88, 16, v85
	v_pk_add_f32 v[72:73], v[72:73], v[40:41]
	v_mul_f32_e32 v1, v70, v1
	v_mul_f32_e32 v70, v66, v87
	v_mul_f32_e32 v66, 0xbfb8aa3b, v71
	v_mul_f32_e32 v71, v67, v84
	v_mul_f32_e32 v67, 0xbfb8aa3b, v72
	v_mul_f32_e32 v72, v68, v88
	v_mul_f32_e32 v68, 0xbfb8aa3b, v73
	v_mul_f32_e32 v69, 0xbfb8aa3b, v69
	v_exp_f32_e32 v66, v66
	v_exp_f32_e32 v67, v67
	v_exp_f32_e32 v68, v68
	v_exp_f32_e32 v69, v69
	v_add_f32_e32 v66, 1.0, v66
	v_add_f32_e32 v67, 1.0, v67
	v_add_f32_e32 v68, 1.0, v68
	v_add_f32_e32 v69, 1.0, v69
	v_rcp_f32_e32 v66, v66
	v_rcp_f32_e32 v67, v67
	v_rcp_f32_e32 v68, v68
	v_rcp_f32_e32 v69, v69
	v_and_b32_e32 v82, 0xffff0000, v82
	v_lshlrev_b32_e32 v86, 16, v83
	v_and_b32_e32 v83, 0xffff0000, v83
	v_and_b32_e32 v85, 0xffff0000, v85
	v_mul_f32_e32 v66, v66, v82
	v_mul_f32_e32 v67, v67, v86
	v_mul_f32_e32 v68, v68, v83
	v_mul_f32_e32 v69, v69, v85
	v_cvt_pk_bf16_f32 v66, v1, v66
	v_cvt_pk_bf16_f32 v67, v67, v68
	v_cvt_pk_bf16_f32 v68, v70, v71
	v_cvt_pk_bf16_f32 v69, v72, v69
	global_store_dwordx4 v[74:75], v[66:69], off offset:256
	global_load_dwordx4 v[66:69], v[80:81], off offset:256
	v_pk_add_f32 v[62:63], v[62:63], v[46:47]
	v_pk_add_f32 v[60:61], v[60:61], v[44:45]
	v_mul_f32_e32 v62, 0xbfb8aa3b, v62
	v_mul_f32_e32 v60, 0xbfb8aa3b, v60
	v_exp_f32_e32 v62, v62
	v_exp_f32_e32 v60, v60
	v_pk_add_f32 v[64:65], v[64:65], v[48:49]
	v_pk_add_f32 v[58:59], v[58:59], v[42:43]
	v_add_f32_e32 v62, 1.0, v62
	v_add_f32_e32 v60, 1.0, v60
	v_rcp_f32_e32 v62, v62
	v_rcp_f32_e32 v60, v60
	v_mul_f32_e32 v58, 0xbfb8aa3b, v58
	v_mul_f32_e32 v59, 0xbfb8aa3b, v59
	v_exp_f32_e32 v58, v58
	v_exp_f32_e32 v59, v59
	s_add_u32 s1, s3, s38
	s_addc_u32 s2, s14, s39
	v_add_f32_e32 v58, 1.0, v58
	v_add_f32_e32 v59, 1.0, v59
	v_lshlrev_b32_e32 v1, 16, v76
	v_lshlrev_b32_e32 v75, 16, v79
	v_mul_f32_e32 v1, v62, v1
	v_mul_f32_e32 v62, 0xbfb8aa3b, v63
	v_mul_f32_e32 v63, 0xbfb8aa3b, v64
	v_mul_f32_e32 v64, v60, v75
	v_mul_f32_e32 v60, 0xbfb8aa3b, v65
	v_exp_f32_e32 v60, v60
	v_and_b32_e32 v72, 0xffff0000, v77
	v_exp_f32_e32 v62, v62
	v_exp_f32_e32 v63, v63
	v_add_f32_e32 v60, 1.0, v60
	v_rcp_f32_e32 v60, v60
	v_add_f32_e32 v62, 1.0, v62
	v_rcp_f32_e32 v58, v58
	v_rcp_f32_e32 v62, v62
	v_mul_f32_e32 v65, v60, v72
	v_mul_f32_e32 v60, 0xbfb8aa3b, v61
	v_exp_f32_e32 v60, v60
	v_rcp_f32_e32 v59, v59
	v_add_f32_e32 v63, 1.0, v63
	v_rcp_f32_e32 v63, v63
	v_add_f32_e32 v60, 1.0, v60
	v_rcp_f32_e32 v60, v60
	v_and_b32_e32 v70, 0xffff0000, v76
	v_lshlrev_b32_e32 v73, 16, v78
	v_and_b32_e32 v74, 0xffff0000, v78
	s_add_u32 s16, s1, s15
	v_lshlrev_b32_e32 v71, 16, v77
	v_and_b32_e32 v76, 0xffff0000, v79
	v_mul_f32_e32 v58, v58, v73
	v_mul_f32_e32 v62, v62, v70
	v_mul_f32_e32 v59, v59, v74
	s_addc_u32 s17, s2, 0
	v_mul_f32_e32 v63, v63, v71
	v_mul_f32_e32 v70, v60, v76
	v_cvt_pk_bf16_f32 v60, v1, v62
	v_cvt_pk_bf16_f32 v61, v63, v65
	v_cvt_pk_bf16_f32 v62, v58, v59
	v_lshl_add_u64 v[58:59], s[16:17], 0, v[186:187]
	s_add_i32 s16, s0, 0xa0
	s_ashr_i32 s17, s16, 31
	s_lshl_b64 s[38:39], s[16:17], 9
	s_add_u32 s1, s12, s38
	s_addc_u32 s2, s13, s39
	s_add_u32 s16, s1, s15
	v_cvt_pk_bf16_f32 v63, v64, v70
	global_store_dwordx4 v[58:59], v[60:63], off
	s_addc_u32 s17, s2, 0
	v_pk_add_f32 v[54:55], v[54:55], v[38:39]
	v_lshl_add_u64 v[60:61], s[16:17], 0, v[186:187]
	v_pk_add_f32 v[52:53], v[52:53], v[36:37]
	v_pk_add_f32 v[50:51], v[50:51], v[34:35]
	global_load_dwordx4 v[62:65], v[60:61], off
	v_mul_f32_e32 v54, 0xbfb8aa3b, v54
	v_mul_f32_e32 v50, 0xbfb8aa3b, v50
	v_mul_f32_e32 v51, 0xbfb8aa3b, v51
	v_mul_f32_e32 v52, 0xbfb8aa3b, v52
	v_exp_f32_e32 v54, v54
	v_exp_f32_e32 v50, v50
	v_exp_f32_e32 v51, v51
	v_exp_f32_e32 v52, v52
	v_add_f32_e32 v54, 1.0, v54
	v_add_f32_e32 v50, 1.0, v50
	v_add_f32_e32 v51, 1.0, v51
	v_add_f32_e32 v52, 1.0, v52
	v_rcp_f32_e32 v54, v54
	v_rcp_f32_e32 v50, v50
	v_rcp_f32_e32 v51, v51
	v_rcp_f32_e32 v52, v52
	s_waitcnt vmcnt(0) lgkmcnt(0)
	v_lshlrev_b32_e32 v1, 16, v66
	v_lshlrev_b32_e32 v71, 16, v68
	v_and_b32_e32 v68, 0xffff0000, v68
	v_lshlrev_b32_e32 v72, 16, v69
	v_pk_add_f32 v[56:57], v[56:57], v[40:41]
	v_mul_f32_e32 v1, v54, v1
	v_mul_f32_e32 v54, v50, v71
	v_mul_f32_e32 v50, 0xbfb8aa3b, v55
	v_mul_f32_e32 v55, v51, v68
	v_mul_f32_e32 v51, 0xbfb8aa3b, v56
	v_mul_f32_e32 v56, v52, v72
	v_mul_f32_e32 v52, 0xbfb8aa3b, v57
	v_mul_f32_e32 v53, 0xbfb8aa3b, v53
	v_exp_f32_e32 v50, v50
	v_exp_f32_e32 v51, v51
	v_exp_f32_e32 v52, v52
	v_exp_f32_e32 v53, v53
	v_add_f32_e32 v50, 1.0, v50
	v_add_f32_e32 v51, 1.0, v51
	v_add_f32_e32 v52, 1.0, v52
	v_add_f32_e32 v53, 1.0, v53
	v_rcp_f32_e32 v50, v50
	v_rcp_f32_e32 v51, v51
	v_rcp_f32_e32 v52, v52
	v_rcp_f32_e32 v53, v53
	v_and_b32_e32 v66, 0xffff0000, v66
	v_lshlrev_b32_e32 v70, 16, v67
	v_and_b32_e32 v67, 0xffff0000, v67
	v_and_b32_e32 v69, 0xffff0000, v69
	v_mul_f32_e32 v50, v50, v66
	v_mul_f32_e32 v51, v51, v70
	v_mul_f32_e32 v52, v52, v67
	v_mul_f32_e32 v53, v53, v69
	v_cvt_pk_bf16_f32 v50, v1, v50
	v_cvt_pk_bf16_f32 v51, v51, v52
	v_cvt_pk_bf16_f32 v52, v54, v55
	v_cvt_pk_bf16_f32 v53, v56, v53
	global_store_dwordx4 v[58:59], v[50:53], off offset:256
	global_load_dwordx4 v[50:53], v[60:61], off offset:256
	v_pk_add_f32 v[30:31], v[30:31], v[46:47]
	v_pk_add_f32 v[28:29], v[28:29], v[44:45]
	v_mul_f32_e32 v30, 0xbfb8aa3b, v30
	v_mul_f32_e32 v28, 0xbfb8aa3b, v28
	v_exp_f32_e32 v30, v30
	v_exp_f32_e32 v28, v28
	v_pk_add_f32 v[32:33], v[32:33], v[48:49]
	v_pk_add_f32 v[26:27], v[26:27], v[42:43]
	v_add_f32_e32 v30, 1.0, v30
	v_add_f32_e32 v28, 1.0, v28
	v_rcp_f32_e32 v30, v30
	v_rcp_f32_e32 v28, v28
	v_mul_f32_e32 v26, 0xbfb8aa3b, v26
	v_mul_f32_e32 v27, 0xbfb8aa3b, v27
	v_exp_f32_e32 v26, v26
	v_exp_f32_e32 v27, v27
	s_add_u32 s1, s3, s38
	v_pk_add_f32 v[22:23], v[22:23], v[38:39]
	v_pk_add_f32 v[20:21], v[20:21], v[36:37]
	v_pk_add_f32 v[18:19], v[18:19], v[34:35]
	s_addc_u32 s2, s14, s39
	v_mul_f32_e32 v22, 0xbfb8aa3b, v22
	v_mul_f32_e32 v18, 0xbfb8aa3b, v18
	v_lshlrev_b32_e32 v1, 16, v62
	v_lshlrev_b32_e32 v59, 16, v65
	v_mul_f32_e32 v1, v30, v1
	v_mul_f32_e32 v30, 0xbfb8aa3b, v31
	v_mul_f32_e32 v31, 0xbfb8aa3b, v32
	v_mul_f32_e32 v32, v28, v59
	v_mul_f32_e32 v28, 0xbfb8aa3b, v33
	v_exp_f32_e32 v28, v28
	v_and_b32_e32 v56, 0xffff0000, v63
	v_exp_f32_e32 v30, v30
	v_exp_f32_e32 v31, v31
	v_add_f32_e32 v28, 1.0, v28
	v_rcp_f32_e32 v28, v28
	v_mul_f32_e32 v19, 0xbfb8aa3b, v19
	v_mul_f32_e32 v20, 0xbfb8aa3b, v20
	v_add_f32_e32 v26, 1.0, v26
	v_mul_f32_e32 v33, v28, v56
	v_mul_f32_e32 v28, 0xbfb8aa3b, v29
	v_exp_f32_e32 v28, v28
	v_add_f32_e32 v30, 1.0, v30
	v_add_f32_e32 v27, 1.0, v27
	s_add_u32 s16, s1, s15
	v_exp_f32_e32 v22, v22
	v_exp_f32_e32 v18, v18
	v_exp_f32_e32 v19, v19
	v_exp_f32_e32 v20, v20
	v_rcp_f32_e32 v26, v26
	v_rcp_f32_e32 v30, v30
	v_rcp_f32_e32 v27, v27
	v_add_f32_e32 v31, 1.0, v31
	v_add_f32_e32 v28, 1.0, v28
	s_addc_u32 s17, s2, 0
	s_addk_i32 s0, 0xb0
	v_rcp_f32_e32 v31, v31
	v_rcp_f32_e32 v28, v28
	s_ashr_i32 s1, s0, 31
	s_lshl_b64 s[0:1], s[0:1], 9
	v_and_b32_e32 v54, 0xffff0000, v62
	v_lshlrev_b32_e32 v57, 16, v64
	v_and_b32_e32 v58, 0xffff0000, v64
	s_add_u32 s2, s12, s0
	v_add_f32_e32 v22, 1.0, v22
	v_add_f32_e32 v18, 1.0, v18
	v_add_f32_e32 v19, 1.0, v19
	v_add_f32_e32 v20, 1.0, v20
	v_lshlrev_b32_e32 v55, 16, v63
	v_and_b32_e32 v62, 0xffff0000, v65
	v_mul_f32_e32 v26, v26, v57
	v_mul_f32_e32 v30, v30, v54
	v_mul_f32_e32 v27, v27, v58
	s_addc_u32 s13, s13, s1
	v_rcp_f32_e32 v22, v22
	v_rcp_f32_e32 v18, v18
	v_rcp_f32_e32 v19, v19
	v_rcp_f32_e32 v20, v20
	v_mul_f32_e32 v31, v31, v55
	v_mul_f32_e32 v54, v28, v62
	v_cvt_pk_bf16_f32 v28, v1, v30
	v_cvt_pk_bf16_f32 v29, v31, v33
	v_cvt_pk_bf16_f32 v30, v26, v27
	v_lshl_add_u64 v[26:27], s[16:17], 0, v[186:187]
	s_add_u32 s12, s2, s15
	v_cvt_pk_bf16_f32 v31, v32, v54
	global_store_dwordx4 v[26:27], v[28:31], off
	s_addc_u32 s13, s13, 0
	s_waitcnt vmcnt(0) lgkmcnt(0)
	v_lshlrev_b32_e32 v1, 16, v50
	v_lshlrev_b32_e32 v55, 16, v52
	v_and_b32_e32 v52, 0xffff0000, v52
	v_lshlrev_b32_e32 v56, 16, v53
	v_lshl_add_u64 v[28:29], s[12:13], 0, v[186:187]
	v_pk_add_f32 v[24:25], v[24:25], v[40:41]
	global_load_dwordx4 v[30:33], v[28:29], off
	v_mul_f32_e32 v1, v22, v1
	v_mul_f32_e32 v22, v18, v55
	v_mul_f32_e32 v18, 0xbfb8aa3b, v23
	v_mul_f32_e32 v23, v19, v52
	v_mul_f32_e32 v19, 0xbfb8aa3b, v24
	v_mul_f32_e32 v24, v20, v56
	v_mul_f32_e32 v20, 0xbfb8aa3b, v25
	v_mul_f32_e32 v21, 0xbfb8aa3b, v21
	v_exp_f32_e32 v18, v18
	v_exp_f32_e32 v19, v19
	v_exp_f32_e32 v20, v20
	v_exp_f32_e32 v21, v21
	v_add_f32_e32 v18, 1.0, v18
	v_add_f32_e32 v19, 1.0, v19
	v_add_f32_e32 v20, 1.0, v20
	v_add_f32_e32 v21, 1.0, v21
	v_rcp_f32_e32 v18, v18
	v_rcp_f32_e32 v19, v19
	v_rcp_f32_e32 v20, v20
	v_rcp_f32_e32 v21, v21
	v_and_b32_e32 v50, 0xffff0000, v50
	v_lshlrev_b32_e32 v54, 16, v51
	v_and_b32_e32 v51, 0xffff0000, v51
	v_and_b32_e32 v53, 0xffff0000, v53
	v_mul_f32_e32 v18, v18, v50
	v_mul_f32_e32 v19, v19, v54
	v_mul_f32_e32 v20, v20, v51
	v_mul_f32_e32 v21, v21, v53
	v_cvt_pk_bf16_f32 v18, v1, v18
	v_cvt_pk_bf16_f32 v19, v19, v20
	v_cvt_pk_bf16_f32 v20, v22, v23
	v_cvt_pk_bf16_f32 v21, v24, v21
	global_store_dwordx4 v[26:27], v[18:21], off offset:256
	global_load_dwordx4 v[18:21], v[28:29], off offset:256
	v_pk_add_f32 v[14:15], v[14:15], v[46:47]
	v_pk_add_f32 v[12:13], v[12:13], v[44:45]
	v_pk_add_f32 v[10:11], v[10:11], v[42:43]
	v_mul_f32_e32 v14, 0xbfb8aa3b, v14
	v_mul_f32_e32 v10, 0xbfb8aa3b, v10
	v_mul_f32_e32 v11, 0xbfb8aa3b, v11
	v_mul_f32_e32 v12, 0xbfb8aa3b, v12
	v_exp_f32_e32 v14, v14
	v_exp_f32_e32 v10, v10
	v_exp_f32_e32 v11, v11
	v_exp_f32_e32 v12, v12
	v_add_f32_e32 v14, 1.0, v14
	v_add_f32_e32 v10, 1.0, v10
	v_add_f32_e32 v11, 1.0, v11
	v_add_f32_e32 v12, 1.0, v12
	v_rcp_f32_e32 v14, v14
	v_rcp_f32_e32 v10, v10
	v_rcp_f32_e32 v11, v11
	v_rcp_f32_e32 v12, v12
	v_pk_add_f32 v[16:17], v[16:17], v[48:49]
	v_mul_f32_e32 v13, 0xbfb8aa3b, v13
	v_exp_f32_e32 v13, v13
	v_pk_add_f32 v[4:5], v[4:5], v[36:37]
	v_pk_add_f32 v[2:3], v[2:3], v[34:35]
	v_mul_f32_e32 v4, 0xbfb8aa3b, v4
	v_mul_f32_e32 v2, 0xbfb8aa3b, v2
	v_mul_f32_e32 v3, 0xbfb8aa3b, v3
	v_exp_f32_e32 v2, v2
	v_exp_f32_e32 v3, v3
	v_exp_f32_e32 v4, v4
	v_add_f32_e32 v13, 1.0, v13
	v_rcp_f32_e32 v13, v13
	s_add_u32 s0, s3, s0
	s_addc_u32 s1, s14, s1
	v_add_f32_e32 v2, 1.0, v2
	v_add_f32_e32 v3, 1.0, v3
	v_add_f32_e32 v4, 1.0, v4
	s_add_u32 s0, s0, s15
	v_rcp_f32_e32 v2, v2
	v_rcp_f32_e32 v3, v3
	v_rcp_f32_e32 v4, v4
	s_addc_u32 s1, s1, 0
	v_pk_add_f32 v[8:9], v[8:9], v[40:41]
	v_pk_add_f32 v[6:7], v[6:7], v[38:39]
	s_waitcnt vmcnt(0) lgkmcnt(0)
	v_lshlrev_b32_e32 v1, 16, v30
	v_lshlrev_b32_e32 v25, 16, v32
	v_and_b32_e32 v26, 0xffff0000, v32
	v_lshlrev_b32_e32 v27, 16, v33
	v_mul_f32_e32 v1, v14, v1
	v_mul_f32_e32 v14, v10, v25
	v_mul_f32_e32 v10, 0xbfb8aa3b, v15
	v_mul_f32_e32 v15, v11, v26
	v_mul_f32_e32 v11, 0xbfb8aa3b, v16
	v_mul_f32_e32 v16, v12, v27
	v_mul_f32_e32 v12, 0xbfb8aa3b, v17
	v_exp_f32_e32 v10, v10
	v_exp_f32_e32 v11, v11
	v_exp_f32_e32 v12, v12
	v_and_b32_e32 v22, 0xffff0000, v30
	v_add_f32_e32 v10, 1.0, v10
	v_add_f32_e32 v11, 1.0, v11
	v_add_f32_e32 v12, 1.0, v12
	v_rcp_f32_e32 v10, v10
	v_rcp_f32_e32 v11, v11
	v_rcp_f32_e32 v12, v12
	v_lshlrev_b32_e32 v23, 16, v31
	v_and_b32_e32 v24, 0xffff0000, v31
	v_and_b32_e32 v30, 0xffff0000, v33
	v_mul_f32_e32 v10, v10, v22
	v_mul_f32_e32 v11, v11, v23
	v_mul_f32_e32 v12, v12, v24
	v_mul_f32_e32 v13, v13, v30
	v_cvt_pk_bf16_f32 v10, v1, v10
	v_cvt_pk_bf16_f32 v11, v11, v12
	v_cvt_pk_bf16_f32 v12, v14, v15
	v_lshl_add_u64 v[14:15], s[0:1], 0, v[186:187]
	v_cvt_pk_bf16_f32 v13, v16, v13
	global_store_dwordx4 v[14:15], v[10:13], off
	v_mul_f32_e32 v5, 0xbfb8aa3b, v5
	v_lshlrev_b32_e32 v1, 16, v20
	v_and_b32_e32 v10, 0xffff0000, v20
	v_lshlrev_b32_e32 v11, 16, v21
	v_mul_f32_e32 v1, v2, v1
	v_mul_f32_e32 v2, 0xbfb8aa3b, v7
	v_mul_f32_e32 v7, v3, v10
	v_mul_f32_e32 v3, 0xbfb8aa3b, v8
	v_mul_f32_e32 v8, v4, v11
	v_mul_f32_e32 v4, 0xbfb8aa3b, v9
	v_mul_f32_e32 v6, 0xbfb8aa3b, v6
	v_exp_f32_e32 v2, v2
	v_exp_f32_e32 v3, v3
	v_exp_f32_e32 v4, v4
	v_exp_f32_e32 v5, v5
	v_exp_f32_e32 v6, v6
	v_add_f32_e32 v2, 1.0, v2
	v_add_f32_e32 v3, 1.0, v3
	v_add_f32_e32 v4, 1.0, v4
	v_add_f32_e32 v5, 1.0, v5
	v_add_f32_e32 v6, 1.0, v6
	v_rcp_f32_e32 v2, v2
	v_rcp_f32_e32 v3, v3
	v_rcp_f32_e32 v4, v4
	v_rcp_f32_e32 v5, v5
	v_rcp_f32_e32 v6, v6
	v_and_b32_e32 v12, 0xffff0000, v21
	v_lshlrev_b32_e32 v13, 16, v18
	v_and_b32_e32 v16, 0xffff0000, v18
	v_lshlrev_b32_e32 v17, 16, v19
	v_and_b32_e32 v18, 0xffff0000, v19
	v_mul_f32_e32 v2, v2, v16
	v_mul_f32_e32 v3, v3, v17
	v_mul_f32_e32 v4, v4, v18
	v_mul_f32_e32 v5, v5, v12
	v_mul_f32_e32 v6, v6, v13
	v_cvt_pk_bf16_f32 v2, v6, v2
	v_cvt_pk_bf16_f32 v3, v3, v4
	v_cvt_pk_bf16_f32 v4, v1, v7
	v_cvt_pk_bf16_f32 v5, v8, v5
	global_store_dwordx4 v[14:15], v[2:5], off offset:256
	s_waitcnt vmcnt(0)
	s_barrier
	s_waitcnt lgkmcnt(0)
	s_barrier

.LBB0_651:
	s_or_b64 exec, exec, s[0:1]
	s_waitcnt lgkmcnt(0)
	ds_read_b128 v[34:37], v192 offset:53376
	ds_read_b128 v[38:41], v192 offset:53408
	s_add_u32 s0, s58, s42
	s_addc_u32 s1, s59, s43
	s_lshl_b32 s2, s3, 12
	s_waitcnt lgkmcnt(1)
	v_rcp_f32_e32 v42, v34
	v_rcp_f32_e32 v43, v35
	s_add_i32 s2, s2, 0
	v_lshlrev_b32_e32 v50, 1, v184
	v_lshlrev_b32_e32 v51, 9, v183
	v_mul_f32_e32 v2, v2, v42
	v_add3_u32 v50, s2, v50, v51
	v_cvt_pk_bf16_f32 v2, v2, s0
	v_rcp_f32_e32 v44, v36
	v_rcp_f32_e32 v45, v37
	s_waitcnt lgkmcnt(0)
	v_rcp_f32_e32 v46, v38
	ds_read_b128 v[34:37], v192 offset:53440
	v_rcp_f32_e32 v47, v39
	v_rcp_f32_e32 v48, v40
	v_rcp_f32_e32 v49, v41
	ds_read_b128 v[38:41], v192 offset:53472
	ds_write_b16 v50, v2 offset:55360
	v_mul_f32_e32 v2, v19, v43
	v_cvt_pk_bf16_f32 v2, v2, s0
	ds_write_b16 v50, v2 offset:55424
	v_mul_f32_e32 v2, v3, v43
	v_cvt_pk_bf16_f32 v2, v2, s0
	ds_write_b16 v50, v2 offset:55488
	v_mul_f32_e32 v2, v20, v44
	v_cvt_pk_bf16_f32 v2, v2, s0
	ds_write_b16 v50, v2 offset:55552
	v_mul_f32_e32 v2, v4, v44
	v_cvt_pk_bf16_f32 v2, v2, s0
	ds_write_b16 v50, v2 offset:55616
	v_mul_f32_e32 v2, v21, v45
	v_cvt_pk_bf16_f32 v2, v2, s0
	ds_write_b16 v50, v2 offset:55680
	v_mul_f32_e32 v2, v5, v45
	v_cvt_pk_bf16_f32 v2, v2, s0
	ds_write_b16 v50, v2 offset:55744
	v_mul_f32_e32 v2, v22, v46
	v_cvt_pk_bf16_f32 v2, v2, s0
	ds_write_b16 v50, v2 offset:56320
	v_mul_f32_e32 v2, v6, v46
	v_cvt_pk_bf16_f32 v2, v2, s0
	ds_write_b16 v50, v2 offset:56384
	v_mul_f32_e32 v2, v23, v47
	v_cvt_pk_bf16_f32 v2, v2, s0
	ds_write_b16 v50, v2 offset:56448
	v_mul_f32_e32 v2, v7, v47
	v_cvt_pk_bf16_f32 v2, v2, s0
	ds_write_b16 v50, v2 offset:56512
	v_mul_f32_e32 v2, v24, v48
	v_cvt_pk_bf16_f32 v2, v2, s0
	ds_write_b16 v50, v2 offset:56576
	v_mul_f32_e32 v2, v8, v48
	v_cvt_pk_bf16_f32 v2, v2, s0
	s_waitcnt lgkmcnt(13)
	v_rcp_f32_e32 v34, v34
	ds_write_b16 v50, v2 offset:56640
	v_mul_f32_e32 v2, v25, v49
	v_cvt_pk_bf16_f32 v2, v2, s0
	ds_write_b16 v50, v2 offset:56704
	v_mul_f32_e32 v2, v9, v49
	v_cvt_pk_bf16_f32 v2, v2, s0
	v_rcp_f32_e32 v35, v35
	ds_write_b16 v50, v2 offset:56768
	v_mul_f32_e32 v2, v26, v34
	v_cvt_pk_bf16_f32 v2, v2, s0
	ds_write_b16 v50, v2 offset:57344
	v_mul_f32_e32 v2, v10, v34
	v_cvt_pk_bf16_f32 v2, v2, s0
	v_rcp_f32_e32 v36, v36
	ds_write_b16 v50, v2 offset:57408
	v_mul_f32_e32 v2, v27, v35
	v_cvt_pk_bf16_f32 v2, v2, s0
	ds_write_b16 v50, v2 offset:57472
	v_mul_f32_e32 v2, v11, v35
	v_cvt_pk_bf16_f32 v2, v2, s0
	v_rcp_f32_e32 v37, v37
	ds_write_b16 v50, v2 offset:57536
	v_mul_f32_e32 v2, v28, v36
	v_cvt_pk_bf16_f32 v2, v2, s0
	ds_write_b16 v50, v2 offset:57600
	v_mul_f32_e32 v2, v12, v36
	v_cvt_pk_bf16_f32 v2, v2, s0
	s_waitcnt lgkmcnt(14)
	v_rcp_f32_e32 v38, v38
	ds_write_b16 v50, v2 offset:57664
	v_mul_f32_e32 v2, v29, v37
	v_cvt_pk_bf16_f32 v2, v2, s0
	ds_write_b16 v50, v2 offset:57728
	v_mul_f32_e32 v2, v13, v37
	v_cvt_pk_bf16_f32 v2, v2, s0
	v_rcp_f32_e32 v39, v39
	ds_write_b16 v50, v2 offset:57792
	v_mul_f32_e32 v2, v30, v38
	v_cvt_pk_bf16_f32 v2, v2, s0
	ds_write_b16 v50, v2 offset:58368
	v_mul_f32_e32 v2, v14, v38
	v_cvt_pk_bf16_f32 v2, v2, s0
	v_rcp_f32_e32 v40, v40
	ds_write_b16 v50, v2 offset:58432
	v_mul_f32_e32 v2, v31, v39
	v_cvt_pk_bf16_f32 v2, v2, s0
	ds_write_b16 v50, v2 offset:58496
	v_mul_f32_e32 v2, v15, v39
	v_cvt_pk_bf16_f32 v2, v2, s0
	v_rcp_f32_e32 v41, v41
	ds_write_b16 v50, v2 offset:58560
	v_mul_f32_e32 v2, v32, v40
	v_cvt_pk_bf16_f32 v2, v2, s0
	ds_write_b16 v50, v2 offset:58624
	v_mul_f32_e32 v2, v16, v40
	v_cvt_pk_bf16_f32 v2, v2, s0
	ds_write_b16 v50, v2 offset:58688
	v_mul_f32_e32 v2, v33, v41
	v_cvt_pk_bf16_f32 v2, v2, s0
	ds_write_b16 v50, v2 offset:58752
	v_mul_f32_e32 v2, v17, v41
	v_mul_f32_e32 v18, v18, v42
	v_cvt_pk_bf16_f32 v2, v2, s0
	v_cvt_pk_bf16_f32 v18, v18, s0
	ds_write_b16 v50, v2 offset:58816
	v_lshrrev_b32_e32 v1, 3, v1
	v_lshlrev_b32_e32 v2, 1, v182
	ds_write_b16 v50, v18 offset:55296
	v_and_b32_e32 v186, 0x70, v2
	v_lshlrev_b32_e32 v2, 7, v1
	s_waitcnt lgkmcnt(0)
	v_add3_u32 v10, s2, v186, v2
	s_lshl_b32 s3, s25, 1
	ds_read_b128 v[2:5], v10 offset:55296
	s_add_u32 s0, s0, s3
	s_addc_u32 s1, s1, 0
	v_mul_u32_u24_e32 v1, 0x1400, v1
	v_lshl_add_u64 v[6:7], s[0:1], 0, v[186:187]
	v_lshlrev_b32_e32 v186, 1, v1
	v_lshl_add_u64 v[6:7], v[6:7], 0, v[186:187]
	s_waitcnt lgkmcnt(0)
	global_store_dwordx4 v[6:7], v[2:5], off
	ds_read_b128 v[2:5], v10 offset:56320
	s_mov_b32 s0, 0x14000
	v_add_co_u32_e32 v8, vcc, s0, v6
	s_mov_b64 s[0:1], 0
	s_nop 0
	v_addc_co_u32_e32 v9, vcc, 0, v7, vcc
	s_waitcnt lgkmcnt(0)
	global_store_dwordx4 v[8:9], v[2:5], off
	ds_read_b128 v[2:5], v10 offset:57344
	v_add_co_u32_e32 v8, vcc, 0x28000, v6
	s_nop 1
	v_addc_co_u32_e32 v9, vcc, 0, v7, vcc
	s_waitcnt lgkmcnt(0)
	global_store_dwordx4 v[8:9], v[2:5], off
	ds_read_b128 v[2:5], v10 offset:58368
	v_add_co_u32_e32 v6, vcc, 0x3c000, v6
	s_nop 1
	v_addc_co_u32_e32 v7, vcc, 0, v7, vcc
	s_waitcnt lgkmcnt(0)
	global_store_dwordx4 v[6:7], v[2:5], off
	s_waitcnt lgkmcnt(0)
	s_barrier

.LBB0_657:
	s_or_b64 exec, exec, s[0:1]
	s_waitcnt vmcnt(0) lgkmcnt(0)
	s_barrier
	s_waitcnt vmcnt(0)
	ds_read_b32 v1, v187 offset:240
	s_waitcnt lgkmcnt(0)
	s_barrier
	s_mov_b64 s[0:1], -1
	s_waitcnt lgkmcnt(0)
	v_readfirstlane_b32 s2, v1
	s_cmpk_gt_i32 s2, 0x7f
	s_cbranch_scc1 .LBB0_652
	s_lshl_b32 s0, s2, 5
	s_and_b32 s12, s0, 0xffffff00
	s_andn2_b32 s33, 7, s2
	s_sub_i32 s0, 0xf00, s12
	s_ashr_i32 s1, s0, 31
	s_lshl_b32 s2, s33, 14
	s_add_u32 s14, s60, s2
	s_addc_u32 s15, s61, 0
	s_lshl_b64 s[2:3], s[0:1], 2
	s_add_u32 s2, s14, s2
	s_addc_u32 s3, s15, s3
	v_mov_b32_e32 v66, v0
	v_mov_b64_e32 v[2:3], s[2:3]
	global_load_dword v1, v[2:3], off
	s_sub_i32 s68, 0x1000, s12
	v_readfirstlane_b32 s2, v66
	v_cmp_gt_i32_e32 vcc, s68, v66
	v_mov_b32_e32 v14, 0
	v_ashrrev_i32_e32 v67, 31, v66
	v_mov_b32_e32 v15, 0
	s_and_saveexec_b64 s[24:25], vcc
	s_cbranch_execz .LBB0_660
	v_lshl_add_u64 v[2:3], v[66:67], 2, s[14:15]
	global_load_dword v15, v[2:3], off
.LBB0_660:
	s_or_b64 exec, exec, s[24:25]
	v_add_u32_e32 v16, 0x200, v66
	v_cmp_gt_i32_e64 s[38:39], s68, v16
	s_and_saveexec_b64 s[24:25], s[38:39]
	s_cbranch_execz .LBB0_662
	v_lshl_add_u64 v[2:3], v[66:67], 2, s[14:15]
	global_load_dword v14, v[2:3], off offset:2048
.LBB0_662:
	s_or_b64 exec, exec, s[24:25]
	v_add_u32_e32 v2, 0x400, v66
	v_cmp_gt_i32_e64 s[40:41], s68, v2
	v_mov_b32_e32 v5, 0
	v_mov_b32_e32 v17, 0
	s_and_saveexec_b64 s[24:25], s[40:41]
	s_cbranch_execz .LBB0_664
	v_ashrrev_i32_e32 v3, 31, v2
	v_lshl_add_u64 v[6:7], v[2:3], 2, s[14:15]
	global_load_dword v17, v[6:7], off
.LBB0_664:
	s_or_b64 exec, exec, s[24:25]
	v_add_u32_e32 v4, 0x600, v66
	v_cmp_gt_i32_e64 s[42:43], s68, v4
	s_and_saveexec_b64 s[24:25], s[42:43]
	s_cbranch_execz .LBB0_666
	v_ashrrev_i32_e32 v5, 31, v4
	v_lshl_add_u64 v[6:7], v[4:5], 2, s[14:15]
	global_load_dword v5, v[6:7], off
.LBB0_666:
	s_or_b64 exec, exec, s[24:25]
	v_add_u32_e32 v6, 0x800, v66
	v_cmp_gt_i32_e64 s[44:45], s68, v6
	v_mov_b32_e32 v3, 0
	v_mov_b32_e32 v18, 0
	s_and_saveexec_b64 s[24:25], s[44:45]
	s_cbranch_execz .LBB0_668
	v_ashrrev_i32_e32 v7, 31, v6
	v_lshl_add_u64 v[8:9], v[6:7], 2, s[14:15]
	global_load_dword v18, v[8:9], off
.LBB0_668:
	s_or_b64 exec, exec, s[24:25]
	v_add_u32_e32 v8, 0xa00, v66
	v_cmp_gt_i32_e64 s[46:47], s68, v8
	s_and_saveexec_b64 s[24:25], s[46:47]
	s_cbranch_execz .LBB0_670
	v_ashrrev_i32_e32 v9, 31, v8
	v_lshl_add_u64 v[10:11], v[8:9], 2, s[14:15]
	global_load_dword v3, v[10:11], off
.LBB0_670:
	s_or_b64 exec, exec, s[24:25]
	v_add_u32_e32 v10, 0xc00, v66
	v_cmp_gt_i32_e64 s[48:49], s68, v10
	v_mov_b32_e32 v7, 0
	v_mov_b32_e32 v9, 0
	s_and_saveexec_b64 s[24:25], s[48:49]
	s_cbranch_execz .LBB0_672
	v_ashrrev_i32_e32 v11, 31, v10
	v_lshl_add_u64 v[12:13], v[10:11], 2, s[14:15]
	global_load_dword v9, v[12:13], off
.LBB0_672:
	s_or_b64 exec, exec, s[24:25]
	v_add_u32_e32 v12, 0xe00, v66
	v_cmp_gt_i32_e64 s[50:51], s68, v12
	s_and_saveexec_b64 s[24:25], s[50:51]
	s_cbranch_execz .LBB0_702
	v_ashrrev_i32_e32 v13, 31, v12
	v_lshl_add_u64 v[20:21], v[12:13], 2, s[14:15]
	global_load_dword v7, v[20:21], off
	s_or_b64 exec, exec, s[24:25]
	s_and_saveexec_b64 s[14:15], vcc
	s_cbranch_execnz .LBB0_703

.LBB0_684:
	s_or_b64 exec, exec, s[24:25]
	s_lshl_b32 s96, s33, 7
	s_add_u32 s12, s54, s96
	s_addc_u32 s13, s55, 0
	s_ashr_i32 s3, s2, 6
	s_lshl_b32 s17, s3, 5
	s_ashr_i32 s16, s17, 31
	s_add_u32 s0, s17, s0
	s_addc_u32 s1, s16, s1
	s_mulk_i32 s1, 0x1400
	s_mul_hi_u32 s16, s0, 0x1400
	s_add_i32 s1, s16, s1
	s_mulk_i32 s0, 0x1400
	s_lshl_b64 s[42:43], s[0:1], 1
	s_add_u32 s0, s28, s42
	s_addc_u32 s1, s29, s43
	s_add_u32 s24, s0, s96
	s_addc_u32 s25, s1, 0
	v_cndmask_b32_e64 v2, 0, 1, s[14:15]
	s_add_u32 s16, s56, s96
	v_cmp_ne_u32_e32 vcc, 0, v2
	s_addc_u32 s34, s57, 0
	s_bcnt1_i32_b64 s0, vcc
	s_and_b32 s0, s0, -2
	s_add_i32 s1, s46, -4
	s_min_i32 s50, s0, s1
	s_lshl_b32 s49, s50, 8
	s_mul_i32 s48, s50, 0xa0000
	s_mul_hi_i32 s47, s50, 0xa0000
	s_add_u32 s0, s12, s48
	s_addc_u32 s1, s13, s47
	v_mul_u32_u24_e32 v2, 0x1400, v1
	s_add_u32 s12, s16, s48
	v_lshlrev_b32_e32 v186, 1, v2
	s_addc_u32 s13, s34, s47
	v_lshl_add_u64 v[2:3], s[0:1], 0, v[186:187]
	s_lshl_b32 s0, s3, 3
	s_ashr_i32 s1, s0, 31
	v_lshl_add_u64 v[68:69], s[0:1], 1, v[2:3]
	s_lshl_b32 s14, s3, 4
	v_lshrrev_b32_e32 v2, 2, v1
	v_and_or_b32 v2, s14, 48, v2
	v_mul_u32_u24_e32 v2, 0x1400, v2
	v_lshlrev_b32_e32 v166, 1, v2
	v_mov_b32_e32 v167, v187
	v_lshl_add_u64 v[2:3], s[12:13], 0, v[166:167]
	s_ashr_i32 s12, s2, 3
	s_and_b32 s40, s12, 0xffffffe0
	s_ashr_i32 s41, s40, 31
	s_lshl_b32 s15, s3, 10
	s_add_i32 s12, 0, 0x1000
	v_lshlrev_b32_e32 v182, 3, v66
	s_cmp_lg_u32 s12, -1
	v_and_b32_e32 v185, 24, v182
	s_cselect_b32 s13, s12, 0
	v_lshl_add_u64 v[2:3], s[40:41], 1, v[2:3]
	v_lshlrev_b32_e32 v4, 1, v185
	v_mov_b32_e32 v5, v187
	s_add_i32 s13, s15, s13
	s_mov_b32 s14, m0
	s_mov_b32 m0, s13
	s_nop 0
	global_load_lds_dwordx4 v[68:69], off
	s_mov_b32 m0, s14
	s_mov_b64 s[34:35], 0xa0000
	v_lshrrev_b32_e32 v183, 5, v1
	v_and_b32_e32 v184, 31, v66
	v_lshl_add_u64 v[70:71], v[2:3], 0, v[4:5]
	s_add_i32 s16, s13, 0x6000
	s_mov_b32 s14, m0
	s_mov_b32 m0, s16
	s_nop 0
	global_load_lds_dwordx4 v[70:71], off
	s_mov_b32 m0, s14
	v_lshl_add_u64 v[2:3], v[68:69], 0, s[34:35]
	s_add_i32 s14, s13, 0x2000
	s_mov_b32 s34, m0
	s_mov_b32 m0, s14
	s_nop 0
	global_load_lds_dwordx4 v[2:3], off
	s_mov_b32 m0, s34
	v_mul_u32_u24_e32 v2, 0x1400, v184
	v_lshlrev_b32_e32 v4, 4, v183
	v_lshl_or_b32 v2, v2, 1, v4
	v_mov_b32_e32 v3, v187
	v_lshl_add_u64 v[2:3], s[24:25], 0, v[2:3]
	global_load_dwordx4 v[114:117], v[2:3], off
	global_load_dwordx4 v[106:109], v[2:3], off offset:32
	global_load_dwordx4 v[102:105], v[2:3], off offset:64
	global_load_dwordx4 v[98:101], v[2:3], off offset:96
	v_lshlrev_b32_e32 v2, 10, v183
	v_lshlrev_b32_e32 v3, 4, v184
	v_add3_u32 v200, 0, v2, v3
	v_lshl_add_u64 v[2:3], v[68:69], 0, s[62:63]
	s_add_i32 s14, s49, 0
	s_add_i32 s24, s13, 0x4000
	s_mov_b32 s25, m0
	s_mov_b32 m0, s24
	s_nop 0
	global_load_lds_dwordx4 v[2:3], off
	s_mov_b32 m0, s25
	v_add_u32_e32 v4, s14, v4
	s_waitcnt vmcnt(3) lgkmcnt(0)
	s_barrier
	v_add_u32_e32 v199, 0x15800, v4
	ds_read_b128 v[18:21], v200 offset:4096
	ds_read_b128 v[2:5], v199
	ds_read_b128 v[6:9], v199 offset:32
	ds_read_b128 v[10:13], v199 offset:64
	ds_read_b128 v[14:17], v199 offset:96
	ds_read_b128 v[34:37], v200 offset:4608
	v_or_b32_e32 v198, s17, v184
	s_sub_i32 s17, s46, s50
	v_lshlrev_b32_e32 v197, 2, v183
	s_cmp_gt_i32 s17, 4
	s_waitcnt vmcnt(0) lgkmcnt(0)
	v_mfma_f32_32x32x16_bf16 v[2:17], v[18:21], v[114:117], v[2:17]
	ds_read_b128 v[18:21], v199 offset:128
	ds_read_b128 v[22:25], v199 offset:160
	ds_read_b128 v[26:29], v199 offset:192
	ds_read_b128 v[30:33], v199 offset:224
	s_waitcnt lgkmcnt(0)
	v_mfma_f32_32x32x16_bf16 v[18:33], v[34:37], v[114:117], v[18:33]
	ds_read_b128 v[34:37], v200 offset:6144
	s_waitcnt lgkmcnt(0)
	v_mfma_f32_32x32x16_bf16 v[2:17], v[34:37], v[106:109], v[2:17]
	ds_read_b128 v[34:37], v200 offset:6656
	s_waitcnt lgkmcnt(0)
	v_mfma_f32_32x32x16_bf16 v[18:33], v[34:37], v[106:109], v[18:33]
	ds_read_b128 v[34:37], v200 offset:8192
	s_waitcnt lgkmcnt(0)
	v_mfma_f32_32x32x16_bf16 v[2:17], v[34:37], v[102:105], v[2:17]
	ds_read_b128 v[34:37], v200 offset:8704
	s_waitcnt lgkmcnt(0)
	v_mfma_f32_32x32x16_bf16 v[18:33], v[34:37], v[102:105], v[18:33]
	ds_read_b128 v[34:37], v200 offset:10240
	s_waitcnt lgkmcnt(0)
	v_mfma_f32_32x32x16_bf16 v[2:17], v[34:37], v[98:101], v[2:17]
	ds_read_b128 v[34:37], v200 offset:10752
	s_waitcnt lgkmcnt(0)
	v_mfma_f32_32x32x16_bf16 v[18:33], v[34:37], v[98:101], v[18:33]
	s_nop 15
	s_nop 7
	s_cbranch_scc1 .LBB0_686
	s_lshl_b32 s24, s17, 6
	v_subrev_u32_e32 v34, s24, v197
	v_add_u32_e32 v36, 0x120, v34
	v_add_u32_e32 v35, 0x100, v34
	v_cmp_le_i32_e32 vcc, v36, v198
	s_nop 5
	v_cndmask_b32_e32 v18, v236, v18, vcc
	v_cmp_lt_i32_e32 vcc, v35, v198
	s_nop 1
	v_cndmask_b32_e32 v3, v236, v3, vcc
	v_cmp_le_i32_e32 vcc, v35, v198
	v_add_u32_e32 v35, 0x121, v34
	s_nop 0
	v_cndmask_b32_e32 v2, v236, v2, vcc
	v_cmp_le_i32_e32 vcc, v35, v198
	v_add_u32_e32 v35, 0x102, v34
	s_nop 0
	v_cndmask_b32_e32 v19, v236, v19, vcc
	v_cmp_le_i32_e32 vcc, v35, v198
	v_add_u32_e32 v35, 0x122, v34
	s_nop 0
	v_cndmask_b32_e32 v4, v236, v4, vcc
	v_cmp_le_i32_e32 vcc, v35, v198
	v_add_u32_e32 v35, 0x103, v34
	s_nop 0
	v_cndmask_b32_e32 v20, v236, v20, vcc
	v_cmp_le_i32_e32 vcc, v35, v198
	v_add_u32_e32 v35, 0x123, v34
	s_nop 0
	v_cndmask_b32_e32 v5, v236, v5, vcc
	v_cmp_le_i32_e32 vcc, v35, v198
	v_add_u32_e32 v35, 0x108, v34
	s_nop 0
	v_cndmask_b32_e32 v21, v236, v21, vcc
	v_cmp_le_i32_e32 vcc, v35, v198
	v_add_u32_e32 v35, 0x128, v34
	s_nop 0
	v_cndmask_b32_e32 v6, v236, v6, vcc
	v_cmp_le_i32_e32 vcc, v35, v198
	v_add_u32_e32 v35, 0x109, v34
	s_nop 0
	v_cndmask_b32_e32 v22, v236, v22, vcc
	v_cmp_le_i32_e32 vcc, v35, v198
	v_add_u32_e32 v35, 0x129, v34
	s_nop 0
	v_cndmask_b32_e32 v7, v236, v7, vcc
	v_cmp_le_i32_e32 vcc, v35, v198
	v_add_u32_e32 v35, 0x10a, v34
	s_nop 0
	v_cndmask_b32_e32 v23, v236, v23, vcc
	v_cmp_le_i32_e32 vcc, v35, v198
	v_add_u32_e32 v35, 0x12a, v34
	s_nop 0
	v_cndmask_b32_e32 v8, v236, v8, vcc
	v_cmp_le_i32_e32 vcc, v35, v198
	v_add_u32_e32 v35, 0x10b, v34
	s_nop 0
	v_cndmask_b32_e32 v24, v236, v24, vcc
	v_cmp_le_i32_e32 vcc, v35, v198
	v_add_u32_e32 v35, 0x12b, v34
	s_nop 0
	v_cndmask_b32_e32 v9, v236, v9, vcc
	v_cmp_le_i32_e32 vcc, v35, v198
	v_add_u32_e32 v35, 0x110, v34
	s_nop 0
	v_cndmask_b32_e32 v25, v236, v25, vcc
	v_cmp_le_i32_e32 vcc, v35, v198
	v_add_u32_e32 v35, 0x130, v34
	s_nop 0
	v_cndmask_b32_e32 v10, v236, v10, vcc
	v_cmp_le_i32_e32 vcc, v35, v198
	v_add_u32_e32 v35, 0x111, v34
	s_nop 0
	v_cndmask_b32_e32 v26, v236, v26, vcc
	v_cmp_le_i32_e32 vcc, v35, v198
	v_add_u32_e32 v35, 0x131, v34
	s_nop 0
	v_cndmask_b32_e32 v11, v236, v11, vcc
	v_cmp_le_i32_e32 vcc, v35, v198
	v_add_u32_e32 v35, 0x112, v34
	s_nop 0
	v_cndmask_b32_e32 v27, v236, v27, vcc
	v_cmp_le_i32_e32 vcc, v35, v198
	v_add_u32_e32 v35, 0x132, v34
	s_nop 0
	v_cndmask_b32_e32 v12, v236, v12, vcc
	v_cmp_le_i32_e32 vcc, v35, v198
	v_add_u32_e32 v35, 0x113, v34
	s_nop 0
	v_cndmask_b32_e32 v28, v236, v28, vcc
	v_cmp_le_i32_e32 vcc, v35, v198
	v_add_u32_e32 v35, 0x133, v34
	s_nop 0
	v_cndmask_b32_e32 v13, v236, v13, vcc
	v_cmp_le_i32_e32 vcc, v35, v198
	v_add_u32_e32 v35, 0x118, v34
	s_nop 0
	v_cndmask_b32_e32 v29, v236, v29, vcc
	v_cmp_le_i32_e32 vcc, v35, v198
	v_add_u32_e32 v35, 0x138, v34
	s_nop 0
	v_cndmask_b32_e32 v14, v236, v14, vcc
	v_cmp_le_i32_e32 vcc, v35, v198
	v_add_u32_e32 v35, 0x119, v34
	s_nop 0
	v_cndmask_b32_e32 v30, v236, v30, vcc
	v_cmp_le_i32_e32 vcc, v35, v198
	v_add_u32_e32 v35, 0x139, v34
	s_nop 0
	v_cndmask_b32_e32 v15, v236, v15, vcc
	v_cmp_le_i32_e32 vcc, v35, v198
	v_add_u32_e32 v35, 0x11a, v34
	s_nop 0
	v_cndmask_b32_e32 v31, v236, v31, vcc
	v_cmp_le_i32_e32 vcc, v35, v198
	v_add_u32_e32 v35, 0x13a, v34
	s_nop 0
	v_cndmask_b32_e32 v16, v236, v16, vcc
	v_cmp_le_i32_e32 vcc, v35, v198
	v_add_u32_e32 v35, 0x11b, v34
	v_add_u32_e32 v34, 0x13b, v34
	v_cndmask_b32_e32 v32, v236, v32, vcc
	v_cmp_le_i32_e32 vcc, v35, v198
	s_nop 1
	v_cndmask_b32_e32 v17, v236, v17, vcc
	v_cmp_le_i32_e32 vcc, v34, v198
	s_nop 1
	v_cndmask_b32_e32 v33, v236, v33, vcc

.LBB0_770:
	v_readlane_b32 s40, v253, 6
	v_readlane_b32 s14, v253, 0
	v_readlane_b32 s42, v253, 8
	v_readlane_b32 s43, v253, 9
	v_readlane_b32 s15, v253, 1
	s_mov_b64 s[0:1], s[42:43]
	s_mov_b64 s[2:3], s[14:15]
	s_waitcnt vmcnt(0) lgkmcnt(0)
	s_barrier
	s_load_dwordx2 s[2:3], s[2:3], 0x18
	v_readlane_b32 s16, v253, 32
	v_readlane_b32 s17, v253, 33
	s_add_u32 s0, s0, 0x4d000000
	s_mov_b32 s17, s97
	s_addc_u32 s1, s1, 0
	s_lshl_b64 s[12:13], s[16:17], 16
	s_waitcnt lgkmcnt(0)
	s_add_u32 s12, s2, s12
	s_addc_u32 s13, s3, s13
	s_mov_b64 s[2:3], s[14:15]
	s_load_dwordx2 s[2:3], s[2:3], 0x20
	s_mov_b32 s14, s16
	v_readlane_b32 s41, v253, 7
	v_readlane_b32 s44, v253, 10
	v_readlane_b32 s45, v253, 11
	v_readlane_b32 s46, v253, 12
	v_readlane_b32 s47, v253, 13
	v_writelane_b32 v253, s14, 32
	s_mov_b64 s[48:49], s[42:43]
	v_mov_b32_e32 v6, v0
	v_writelane_b32 v253, s15, 33
	s_lshl_b64 s[14:15], s[16:17], 10
	s_waitcnt lgkmcnt(0)
	s_add_u32 s38, s2, s14
	s_mov_b32 s2, s84
	s_addc_u32 s39, s3, s15
	v_ashrrev_i32_e32 v1, 7, v6
	v_bfe_u32 v8, v6, 5, 1
	v_and_b32_e32 v7, 31, v6
	v_lshlrev_b32_e32 v2, 12, v1
	v_lshlrev_b32_e32 v3, 9, v8
	v_or3_b32 v2, v3, v2, v7
	v_ashrrev_i32_e32 v3, 31, v2
	v_lshl_add_u64 v[2:3], v[2:3], 2, s[12:13]
	global_load_dword v98, v[2:3], off
	global_load_dword v99, v[2:3], off offset:256
	s_movk_i32 s3, 0x1000
	v_ashrrev_i32_e32 v97, 5, v6
	s_movk_i32 s13, 0x9e0
	v_mov_b32_e32 v66, 0
	v_mov_b32_e32 v70, 0
	v_mov_b32_e32 v71, 0
	v_mov_b32_e32 v72, 0
	v_mov_b32_e32 v73, 0
	global_load_dword v100, v[2:3], off offset:512
	global_load_dword v101, v[2:3], off offset:768
	global_load_dword v102, v[2:3], off offset:1024
	global_load_dword v103, v[2:3], off offset:1280
	global_load_dword v104, v[2:3], off offset:1536
	global_load_dword v105, v[2:3], off offset:1792
	global_load_dword v106, v[2:3], off offset:128
	global_load_dword v107, v[2:3], off offset:384
	global_load_dword v108, v[2:3], off offset:640
	global_load_dword v109, v[2:3], off offset:896
	global_load_dword v110, v[2:3], off offset:1152
	global_load_dword v111, v[2:3], off offset:1408
	global_load_dword v112, v[2:3], off offset:1664
	global_load_dword v113, v[2:3], off offset:1920
	v_add_co_u32_e32 v4, vcc, s3, v2
	s_movk_i32 s3, 0x2000
	s_nop 0
	v_addc_co_u32_e32 v5, vcc, 0, v3, vcc
	v_add_co_u32_e32 v10, vcc, s3, v2
	s_movk_i32 s3, 0x3000
	s_nop 0
	v_addc_co_u32_e32 v11, vcc, 0, v3, vcc
	global_load_dword v114, v[10:11], off offset:-4096
	global_load_dword v115, v[4:5], off offset:256
	v_add_co_u32_e32 v2, vcc, s3, v2
	s_lshl_b32 s3, s2, 6
	s_nop 0
	v_addc_co_u32_e32 v3, vcc, 0, v3, vcc
	s_add_i32 s12, s3, -15
	s_cmpk_lt_i32 s2, 0x200
	s_cselect_b64 s[14:15], -1, 0
	global_load_dword v116, v[4:5], off offset:512
	global_load_dword v117, v[4:5], off offset:768
	global_load_dword v118, v[4:5], off offset:1024
	global_load_dword v119, v[4:5], off offset:1280
	global_load_dword v120, v[4:5], off offset:1536
	global_load_dword v121, v[4:5], off offset:1792
	global_load_dword v122, v[4:5], off offset:128
	global_load_dword v123, v[4:5], off offset:384
	global_load_dword v124, v[4:5], off offset:640
	global_load_dword v125, v[4:5], off offset:896
	global_load_dword v126, v[4:5], off offset:1152
	global_load_dword v127, v[4:5], off offset:1408
	global_load_dword v128, v[4:5], off offset:1664
	s_nop 0
	global_load_dword v129, v[4:5], off offset:1920
	global_load_dword v130, v[10:11], off
	global_load_dword v131, v[10:11], off offset:256
	v_lshlrev_b32_e32 v9, 3, v6
	global_load_dword v132, v[10:11], off offset:512
	global_load_dword v133, v[10:11], off offset:768
	global_load_dword v134, v[10:11], off offset:1024
	global_load_dword v135, v[10:11], off offset:1280
	global_load_dword v138, v[10:11], off offset:1536
	global_load_dword v139, v[10:11], off offset:1792
	global_load_dword v140, v[10:11], off offset:128
	global_load_dword v141, v[10:11], off offset:384
	global_load_dword v142, v[10:11], off offset:640
	global_load_dword v143, v[10:11], off offset:896
	global_load_dword v144, v[10:11], off offset:1152
	global_load_dword v145, v[10:11], off offset:1408
	global_load_dword v146, v[10:11], off offset:1664
	global_load_dword v147, v[10:11], off offset:1920
	global_load_dword v148, v[2:3], off
	global_load_dword v149, v[2:3], off offset:256
	global_load_dword v150, v[2:3], off offset:512
	global_load_dword v151, v[2:3], off offset:768
	global_load_dword v152, v[2:3], off offset:1024
	global_load_dword v153, v[2:3], off offset:1280
	global_load_dword v154, v[2:3], off offset:1536
	global_load_dword v155, v[2:3], off offset:1792
	global_load_dword v156, v[2:3], off offset:128
	global_load_dword v157, v[2:3], off offset:384
	global_load_dword v158, v[2:3], off offset:640
	global_load_dword v159, v[2:3], off offset:896
	global_load_dword v160, v[2:3], off offset:1152
	global_load_dword v161, v[2:3], off offset:1408
	global_load_dword v162, v[2:3], off offset:1664
	s_nop 0
	global_load_dword v163, v[2:3], off offset:1920
	v_add_u32_e32 v3, s12, v97
	v_cmp_lt_i32_e32 vcc, -1, v3
	s_waitcnt vmcnt(0)
	v_cvt_pk_bf16_f32 v34, v98, v99
	v_cvt_pk_bf16_f32 v35, v100, v101
	v_cvt_pk_bf16_f32 v36, v102, v103
	v_cvt_pk_bf16_f32 v37, v104, v105
	v_cvt_pk_bf16_f32 v38, v106, v107
	v_cvt_pk_bf16_f32 v39, v108, v109
	v_cvt_pk_bf16_f32 v40, v110, v111
	v_cvt_pk_bf16_f32 v41, v112, v113
	v_cvt_pk_bf16_f32 v42, v114, v115
	v_cvt_pk_bf16_f32 v43, v116, v117
	v_cvt_pk_bf16_f32 v44, v118, v119
	v_cvt_pk_bf16_f32 v45, v120, v121
	v_cvt_pk_bf16_f32 v46, v122, v123
	v_cvt_pk_bf16_f32 v47, v124, v125
	v_cvt_pk_bf16_f32 v48, v126, v127
	v_cvt_pk_bf16_f32 v49, v128, v129
	v_cvt_pk_bf16_f32 v50, v130, v131
	v_cvt_pk_bf16_f32 v51, v132, v133
	v_cvt_pk_bf16_f32 v52, v134, v135
	v_cvt_pk_bf16_f32 v53, v138, v139
	v_cvt_pk_bf16_f32 v54, v140, v141
	v_cvt_pk_bf16_f32 v55, v142, v143
	v_cvt_pk_bf16_f32 v56, v144, v145
	v_cvt_pk_bf16_f32 v57, v146, v147
	v_cvt_pk_bf16_f32 v58, v148, v149
	v_cvt_pk_bf16_f32 v59, v150, v151
	v_cvt_pk_bf16_f32 v60, v152, v153
	v_cvt_pk_bf16_f32 v61, v154, v155
	v_cvt_pk_bf16_f32 v62, v156, v157
	v_cvt_pk_bf16_f32 v63, v158, v159
	v_cvt_pk_bf16_f32 v64, v160, v161
	v_cvt_pk_bf16_f32 v65, v162, v163
	v_lshlrev_b32_e32 v2, 6, v1
	v_or_b32_e32 v4, v2, v7
	v_ashrrev_i32_e32 v5, 31, v4
	v_lshl_add_u64 v[4:5], v[4:5], 2, s[38:39]
	global_load_dword v1, v[4:5], off
	global_load_dword v96, v[4:5], off offset:128
	v_cmp_gt_i32_e64 s[38:39], s13, v6
	v_and_b32_e32 v4, 0xf8, v9
	s_and_b64 s[16:17], s[14:15], s[38:39]
	s_and_b64 s[16:17], s[16:17], vcc
	v_lshlrev_b32_e32 v4, 1, v4
	s_and_saveexec_b64 s[24:25], s[16:17]
	s_cbranch_execz .LBB0_772
	v_mov_b64_e32 v[10:11], s[0:1]
	s_movk_i32 s13, 0x2800
	v_mad_u64_u32 v[10:11], s[16:17], v3, s13, v[10:11]
	v_mov_b32_e32 v5, v187
	v_lshl_add_u64 v[10:11], v[10:11], 0, v[4:5]
	global_load_dwordx4 v[70:73], v[10:11], off offset:3072

.LBB0_782:
	s_waitcnt lgkmcnt(0)
	s_barrier
	ds_read_b128 v[2:5], v115 offset:44544
	ds_read_b128 v[90:93], v115 offset:44576
	s_waitcnt lgkmcnt(1)
	v_mfma_f32_32x32x16_bf16 v[18:33], v[2:5], v[34:37], 0
	s_and_b64 vcc, exec, s[0:1]
	v_mfma_f32_32x32x16_bf16 v[2:17], v[2:5], v[38:41], 0
	s_waitcnt lgkmcnt(0)
	v_mfma_f32_32x32x16_bf16 v[18:33], v[90:93], v[42:45], v[18:33]
	v_mfma_f32_32x32x16_bf16 v[2:17], v[90:93], v[46:49], v[2:17]
	ds_read_b128 v[90:93], v115 offset:44608
	s_waitcnt lgkmcnt(0)
	v_mfma_f32_32x32x16_bf16 v[18:33], v[90:93], v[50:53], v[18:33]
	v_mfma_f32_32x32x16_bf16 v[2:17], v[90:93], v[54:57], v[2:17]
	ds_read_b128 v[90:93], v115 offset:44640
	s_waitcnt lgkmcnt(0)
	v_mfma_f32_32x32x16_bf16 v[18:33], v[90:93], v[58:61], v[18:33]
	v_mfma_f32_32x32x16_bf16 v[2:17], v[90:93], v[62:65], v[2:17]
	s_nop 10
	v_mul_f32_e32 v18, v1, v18
	v_or_b32_e32 v90, s2, v104
	v_bfe_u32 v91, v18, 16, 1
	v_add3_u32 v18, v18, v91, s11
	v_ashrrev_i32_e32 v91, 31, v90
	v_lshlrev_b64 v[92:93], 9, v[90:91]
	v_lshl_add_u64 v[92:93], v[86:87], 0, v[92:93]
	v_mul_f32_e32 v19, v1, v19
	global_store_short_d16_hi v[92:93], v18, off
	v_or_b32_e32 v18, 1, v90
	v_bfe_u32 v91, v19, 16, 1
	v_add3_u32 v91, v19, v91, s11
	v_ashrrev_i32_e32 v19, 31, v18
	v_lshlrev_b64 v[18:19], 9, v[18:19]
	v_or_b32_e32 v94, 2, v90
	v_lshl_add_u64 v[18:19], v[86:87], 0, v[18:19]
	v_mul_f32_e32 v20, v1, v20
	v_ashrrev_i32_e32 v95, 31, v94
	global_store_short_d16_hi v[18:19], v91, off
	v_bfe_u32 v91, v20, 16, 1
	v_lshlrev_b64 v[94:95], 9, v[94:95]
	v_add3_u32 v20, v20, v91, s11
	v_lshl_add_u64 v[94:95], v[86:87], 0, v[94:95]
	v_mul_f32_e32 v21, v1, v21
	global_store_short_d16_hi v[94:95], v20, off
	v_or_b32_e32 v20, 3, v90
	v_bfe_u32 v91, v21, 16, 1
	v_add3_u32 v91, v21, v91, s11
	v_ashrrev_i32_e32 v21, 31, v20
	v_lshlrev_b64 v[20:21], 9, v[20:21]
	v_or_b32_e32 v116, 8, v90
	v_lshl_add_u64 v[20:21], v[86:87], 0, v[20:21]
	v_mul_f32_e32 v22, v1, v22
	v_ashrrev_i32_e32 v117, 31, v116
	global_store_short_d16_hi v[20:21], v91, off
	v_bfe_u32 v91, v22, 16, 1
	v_lshlrev_b64 v[116:117], 9, v[116:117]
	v_add3_u32 v22, v22, v91, s11
	v_lshl_add_u64 v[116:117], v[86:87], 0, v[116:117]
	v_mul_f32_e32 v23, v1, v23
	global_store_short_d16_hi v[116:117], v22, off
	v_or_b32_e32 v22, 9, v90
	v_bfe_u32 v91, v23, 16, 1
	v_add3_u32 v91, v23, v91, s11
	v_ashrrev_i32_e32 v23, 31, v22
	v_lshlrev_b64 v[22:23], 9, v[22:23]
	v_or_b32_e32 v118, 10, v90
	v_lshl_add_u64 v[22:23], v[86:87], 0, v[22:23]
	v_mul_f32_e32 v24, v1, v24
	v_ashrrev_i32_e32 v119, 31, v118
	global_store_short_d16_hi v[22:23], v91, off
	v_bfe_u32 v91, v24, 16, 1
	v_lshlrev_b64 v[118:119], 9, v[118:119]
	v_add3_u32 v24, v24, v91, s11
	v_lshl_add_u64 v[118:119], v[86:87], 0, v[118:119]
	v_mul_f32_e32 v25, v1, v25
	global_store_short_d16_hi v[118:119], v24, off
	v_or_b32_e32 v24, 11, v90
	v_bfe_u32 v91, v25, 16, 1
	v_add3_u32 v91, v25, v91, s11
	v_ashrrev_i32_e32 v25, 31, v24
	v_lshlrev_b64 v[24:25], 9, v[24:25]
	v_or_b32_e32 v120, 16, v90
	v_lshl_add_u64 v[24:25], v[86:87], 0, v[24:25]
	v_mul_f32_e32 v26, v1, v26
	v_ashrrev_i32_e32 v121, 31, v120
	global_store_short_d16_hi v[24:25], v91, off
	v_bfe_u32 v91, v26, 16, 1
	v_lshlrev_b64 v[120:121], 9, v[120:121]
	v_add3_u32 v26, v26, v91, s11
	v_lshl_add_u64 v[120:121], v[86:87], 0, v[120:121]
	v_mul_f32_e32 v27, v1, v27
	global_store_short_d16_hi v[120:121], v26, off
	v_or_b32_e32 v26, 17, v90
	v_bfe_u32 v91, v27, 16, 1
	v_add3_u32 v91, v27, v91, s11
	v_ashrrev_i32_e32 v27, 31, v26
	v_lshlrev_b64 v[26:27], 9, v[26:27]
	v_or_b32_e32 v122, 18, v90
	v_lshl_add_u64 v[26:27], v[86:87], 0, v[26:27]
	v_mul_f32_e32 v28, v1, v28
	v_ashrrev_i32_e32 v123, 31, v122
	global_store_short_d16_hi v[26:27], v91, off
	v_bfe_u32 v91, v28, 16, 1
	v_lshlrev_b64 v[122:123], 9, v[122:123]
	v_add3_u32 v28, v28, v91, s11
	v_lshl_add_u64 v[122:123], v[86:87], 0, v[122:123]
	v_mul_f32_e32 v29, v1, v29
	global_store_short_d16_hi v[122:123], v28, off
	v_or_b32_e32 v28, 19, v90
	v_bfe_u32 v91, v29, 16, 1
	v_add3_u32 v91, v29, v91, s11
	v_ashrrev_i32_e32 v29, 31, v28
	v_lshlrev_b64 v[28:29], 9, v[28:29]
	v_or_b32_e32 v124, 24, v90
	v_lshl_add_u64 v[28:29], v[86:87], 0, v[28:29]
	v_mul_f32_e32 v30, v1, v30
	v_ashrrev_i32_e32 v125, 31, v124
	global_store_short_d16_hi v[28:29], v91, off
	v_bfe_u32 v91, v30, 16, 1
	v_lshlrev_b64 v[124:125], 9, v[124:125]
	v_add3_u32 v30, v30, v91, s11
	v_lshl_add_u64 v[124:125], v[86:87], 0, v[124:125]
	v_mul_f32_e32 v31, v1, v31
	global_store_short_d16_hi v[124:125], v30, off
	v_or_b32_e32 v30, 25, v90
	v_bfe_u32 v91, v31, 16, 1
	v_add3_u32 v91, v31, v91, s11
	v_ashrrev_i32_e32 v31, 31, v30
	v_lshlrev_b64 v[30:31], 9, v[30:31]
	v_or_b32_e32 v126, 26, v90
	v_lshl_add_u64 v[30:31], v[86:87], 0, v[30:31]
	v_mul_f32_e32 v32, v1, v32
	v_ashrrev_i32_e32 v127, 31, v126
	global_store_short_d16_hi v[30:31], v91, off
	v_bfe_u32 v91, v32, 16, 1
	v_lshlrev_b64 v[126:127], 9, v[126:127]
	v_add3_u32 v32, v32, v91, s11
	v_lshl_add_u64 v[126:127], v[86:87], 0, v[126:127]
	v_mul_f32_e32 v33, v1, v33
	global_store_short_d16_hi v[126:127], v32, off
	v_or_b32_e32 v32, 27, v90
	v_bfe_u32 v90, v33, 16, 1
	v_add3_u32 v90, v33, v90, s11
	v_ashrrev_i32_e32 v33, 31, v32
	v_lshlrev_b64 v[32:33], 9, v[32:33]
	v_lshl_add_u64 v[32:33], v[86:87], 0, v[32:33]
	v_mul_f32_e32 v2, v96, v2
	global_store_short_d16_hi v[32:33], v90, off
	v_bfe_u32 v90, v2, 16, 1
	v_add3_u32 v2, v2, v90, s11
	global_store_short_d16_hi v[92:93], v2, off offset:64
	v_mul_f32_e32 v2, v96, v3
	v_bfe_u32 v3, v2, 16, 1
	v_add3_u32 v2, v2, v3, s11
	global_store_short_d16_hi v[18:19], v2, off offset:64
	v_mul_f32_e32 v2, v96, v4
	v_bfe_u32 v3, v2, 16, 1
	v_add3_u32 v2, v2, v3, s11
	global_store_short_d16_hi v[94:95], v2, off offset:64
	v_mul_f32_e32 v2, v96, v5
	v_bfe_u32 v3, v2, 16, 1
	v_add3_u32 v2, v2, v3, s11
	global_store_short_d16_hi v[20:21], v2, off offset:64
	v_mul_f32_e32 v2, v96, v6
	v_bfe_u32 v3, v2, 16, 1
	v_add3_u32 v2, v2, v3, s11
	global_store_short_d16_hi v[116:117], v2, off offset:64
	v_mul_f32_e32 v2, v96, v7
	v_bfe_u32 v3, v2, 16, 1
	v_add3_u32 v2, v2, v3, s11
	global_store_short_d16_hi v[22:23], v2, off offset:64
	v_mul_f32_e32 v2, v96, v8
	v_bfe_u32 v3, v2, 16, 1
	v_add3_u32 v2, v2, v3, s11
	global_store_short_d16_hi v[118:119], v2, off offset:64
	v_mul_f32_e32 v2, v96, v9
	v_bfe_u32 v3, v2, 16, 1
	v_add3_u32 v2, v2, v3, s11
	global_store_short_d16_hi v[24:25], v2, off offset:64
	v_mul_f32_e32 v2, v96, v10
	v_bfe_u32 v3, v2, 16, 1
	v_add3_u32 v2, v2, v3, s11
	global_store_short_d16_hi v[120:121], v2, off offset:64
	v_mul_f32_e32 v2, v96, v11
	v_bfe_u32 v3, v2, 16, 1
	v_add3_u32 v2, v2, v3, s11
	global_store_short_d16_hi v[26:27], v2, off offset:64
	v_mul_f32_e32 v2, v96, v12
	v_bfe_u32 v3, v2, 16, 1
	v_add3_u32 v2, v2, v3, s11
	global_store_short_d16_hi v[122:123], v2, off offset:64
	v_mul_f32_e32 v2, v96, v13
	v_bfe_u32 v3, v2, 16, 1
	v_add3_u32 v2, v2, v3, s11
	global_store_short_d16_hi v[28:29], v2, off offset:64
	v_mul_f32_e32 v2, v96, v14
	v_bfe_u32 v3, v2, 16, 1
	v_add3_u32 v2, v2, v3, s11
	global_store_short_d16_hi v[124:125], v2, off offset:64
	v_mul_f32_e32 v2, v96, v15
	v_bfe_u32 v3, v2, 16, 1
	v_add3_u32 v2, v2, v3, s11
	global_store_short_d16_hi v[30:31], v2, off offset:64
	v_mul_f32_e32 v2, v96, v16
	v_bfe_u32 v3, v2, 16, 1
	v_add3_u32 v2, v2, v3, s11
	global_store_short_d16_hi v[126:127], v2, off offset:64
	v_mul_f32_e32 v2, v96, v17
	v_bfe_u32 v3, v2, 16, 1
	v_readlane_b32 s2, v254, 34
	v_add3_u32 v2, v2, v3, s11
	global_store_short_d16_hi v[32:33], v2, off offset:64
	v_add_u32_e32 v114, s2, v114
	s_mov_b32 s2, s3
	s_waitcnt lgkmcnt(0)
	s_barrier
	s_cbranch_vccnz .LBB0_817

.LBB0_884:
	s_add_u32 s0, s0, 0x62800000
	v_writelane_b32 v254, s0, 46
	s_addc_u32 s0, s1, 0
	v_writelane_b32 v254, s0, 48
	s_add_u32 s0, s14, 0xa5000000
	v_writelane_b32 v254, s0, 50
	s_addc_u32 s0, s15, 0
	v_bfe_u32 v9, v6, 4, 2
	v_writelane_b32 v254, s0, 52
	v_and_b32_e32 v8, 15, v6
	s_lshl_b32 s0, s24, 6
	v_lshlrev_b32_e32 v10, 4, v9
	v_lshlrev_b32_e32 v6, 2, v6
	v_writelane_b32 v254, s0, 54
	v_lshl_or_b32 v7, v8, 6, v10
	s_lshl_b32 s0, s24, 13
	v_and_b32_e32 v6, 32, v6
	v_bitop3_b32 v11, v7, s0, v6 bitop3:0xde
	s_lshl_b32 s0, s3, 5
	s_and_b32 s3, s0, 0x60
	s_lshl_b32 s0, s3, 7
	v_bitop3_b32 v166, v7, s0, v6 bitop3:0xde
	v_lshl_add_u64 v[6:7], v[2:3], 0, s[92:93]
	s_add_i32 m0, s33, 0x19000
	s_mov_b64 s[0:1], 0x10080
	s_waitcnt vmcnt(2)
	s_barrier
	global_load_lds_dwordx4 v[6:7], off
	v_lshl_add_u64 v[6:7], v[2:3], 0, s[0:1]
	s_add_i32 m0, s33, 0x1b000
	s_add_i32 s90, s33, 0x9000
	global_load_lds_dwordx4 v[6:7], off
	v_lshl_add_u64 v[6:7], v[4:5], 0, s[92:93]
	s_mov_b32 m0, s90
	s_mov_b64 s[0:1], 0xa0080
	s_add_i32 s91, s33, 0xb000
	global_load_lds_dwordx4 v[6:7], off
	v_lshl_add_u64 v[4:5], v[4:5], 0, s[0:1]
	s_mov_b32 m0, s91
	s_mov_b64 s[0:1], 0x30080
	global_load_lds_dwordx4 v[4:5], off
	s_add_i32 m0, s33, 0x1d000
	v_lshl_add_u64 v[4:5], v[2:3], 0, s[4:5]
	global_load_lds_dwordx4 v[4:5], off
	v_lshl_add_u64 v[2:3], v[2:3], 0, s[0:1]
	s_add_i32 m0, s33, 0x1f000
	s_cmpk_lt_u32 s2, 0x100
	global_load_lds_dwordx4 v[2:3], off
	s_cselect_b64 s[0:1], -1, 0
	v_writelane_b32 v254, s0, 56
	s_waitcnt vmcnt(6)
	v_mul_u32_u24_e32 v2, 0xc00, v8
	v_lshl_or_b32 v138, v9, 3, v2
	v_writelane_b32 v254, s1, 57
	v_readlane_b32 s0, v253, 34
	s_ashr_i32 s0, s0, 31
	v_mov_b32_e32 v2, 0
	v_writelane_b32 v254, s0, 58
	v_writelane_b32 v254, s3, 55
	s_lshl_b32 s0, s3, 1
	v_lshl_or_b32 v140, v8, 11, v10
	v_mov_b32_e32 v139, v187
	v_mov_b32_e32 v141, v187
	s_mov_b64 s[44:45], 0x10000
	s_mov_b64 s[42:43], 0xa0000
	s_mov_b32 s35, 8
	s_mov_b32 s85, 0
	v_add_u32_e32 v167, 0, v11
	v_writelane_b32 v254, s0, 59
	s_mov_b32 s84, 0
	v_mov_b32_e32 v3, 0
	v_mov_b64_e32 v[4:5], 0
	v_mov_b64_e32 v[6:7], 0
	v_mov_b64_e32 v[8:9], 0
	v_mov_b64_e32 v[10:11], 0
	v_mov_b64_e32 v[12:13], 0
	v_mov_b64_e32 v[14:15], 0
	v_mov_b64_e32 v[16:17], 0
	v_mov_b64_e32 v[18:19], 0
	v_mov_b64_e32 v[20:21], 0
	v_mov_b64_e32 v[22:23], 0
	v_mov_b64_e32 v[24:25], 0
	v_mov_b64_e32 v[26:27], 0
	v_mov_b64_e32 v[28:29], 0
	v_mov_b64_e32 v[30:31], 0
	v_mov_b64_e32 v[32:33], 0
	v_mov_b64_e32 v[34:35], 0
	v_mov_b64_e32 v[36:37], 0
	v_mov_b64_e32 v[38:39], 0
	v_mov_b64_e32 v[40:41], 0
	v_mov_b64_e32 v[42:43], 0
	v_mov_b64_e32 v[44:45], 0
	v_mov_b64_e32 v[46:47], 0
	v_mov_b64_e32 v[48:49], 0
	v_mov_b64_e32 v[50:51], 0
	v_mov_b64_e32 v[52:53], 0
	v_mov_b64_e32 v[54:55], 0
	v_mov_b64_e32 v[56:57], 0
	v_mov_b64_e32 v[58:59], 0
	v_mov_b64_e32 v[60:61], 0
	v_mov_b64_e32 v[62:63], 0
	v_mov_b64_e32 v[64:65], 0
	v_mov_b64_e32 v[66:67], 0
	v_mov_b64_e32 v[68:69], 0
	v_mov_b64_e32 v[70:71], 0
	v_mov_b64_e32 v[72:73], 0
	v_mov_b64_e32 v[74:75], 0
	v_mov_b64_e32 v[76:77], 0
	v_mov_b64_e32 v[78:79], 0
	v_mov_b64_e32 v[80:81], 0
	v_mov_b64_e32 v[82:83], 0
	v_mov_b64_e32 v[84:85], 0
	v_mov_b64_e32 v[86:87], 0
	v_mov_b64_e32 v[88:89], 0
	v_mov_b64_e32 v[90:91], 0
	v_mov_b64_e32 v[92:93], 0
	v_mov_b64_e32 v[94:95], 0
	v_mov_b64_e32 v[96:97], 0
	v_mov_b64_e32 v[98:99], 0
	v_mov_b64_e32 v[100:101], 0
	v_mov_b64_e32 v[102:103], 0
	v_mov_b64_e32 v[104:105], 0
	v_mov_b64_e32 v[106:107], 0
	v_mov_b64_e32 v[108:109], 0
	v_mov_b64_e32 v[110:111], 0
	v_mov_b64_e32 v[112:113], 0
	v_mov_b64_e32 v[114:115], 0
	v_mov_b64_e32 v[116:117], 0
	v_mov_b64_e32 v[118:119], 0
	v_mov_b64_e32 v[120:121], 0
	v_mov_b64_e32 v[122:123], 0
	v_mov_b64_e32 v[124:125], 0
	v_mov_b64_e32 v[126:127], 0
	v_mov_b64_e32 v[128:129], 0
	s_mov_b64 s[76:77], s[50:51]
	s_mov_b64 s[24:25], s[48:49]
	s_barrier
	s_branch .LBB0_887

.LBB0_901:
	s_lshl_b32 s0, s12, 8
	v_readlane_b32 s1, v254, 54
	s_add_i32 s44, s0, s1
	s_mul_i32 s1, s44, 0xc00
	v_readlane_b32 s12, v254, 50
	s_mul_hi_i32 s0, s44, 0xc00
	s_add_u32 s1, s12, s1
	v_readlane_b32 s12, v254, 52
	s_addc_u32 s0, s12, s0
	s_lshl_b32 s12, s85, 10
	s_ashr_i32 s28, s12, 31
	s_add_u32 s1, s1, s12
	s_addc_u32 s0, s0, s28
	s_lshl_b32 s46, s88, 8
	s_ashr_i32 s47, s46, 31
	s_add_u32 s1, s1, s46
	s_addc_u32 s12, s0, s47
	v_readlane_b32 s0, v254, 55
	s_add_u32 s0, s1, s0
	s_addc_u32 s1, s12, 0
	v_lshl_add_u64 v[146:147], s[0:1], 0, v[138:139]
	global_load_dwordx2 v[130:131], v[146:147], off
	s_cmp_lt_i32 s85, 2
	s_cselect_b64 s[28:29], -1, 0
	s_cmp_gt_i32 s85, 1
	s_cselect_b64 s[0:1], -1, 0
	v_mov_b32_e32 v148, -1
	s_and_b64 vcc, exec, s[0:1]
	v_mov_b32_e32 v144, -1
	v_mov_b32_e32 v145, -1
	s_cbranch_vccnz .LBB0_903
	global_load_dwordx2 v[144:145], v[146:147], off offset:1024
.LBB0_903:
	global_load_dwordx2 v[152:153], v[146:147], off offset:128
	v_cndmask_b32_e64 v132, 0, 1, s[28:29]
	v_cmp_ne_u32_e64 s[42:43], 1, v132
	s_andn2_b64 vcc, exec, s[28:29]
	v_mov_b32_e32 v149, -1
	s_cbranch_vccnz .LBB0_905
	global_load_dwordx2 v[148:149], v[146:147], off offset:1152
.LBB0_905:
	v_cndmask_b32_e64 v132, 0, 1, s[0:1]
	s_mov_b64 s[28:29], -1
	v_cmp_ne_u32_e64 s[40:41], 1, v132
	s_andn2_b64 vcc, exec, s[0:1]
	s_waitcnt vmcnt(1)
	v_cvt_f32_ubyte1_e32 v155, v130
	v_cvt_f32_ubyte3_e32 v159, v130
	v_cvt_f32_ubyte2_e32 v158, v130
	v_cvt_f32_ubyte0_e32 v154, v130
	v_cvt_f32_ubyte1_e32 v151, v131
	v_cvt_f32_ubyte0_e32 v150, v131
	v_cvt_f32_ubyte3_e32 v157, v131
	v_cvt_f32_ubyte2_e32 v156, v131
	s_cbranch_vccnz .LBB0_907
	s_mov_b32 s0, 0x3b808081
	v_pk_mul_f32 v[132:133], v[158:159], s[0:1] op_sel_hi:[1,0]
	v_pk_mul_f32 v[130:131], v[154:155], s[0:1] op_sel_hi:[1,0]
	v_pk_mul_f32 v[136:137], v[156:157], s[0:1] op_sel_hi:[1,0]
	v_pk_mul_f32 v[134:135], v[150:151], s[0:1] op_sel_hi:[1,0]
	s_mov_b64 s[28:29], 0

.LBB0_909:
	s_ashr_i32 s45, s44, 31
	s_cmp_eq_u32 s85, 2
	s_cselect_b64 s[0:1], -1, 0
	s_lshl_b64 s[28:29], s[44:45], 11
	v_readlane_b32 s12, v254, 46
	s_add_u32 s12, s12, s28
	v_readlane_b32 s28, v254, 48
	s_addc_u32 s35, s28, s29
	s_lshl_b64 s[28:29], s[46:47], 1
	s_add_u32 s12, s12, s28
	s_addc_u32 s29, s35, s29
	v_readlane_b32 s28, v254, 59
	s_add_u32 s28, s12, s28
	s_addc_u32 s29, s29, 0
	s_cmp_lg_u32 s85, 2
	v_pk_mul_f32 v[128:129], v[128:129], v[132:133]
	v_pk_mul_f32 v[126:127], v[126:127], v[130:131]
	v_pk_mul_f32 v[124:125], v[124:125], v[136:137]
	v_pk_mul_f32 v[122:123], v[122:123], v[134:135]
	v_lshl_add_u64 v[144:145], s[28:29], 0, v[140:141]
	s_cbranch_scc1 .LBB0_911
	v_cvt_pk_bf16_f32 v130, v126, v127
	v_cvt_pk_bf16_f32 v131, v128, v129
	v_cvt_pk_bf16_f32 v132, v122, v123
	v_cvt_pk_bf16_f32 v133, v124, v125
	global_store_dwordx4 v[144:145], v[130:133], off
.LBB0_911:
	s_nop 1
	v_add_co_u32_e32 v130, vcc, 0xc000, v146
	v_mov_b32_e32 v150, -1
	s_nop 0
	v_addc_co_u32_e32 v131, vcc, 0, v147, vcc
	global_load_dwordx2 v[154:155], v[130:131], off
	s_and_b64 vcc, exec, s[42:43]
	v_mov_b32_e32 v151, -1
	s_cbranch_vccnz .LBB0_913
	v_add_co_u32_e32 v130, vcc, 0xc000, v146
	s_nop 1
	v_addc_co_u32_e32 v131, vcc, 0, v147, vcc
	global_load_dwordx2 v[150:151], v[130:131], off offset:1024
.LBB0_913:
	s_waitcnt vmcnt(2)
	s_mov_b64 s[28:29], -1
	s_and_b64 vcc, exec, s[40:41]
	v_cvt_f32_ubyte1_e32 v159, v152
	v_cvt_f32_ubyte3_e32 v163, v152
	v_cvt_f32_ubyte2_e32 v162, v152
	v_cvt_f32_ubyte0_e32 v158, v152
	v_cvt_f32_ubyte1_e32 v157, v153
	v_cvt_f32_ubyte0_e32 v156, v153
	v_cvt_f32_ubyte3_e32 v161, v153
	v_cvt_f32_ubyte2_e32 v160, v153
	s_cbranch_vccnz .LBB0_915
	s_mov_b32 s12, 0x3b808081
	v_pk_mul_f32 v[132:133], v[162:163], s[12:13] op_sel_hi:[1,0]
	v_pk_mul_f32 v[130:131], v[158:159], s[12:13] op_sel_hi:[1,0]
	v_pk_mul_f32 v[136:137], v[160:161], s[12:13] op_sel_hi:[1,0]
	v_pk_mul_f32 v[134:135], v[156:157], s[12:13] op_sel_hi:[1,0]
	s_mov_b64 s[28:29], 0

.LBB0_917:
	v_pk_mul_f32 v[94:95], v[94:95], v[130:131]
	v_cndmask_b32_e64 v130, 0, 1, s[0:1]
	v_pk_mul_f32 v[96:97], v[96:97], v[132:133]
	v_pk_mul_f32 v[92:93], v[92:93], v[136:137]
	v_cmp_ne_u32_e64 s[44:45], 1, v130
	s_andn2_b64 vcc, exec, s[0:1]
	v_pk_mul_f32 v[90:91], v[90:91], v[134:135]
	s_cbranch_vccnz .LBB0_919
	v_cvt_pk_bf16_f32 v130, v94, v95
	v_cvt_pk_bf16_f32 v131, v96, v97
	v_cvt_pk_bf16_f32 v132, v90, v91
	v_cvt_pk_bf16_f32 v133, v92, v93
	global_store_dwordx4 v[144:145], v[130:133], off offset:256
.LBB0_919:
	s_nop 1
	v_add_co_u32_e32 v130, vcc, 0xc000, v146
	v_mov_b32_e32 v148, -1
	s_nop 0
	v_addc_co_u32_e32 v131, vcc, 0, v147, vcc
	global_load_dwordx2 v[152:153], v[130:131], off offset:128
	s_and_b64 vcc, exec, s[42:43]
	v_mov_b32_e32 v149, -1
	s_cbranch_vccnz .LBB0_921
	v_add_co_u32_e32 v130, vcc, 0xc000, v146
	s_nop 1
	v_addc_co_u32_e32 v131, vcc, 0, v147, vcc
	global_load_dwordx2 v[148:149], v[130:131], off offset:1152
.LBB0_921:
	s_mov_b64 s[0:1], -1
	s_and_b64 vcc, exec, s[40:41]
	s_waitcnt vmcnt(2)
	v_cvt_f32_ubyte1_e32 v159, v154
	v_cvt_f32_ubyte3_e32 v163, v154
	v_cvt_f32_ubyte2_e32 v162, v154
	v_cvt_f32_ubyte0_e32 v158, v154
	v_cvt_f32_ubyte1_e32 v157, v155
	v_cvt_f32_ubyte0_e32 v156, v155
	v_cvt_f32_ubyte3_e32 v161, v155
	v_cvt_f32_ubyte2_e32 v160, v155
	s_cbranch_vccnz .LBB0_923
	s_mov_b32 s0, 0x3b808081
	v_pk_mul_f32 v[132:133], v[162:163], s[0:1] op_sel_hi:[1,0]
	v_pk_mul_f32 v[130:131], v[158:159], s[0:1] op_sel_hi:[1,0]
	v_pk_mul_f32 v[136:137], v[160:161], s[0:1] op_sel_hi:[1,0]
	v_pk_mul_f32 v[134:135], v[156:157], s[0:1] op_sel_hi:[1,0]
	s_mov_b64 s[0:1], 0

.LBB0_925:
	v_pk_mul_f32 v[120:121], v[120:121], v[132:133]
	v_pk_mul_f32 v[118:119], v[118:119], v[130:131]
	v_pk_mul_f32 v[116:117], v[116:117], v[136:137]
	s_and_b64 vcc, exec, s[44:45]
	v_pk_mul_f32 v[114:115], v[114:115], v[134:135]
	s_cbranch_vccnz .LBB0_927
	v_add_co_u32_e32 v134, vcc, 0x8000, v144
	v_cvt_pk_bf16_f32 v130, v118, v119
	v_cvt_pk_bf16_f32 v131, v120, v121
	v_cvt_pk_bf16_f32 v132, v114, v115
	v_cvt_pk_bf16_f32 v133, v116, v117
	s_nop 1
	v_addc_co_u32_e32 v135, vcc, 0, v145, vcc
	global_store_dwordx4 v[134:135], v[130:133], off
.LBB0_927:
	s_nop 1
	v_add_co_u32_e32 v130, vcc, 0x18000, v146
	v_mov_b32_e32 v150, -1
	s_nop 0
	v_addc_co_u32_e32 v131, vcc, 0, v147, vcc
	global_load_dwordx2 v[154:155], v[130:131], off
	s_and_b64 vcc, exec, s[42:43]
	v_mov_b32_e32 v151, -1
	s_cbranch_vccnz .LBB0_929
	v_add_co_u32_e32 v130, vcc, 0x18000, v146
	s_nop 1
	v_addc_co_u32_e32 v131, vcc, 0, v147, vcc
	global_load_dwordx2 v[150:151], v[130:131], off offset:1024
.LBB0_929:
	s_waitcnt vmcnt(2)
	s_mov_b64 s[0:1], -1
	s_and_b64 vcc, exec, s[40:41]
	v_cvt_f32_ubyte1_e32 v159, v152
	v_cvt_f32_ubyte3_e32 v163, v152
	v_cvt_f32_ubyte2_e32 v162, v152
	v_cvt_f32_ubyte0_e32 v158, v152
	v_cvt_f32_ubyte1_e32 v157, v153
	v_cvt_f32_ubyte0_e32 v156, v153
	v_cvt_f32_ubyte3_e32 v161, v153
	v_cvt_f32_ubyte2_e32 v160, v153
	s_cbranch_vccnz .LBB0_931
	s_mov_b32 s0, 0x3b808081
	v_pk_mul_f32 v[132:133], v[162:163], s[0:1] op_sel_hi:[1,0]
	v_pk_mul_f32 v[130:131], v[158:159], s[0:1] op_sel_hi:[1,0]
	v_pk_mul_f32 v[136:137], v[160:161], s[0:1] op_sel_hi:[1,0]
	v_pk_mul_f32 v[134:135], v[156:157], s[0:1] op_sel_hi:[1,0]
	s_mov_b64 s[0:1], 0

.LBB0_933:
	v_pk_mul_f32 v[88:89], v[88:89], v[132:133]
	v_pk_mul_f32 v[86:87], v[86:87], v[130:131]
	v_pk_mul_f32 v[84:85], v[84:85], v[136:137]
	s_and_b64 vcc, exec, s[44:45]
	v_pk_mul_f32 v[82:83], v[82:83], v[134:135]
	s_cbranch_vccnz .LBB0_935
	v_add_co_u32_e32 v134, vcc, 0x8000, v144
	v_cvt_pk_bf16_f32 v130, v86, v87
	v_cvt_pk_bf16_f32 v131, v88, v89
	v_cvt_pk_bf16_f32 v132, v82, v83
	v_cvt_pk_bf16_f32 v133, v84, v85
	s_nop 1
	v_addc_co_u32_e32 v135, vcc, 0, v145, vcc
	global_store_dwordx4 v[134:135], v[130:133], off offset:256
.LBB0_935:
	s_nop 1
	v_add_co_u32_e32 v130, vcc, 0x18000, v146
	v_mov_b32_e32 v148, -1
	s_nop 0
	v_addc_co_u32_e32 v131, vcc, 0, v147, vcc
	global_load_dwordx2 v[152:153], v[130:131], off offset:128
	s_and_b64 vcc, exec, s[42:43]
	v_mov_b32_e32 v149, -1
	s_cbranch_vccnz .LBB0_937
	v_add_co_u32_e32 v130, vcc, 0x18000, v146
	s_nop 1
	v_addc_co_u32_e32 v131, vcc, 0, v147, vcc
	global_load_dwordx2 v[148:149], v[130:131], off offset:1152

.LBB0_941:
	v_pk_mul_f32 v[112:113], v[112:113], v[132:133]
	v_pk_mul_f32 v[110:111], v[110:111], v[130:131]
	v_pk_mul_f32 v[108:109], v[108:109], v[136:137]
	s_and_b64 vcc, exec, s[44:45]
	v_pk_mul_f32 v[106:107], v[106:107], v[134:135]
	s_cbranch_vccnz .LBB0_943
	v_add_co_u32_e32 v134, vcc, 0x10000, v144
	v_cvt_pk_bf16_f32 v130, v110, v111
	v_cvt_pk_bf16_f32 v131, v112, v113
	v_cvt_pk_bf16_f32 v132, v106, v107
	v_cvt_pk_bf16_f32 v133, v108, v109
	s_nop 1
	v_addc_co_u32_e32 v135, vcc, 0, v145, vcc
	global_store_dwordx4 v[134:135], v[130:133], off
.LBB0_943:
	s_nop 1
	v_add_co_u32_e32 v130, vcc, 0x24000, v146
	v_mov_b32_e32 v150, -1
	s_nop 0
	v_addc_co_u32_e32 v131, vcc, 0, v147, vcc
	global_load_dwordx2 v[154:155], v[130:131], off
	s_and_b64 vcc, exec, s[42:43]
	v_mov_b32_e32 v151, -1
	s_cbranch_vccnz .LBB0_945
	v_add_co_u32_e32 v130, vcc, 0x24000, v146
	s_nop 1
	v_addc_co_u32_e32 v131, vcc, 0, v147, vcc
	global_load_dwordx2 v[150:151], v[130:131], off offset:1024

.LBB0_949:
	v_pk_mul_f32 v[80:81], v[80:81], v[132:133]
	v_pk_mul_f32 v[78:79], v[78:79], v[130:131]
	v_pk_mul_f32 v[76:77], v[76:77], v[136:137]
	s_and_b64 vcc, exec, s[44:45]
	v_pk_mul_f32 v[74:75], v[74:75], v[134:135]
	s_cbranch_vccnz .LBB0_951
	v_add_co_u32_e32 v134, vcc, 0x10000, v144
	v_cvt_pk_bf16_f32 v130, v78, v79
	v_cvt_pk_bf16_f32 v131, v80, v81
	v_cvt_pk_bf16_f32 v132, v74, v75
	v_cvt_pk_bf16_f32 v133, v76, v77
	s_nop 1
	v_addc_co_u32_e32 v135, vcc, 0, v145, vcc
	global_store_dwordx4 v[134:135], v[130:133], off offset:256
.LBB0_951:
	s_nop 1
	v_add_co_u32_e32 v130, vcc, 0x24000, v146
	v_mov_b32_e32 v148, -1
	s_nop 0
	v_addc_co_u32_e32 v131, vcc, 0, v147, vcc
	global_load_dwordx2 v[152:153], v[130:131], off offset:128
	s_and_b64 vcc, exec, s[42:43]
	v_mov_b32_e32 v149, -1
	s_cbranch_vccnz .LBB0_953
	v_add_co_u32_e32 v130, vcc, 0x24000, v146
	s_nop 1
	v_addc_co_u32_e32 v131, vcc, 0, v147, vcc
	global_load_dwordx2 v[148:149], v[130:131], off offset:1152

.LBB0_957:
	v_pk_mul_f32 v[104:105], v[104:105], v[132:133]
	v_pk_mul_f32 v[102:103], v[102:103], v[130:131]
	v_pk_mul_f32 v[100:101], v[100:101], v[136:137]
	s_and_b64 vcc, exec, s[44:45]
	v_pk_mul_f32 v[98:99], v[98:99], v[134:135]
	s_cbranch_vccnz .LBB0_959
	v_add_co_u32_e32 v134, vcc, 0x18000, v144
	v_cvt_pk_bf16_f32 v130, v102, v103
	v_cvt_pk_bf16_f32 v131, v104, v105
	v_cvt_pk_bf16_f32 v132, v98, v99
	v_cvt_pk_bf16_f32 v133, v100, v101
	s_nop 1
	v_addc_co_u32_e32 v135, vcc, 0, v145, vcc
	global_store_dwordx4 v[134:135], v[130:133], off
.LBB0_959:
	s_nop 1
	v_add_co_u32_e32 v130, vcc, 0x60000, v146
	v_mov_b32_e32 v150, -1
	s_nop 0
	v_addc_co_u32_e32 v131, vcc, 0, v147, vcc
	global_load_dwordx2 v[154:155], v[130:131], off
	s_and_b64 vcc, exec, s[42:43]
	v_mov_b32_e32 v151, -1
	s_cbranch_vccnz .LBB0_961
	v_add_co_u32_e32 v130, vcc, 0x60000, v146
	s_nop 1
	v_addc_co_u32_e32 v131, vcc, 0, v147, vcc
	global_load_dwordx2 v[150:151], v[130:131], off offset:1024

.LBB0_965:
	v_pk_mul_f32 v[72:73], v[72:73], v[132:133]
	v_pk_mul_f32 v[70:71], v[70:71], v[130:131]
	v_pk_mul_f32 v[68:69], v[68:69], v[136:137]
	s_and_b64 vcc, exec, s[44:45]
	v_pk_mul_f32 v[66:67], v[66:67], v[134:135]
	s_cbranch_vccnz .LBB0_967
	v_add_co_u32_e32 v134, vcc, 0x18000, v144
	v_cvt_pk_bf16_f32 v130, v70, v71
	v_cvt_pk_bf16_f32 v131, v72, v73
	v_cvt_pk_bf16_f32 v132, v66, v67
	v_cvt_pk_bf16_f32 v133, v68, v69
	s_nop 1
	v_addc_co_u32_e32 v135, vcc, 0, v145, vcc
	global_store_dwordx4 v[134:135], v[130:133], off offset:256
.LBB0_967:
	s_nop 1
	v_add_co_u32_e32 v130, vcc, 0x60000, v146
	v_mov_b32_e32 v148, -1
	s_nop 0
	v_addc_co_u32_e32 v131, vcc, 0, v147, vcc
	global_load_dwordx2 v[152:153], v[130:131], off offset:128
	s_and_b64 vcc, exec, s[42:43]
	v_mov_b32_e32 v149, -1
	s_cbranch_vccnz .LBB0_969
	v_add_co_u32_e32 v130, vcc, 0x60000, v146
	s_nop 1
	v_addc_co_u32_e32 v131, vcc, 0, v147, vcc
	global_load_dwordx2 v[148:149], v[130:131], off offset:1152

.LBB0_973:
	v_pk_mul_f32 v[64:65], v[64:65], v[132:133]
	v_pk_mul_f32 v[62:63], v[62:63], v[130:131]
	v_pk_mul_f32 v[60:61], v[60:61], v[136:137]
	s_and_b64 vcc, exec, s[44:45]
	v_pk_mul_f32 v[58:59], v[58:59], v[134:135]
	s_cbranch_vccnz .LBB0_975
	v_add_co_u32_e32 v134, vcc, 0x40000, v144
	v_cvt_pk_bf16_f32 v130, v62, v63
	v_cvt_pk_bf16_f32 v131, v64, v65
	v_cvt_pk_bf16_f32 v132, v58, v59
	v_cvt_pk_bf16_f32 v133, v60, v61
	s_nop 1
	v_addc_co_u32_e32 v135, vcc, 0, v145, vcc
	global_store_dwordx4 v[134:135], v[130:133], off
.LBB0_975:
	s_nop 1
	v_add_co_u32_e32 v130, vcc, 0x6c000, v146
	v_mov_b32_e32 v150, -1
	s_nop 0
	v_addc_co_u32_e32 v131, vcc, 0, v147, vcc
	global_load_dwordx2 v[154:155], v[130:131], off
	s_and_b64 vcc, exec, s[42:43]
	v_mov_b32_e32 v151, -1
	s_cbranch_vccnz .LBB0_977
	v_add_co_u32_e32 v130, vcc, 0x6c000, v146
	s_nop 1
	v_addc_co_u32_e32 v131, vcc, 0, v147, vcc
	global_load_dwordx2 v[150:151], v[130:131], off offset:1024

.LBB0_981:
	v_pk_mul_f32 v[32:33], v[32:33], v[132:133]
	v_pk_mul_f32 v[30:31], v[30:31], v[130:131]
	v_pk_mul_f32 v[28:29], v[28:29], v[136:137]
	s_and_b64 vcc, exec, s[44:45]
	v_pk_mul_f32 v[26:27], v[26:27], v[134:135]
	s_cbranch_vccnz .LBB0_983
	v_add_co_u32_e32 v134, vcc, 0x40000, v144
	v_cvt_pk_bf16_f32 v130, v30, v31
	v_cvt_pk_bf16_f32 v131, v32, v33
	v_cvt_pk_bf16_f32 v132, v26, v27
	v_cvt_pk_bf16_f32 v133, v28, v29
	s_nop 1
	v_addc_co_u32_e32 v135, vcc, 0, v145, vcc
	global_store_dwordx4 v[134:135], v[130:133], off offset:256
.LBB0_983:
	s_nop 1
	v_add_co_u32_e32 v130, vcc, 0x6c000, v146
	v_mov_b32_e32 v148, -1
	s_nop 0
	v_addc_co_u32_e32 v131, vcc, 0, v147, vcc
	global_load_dwordx2 v[152:153], v[130:131], off offset:128
	s_and_b64 vcc, exec, s[42:43]
	v_mov_b32_e32 v149, -1
	s_cbranch_vccnz .LBB0_985
	v_add_co_u32_e32 v130, vcc, 0x6c000, v146
	s_nop 1
	v_addc_co_u32_e32 v131, vcc, 0, v147, vcc
	global_load_dwordx2 v[148:149], v[130:131], off offset:1152

.LBB0_989:
	v_pk_mul_f32 v[56:57], v[56:57], v[132:133]
	v_pk_mul_f32 v[54:55], v[54:55], v[130:131]
	v_pk_mul_f32 v[52:53], v[52:53], v[136:137]
	s_and_b64 vcc, exec, s[44:45]
	v_pk_mul_f32 v[50:51], v[50:51], v[134:135]
	s_cbranch_vccnz .LBB0_991
	v_add_co_u32_e32 v134, vcc, 0x48000, v144
	v_cvt_pk_bf16_f32 v130, v54, v55
	v_cvt_pk_bf16_f32 v131, v56, v57
	v_cvt_pk_bf16_f32 v132, v50, v51
	v_cvt_pk_bf16_f32 v133, v52, v53
	s_nop 1
	v_addc_co_u32_e32 v135, vcc, 0, v145, vcc
	global_store_dwordx4 v[134:135], v[130:133], off
.LBB0_991:
	s_nop 1
	v_add_co_u32_e32 v130, vcc, 0x78000, v146
	v_mov_b32_e32 v150, -1
	s_nop 0
	v_addc_co_u32_e32 v131, vcc, 0, v147, vcc
	global_load_dwordx2 v[154:155], v[130:131], off
	s_and_b64 vcc, exec, s[42:43]
	v_mov_b32_e32 v151, -1
	s_cbranch_vccnz .LBB0_993
	v_add_co_u32_e32 v130, vcc, 0x78000, v146
	s_nop 1
	v_addc_co_u32_e32 v131, vcc, 0, v147, vcc
	global_load_dwordx2 v[150:151], v[130:131], off offset:1024

.LBB0_997:
	v_pk_mul_f32 v[24:25], v[24:25], v[132:133]
	v_pk_mul_f32 v[22:23], v[22:23], v[130:131]
	v_pk_mul_f32 v[20:21], v[20:21], v[136:137]
	s_and_b64 vcc, exec, s[44:45]
	v_pk_mul_f32 v[18:19], v[18:19], v[134:135]
	s_cbranch_vccnz .LBB0_999
	v_add_co_u32_e32 v134, vcc, 0x48000, v144
	v_cvt_pk_bf16_f32 v130, v22, v23
	v_cvt_pk_bf16_f32 v131, v24, v25
	v_cvt_pk_bf16_f32 v132, v18, v19
	v_cvt_pk_bf16_f32 v133, v20, v21
	s_nop 1
	v_addc_co_u32_e32 v135, vcc, 0, v145, vcc
	global_store_dwordx4 v[134:135], v[130:133], off offset:256
.LBB0_999:
	s_nop 1
	v_add_co_u32_e32 v130, vcc, 0x78000, v146
	v_mov_b32_e32 v148, -1
	s_nop 0
	v_addc_co_u32_e32 v131, vcc, 0, v147, vcc
	global_load_dwordx2 v[152:153], v[130:131], off offset:128
	s_and_b64 vcc, exec, s[42:43]
	v_mov_b32_e32 v149, -1
	s_cbranch_vccnz .LBB0_1001
	v_add_co_u32_e32 v130, vcc, 0x78000, v146
	s_nop 1
	v_addc_co_u32_e32 v131, vcc, 0, v147, vcc
	global_load_dwordx2 v[148:149], v[130:131], off offset:1152

.LBB0_1005:
	v_pk_mul_f32 v[48:49], v[48:49], v[132:133]
	v_pk_mul_f32 v[46:47], v[46:47], v[130:131]
	v_pk_mul_f32 v[44:45], v[44:45], v[136:137]
	s_and_b64 vcc, exec, s[44:45]
	v_pk_mul_f32 v[42:43], v[42:43], v[134:135]
	s_cbranch_vccnz .LBB0_1007
	v_add_co_u32_e32 v134, vcc, 0x50000, v144
	v_cvt_pk_bf16_f32 v130, v46, v47
	v_cvt_pk_bf16_f32 v131, v48, v49
	v_cvt_pk_bf16_f32 v132, v42, v43
	v_cvt_pk_bf16_f32 v133, v44, v45
	s_nop 1
	v_addc_co_u32_e32 v135, vcc, 0, v145, vcc
	global_store_dwordx4 v[134:135], v[130:133], off
.LBB0_1007:
	s_nop 1
	v_add_co_u32_e32 v130, vcc, 0x84000, v146
	v_mov_b32_e32 v150, -1
	s_nop 0
	v_addc_co_u32_e32 v131, vcc, 0, v147, vcc
	global_load_dwordx2 v[154:155], v[130:131], off
	s_and_b64 vcc, exec, s[42:43]
	v_mov_b32_e32 v151, -1
	s_cbranch_vccnz .LBB0_1009
	v_add_co_u32_e32 v130, vcc, 0x84000, v146
	s_nop 1
	v_addc_co_u32_e32 v131, vcc, 0, v147, vcc
	global_load_dwordx2 v[150:151], v[130:131], off offset:1024

.LBB0_1013:
	v_pk_mul_f32 v[16:17], v[16:17], v[132:133]
	v_pk_mul_f32 v[14:15], v[14:15], v[130:131]
	v_pk_mul_f32 v[12:13], v[12:13], v[136:137]
	s_and_b64 vcc, exec, s[44:45]
	v_pk_mul_f32 v[10:11], v[10:11], v[134:135]
	s_cbranch_vccnz .LBB0_1015
	v_add_co_u32_e32 v134, vcc, 0x50000, v144
	v_cvt_pk_bf16_f32 v130, v14, v15
	v_cvt_pk_bf16_f32 v131, v16, v17
	v_cvt_pk_bf16_f32 v132, v10, v11
	v_cvt_pk_bf16_f32 v133, v12, v13
	s_nop 1
	v_addc_co_u32_e32 v135, vcc, 0, v145, vcc
	global_store_dwordx4 v[134:135], v[130:133], off offset:256
.LBB0_1015:
	s_nop 1
	v_add_co_u32_e32 v130, vcc, 0x84000, v146
	v_mov_b32_e32 v148, -1
	s_nop 0
	v_addc_co_u32_e32 v131, vcc, 0, v147, vcc
	global_load_dwordx2 v[152:153], v[130:131], off offset:128
	s_and_b64 vcc, exec, s[42:43]
	v_mov_b32_e32 v149, -1
	s_cbranch_vccnz .LBB0_1017
	v_add_co_u32_e32 v130, vcc, 0x84000, v146
	s_nop 1
	v_addc_co_u32_e32 v131, vcc, 0, v147, vcc
	global_load_dwordx2 v[148:149], v[130:131], off offset:1152
.LBB0_1017:
	s_mov_b64 s[0:1], -1
	s_and_b64 vcc, exec, s[40:41]
	s_waitcnt vmcnt(2)
	v_cvt_f32_ubyte1_e32 v157, v154
	v_cvt_f32_ubyte3_e32 v161, v154
	v_cvt_f32_ubyte2_e32 v160, v154
	v_cvt_f32_ubyte0_e32 v156, v154
	v_cvt_f32_ubyte1_e32 v147, v155
	v_cvt_f32_ubyte0_e32 v146, v155
	v_cvt_f32_ubyte3_e32 v159, v155
	v_cvt_f32_ubyte2_e32 v158, v155
	s_cbranch_vccnz .LBB0_1019
	s_mov_b32 s0, 0x3b808081
	v_pk_mul_f32 v[132:133], v[160:161], s[0:1] op_sel_hi:[1,0]
	v_pk_mul_f32 v[130:131], v[156:157], s[0:1] op_sel_hi:[1,0]
	v_pk_mul_f32 v[136:137], v[158:159], s[0:1] op_sel_hi:[1,0]
	v_pk_mul_f32 v[134:135], v[146:147], s[0:1] op_sel_hi:[1,0]
	s_mov_b64 s[0:1], 0

.LBB0_1021:
	v_pk_mul_f32 v[40:41], v[40:41], v[132:133]
	v_pk_mul_f32 v[38:39], v[38:39], v[130:131]
	v_pk_mul_f32 v[36:37], v[36:37], v[136:137]
	s_and_b64 vcc, exec, s[44:45]
	v_pk_mul_f32 v[34:35], v[34:35], v[134:135]
	s_cbranch_vccnz .LBB0_1023
	v_add_co_u32_e32 v134, vcc, 0x58000, v144
	v_cvt_pk_bf16_f32 v130, v38, v39
	v_cvt_pk_bf16_f32 v131, v40, v41
	v_cvt_pk_bf16_f32 v132, v34, v35
	v_cvt_pk_bf16_f32 v133, v36, v37
	s_nop 1
	v_addc_co_u32_e32 v135, vcc, 0, v145, vcc
	global_store_dwordx4 v[134:135], v[130:133], off
.LBB0_1023:
	s_waitcnt vmcnt(0)
	s_mov_b64 s[0:1], -1
	s_and_b64 vcc, exec, s[40:41]
	v_cvt_f32_ubyte1_e32 v151, v152
	v_cvt_f32_ubyte3_e32 v157, v152
	v_cvt_f32_ubyte2_e32 v156, v152
	v_cvt_f32_ubyte0_e32 v150, v152
	v_cvt_f32_ubyte1_e32 v147, v153
	v_cvt_f32_ubyte0_e32 v146, v153
	v_cvt_f32_ubyte3_e32 v155, v153
	v_cvt_f32_ubyte2_e32 v154, v153
	s_cbranch_vccnz .LBB0_1025
	s_mov_b32 s0, 0x3b808081
	v_pk_mul_f32 v[132:133], v[156:157], s[0:1] op_sel_hi:[1,0]
	v_pk_mul_f32 v[130:131], v[150:151], s[0:1] op_sel_hi:[1,0]
	v_pk_mul_f32 v[136:137], v[154:155], s[0:1] op_sel_hi:[1,0]
	v_pk_mul_f32 v[134:135], v[146:147], s[0:1] op_sel_hi:[1,0]
	s_mov_b64 s[0:1], 0

.LBB0_1027:
	v_pk_mul_f32 v[8:9], v[8:9], v[132:133]
	v_pk_mul_f32 v[6:7], v[6:7], v[130:131]
	v_pk_mul_f32 v[4:5], v[4:5], v[136:137]
	s_and_b64 vcc, exec, s[44:45]
	v_pk_mul_f32 v[2:3], v[2:3], v[134:135]
	s_cbranch_vccnz .LBB0_1029
	v_add_co_u32_e32 v134, vcc, 0x58000, v144
	v_cvt_pk_bf16_f32 v130, v6, v7
	v_cvt_pk_bf16_f32 v131, v8, v9
	v_cvt_pk_bf16_f32 v132, v2, v3
	v_cvt_pk_bf16_f32 v133, v4, v5
	s_nop 1
	v_addc_co_u32_e32 v135, vcc, 0, v145, vcc
	global_store_dwordx4 v[134:135], v[130:133], off offset:256
.LBB0_1029:
	s_and_b64 vcc, exec, s[38:39]
	s_mov_b64 s[38:39], -1
	s_cbranch_vccnz .LBB0_886
	s_and_b64 vcc, exec, s[40:41]
	s_cbranch_vccnz .LBB0_1032
	v_mov_b64_e32 v[2:3], 0
	v_mov_b64_e32 v[4:5], 0
	v_mov_b64_e32 v[6:7], 0
	v_mov_b64_e32 v[8:9], 0
	v_mov_b64_e32 v[10:11], 0
	v_mov_b64_e32 v[12:13], 0
	v_mov_b64_e32 v[14:15], 0
	v_mov_b64_e32 v[16:17], 0
	v_mov_b64_e32 v[18:19], 0
	v_mov_b64_e32 v[20:21], 0
	v_mov_b64_e32 v[22:23], 0
	v_mov_b64_e32 v[24:25], 0
	v_mov_b64_e32 v[26:27], 0
	v_mov_b64_e32 v[28:29], 0
	v_mov_b64_e32 v[30:31], 0
	v_mov_b64_e32 v[32:33], 0
	v_mov_b64_e32 v[34:35], 0
	v_mov_b64_e32 v[36:37], 0
	v_mov_b64_e32 v[38:39], 0
	v_mov_b64_e32 v[40:41], 0
	v_mov_b64_e32 v[42:43], 0
	v_mov_b64_e32 v[44:45], 0
	v_mov_b64_e32 v[46:47], 0
	v_mov_b64_e32 v[48:49], 0
	v_mov_b64_e32 v[50:51], 0
	v_mov_b64_e32 v[52:53], 0
	v_mov_b64_e32 v[54:55], 0
	v_mov_b64_e32 v[56:57], 0
	v_mov_b64_e32 v[58:59], 0
	v_mov_b64_e32 v[60:61], 0
	v_mov_b64_e32 v[62:63], 0
	v_mov_b64_e32 v[64:65], 0
	v_mov_b64_e32 v[66:67], 0
	v_mov_b64_e32 v[68:69], 0
	v_mov_b64_e32 v[70:71], 0
	v_mov_b64_e32 v[72:73], 0
	v_mov_b64_e32 v[74:75], 0
	v_mov_b64_e32 v[76:77], 0
	v_mov_b64_e32 v[78:79], 0
	v_mov_b64_e32 v[80:81], 0
	v_mov_b64_e32 v[82:83], 0
	v_mov_b64_e32 v[84:85], 0
	v_mov_b64_e32 v[86:87], 0
	v_mov_b64_e32 v[88:89], 0
	v_mov_b64_e32 v[90:91], 0
	v_mov_b64_e32 v[92:93], 0
	v_mov_b64_e32 v[94:95], 0
	v_mov_b64_e32 v[96:97], 0
	v_mov_b64_e32 v[98:99], 0
	v_mov_b64_e32 v[100:101], 0
	v_mov_b64_e32 v[102:103], 0
	v_mov_b64_e32 v[104:105], 0
	v_mov_b64_e32 v[106:107], 0
	v_mov_b64_e32 v[108:109], 0
	v_mov_b64_e32 v[110:111], 0
	v_mov_b64_e32 v[112:113], 0
	v_mov_b64_e32 v[114:115], 0
	v_mov_b64_e32 v[116:117], 0
	v_mov_b64_e32 v[118:119], 0
	v_mov_b64_e32 v[120:121], 0
	v_mov_b64_e32 v[122:123], 0
	v_mov_b64_e32 v[124:125], 0
	v_mov_b64_e32 v[126:127], 0
	v_mov_b64_e32 v[128:129], 0

.LBB0_1110:
	s_add_u32 s24, s54, 0x100
	v_mov_b32_e32 v2, 0
	v_lshl_add_u64 v[140:141], s[52:53], 0, v[138:139]
	s_addc_u32 s25, s55, 0
	s_mov_b32 s43, -2
	s_mov_b64 s[54:55], 0
	v_mov_b32_e32 v3, 0
	v_mov_b64_e32 v[4:5], 0
	v_mov_b64_e32 v[6:7], 0
	v_mov_b64_e32 v[8:9], 0
	v_mov_b64_e32 v[18:19], 0
	v_mov_b64_e32 v[20:21], 0
	v_mov_b64_e32 v[22:23], 0
	v_mov_b64_e32 v[24:25], 0
	v_mov_b64_e32 v[34:35], 0
	v_mov_b64_e32 v[36:37], 0
	v_mov_b64_e32 v[38:39], 0
	v_mov_b64_e32 v[40:41], 0
	v_mov_b64_e32 v[50:51], 0
	v_mov_b64_e32 v[52:53], 0
	v_mov_b64_e32 v[54:55], 0
	v_mov_b64_e32 v[56:57], 0
	v_mov_b64_e32 v[10:11], 0
	v_mov_b64_e32 v[12:13], 0
	v_mov_b64_e32 v[14:15], 0
	v_mov_b64_e32 v[16:17], 0
	v_mov_b64_e32 v[26:27], 0
	v_mov_b64_e32 v[28:29], 0
	v_mov_b64_e32 v[30:31], 0
	v_mov_b64_e32 v[32:33], 0
	v_mov_b64_e32 v[42:43], 0
	v_mov_b64_e32 v[44:45], 0
	v_mov_b64_e32 v[46:47], 0
	v_mov_b64_e32 v[48:49], 0
	v_mov_b64_e32 v[58:59], 0
	v_mov_b64_e32 v[60:61], 0
	v_mov_b64_e32 v[62:63], 0
	v_mov_b64_e32 v[64:65], 0
	v_mov_b64_e32 v[66:67], 0
	v_mov_b64_e32 v[68:69], 0
	v_mov_b64_e32 v[70:71], 0
	v_mov_b64_e32 v[72:73], 0
	v_mov_b64_e32 v[82:83], 0
	v_mov_b64_e32 v[84:85], 0
	v_mov_b64_e32 v[86:87], 0
	v_mov_b64_e32 v[88:89], 0
	v_mov_b64_e32 v[98:99], 0
	v_mov_b64_e32 v[100:101], 0
	v_mov_b64_e32 v[102:103], 0
	v_mov_b64_e32 v[104:105], 0
	v_mov_b64_e32 v[114:115], 0
	v_mov_b64_e32 v[116:117], 0
	v_mov_b64_e32 v[118:119], 0
	v_mov_b64_e32 v[120:121], 0
	v_mov_b64_e32 v[74:75], 0
	v_mov_b64_e32 v[76:77], 0
	v_mov_b64_e32 v[78:79], 0
	v_mov_b64_e32 v[80:81], 0
	v_mov_b64_e32 v[90:91], 0
	v_mov_b64_e32 v[92:93], 0
	v_mov_b64_e32 v[94:95], 0
	v_mov_b64_e32 v[96:97], 0
	v_mov_b64_e32 v[106:107], 0
	v_mov_b64_e32 v[108:109], 0
	v_mov_b64_e32 v[110:111], 0
	v_mov_b64_e32 v[112:113], 0
	v_mov_b64_e32 v[122:123], 0
	v_mov_b64_e32 v[124:125], 0
	v_mov_b64_e32 v[126:127], 0
	v_mov_b64_e32 v[128:129], 0

.LBB0_1114:
	s_lshl_b32 s43, s50, 8
	s_add_i32 s52, s43, s61
	s_lshl_b32 s14, s51, 8
	s_ashr_i32 s53, s52, 31
	s_ashr_i32 s15, s14, 31
	s_lshl_b64 s[24:25], s[52:53], 11
	s_add_u32 s24, s57, s24
	s_addc_u32 s25, s58, s25
	s_lshl_b64 s[50:51], s[14:15], 1
	s_add_u32 s14, s24, s50
	s_addc_u32 s15, s25, s51
	s_add_u32 s14, s14, s72
	s_addc_u32 s15, s15, 0
	v_pk_add_f32 v[126:127], v[126:127], 0 op_sel_hi:[1,0]
	v_pk_add_f32 v[136:137], v[124:125], 0 op_sel_hi:[1,0]
	v_pk_add_f32 v[124:125], v[122:123], 0 op_sel_hi:[1,0]
	v_cvt_pk_bf16_f32 v122, v126, v127
	v_lshl_add_u64 v[126:127], s[14:15], 0, v[134:135]
	s_add_i32 s14, s68, s43
	s_ashr_i32 s15, s14, 31
	s_lshl_b64 s[14:15], s[14:15], 11
	s_add_u32 s14, s57, s14
	s_addc_u32 s15, s58, s15
	s_add_u32 s14, s14, s50
	s_addc_u32 s15, s15, s51
	v_pk_add_f32 v[128:129], v[128:129], 0 op_sel_hi:[1,0]
	s_add_u32 s14, s14, s72
	v_cvt_pk_bf16_f32 v123, v128, v129
	v_cvt_pk_bf16_f32 v124, v124, v125
	v_cvt_pk_bf16_f32 v125, v136, v137
	global_store_dwordx4 v[126:127], v[122:125], off
	v_pk_add_f32 v[120:121], v[120:121], 0 op_sel_hi:[1,0]
	v_pk_add_f32 v[118:119], v[118:119], 0 op_sel_hi:[1,0]
	v_pk_add_f32 v[122:123], v[116:117], 0 op_sel_hi:[1,0]
	v_pk_add_f32 v[116:117], v[114:115], 0 op_sel_hi:[1,0]
	v_cvt_pk_bf16_f32 v114, v118, v119
	v_cvt_pk_bf16_f32 v115, v120, v121
	s_addc_u32 s15, s15, 0
	v_pk_add_f32 v[110:111], v[110:111], 0 op_sel_hi:[1,0]
	v_cvt_pk_bf16_f32 v116, v116, v117
	v_cvt_pk_bf16_f32 v117, v122, v123
	global_store_dwordx4 v[126:127], v[114:117], off offset:256
	v_pk_add_f32 v[112:113], v[112:113], 0 op_sel_hi:[1,0]
	v_pk_add_f32 v[104:105], v[104:105], 0 op_sel_hi:[1,0]
	v_pk_add_f32 v[114:115], v[108:109], 0 op_sel_hi:[1,0]
	v_pk_add_f32 v[108:109], v[106:107], 0 op_sel_hi:[1,0]
	v_cvt_pk_bf16_f32 v106, v110, v111
	v_lshl_add_u64 v[110:111], s[14:15], 0, v[134:135]
	s_add_i32 s14, s69, s43
	s_ashr_i32 s15, s14, 31
	s_lshl_b64 s[14:15], s[14:15], 11
	s_add_u32 s14, s57, s14
	s_addc_u32 s15, s58, s15
	s_add_u32 s14, s14, s50
	s_addc_u32 s15, s15, s51
	v_cvt_pk_bf16_f32 v107, v112, v113
	s_add_u32 s14, s14, s72
	v_cvt_pk_bf16_f32 v108, v108, v109
	v_cvt_pk_bf16_f32 v109, v114, v115
	global_store_dwordx4 v[110:111], v[106:109], off
	v_pk_add_f32 v[102:103], v[102:103], 0 op_sel_hi:[1,0]
	s_addc_u32 s15, s15, 0
	v_pk_add_f32 v[106:107], v[100:101], 0 op_sel_hi:[1,0]
	v_pk_add_f32 v[100:101], v[98:99], 0 op_sel_hi:[1,0]
	v_cvt_pk_bf16_f32 v98, v102, v103
	v_cvt_pk_bf16_f32 v99, v104, v105
	v_pk_add_f32 v[94:95], v[94:95], 0 op_sel_hi:[1,0]
	v_cvt_pk_bf16_f32 v100, v100, v101
	v_cvt_pk_bf16_f32 v101, v106, v107
	global_store_dwordx4 v[110:111], v[98:101], off offset:256
	v_pk_add_f32 v[96:97], v[96:97], 0 op_sel_hi:[1,0]
	v_pk_add_f32 v[88:89], v[88:89], 0 op_sel_hi:[1,0]
	v_pk_add_f32 v[98:99], v[92:93], 0 op_sel_hi:[1,0]
	v_pk_add_f32 v[92:93], v[90:91], 0 op_sel_hi:[1,0]
	v_cvt_pk_bf16_f32 v90, v94, v95
	v_lshl_add_u64 v[94:95], s[14:15], 0, v[134:135]
	s_add_i32 s14, s70, s43
	s_ashr_i32 s15, s14, 31
	s_lshl_b64 s[14:15], s[14:15], 11
	s_add_u32 s14, s57, s14
	s_addc_u32 s15, s58, s15
	s_add_u32 s14, s14, s50
	s_addc_u32 s15, s15, s51
	v_cvt_pk_bf16_f32 v91, v96, v97
	s_add_u32 s14, s14, s72
	v_cvt_pk_bf16_f32 v92, v92, v93
	v_cvt_pk_bf16_f32 v93, v98, v99
	global_store_dwordx4 v[94:95], v[90:93], off
	v_pk_add_f32 v[86:87], v[86:87], 0 op_sel_hi:[1,0]
	s_addc_u32 s15, s15, 0
	v_pk_add_f32 v[90:91], v[84:85], 0 op_sel_hi:[1,0]
	v_pk_add_f32 v[84:85], v[82:83], 0 op_sel_hi:[1,0]
	v_cvt_pk_bf16_f32 v82, v86, v87
	v_cvt_pk_bf16_f32 v83, v88, v89
	v_pk_add_f32 v[78:79], v[78:79], 0 op_sel_hi:[1,0]
	v_cvt_pk_bf16_f32 v84, v84, v85
	v_cvt_pk_bf16_f32 v85, v90, v91
	global_store_dwordx4 v[94:95], v[82:85], off offset:256
	v_pk_add_f32 v[80:81], v[80:81], 0 op_sel_hi:[1,0]
	v_pk_add_f32 v[72:73], v[72:73], 0 op_sel_hi:[1,0]
	v_pk_add_f32 v[82:83], v[76:77], 0 op_sel_hi:[1,0]
	v_pk_add_f32 v[76:77], v[74:75], 0 op_sel_hi:[1,0]
	v_cvt_pk_bf16_f32 v74, v78, v79
	v_lshl_add_u64 v[78:79], s[14:15], 0, v[134:135]
	s_add_i32 s14, s52, 0x80
	s_ashr_i32 s15, s14, 31
	s_lshl_b64 s[14:15], s[14:15], 11
	s_add_u32 s14, s57, s14
	s_addc_u32 s15, s58, s15
	s_add_u32 s14, s14, s50
	s_addc_u32 s15, s15, s51
	v_cvt_pk_bf16_f32 v75, v80, v81
	s_add_u32 s14, s14, s72
	v_cvt_pk_bf16_f32 v76, v76, v77
	v_cvt_pk_bf16_f32 v77, v82, v83
	global_store_dwordx4 v[78:79], v[74:77], off
	v_pk_add_f32 v[70:71], v[70:71], 0 op_sel_hi:[1,0]
	s_addc_u32 s15, s15, 0
	v_pk_add_f32 v[74:75], v[68:69], 0 op_sel_hi:[1,0]
	v_pk_add_f32 v[68:69], v[66:67], 0 op_sel_hi:[1,0]
	v_cvt_pk_bf16_f32 v66, v70, v71
	v_cvt_pk_bf16_f32 v67, v72, v73
	v_pk_add_f32 v[62:63], v[62:63], 0 op_sel_hi:[1,0]
	v_cvt_pk_bf16_f32 v68, v68, v69
	v_cvt_pk_bf16_f32 v69, v74, v75
	global_store_dwordx4 v[78:79], v[66:69], off offset:256
	v_pk_add_f32 v[64:65], v[64:65], 0 op_sel_hi:[1,0]
	v_pk_add_f32 v[56:57], v[56:57], 0 op_sel_hi:[1,0]
	v_pk_add_f32 v[66:67], v[60:61], 0 op_sel_hi:[1,0]
	v_pk_add_f32 v[60:61], v[58:59], 0 op_sel_hi:[1,0]
	v_cvt_pk_bf16_f32 v58, v62, v63
	v_lshl_add_u64 v[62:63], s[14:15], 0, v[134:135]
	s_add_i32 s14, s52, 0x90
	s_ashr_i32 s15, s14, 31
	s_lshl_b64 s[14:15], s[14:15], 11
	s_add_u32 s14, s57, s14
	s_addc_u32 s15, s58, s15
	s_add_u32 s14, s14, s50
	s_addc_u32 s15, s15, s51
	v_cvt_pk_bf16_f32 v59, v64, v65
	s_add_u32 s14, s14, s72
	v_cvt_pk_bf16_f32 v60, v60, v61
	v_cvt_pk_bf16_f32 v61, v66, v67
	global_store_dwordx4 v[62:63], v[58:61], off
	v_pk_add_f32 v[54:55], v[54:55], 0 op_sel_hi:[1,0]
	s_addc_u32 s15, s15, 0
	v_pk_add_f32 v[58:59], v[52:53], 0 op_sel_hi:[1,0]
	v_pk_add_f32 v[52:53], v[50:51], 0 op_sel_hi:[1,0]
	v_cvt_pk_bf16_f32 v50, v54, v55
	v_cvt_pk_bf16_f32 v51, v56, v57
	v_pk_add_f32 v[46:47], v[46:47], 0 op_sel_hi:[1,0]
	v_cvt_pk_bf16_f32 v52, v52, v53
	v_cvt_pk_bf16_f32 v53, v58, v59
	global_store_dwordx4 v[62:63], v[50:53], off offset:256
	v_pk_add_f32 v[48:49], v[48:49], 0 op_sel_hi:[1,0]
	v_pk_add_f32 v[40:41], v[40:41], 0 op_sel_hi:[1,0]
	v_pk_add_f32 v[50:51], v[44:45], 0 op_sel_hi:[1,0]
	v_pk_add_f32 v[44:45], v[42:43], 0 op_sel_hi:[1,0]
	v_cvt_pk_bf16_f32 v42, v46, v47
	v_lshl_add_u64 v[46:47], s[14:15], 0, v[134:135]
	s_add_i32 s14, s52, 0xa0
	s_ashr_i32 s15, s14, 31
	s_lshl_b64 s[14:15], s[14:15], 11
	s_add_u32 s14, s57, s14
	s_addc_u32 s15, s58, s15
	s_add_u32 s14, s14, s50
	s_addc_u32 s15, s15, s51
	v_cvt_pk_bf16_f32 v43, v48, v49
	s_add_u32 s14, s14, s72
	v_cvt_pk_bf16_f32 v44, v44, v45
	v_cvt_pk_bf16_f32 v45, v50, v51
	global_store_dwordx4 v[46:47], v[42:45], off
	v_pk_add_f32 v[38:39], v[38:39], 0 op_sel_hi:[1,0]
	s_addc_u32 s15, s15, 0
	v_pk_add_f32 v[42:43], v[36:37], 0 op_sel_hi:[1,0]
	v_pk_add_f32 v[36:37], v[34:35], 0 op_sel_hi:[1,0]
	v_cvt_pk_bf16_f32 v34, v38, v39
	v_cvt_pk_bf16_f32 v35, v40, v41
	v_pk_add_f32 v[30:31], v[30:31], 0 op_sel_hi:[1,0]
	v_cvt_pk_bf16_f32 v36, v36, v37
	v_cvt_pk_bf16_f32 v37, v42, v43
	global_store_dwordx4 v[46:47], v[34:37], off offset:256
	v_pk_add_f32 v[32:33], v[32:33], 0 op_sel_hi:[1,0]
	v_pk_add_f32 v[24:25], v[24:25], 0 op_sel_hi:[1,0]
	v_pk_add_f32 v[34:35], v[28:29], 0 op_sel_hi:[1,0]
	v_pk_add_f32 v[28:29], v[26:27], 0 op_sel_hi:[1,0]
	v_cvt_pk_bf16_f32 v26, v30, v31
	v_lshl_add_u64 v[30:31], s[14:15], 0, v[134:135]
	s_add_i32 s14, s52, 0xb0
	s_ashr_i32 s15, s14, 31
	s_lshl_b64 s[14:15], s[14:15], 11
	s_add_u32 s14, s57, s14
	s_addc_u32 s15, s58, s15
	s_add_u32 s14, s14, s50
	s_addc_u32 s15, s15, s51
	v_cvt_pk_bf16_f32 v27, v32, v33
	s_add_u32 s14, s14, s72
	v_cvt_pk_bf16_f32 v28, v28, v29
	v_cvt_pk_bf16_f32 v29, v34, v35
	global_store_dwordx4 v[30:31], v[26:29], off
	v_pk_add_f32 v[22:23], v[22:23], 0 op_sel_hi:[1,0]
	s_addc_u32 s15, s15, 0
	v_pk_add_f32 v[26:27], v[20:21], 0 op_sel_hi:[1,0]
	v_pk_add_f32 v[20:21], v[18:19], 0 op_sel_hi:[1,0]
	v_cvt_pk_bf16_f32 v18, v22, v23
	v_cvt_pk_bf16_f32 v19, v24, v25
	v_pk_add_f32 v[14:15], v[14:15], 0 op_sel_hi:[1,0]
	v_cvt_pk_bf16_f32 v20, v20, v21
	v_cvt_pk_bf16_f32 v21, v26, v27
	global_store_dwordx4 v[30:31], v[18:21], off offset:256
	v_pk_add_f32 v[16:17], v[16:17], 0 op_sel_hi:[1,0]
	s_andn2_b64 vcc, exec, s[38:39]
	v_pk_add_f32 v[18:19], v[12:13], 0 op_sel_hi:[1,0]
	v_pk_add_f32 v[12:13], v[10:11], 0 op_sel_hi:[1,0]
	v_cvt_pk_bf16_f32 v10, v14, v15
	v_cvt_pk_bf16_f32 v11, v16, v17
	v_lshl_add_u64 v[14:15], s[14:15], 0, v[134:135]
	v_cvt_pk_bf16_f32 v12, v12, v13
	v_cvt_pk_bf16_f32 v13, v18, v19
	global_store_dwordx4 v[14:15], v[10:13], off
	s_mov_b64 s[14:15], -1
	v_pk_add_f32 v[8:9], v[8:9], 0 op_sel_hi:[1,0]
	v_pk_add_f32 v[10:11], v[4:5], 0 op_sel_hi:[1,0]
	v_pk_add_f32 v[4:5], v[2:3], 0 op_sel_hi:[1,0]
	v_pk_add_f32 v[6:7], v[6:7], 0 op_sel_hi:[1,0]
	s_nop 0
	v_cvt_pk_bf16_f32 v2, v6, v7
	v_cvt_pk_bf16_f32 v3, v8, v9
	v_cvt_pk_bf16_f32 v4, v4, v5
	v_cvt_pk_bf16_f32 v5, v10, v11
	global_store_dwordx4 v[14:15], v[2:5], off offset:256
	s_cbranch_vccnz .LBB0_1101
	s_andn2_b64 vcc, exec, s[0:1]
	s_cbranch_vccnz .LBB0_1100
	s_barrier
	s_branch .LBB0_1100

.LBB0_1235:
	v_lshl_add_u64 v[68:69], v[64:65], 0, v[56:57]
	v_lshl_add_u64 v[70:71], v[66:67], 0, v[56:57]
	v_add_u32_e32 v59, s2, v111
	global_load_dwordx4 v[122:125], v[68:69], off
	global_load_dwordx4 v[126:129], v[70:71], off
	v_add_u32_e32 v84, 0x11200, v59
	v_add_u32_e32 v85, 0x19300, v59
	ds_read_b128 v[196:199], v59 offset:4096
	ds_read_b128 v[200:203], v59 offset:37120
	ds_read_b128 v[204:207], v84
	ds_read_b128 v[208:211], v85
	global_load_dwordx4 v[130:133], v[68:69], off offset:64
	global_load_dwordx4 v[134:137], v[70:71], off offset:64
	global_load_dwordx4 v[138:141], v[68:69], off offset:128
	global_load_dwordx4 v[142:145], v[70:71], off offset:128
	global_load_dwordx4 v[146:149], v[68:69], off offset:192
	global_load_dwordx4 v[150:153], v[70:71], off offset:192
	global_load_dwordx4 v[154:157], v[68:69], off offset:256
	global_load_dwordx4 v[158:161], v[70:71], off offset:256
	global_load_dwordx4 v[162:165], v[68:69], off offset:320
	global_load_dwordx4 v[166:169], v[70:71], off offset:320
	global_load_dwordx4 v[170:173], v[68:69], off offset:384
	global_load_dwordx4 v[174:177], v[70:71], off offset:384
	global_load_dwordx4 v[178:181], v[68:69], off offset:448
	global_load_dwordx4 v[182:185], v[70:71], off offset:448
	v_lshl_add_u64 v[64:65], v[64:65], 0, s[94:95]
	v_lshl_add_u64 v[66:67], v[66:67], 0, s[94:95]
	ds_read_b128 v[212:215], v59 offset:4160
	ds_read_b128 v[216:219], v59 offset:37184
	ds_read_b128 v[220:223], v84 offset:64
	ds_read_b128 v[240:243], v85 offset:64
	s_waitcnt vmcnt(14) lgkmcnt(4)
	v_mfma_f32_16x16x32_bf16 v[10:13], v[196:199], v[122:125], v[10:13]
	v_mfma_f32_16x16x32_bf16 v[6:9], v[196:199], v[126:129], v[6:9]
	v_mfma_f32_16x16x32_bf16 v[26:29], v[200:203], v[122:125], v[26:29]
	v_mfma_f32_16x16x32_bf16 v[22:25], v[200:203], v[126:129], v[22:25]
	v_mfma_f32_16x16x32_bf16 v[18:21], v[204:207], v[122:125], v[18:21]
	v_mfma_f32_16x16x32_bf16 v[14:17], v[204:207], v[126:129], v[14:17]
	v_mfma_f32_16x16x32_bf16 v[34:37], v[208:211], v[122:125], v[34:37]
	v_mfma_f32_16x16x32_bf16 v[30:33], v[208:211], v[126:129], v[30:33]
	ds_read_b128 v[196:199], v59 offset:4224
	ds_read_b128 v[200:203], v59 offset:37248
	ds_read_b128 v[204:207], v84 offset:128
	ds_read_b128 v[208:211], v85 offset:128
	s_waitcnt vmcnt(12) lgkmcnt(4)
	v_mfma_f32_16x16x32_bf16 v[10:13], v[212:215], v[130:133], v[10:13]
	v_mfma_f32_16x16x32_bf16 v[6:9], v[212:215], v[134:137], v[6:9]
	v_mfma_f32_16x16x32_bf16 v[26:29], v[216:219], v[130:133], v[26:29]
	v_mfma_f32_16x16x32_bf16 v[22:25], v[216:219], v[134:137], v[22:25]
	v_mfma_f32_16x16x32_bf16 v[18:21], v[220:223], v[130:133], v[18:21]
	v_mfma_f32_16x16x32_bf16 v[14:17], v[220:223], v[134:137], v[14:17]
	v_mfma_f32_16x16x32_bf16 v[34:37], v[240:243], v[130:133], v[34:37]
	v_mfma_f32_16x16x32_bf16 v[30:33], v[240:243], v[134:137], v[30:33]
	ds_read_b128 v[212:215], v59 offset:4288
	ds_read_b128 v[216:219], v59 offset:37312
	ds_read_b128 v[220:223], v84 offset:192
	ds_read_b128 v[240:243], v85 offset:192
	s_waitcnt vmcnt(10) lgkmcnt(4)
	v_mfma_f32_16x16x32_bf16 v[10:13], v[196:199], v[138:141], v[10:13]
	v_mfma_f32_16x16x32_bf16 v[6:9], v[196:199], v[142:145], v[6:9]
	v_mfma_f32_16x16x32_bf16 v[26:29], v[200:203], v[138:141], v[26:29]
	v_mfma_f32_16x16x32_bf16 v[22:25], v[200:203], v[142:145], v[22:25]
	v_mfma_f32_16x16x32_bf16 v[18:21], v[204:207], v[138:141], v[18:21]
	v_mfma_f32_16x16x32_bf16 v[14:17], v[204:207], v[142:145], v[14:17]
	v_mfma_f32_16x16x32_bf16 v[34:37], v[208:211], v[138:141], v[34:37]
	v_mfma_f32_16x16x32_bf16 v[30:33], v[208:211], v[142:145], v[30:33]
	ds_read_b128 v[196:199], v59 offset:4352
	ds_read_b128 v[200:203], v59 offset:37376
	ds_read_b128 v[204:207], v84 offset:256
	ds_read_b128 v[208:211], v85 offset:256
	s_waitcnt vmcnt(8) lgkmcnt(4)
	v_mfma_f32_16x16x32_bf16 v[10:13], v[212:215], v[146:149], v[10:13]
	v_mfma_f32_16x16x32_bf16 v[6:9], v[212:215], v[150:153], v[6:9]
	v_mfma_f32_16x16x32_bf16 v[26:29], v[216:219], v[146:149], v[26:29]
	v_mfma_f32_16x16x32_bf16 v[22:25], v[216:219], v[150:153], v[22:25]
	v_mfma_f32_16x16x32_bf16 v[18:21], v[220:223], v[146:149], v[18:21]
	v_mfma_f32_16x16x32_bf16 v[14:17], v[220:223], v[150:153], v[14:17]
	v_mfma_f32_16x16x32_bf16 v[34:37], v[240:243], v[146:149], v[34:37]
	v_mfma_f32_16x16x32_bf16 v[30:33], v[240:243], v[150:153], v[30:33]
	ds_read_b128 v[212:215], v59 offset:4416
	ds_read_b128 v[216:219], v59 offset:37440
	ds_read_b128 v[220:223], v84 offset:320
	ds_read_b128 v[240:243], v85 offset:320
	s_waitcnt vmcnt(6) lgkmcnt(4)
	v_mfma_f32_16x16x32_bf16 v[10:13], v[196:199], v[154:157], v[10:13]
	v_mfma_f32_16x16x32_bf16 v[6:9], v[196:199], v[158:161], v[6:9]
	v_mfma_f32_16x16x32_bf16 v[26:29], v[200:203], v[154:157], v[26:29]
	v_mfma_f32_16x16x32_bf16 v[22:25], v[200:203], v[158:161], v[22:25]
	v_mfma_f32_16x16x32_bf16 v[18:21], v[204:207], v[154:157], v[18:21]
	v_mfma_f32_16x16x32_bf16 v[14:17], v[204:207], v[158:161], v[14:17]
	v_mfma_f32_16x16x32_bf16 v[34:37], v[208:211], v[154:157], v[34:37]
	v_mfma_f32_16x16x32_bf16 v[30:33], v[208:211], v[158:161], v[30:33]
	ds_read_b128 v[196:199], v59 offset:4480
	ds_read_b128 v[200:203], v59 offset:37504
	ds_read_b128 v[204:207], v84 offset:384
	ds_read_b128 v[208:211], v85 offset:384
	s_waitcnt vmcnt(4) lgkmcnt(4)
	v_mfma_f32_16x16x32_bf16 v[10:13], v[212:215], v[162:165], v[10:13]
	v_mfma_f32_16x16x32_bf16 v[6:9], v[212:215], v[166:169], v[6:9]
	v_mfma_f32_16x16x32_bf16 v[26:29], v[216:219], v[162:165], v[26:29]
	v_mfma_f32_16x16x32_bf16 v[22:25], v[216:219], v[166:169], v[22:25]
	v_mfma_f32_16x16x32_bf16 v[18:21], v[220:223], v[162:165], v[18:21]
	v_mfma_f32_16x16x32_bf16 v[14:17], v[220:223], v[166:169], v[14:17]
	v_mfma_f32_16x16x32_bf16 v[34:37], v[240:243], v[162:165], v[34:37]
	v_mfma_f32_16x16x32_bf16 v[30:33], v[240:243], v[166:169], v[30:33]
	ds_read_b128 v[212:215], v59 offset:4544
	ds_read_b128 v[216:219], v59 offset:37568
	ds_read_b128 v[220:223], v84 offset:448
	ds_read_b128 v[240:243], v85 offset:448
	s_waitcnt vmcnt(2) lgkmcnt(4)
	v_mfma_f32_16x16x32_bf16 v[10:13], v[196:199], v[170:173], v[10:13]
	v_mfma_f32_16x16x32_bf16 v[6:9], v[196:199], v[174:177], v[6:9]
	v_mfma_f32_16x16x32_bf16 v[26:29], v[200:203], v[170:173], v[26:29]
	v_mfma_f32_16x16x32_bf16 v[22:25], v[200:203], v[174:177], v[22:25]
	v_mfma_f32_16x16x32_bf16 v[18:21], v[204:207], v[170:173], v[18:21]
	v_mfma_f32_16x16x32_bf16 v[14:17], v[204:207], v[174:177], v[14:17]
	v_mfma_f32_16x16x32_bf16 v[34:37], v[208:211], v[170:173], v[34:37]
	v_mfma_f32_16x16x32_bf16 v[30:33], v[208:211], v[174:177], v[30:33]
	s_waitcnt vmcnt(0) lgkmcnt(0)
	v_mfma_f32_16x16x32_bf16 v[10:13], v[212:215], v[178:181], v[10:13]
	v_mfma_f32_16x16x32_bf16 v[6:9], v[212:215], v[182:185], v[6:9]
	v_mfma_f32_16x16x32_bf16 v[26:29], v[216:219], v[178:181], v[26:29]
	v_mfma_f32_16x16x32_bf16 v[22:25], v[216:219], v[182:185], v[22:25]
	v_mfma_f32_16x16x32_bf16 v[18:21], v[220:223], v[178:181], v[18:21]
	v_mfma_f32_16x16x32_bf16 v[14:17], v[220:223], v[182:185], v[14:17]
	v_mfma_f32_16x16x32_bf16 v[34:37], v[240:243], v[178:181], v[34:37]
	v_mfma_f32_16x16x32_bf16 v[30:33], v[240:243], v[182:185], v[30:33]
	s_addk_i32 s2, 0x200
	s_cmpk_eq_i32 s2, 0x800
	s_cbranch_scc0 .LBB0_1235
	ds_read_b32 v68, v110 offset:1024
	ds_read_b32 v70, v110 offset:1152
	ds_read_b32 v69, v110 offset:1028
	ds_read_b32 v71, v110 offset:1156
	ds_read_b32 v72, v110 offset:1032
	ds_read_b32 v74, v110 offset:1160
	ds_read_b32 v73, v110 offset:1036
	ds_read_b32 v75, v110 offset:1164
	ds_read_b32 v191, v110 offset:1088
	v_add_f32_e32 v60, v26, v34
	v_pk_add_f32 v[22:23], v[22:23], v[30:31]
	v_pk_add_f32 v[24:25], v[24:25], v[32:33]
	v_pk_add_f32 v[10:11], v[10:11], v[18:19]
	s_waitcnt lgkmcnt(0)
	v_pk_mul_f32 v[64:65], v[60:61], v[190:191]
	ds_read_b32 v26, v110 offset:1216
	ds_read_b32 v191, v110 offset:1092
	v_add_f32_e32 v60, v27, v35
	v_pk_add_f32 v[6:7], v[6:7], v[14:15]
	v_pk_add_f32 v[12:13], v[12:13], v[20:21]
	v_pk_add_f32 v[8:9], v[8:9], v[16:17]
	s_waitcnt lgkmcnt(0)
	v_pk_mul_f32 v[34:35], v[60:61], v[190:191]
	ds_read_b32 v27, v110 offset:1220
	ds_read_b32 v191, v110 offset:1096
	v_add_f32_e32 v60, v28, v36
	v_mov_b32_e32 v28, v64
	v_pk_fma_f32 v[6:7], v[10:11], s[36:37], v[6:7] op_sel_hi:[1,0,1]
	v_mov_b32_e32 v10, v61
	s_waitcnt lgkmcnt(0)
	v_pk_mul_f32 v[66:67], v[60:61], v[190:191]
	ds_read_b32 v36, v110 offset:1224
	ds_read_b32 v191, v110 offset:1100
	v_add_f32_e32 v60, v29, v37
	v_mov_b32_e32 v29, v34
	ds_read_b32 v37, v110 offset:1228
	v_pk_add_f32 v[22:23], v[28:29], v[22:23]
	v_mov_b32_e32 v34, v65
	s_waitcnt lgkmcnt(1)
	v_pk_mul_f32 v[76:77], v[60:61], v[190:191]
	v_pk_add_f32 v[22:23], v[22:23], v[34:35] neg_lo:[0,1] neg_hi:[0,1]
	v_mov_b32_e32 v30, v66
	v_pk_fma_f32 v[22:23], v[62:63], v[22:23], v[26:27] op_sel_hi:[0,1,1]
	v_mov_b32_e32 v31, v76
	v_ashrrev_i32_e32 v26, 31, v23
	v_pk_add_f32 v[24:25], v[30:31], v[24:25]
	v_mov_b32_e32 v76, v67
	v_and_b32_e32 v26, 0x7fffffe0, v26
	v_ashrrev_i32_e32 v27, 31, v22
	v_and_b32_e32 v28, 0xffffffe0, v23
	v_pk_add_f32 v[24:25], v[24:25], v[76:77] neg_lo:[0,1] neg_hi:[0,1]
	v_and_b32_e32 v27, 0x7fffffe0, v27
	v_and_b32_e32 v29, 0xffffffe0, v22
	v_xor_b32_e32 v26, v26, v28
	s_waitcnt lgkmcnt(0)
	v_pk_fma_f32 v[24:25], v[62:63], v[24:25], v[36:37] op_sel_hi:[0,1,1]
	v_xor_b32_e32 v27, v27, v29
	v_or_b32_e32 v28, v26, v5
	v_ashrrev_i32_e32 v26, 31, v25
	v_ashrrev_i32_e32 v29, 31, v24
	v_or_b32_e32 v27, v27, v46
	v_and_b32_e32 v26, 0x7fffffe0, v26
	v_and_b32_e32 v29, 0x7fffffe0, v29
	v_and_b32_e32 v30, 0xffffffe0, v25
	v_and_b32_e32 v31, 0xffffffe0, v24
	v_xor_b32_e32 v26, v26, v30
	v_xor_b32_e32 v29, v29, v31
	ds_bpermute_b32 v30, v108, v27
	v_or_b32_e32 v31, v29, v48
	v_or_b32_e32 v26, v26, v47
	v_cmp_gt_i32_e32 vcc, v31, v27
	ds_bpermute_b32 v29, v108, v28
	ds_bpermute_b32 v32, v108, v26
	v_cndmask_b32_e64 v59, 0, 1, vcc
	v_cmp_gt_i32_e32 vcc, v31, v28
	v_pk_fma_f32 v[8:9], v[12:13], s[36:37], v[8:9] op_sel_hi:[1,0,1]
	v_pk_fma_f32 v[12:13], v[10:11], v[68:69], v[6:7] op_sel_hi:[0,1,1] neg_lo:[1,0,0] neg_hi:[1,0,0]
	v_cndmask_b32_e64 v36, 0, 1, vcc
	v_cmp_gt_i32_e32 vcc, v28, v31
	v_pk_fma_f32 v[6:7], v[10:11], v[72:73], v[8:9] op_sel_hi:[0,1,1] neg_lo:[1,0,0] neg_hi:[1,0,0]
	v_pk_fma_f32 v[8:9], v[62:63], v[12:13], v[70:71] op_sel_hi:[0,1,1]
	v_cndmask_b32_e64 v34, 0, 1, vcc
	s_waitcnt lgkmcnt(2)
	v_cmp_gt_i32_e32 vcc, v30, v27
	v_pk_fma_f32 v[6:7], v[62:63], v[6:7], v[74:75] op_sel_hi:[0,1,1]
	v_and_b32_e32 v14, 0xffffffe0, v9
	v_cndmask_b32_e64 v65, 0, 1, vcc
	v_cmp_gt_i32_e32 vcc, v30, v28
	v_and_b32_e32 v15, 0xffffffe0, v8
	v_and_b32_e32 v16, 0xffffffe0, v6
	v_cndmask_b32_e64 v60, 0, 1, vcc
	s_waitcnt lgkmcnt(1)
	v_cmp_gt_i32_e32 vcc, v29, v31
	v_and_b32_e32 v17, 0xffffffe0, v7
	ds_bpermute_b32 v132, v109, v27
	v_cndmask_b32_e64 v35, 0, 1, vcc
	s_waitcnt lgkmcnt(1)
	v_cmp_gt_i32_e32 vcc, v32, v27
	ds_bpermute_b32 v141, v109, v31
	ds_bpermute_b32 v168, v115, v27
	v_cndmask_b32_e64 v66, 0, 1, vcc
	v_cmp_gt_i32_e32 vcc, v32, v28
	ds_bpermute_b32 v177, v115, v31
	ds_bpermute_b32 v33, v108, v31
	v_cndmask_b32_e64 v64, 0, 1, vcc
	v_cmp_gt_i32_e32 vcc, v32, v31
	ds_bpermute_b32 v144, v109, v28
	ds_bpermute_b32 v153, v109, v26
	v_cndmask_b32_e64 v37, 0, 1, vcc
	v_cmp_lt_i32_e32 vcc, -1, v9
	ds_bpermute_b32 v180, v115, v28
	ds_bpermute_b32 v192, v115, v26
	v_cndmask_b32_e64 v11, v237, 0, vcc
	v_cmp_lt_i32_e32 vcc, -1, v8
	v_bitop3_b32 v11, v11, v1, v14 bitop3:0xde
	ds_bpermute_b32 v126, v109, v11
	v_cndmask_b32_e64 v10, v237, 0, vcc
	v_cmp_lt_i32_e32 vcc, -1, v6
	v_bitop3_b32 v10, v10, v2, v15 bitop3:0xde
	ds_bpermute_b32 v18, v108, v10
	v_cndmask_b32_e64 v13, v237, 0, vcc
	v_cmp_lt_i32_e32 vcc, -1, v7
	v_bitop3_b32 v13, v13, v4, v16 bitop3:0xde
	ds_bpermute_b32 v16, v108, v11
	v_cndmask_b32_e64 v12, v237, 0, vcc
	v_cmp_gt_i32_e32 vcc, v11, v10
	v_bitop3_b32 v12, v12, v3, v17 bitop3:0xde
	ds_bpermute_b32 v17, v108, v13
	v_cndmask_b32_e64 v14, 0, 1, vcc
	v_cmp_gt_i32_e32 vcc, v13, v10
	ds_bpermute_b32 v123, v109, v13
	ds_bpermute_b32 v150, v115, v10
	v_cndmask_b32_e64 v15, 0, 1, vcc
	v_cmp_gt_i32_e32 vcc, v12, v10
	ds_bpermute_b32 v159, v115, v13
	ds_bpermute_b32 v135, v109, v12
	v_addc_co_u32_e32 v19, vcc, v15, v14, vcc
	v_cmp_gt_i32_e32 vcc, v27, v10
	ds_bpermute_b32 v162, v115, v11
	ds_bpermute_b32 v171, v115, v12
	v_cndmask_b32_e64 v20, 0, 1, vcc
	v_cmp_gt_i32_e32 vcc, v31, v10
	s_movk_i32 s2, 0xff
	s_nop 0
	v_cndmask_b32_e64 v21, 0, 1, vcc
	v_cmp_gt_i32_e32 vcc, v10, v11
	s_nop 1
	v_cndmask_b32_e64 v14, 0, 1, vcc
	v_cmp_gt_i32_e32 vcc, v13, v11
	s_nop 1
	v_cndmask_b32_e64 v15, 0, 1, vcc
	v_cmp_gt_i32_e32 vcc, v12, v11
	s_nop 1
	v_addc_co_u32_e32 v61, vcc, v15, v14, vcc
	v_cmp_gt_i32_e32 vcc, v27, v11
	s_nop 1
	v_cndmask_b32_e64 v62, 0, 1, vcc
	v_cmp_gt_i32_e32 vcc, v31, v11
	s_nop 1
	v_cndmask_b32_e64 v67, 0, 1, vcc
	v_cmp_gt_i32_e32 vcc, v10, v13
	s_nop 1
	v_cndmask_b32_e64 v14, 0, 1, vcc
	v_cmp_gt_i32_e32 vcc, v11, v13
	s_nop 1
	v_cndmask_b32_e64 v15, 0, 1, vcc
	v_cmp_gt_i32_e32 vcc, v12, v13
	s_nop 1
	v_addc_co_u32_e32 v68, vcc, v14, v15, vcc
	v_cmp_gt_i32_e32 vcc, v27, v13
	s_nop 1
	v_cndmask_b32_e64 v69, 0, 1, vcc
	v_cmp_gt_i32_e32 vcc, v31, v13
	s_nop 1
	v_cndmask_b32_e64 v70, 0, 1, vcc
	v_cmp_gt_i32_e32 vcc, v10, v12
	s_nop 1
	v_cndmask_b32_e64 v14, 0, 1, vcc
	v_cmp_gt_i32_e32 vcc, v11, v12
	s_nop 1
	v_cndmask_b32_e64 v15, 0, 1, vcc
	v_cmp_gt_i32_e32 vcc, v13, v12
	s_nop 1
	v_addc_co_u32_e32 v71, vcc, v14, v15, vcc
	v_cmp_gt_i32_e32 vcc, v27, v12
	s_nop 1
	v_cndmask_b32_e64 v72, 0, 1, vcc
	v_cmp_gt_i32_e32 vcc, v31, v12
	s_nop 1
	v_cndmask_b32_e64 v73, 0, 1, vcc
	v_cmp_gt_i32_e32 vcc, v10, v27
	s_nop 1
	v_cndmask_b32_e64 v14, 0, 1, vcc
	v_cmp_gt_i32_e32 vcc, v11, v27
	s_nop 1
	v_cndmask_b32_e64 v15, 0, 1, vcc
	v_cmp_gt_i32_e32 vcc, v13, v27
	s_nop 1
	v_addc_co_u32_e32 v74, vcc, v14, v15, vcc
	v_cmp_gt_i32_e32 vcc, v12, v27
	s_nop 1
	v_cndmask_b32_e64 v75, 0, 1, vcc
	v_cmp_gt_i32_e32 vcc, v10, v28
	s_nop 1
	v_cndmask_b32_e64 v14, 0, 1, vcc
	v_cmp_gt_i32_e32 vcc, v11, v28
	s_nop 1
	v_cndmask_b32_e64 v15, 0, 1, vcc
	v_cmp_gt_i32_e32 vcc, v13, v28
	s_nop 1
	v_addc_co_u32_e32 v14, vcc, v14, v15, vcc
	v_cmp_gt_i32_e32 vcc, v12, v28
	s_nop 1
	v_cndmask_b32_e64 v15, 0, 1, vcc
	v_cmp_gt_i32_e32 vcc, v27, v28
	s_nop 1
	v_addc_co_u32_e32 v76, vcc, v14, v15, vcc
	v_cmp_gt_i32_e32 vcc, v10, v31
	s_nop 1
	v_cndmask_b32_e64 v14, 0, 1, vcc
	v_cmp_gt_i32_e32 vcc, v11, v31
	s_nop 1
	v_cndmask_b32_e64 v15, 0, 1, vcc
	v_cmp_gt_i32_e32 vcc, v13, v31
	s_nop 1
	v_addc_co_u32_e32 v14, vcc, v14, v15, vcc
	v_cmp_gt_i32_e32 vcc, v12, v31
	s_nop 1
	v_cndmask_b32_e64 v15, 0, 1, vcc
	v_cmp_gt_i32_e32 vcc, v27, v31
	s_nop 1
	v_addc_co_u32_e32 v77, vcc, v14, v15, vcc
	s_waitcnt lgkmcnt(8)
	v_cmp_gt_i32_e32 vcc, v18, v10
	ds_bpermute_b32 v15, v108, v12
	ds_bpermute_b32 v14, v109, v10
	v_cndmask_b32_e64 v78, 0, 1, vcc
	v_cmp_gt_i32_e32 vcc, v18, v11
	s_nop 1
	v_cndmask_b32_e64 v79, 0, 1, vcc
	v_cmp_gt_i32_e32 vcc, v18, v13
	s_nop 1
	v_cndmask_b32_e64 v80, 0, 1, vcc
	v_cmp_gt_i32_e32 vcc, v18, v12
	s_nop 1
	v_cndmask_b32_e64 v81, 0, 1, vcc
	v_cmp_gt_i32_e32 vcc, v18, v28
	s_nop 1
	v_cndmask_b32_e64 v82, 0, 1, vcc
	s_waitcnt lgkmcnt(9)
	v_cmp_gt_i32_e32 vcc, v16, v27
	s_nop 1
	v_cndmask_b32_e64 v83, 0, 1, vcc
	v_cmp_gt_i32_e32 vcc, v16, v31
	s_nop 1
	v_cndmask_b32_e64 v84, 0, 1, vcc
	s_waitcnt lgkmcnt(8)
	v_cmp_gt_i32_e32 vcc, v17, v28
	s_nop 1
	v_cndmask_b32_e64 v85, 0, 1, vcc
	s_waitcnt lgkmcnt(1)
	v_cmp_gt_i32_e32 vcc, v15, v10
	s_nop 1
	v_cndmask_b32_e64 v86, 0, 1, vcc
	v_cmp_gt_i32_e32 vcc, v15, v11
	s_nop 1
	v_cndmask_b32_e64 v87, 0, 1, vcc
	v_cmp_gt_i32_e32 vcc, v15, v13
	s_nop 1
	v_cndmask_b32_e64 v88, 0, 1, vcc
	v_cmp_gt_i32_e32 vcc, v15, v12
	s_nop 1
	v_cndmask_b32_e64 v89, 0, 1, vcc
	v_cmp_gt_i32_e32 vcc, v15, v27
	s_nop 1
	v_cndmask_b32_e64 v90, 0, 1, vcc
	v_cmp_gt_i32_e32 vcc, v15, v31
	s_nop 1
	v_cndmask_b32_e64 v91, 0, 1, vcc
	v_cmp_gt_i32_e32 vcc, v30, v10
	s_nop 1
	v_cndmask_b32_e64 v92, 0, 1, vcc
	v_cmp_gt_i32_e32 vcc, v30, v11
	s_nop 1
	v_cndmask_b32_e64 v93, 0, 1, vcc
	v_cmp_gt_i32_e32 vcc, v30, v13
	s_nop 1
	v_cndmask_b32_e64 v94, 0, 1, vcc
	v_cmp_gt_i32_e32 vcc, v30, v12
	s_nop 1
	v_cndmask_b32_e64 v95, 0, 1, vcc
	v_cmp_gt_i32_e32 vcc, v32, v10
	s_nop 1
	v_cndmask_b32_e64 v96, 0, 1, vcc
	v_cmp_gt_i32_e32 vcc, v32, v11
	s_nop 1
	v_cndmask_b32_e64 v97, 0, 1, vcc
	v_cmp_gt_i32_e32 vcc, v32, v13
	s_nop 1
	v_cndmask_b32_e64 v98, 0, 1, vcc
	v_cmp_gt_i32_e32 vcc, v32, v12
	s_nop 1
	v_cndmask_b32_e64 v99, 0, 1, vcc
	s_waitcnt lgkmcnt(0)
	v_cmp_gt_i32_e32 vcc, v14, v10
	s_nop 1
	v_cndmask_b32_e64 v100, 0, 1, vcc
	v_cmp_gt_i32_e32 vcc, v14, v11
	s_nop 1
	v_cndmask_b32_e64 v101, 0, 1, vcc
	v_cmp_gt_i32_e32 vcc, v14, v13
	s_nop 1
	v_cndmask_b32_e64 v102, 0, 1, vcc
	v_cmp_gt_i32_e32 vcc, v14, v12
	s_nop 1
	v_cndmask_b32_e64 v103, 0, 1, vcc
	v_cmp_gt_i32_e32 vcc, v14, v27
	s_nop 1
	v_cndmask_b32_e64 v122, 0, 1, vcc
	v_cmp_gt_i32_e32 vcc, v14, v28
	s_nop 1
	v_cndmask_b32_e64 v124, 0, 1, vcc
	v_cmp_gt_i32_e32 vcc, v14, v31
	s_nop 1
	v_cndmask_b32_e64 v125, 0, 1, vcc
	v_cmp_gt_i32_e32 vcc, v123, v10
	s_nop 1
	v_cndmask_b32_e64 v127, 0, 1, vcc
	v_cmp_gt_i32_e32 vcc, v123, v11
	s_nop 1
	v_cndmask_b32_e64 v128, 0, 1, vcc
	v_cmp_gt_i32_e32 vcc, v123, v13
	s_nop 1
	v_cndmask_b32_e64 v129, 0, 1, vcc
	v_cmp_gt_i32_e32 vcc, v123, v12
	s_nop 1
	v_cndmask_b32_e64 v130, 0, 1, vcc
	v_cmp_gt_i32_e32 vcc, v123, v27
	s_nop 1
	v_cndmask_b32_e64 v131, 0, 1, vcc
	v_cmp_gt_i32_e32 vcc, v123, v28
	s_nop 1
	v_cndmask_b32_e64 v133, 0, 1, vcc
	v_cmp_gt_i32_e32 vcc, v123, v31
	s_nop 1
	v_cndmask_b32_e64 v134, 0, 1, vcc
	v_cmp_gt_i32_e32 vcc, v132, v10
	s_nop 1
	v_cndmask_b32_e64 v136, 0, 1, vcc
	v_cmp_gt_i32_e32 vcc, v132, v11
	s_nop 1
	v_cndmask_b32_e64 v137, 0, 1, vcc
	v_cmp_gt_i32_e32 vcc, v132, v13
	s_nop 1
	v_cndmask_b32_e64 v138, 0, 1, vcc
	v_cmp_gt_i32_e32 vcc, v132, v12
	s_nop 1
	v_cndmask_b32_e64 v139, 0, 1, vcc
	v_cmp_gt_i32_e32 vcc, v132, v27
	s_nop 1
	v_cndmask_b32_e64 v140, 0, 1, vcc
	v_cmp_gt_i32_e32 vcc, v132, v28
	s_nop 1
	v_cndmask_b32_e64 v142, 0, 1, vcc
	v_cmp_gt_i32_e32 vcc, v132, v31
	s_nop 1
	v_cndmask_b32_e64 v143, 0, 1, vcc
	v_cmp_gt_i32_e32 vcc, v141, v10
	s_nop 1
	v_cndmask_b32_e64 v145, 0, 1, vcc
	v_cmp_gt_i32_e32 vcc, v141, v11
	s_nop 1
	v_cndmask_b32_e64 v146, 0, 1, vcc
	v_cmp_gt_i32_e32 vcc, v141, v13
	s_nop 1
	v_cndmask_b32_e64 v147, 0, 1, vcc
	v_cmp_gt_i32_e32 vcc, v141, v12
	s_nop 1
	v_cndmask_b32_e64 v148, 0, 1, vcc
	v_cmp_gt_i32_e32 vcc, v141, v27
	s_nop 1
	v_cndmask_b32_e64 v149, 0, 1, vcc
	v_cmp_gt_i32_e32 vcc, v141, v28
	s_nop 1
	v_cndmask_b32_e64 v151, 0, 1, vcc
	v_cmp_gt_i32_e32 vcc, v141, v31
	s_nop 1
	v_cndmask_b32_e64 v152, 0, 1, vcc
	v_cmp_gt_i32_e32 vcc, v150, v10
	s_nop 1
	v_cndmask_b32_e64 v154, 0, 1, vcc
	v_cmp_gt_i32_e32 vcc, v150, v11
	s_nop 1
	v_cndmask_b32_e64 v155, 0, 1, vcc
	v_cmp_gt_i32_e32 vcc, v150, v13
	s_nop 1
	v_cndmask_b32_e64 v156, 0, 1, vcc
	v_cmp_gt_i32_e32 vcc, v150, v12
	s_nop 1
	v_cndmask_b32_e64 v157, 0, 1, vcc
	v_cmp_gt_i32_e32 vcc, v150, v27
	s_nop 1
	v_cndmask_b32_e64 v158, 0, 1, vcc
	v_cmp_gt_i32_e32 vcc, v150, v28
	s_nop 1
	v_cndmask_b32_e64 v160, 0, 1, vcc
	v_cmp_gt_i32_e32 vcc, v150, v31
	s_nop 1
	v_cndmask_b32_e64 v161, 0, 1, vcc
	v_cmp_gt_i32_e32 vcc, v159, v10
	s_nop 1
	v_cndmask_b32_e64 v163, 0, 1, vcc
	v_cmp_gt_i32_e32 vcc, v159, v11
	s_nop 1
	v_cndmask_b32_e64 v164, 0, 1, vcc
	v_cmp_gt_i32_e32 vcc, v159, v13
	s_nop 1
	v_cndmask_b32_e64 v165, 0, 1, vcc
	v_cmp_gt_i32_e32 vcc, v159, v12
	s_nop 1
	v_cndmask_b32_e64 v166, 0, 1, vcc
	v_cmp_gt_i32_e32 vcc, v159, v27
	s_nop 1
	v_cndmask_b32_e64 v167, 0, 1, vcc
	v_cmp_gt_i32_e32 vcc, v159, v28
	s_nop 1
	v_cndmask_b32_e64 v169, 0, 1, vcc
	v_cmp_gt_i32_e32 vcc, v159, v31
	s_nop 1
	v_cndmask_b32_e64 v170, 0, 1, vcc
	v_cmp_gt_i32_e32 vcc, v168, v10
	s_nop 1
	v_cndmask_b32_e64 v172, 0, 1, vcc
	v_cmp_gt_i32_e32 vcc, v168, v11
	s_nop 1
	v_cndmask_b32_e64 v173, 0, 1, vcc
	v_cmp_gt_i32_e32 vcc, v168, v13
	s_nop 1
	v_cndmask_b32_e64 v174, 0, 1, vcc
	v_cmp_gt_i32_e32 vcc, v168, v12
	s_nop 1
	v_cndmask_b32_e64 v175, 0, 1, vcc
	v_cmp_gt_i32_e32 vcc, v168, v27
	s_nop 1
	v_cndmask_b32_e64 v176, 0, 1, vcc
	v_cmp_gt_i32_e32 vcc, v168, v28
	s_nop 1
	v_cndmask_b32_e64 v178, 0, 1, vcc
	v_cmp_gt_i32_e32 vcc, v168, v31
	s_nop 1
	v_cndmask_b32_e64 v179, 0, 1, vcc
	v_cmp_gt_i32_e32 vcc, v177, v10
	s_nop 1
	v_cndmask_b32_e64 v181, 0, 1, vcc
	v_cmp_gt_i32_e32 vcc, v177, v11
	s_nop 1
	v_cndmask_b32_e64 v182, 0, 1, vcc
	v_cmp_gt_i32_e32 vcc, v177, v13
	s_nop 1
	v_cndmask_b32_e64 v183, 0, 1, vcc
	v_cmp_gt_i32_e32 vcc, v177, v12
	s_nop 1
	v_cndmask_b32_e64 v184, 0, 1, vcc
	v_cmp_gt_i32_e32 vcc, v177, v27
	s_nop 1
	v_cndmask_b32_e64 v185, 0, 1, vcc
	v_cmp_gt_i32_e32 vcc, v177, v28
	s_nop 1
	v_cndmask_b32_e64 v186, 0, 1, vcc
	v_cmp_gt_i32_e32 vcc, v177, v31
	s_nop 1
	v_cndmask_b32_e64 v191, 0, 1, vcc
	v_cmp_gt_i32_e32 vcc, v16, v10
	s_nop 1
	v_addc_co_u32_e32 v19, vcc, v19, v78, vcc
	v_cmp_gt_i32_e32 vcc, v17, v10
	s_nop 1
	v_addc_co_u32_e32 v19, vcc, v19, v20, vcc
	v_cmp_gt_i32_e32 vcc, v28, v10
	s_nop 1
	v_addc_co_u32_e32 v19, vcc, v19, v86, vcc
	v_cmp_gt_i32_e32 vcc, v29, v10
	s_nop 1
	v_addc_co_u32_e32 v19, vcc, v19, v92, vcc
	v_cmp_gt_i32_e32 vcc, v33, v10
	s_nop 1
	v_addc_co_u32_e32 v19, vcc, v19, v21, vcc
	v_cmp_gt_i32_e32 vcc, v26, v10
	s_nop 1
	v_addc_co_u32_e32 v19, vcc, v19, v96, vcc
	v_cmp_gt_i32_e32 vcc, v126, v10
	s_nop 1
	v_addc_co_u32_e32 v19, vcc, v19, v100, vcc
	v_cmp_gt_i32_e32 vcc, v135, v10
	s_nop 1
	v_addc_co_u32_e32 v19, vcc, v19, v127, vcc
	v_cmp_gt_i32_e32 vcc, v144, v10
	s_nop 1
	v_addc_co_u32_e32 v19, vcc, v19, v136, vcc
	v_cmp_gt_i32_e32 vcc, v153, v10
	s_nop 1
	v_addc_co_u32_e32 v19, vcc, v19, v145, vcc
	v_cmp_gt_i32_e32 vcc, v162, v10
	s_nop 1
	v_addc_co_u32_e32 v19, vcc, v19, v154, vcc
	v_cmp_gt_i32_e32 vcc, v171, v10
	s_nop 1
	v_addc_co_u32_e32 v19, vcc, v19, v163, vcc
	v_cmp_gt_i32_e32 vcc, v180, v10
	s_nop 1
	v_addc_co_u32_e32 v19, vcc, v19, v172, vcc
	v_cmp_gt_i32_e32 vcc, v192, v10
	s_nop 1
	v_addc_co_u32_e32 v19, vcc, v19, v181, vcc
	v_cmp_gt_i32_e32 vcc, v16, v11
	s_nop 1
	v_addc_co_u32_e32 v20, vcc, v61, v79, vcc
	v_cmp_gt_i32_e32 vcc, v17, v11
	s_nop 1
	v_addc_co_u32_e32 v20, vcc, v20, v62, vcc
	v_cmp_gt_i32_e32 vcc, v28, v11
	s_nop 1
	v_addc_co_u32_e32 v20, vcc, v20, v87, vcc
	v_cmp_gt_i32_e32 vcc, v29, v11
	s_nop 1
	v_addc_co_u32_e32 v20, vcc, v20, v93, vcc
	v_cmp_gt_i32_e32 vcc, v33, v11
	s_nop 1
	v_addc_co_u32_e32 v20, vcc, v20, v67, vcc
	v_cmp_gt_i32_e32 vcc, v26, v11
	s_nop 1
	v_addc_co_u32_e32 v20, vcc, v20, v97, vcc
	v_cmp_gt_i32_e32 vcc, v126, v11
	s_nop 1
	v_addc_co_u32_e32 v20, vcc, v20, v101, vcc
	v_cmp_gt_i32_e32 vcc, v135, v11
	s_nop 1
	v_addc_co_u32_e32 v20, vcc, v20, v128, vcc
	v_cmp_gt_i32_e32 vcc, v144, v11
	s_nop 1
	v_addc_co_u32_e32 v20, vcc, v20, v137, vcc
	v_cmp_gt_i32_e32 vcc, v153, v11
	s_nop 1
	v_addc_co_u32_e32 v20, vcc, v20, v146, vcc
	v_cmp_gt_i32_e32 vcc, v162, v11
	s_nop 1
	v_addc_co_u32_e32 v20, vcc, v20, v155, vcc
	v_cmp_gt_i32_e32 vcc, v171, v11
	s_nop 1
	v_addc_co_u32_e32 v20, vcc, v20, v164, vcc
	v_cmp_gt_i32_e32 vcc, v180, v11
	s_nop 1
	v_addc_co_u32_e32 v20, vcc, v20, v173, vcc
	v_cmp_gt_i32_e32 vcc, v192, v11
	s_nop 1
	v_addc_co_u32_e32 v20, vcc, v20, v182, vcc
	v_cmp_gt_i32_e32 vcc, v16, v13
	s_nop 1
	v_addc_co_u32_e32 v21, vcc, v68, v80, vcc
	v_cmp_gt_i32_e32 vcc, v17, v13
	s_nop 1
	v_addc_co_u32_e32 v21, vcc, v21, v69, vcc
	v_cmp_gt_i32_e32 vcc, v28, v13
	s_nop 1
	v_addc_co_u32_e32 v21, vcc, v21, v88, vcc
	v_cmp_gt_i32_e32 vcc, v29, v13
	s_nop 1
	v_addc_co_u32_e32 v21, vcc, v21, v94, vcc
	v_cmp_gt_i32_e32 vcc, v33, v13
	s_nop 1
	v_addc_co_u32_e32 v21, vcc, v21, v70, vcc
	v_cmp_gt_i32_e32 vcc, v26, v13
	s_nop 1
	v_addc_co_u32_e32 v21, vcc, v21, v98, vcc
	v_cmp_gt_i32_e32 vcc, v126, v13
	s_nop 1
	v_addc_co_u32_e32 v21, vcc, v21, v102, vcc
	v_cmp_gt_i32_e32 vcc, v135, v13
	s_nop 1
	v_addc_co_u32_e32 v21, vcc, v21, v129, vcc
	v_cmp_gt_i32_e32 vcc, v144, v13
	s_nop 1
	v_addc_co_u32_e32 v21, vcc, v21, v138, vcc
	v_cmp_gt_i32_e32 vcc, v153, v13
	s_nop 1
	v_addc_co_u32_e32 v21, vcc, v21, v147, vcc
	v_cmp_gt_i32_e32 vcc, v162, v13
	s_nop 1
	v_addc_co_u32_e32 v21, vcc, v21, v156, vcc
	v_cmp_gt_i32_e32 vcc, v171, v13
	s_nop 1
	v_addc_co_u32_e32 v21, vcc, v21, v165, vcc
	v_cmp_gt_i32_e32 vcc, v180, v13
	s_nop 1
	v_addc_co_u32_e32 v21, vcc, v21, v174, vcc
	v_cmp_gt_i32_e32 vcc, v192, v13
	s_nop 1
	v_addc_co_u32_e32 v21, vcc, v21, v183, vcc
	v_cmp_gt_i32_e32 vcc, v16, v12
	s_nop 1
	v_addc_co_u32_e32 v61, vcc, v71, v81, vcc
	v_cmp_gt_i32_e32 vcc, v17, v12
	s_nop 1
	v_addc_co_u32_e32 v61, vcc, v61, v72, vcc
	v_cmp_gt_i32_e32 vcc, v28, v12
	s_nop 1
	v_addc_co_u32_e32 v61, vcc, v61, v89, vcc
	v_cmp_gt_i32_e32 vcc, v29, v12
	s_nop 1
	v_addc_co_u32_e32 v61, vcc, v61, v95, vcc
	v_cmp_gt_i32_e32 vcc, v33, v12
	s_nop 1
	v_addc_co_u32_e32 v61, vcc, v61, v73, vcc
	v_cmp_gt_i32_e32 vcc, v26, v12
	s_nop 1
	v_addc_co_u32_e32 v61, vcc, v61, v99, vcc
	v_cmp_gt_i32_e32 vcc, v126, v12
	s_nop 1
	v_addc_co_u32_e32 v61, vcc, v61, v103, vcc
	v_cmp_gt_i32_e32 vcc, v135, v12
	s_nop 1
	v_addc_co_u32_e32 v61, vcc, v61, v130, vcc
	v_cmp_gt_i32_e32 vcc, v144, v12
	s_nop 1
	v_addc_co_u32_e32 v61, vcc, v61, v139, vcc
	v_cmp_gt_i32_e32 vcc, v153, v12
	s_nop 1
	v_addc_co_u32_e32 v61, vcc, v61, v148, vcc
	v_cmp_gt_i32_e32 vcc, v162, v12
	s_nop 1
	v_addc_co_u32_e32 v61, vcc, v61, v157, vcc
	v_cmp_gt_i32_e32 vcc, v171, v12
	s_nop 1
	v_addc_co_u32_e32 v61, vcc, v61, v166, vcc
	v_cmp_gt_i32_e32 vcc, v180, v12
	s_nop 1
	v_addc_co_u32_e32 v61, vcc, v61, v175, vcc
	v_cmp_gt_i32_e32 vcc, v192, v12
	s_nop 1
	v_addc_co_u32_e32 v61, vcc, v61, v184, vcc
	v_cmp_gt_i32_e32 vcc, v18, v27
	s_nop 1
	v_addc_co_u32_e32 v62, vcc, v74, v75, vcc
	v_cmp_gt_i32_e32 vcc, v17, v27
	s_nop 1
	v_addc_co_u32_e32 v62, vcc, v62, v83, vcc
	v_cmp_gt_i32_e32 vcc, v28, v27
	s_nop 1
	v_addc_co_u32_e32 v62, vcc, v62, v90, vcc
	v_cmp_gt_i32_e32 vcc, v29, v27
	s_nop 1
	v_addc_co_u32_e32 v62, vcc, v62, v65, vcc
	v_cmp_gt_i32_e32 vcc, v33, v27
	s_nop 1
	v_addc_co_u32_e32 v59, vcc, v62, v59, vcc
	v_cmp_gt_i32_e32 vcc, v26, v27
	s_nop 1
	v_addc_co_u32_e32 v59, vcc, v59, v66, vcc
	v_cmp_gt_i32_e32 vcc, v126, v27
	s_nop 1
	v_addc_co_u32_e32 v59, vcc, v59, v122, vcc
	v_cmp_gt_i32_e32 vcc, v135, v27
	s_nop 1
	v_addc_co_u32_e32 v59, vcc, v59, v131, vcc
	v_cmp_gt_i32_e32 vcc, v144, v27
	s_nop 1
	v_addc_co_u32_e32 v59, vcc, v59, v140, vcc
	v_cmp_gt_i32_e32 vcc, v153, v27
	s_nop 1
	v_addc_co_u32_e32 v59, vcc, v59, v149, vcc
	v_cmp_gt_i32_e32 vcc, v162, v27
	s_nop 1
	v_addc_co_u32_e32 v59, vcc, v59, v158, vcc
	v_cmp_gt_i32_e32 vcc, v171, v27
	s_nop 1
	v_addc_co_u32_e32 v59, vcc, v59, v167, vcc
	v_cmp_gt_i32_e32 vcc, v180, v27
	s_nop 1
	v_addc_co_u32_e32 v59, vcc, v59, v176, vcc
	v_cmp_gt_i32_e32 vcc, v192, v27
	s_nop 1
	v_addc_co_u32_e32 v59, vcc, v59, v185, vcc
	v_cmp_gt_i32_e32 vcc, v16, v28
	s_nop 1
	v_addc_co_u32_e32 v62, vcc, v76, v82, vcc
	v_cmp_gt_i32_e32 vcc, v15, v28
	s_nop 1
	v_addc_co_u32_e32 v62, vcc, v62, v85, vcc
	v_cmp_gt_i32_e32 vcc, v29, v28
	s_nop 1
	v_addc_co_u32_e32 v60, vcc, v62, v60, vcc
	v_cmp_gt_i32_e32 vcc, v33, v28
	s_nop 1
	v_addc_co_u32_e32 v36, vcc, v60, v36, vcc
	v_cmp_gt_i32_e32 vcc, v26, v28
	s_nop 1
	v_addc_co_u32_e32 v36, vcc, v36, v64, vcc
	v_cmp_gt_i32_e32 vcc, v126, v28
	s_nop 1
	v_addc_co_u32_e32 v36, vcc, v36, v124, vcc
	v_cmp_gt_i32_e32 vcc, v135, v28
	s_nop 1
	v_addc_co_u32_e32 v36, vcc, v36, v133, vcc
	v_cmp_gt_i32_e32 vcc, v144, v28
	s_nop 1
	v_addc_co_u32_e32 v36, vcc, v36, v142, vcc
	v_cmp_gt_i32_e32 vcc, v153, v28
	s_nop 1
	v_addc_co_u32_e32 v36, vcc, v36, v151, vcc
	v_cmp_gt_i32_e32 vcc, v162, v28
	s_nop 1
	v_addc_co_u32_e32 v36, vcc, v36, v160, vcc
	v_cmp_gt_i32_e32 vcc, v171, v28
	s_nop 1
	v_addc_co_u32_e32 v36, vcc, v36, v169, vcc
	v_cmp_gt_i32_e32 vcc, v180, v28
	s_nop 1
	v_addc_co_u32_e32 v36, vcc, v36, v178, vcc
	v_cmp_gt_i32_e32 vcc, v192, v28
	s_nop 1
	v_addc_co_u32_e32 v36, vcc, v36, v186, vcc
	v_cmp_gt_i32_e32 vcc, v18, v31
	s_nop 1
	v_addc_co_u32_e32 v34, vcc, v77, v34, vcc
	v_cmp_gt_i32_e32 vcc, v17, v31
	s_nop 1
	v_addc_co_u32_e32 v34, vcc, v34, v84, vcc
	v_cmp_gt_i32_e32 vcc, v30, v31
	s_nop 1
	v_addc_co_u32_e32 v34, vcc, v34, v91, vcc
	v_cmp_gt_i32_e32 vcc, v33, v31
	s_nop 1
	v_addc_co_u32_e32 v34, vcc, v34, v35, vcc
	v_cmp_gt_i32_e32 vcc, v26, v31
	s_nop 1
	v_addc_co_u32_e32 v34, vcc, v34, v37, vcc
	v_cmp_gt_i32_e32 vcc, v126, v31
	s_nop 1
	v_addc_co_u32_e32 v34, vcc, v34, v125, vcc
	v_cmp_gt_i32_e32 vcc, v135, v31
	s_nop 1
	v_addc_co_u32_e32 v34, vcc, v34, v134, vcc
	v_cmp_gt_i32_e32 vcc, v144, v31
	s_nop 1
	v_addc_co_u32_e32 v34, vcc, v34, v143, vcc
	v_cmp_gt_i32_e32 vcc, v153, v31
	s_nop 1
	v_addc_co_u32_e32 v34, vcc, v34, v152, vcc
	v_cmp_gt_i32_e32 vcc, v162, v31
	s_nop 1
	v_addc_co_u32_e32 v34, vcc, v34, v161, vcc
	v_cmp_gt_i32_e32 vcc, v171, v31
	s_nop 1
	v_addc_co_u32_e32 v34, vcc, v34, v170, vcc
	v_cmp_gt_i32_e32 vcc, v180, v31
	s_nop 1
	v_addc_co_u32_e32 v34, vcc, v34, v179, vcc
	v_cmp_gt_i32_e32 vcc, v192, v31
	s_nop 1
	v_addc_co_u32_e32 v34, vcc, v34, v191, vcc
	v_cmp_gt_i32_e32 vcc, v192, v26
	s_nop 1
	v_cndmask_b32_e64 v35, 0, 1, vcc
	v_cmp_gt_i32_e32 vcc, v13, v26
	s_nop 1
	v_cndmask_b32_e64 v13, 0, 1, vcc
	v_cmp_gt_i32_e32 vcc, v12, v26
	v_lshlrev_b16_e32 v13, 2, v13
	s_nop 0
	v_cndmask_b32_e64 v12, 0, 1, vcc
	v_cmp_gt_i32_e32 vcc, v11, v26
	v_lshlrev_b16_e32 v12, 3, v12
	v_or_b32_e32 v12, v12, v13
	v_cndmask_b32_e64 v11, 0, 1, vcc
	v_cmp_gt_i32_e32 vcc, v10, v26
	v_lshlrev_b16_e32 v11, 1, v11
	s_nop 0
	v_cndmask_b32_e64 v10, 0, 1, vcc
	v_cmp_gt_i32_e32 vcc, v28, v26
	v_or_b32_e32 v10, v10, v11
	v_bitop3_b16 v10, v10, v12, 3 bitop3:0xec
	v_cndmask_b32_e64 v11, 0, 1, vcc
	v_cmp_gt_i32_e32 vcc, v27, v26
	v_lshlrev_b16_e32 v11, 1, v11
	s_nop 0
	v_cndmask_b32_e64 v12, 0, 1, vcc
	v_cmp_gt_i32_e32 vcc, v31, v26
	v_or_b32_e32 v11, v12, v11
	s_nop 0
	v_cndmask_b32_e64 v12, 0, 1, vcc
	v_cmp_gt_i32_e32 vcc, v18, v26
	v_lshlrev_b16_e32 v12, 2, v12
	s_nop 0
	v_cndmask_b32_e64 v13, 0, 1, vcc
	v_lshlrev_b16_e32 v13, 3, v13
	v_or_b32_e32 v12, v13, v12
	v_bitop3_b16 v11, v11, v12, 3 bitop3:0xec
	v_lshlrev_b16_e32 v11, 4, v11
	v_cmp_gt_i32_e32 vcc, v17, v26
	v_bitop3_b16 v10, v10, v11, 15 bitop3:0xec
	s_nop 0
	v_cndmask_b32_e64 v11, 0, 1, vcc
	v_cmp_gt_i32_e32 vcc, v16, v26
	v_lshlrev_b16_e32 v11, 1, v11
	s_nop 0
	v_cndmask_b32_e64 v12, 0, 1, vcc
	v_cmp_gt_i32_e32 vcc, v30, v26
	v_bitop3_b16 v11, v12, 3, v11 bitop3:0xc8
	s_nop 0
	v_cndmask_b32_e64 v12, 0, 1, vcc
	v_cmp_gt_i32_e32 vcc, v15, v26
	v_lshlrev_b16_e32 v12, 3, v12
	s_nop 0
	v_cndmask_b32_e64 v13, 0, 1, vcc
	v_lshlrev_b16_e32 v13, 2, v13
	v_or_b32_e32 v12, v12, v13
	v_cmp_gt_i32_e32 vcc, v33, v26
	v_bitop3_b16 v11, v11, 15, v12 bitop3:0xc8
	v_lshlrev_b16_e32 v11, 8, v11
	v_cndmask_b32_e64 v12, 0, 1, vcc
	v_cmp_gt_i32_e32 vcc, v29, v26
	v_lshlrev_b16_e32 v12, 1, v12
	s_nop 0
	v_cndmask_b32_e64 v13, 0, 1, vcc
	v_cmp_gt_i32_e32 vcc, v32, v26
	v_or_b32_e32 v12, v13, v12
	s_nop 0
	v_cndmask_b32_e64 v13, 0, 1, vcc
	v_cmp_gt_i32_e32 vcc, v14, v26
	v_lshlrev_b16_e32 v13, 2, v13
	s_nop 0
	v_cndmask_b32_e64 v14, 0, 1, vcc
	v_lshlrev_b16_e32 v14, 3, v14
	v_or_b32_e32 v13, v14, v13
	v_bitop3_b16 v12, v12, v13, 3 bitop3:0xec
	v_lshlrev_b16_e32 v12, 12, v12
	v_or_b32_e32 v11, v12, v11
	v_cmp_gt_i32_e32 vcc, v132, v26
	v_bitop3_b16 v10, v10, v11, s2 bitop3:0xec
	s_nop 0
	v_cndmask_b32_e64 v11, 0, 1, vcc
	v_cmp_gt_i32_e32 vcc, v135, v26
	v_lshlrev_b16_e32 v11, 3, v11
	s_nop 0
	v_cndmask_b32_e64 v12, 0, 1, vcc
	v_lshlrev_b16_e32 v12, 2, v12
	v_cmp_gt_i32_e32 vcc, v123, v26
	v_or_b32_e32 v11, v11, v12
	s_nop 0
	v_cndmask_b32_e64 v12, 0, 1, vcc
	v_cmp_gt_i32_e32 vcc, v126, v26
	v_lshlrev_b16_e32 v12, 1, v12
	s_nop 0
	v_cndmask_b32_e64 v13, 0, 1, vcc
	v_or_b32_e32 v12, v13, v12
	v_cmp_gt_i32_e32 vcc, v141, v26
	v_bitop3_b16 v11, v12, v11, 3 bitop3:0xec
	s_nop 0
	v_cndmask_b32_e64 v12, 0, 1, vcc
	v_cmp_gt_i32_e32 vcc, v144, v26
	v_lshlrev_b16_e32 v12, 1, v12
	s_nop 0
	v_cndmask_b32_e64 v13, 0, 1, vcc
	v_cmp_gt_i32_e32 vcc, v153, v26
	v_or_b32_e32 v12, v13, v12
	s_nop 0
	v_cndmask_b32_e64 v13, 0, 1, vcc
	v_cmp_gt_i32_e32 vcc, v150, v26
	v_lshlrev_b16_e32 v13, 2, v13
	s_nop 0
	v_cndmask_b32_e64 v14, 0, 1, vcc
	v_lshlrev_b16_e32 v14, 3, v14
	v_or_b32_e32 v13, v14, v13
	v_bitop3_b16 v12, v12, v13, 3 bitop3:0xec
	v_lshlrev_b16_e32 v12, 4, v12
	v_cmp_gt_i32_e32 vcc, v159, v26
	v_bitop3_b16 v11, v11, v12, 15 bitop3:0xec
	s_nop 0
	v_cndmask_b32_e64 v12, 0, 1, vcc
	v_cmp_gt_i32_e32 vcc, v162, v26
	v_lshlrev_b16_e32 v12, 1, v12
	s_nop 0
	v_cndmask_b32_e64 v13, 0, 1, vcc
	v_cmp_gt_i32_e32 vcc, v168, v26
	v_bitop3_b16 v12, v13, 3, v12 bitop3:0xc8
	s_nop 0
	v_cndmask_b32_e64 v13, 0, 1, vcc
	v_cmp_gt_i32_e32 vcc, v171, v26
	v_lshlrev_b16_e32 v13, 3, v13
	s_nop 0
	v_cndmask_b32_e64 v14, 0, 1, vcc
	v_lshlrev_b16_e32 v14, 2, v14
	v_or_b32_e32 v13, v13, v14
	v_bitop3_b16 v12, v12, 15, v13 bitop3:0xc8
	v_lshlrev_b16_e32 v12, 8, v12
	v_bitop3_b16 v11, v11, v12, s2 bitop3:0xec
	v_lshlrev_b32_e32 v11, 16, v11
	v_cmp_gt_i32_e32 vcc, v177, v26
	v_or_b32_sdwa v10, v10, v11 dst_sel:DWORD dst_unused:UNUSED_PAD src0_sel:WORD_0 src1_sel:DWORD
	v_bcnt_u32_b32 v10, v10, 0
	v_addc_co_u32_e32 v11, vcc, 0, v35, vcc
	v_cmp_gt_i32_e32 vcc, v180, v26
	s_nop 1
	v_addc_co_u32_e32 v14, vcc, v11, v10, vcc
	v_cmp_eq_u32_e32 vcc, 0, v19
	v_cmp_eq_u32_e64 s[46:47], 0, v14
	s_nop 0
	v_cndmask_b32_e32 v10, 0, v112, vcc
	v_cndmask_b32_e32 v11, 0, v8, vcc
	v_cmp_eq_u32_e32 vcc, 0, v20
	v_cndmask_b32_e64 v16, 0, v120, s[46:47]
	s_nop 0
	v_cndmask_b32_e32 v12, 0, v113, vcc
	v_or_b32_e32 v10, v12, v10
	v_cndmask_b32_e32 v12, 0, v9, vcc
	v_cmp_eq_u32_e32 vcc, 0, v21
	v_or_b32_e32 v11, v12, v11
	s_nop 0
	v_cndmask_b32_e32 v12, 0, v114, vcc
	v_cndmask_b32_e32 v13, 0, v6, vcc
	v_cmp_eq_u32_e32 vcc, 0, v61
	s_nop 1
	v_cndmask_b32_e32 v15, 0, v116, vcc
	v_or3_b32 v10, v10, v12, v15
	v_cndmask_b32_e32 v12, 0, v7, vcc
	v_cmp_eq_u32_e32 vcc, 0, v59
	v_or3_b32 v11, v11, v13, v12
	s_nop 0
	v_cndmask_b32_e32 v12, 0, v117, vcc
	v_cndmask_b32_e32 v13, 0, v22, vcc
	v_cmp_eq_u32_e32 vcc, 0, v36
	s_nop 1
	v_cndmask_b32_e32 v15, 0, v118, vcc
	v_or3_b32 v10, v10, v12, v15
	v_cndmask_b32_e32 v12, 0, v23, vcc
	v_cmp_eq_u32_e32 vcc, 0, v34
	v_or3_b32 v11, v11, v13, v12
	v_cndmask_b32_e64 v13, 0, v25, s[46:47]
	v_cndmask_b32_e32 v15, 0, v119, vcc
	v_or3_b32 v10, v10, v15, v16
	ds_bpermute_b32 v15, v108, v10
	v_cndmask_b32_e32 v12, 0, v24, vcc
	v_cmp_eq_u32_e32 vcc, 1, v19
	v_or3_b32 v11, v11, v12, v13
	v_cmp_eq_u32_e64 s[46:47], 1, v14
	s_waitcnt lgkmcnt(0)
	v_or_b32_e32 v12, v10, v15
	v_cndmask_b32_e32 v15, 0, v112, vcc
	v_cndmask_b32_e32 v16, 0, v8, vcc
	v_cmp_eq_u32_e32 vcc, 1, v20
	v_cndmask_b32_e64 v27, 0, v120, s[46:47]
	ds_bpermute_b32 v13, v109, v12
	v_cndmask_b32_e32 v17, 0, v113, vcc
	v_or_b32_e32 v15, v17, v15
	v_cndmask_b32_e32 v17, 0, v9, vcc
	v_cmp_eq_u32_e32 vcc, 1, v21
	v_or_b32_e32 v16, v17, v16
	ds_bpermute_b32 v10, v108, v11
	v_cndmask_b32_e32 v17, 0, v114, vcc
	v_cndmask_b32_e32 v18, 0, v6, vcc
	v_cmp_eq_u32_e32 vcc, 1, v61
	s_waitcnt lgkmcnt(0)
	v_or_b32_e32 v10, v11, v10
	v_cndmask_b32_e32 v26, 0, v116, vcc
	v_or3_b32 v15, v15, v17, v26
	v_cndmask_b32_e32 v17, 0, v7, vcc
	v_cmp_eq_u32_e32 vcc, 1, v59
	v_or3_b32 v16, v16, v18, v17
	ds_bpermute_b32 v11, v109, v10
	v_cndmask_b32_e32 v17, 0, v117, vcc
	v_cndmask_b32_e32 v18, 0, v22, vcc
	v_cmp_eq_u32_e32 vcc, 1, v36
	s_nop 1
	v_cndmask_b32_e32 v26, 0, v118, vcc
	v_or3_b32 v15, v15, v17, v26
	v_cndmask_b32_e32 v17, 0, v23, vcc
	v_cmp_eq_u32_e32 vcc, 1, v34
	v_or3_b32 v16, v16, v18, v17
	v_cndmask_b32_e64 v18, 0, v25, s[46:47]
	v_cndmask_b32_e32 v26, 0, v119, vcc
	v_or3_b32 v15, v15, v26, v27
	ds_bpermute_b32 v26, v108, v15
	v_cndmask_b32_e32 v17, 0, v24, vcc
	v_or3_b32 v16, v16, v17, v18
	ds_bpermute_b32 v17, v108, v16
	v_cmp_eq_u32_e32 vcc, 2, v19
	s_waitcnt lgkmcnt(1)
	v_or_b32_e32 v15, v15, v26
	ds_bpermute_b32 v18, v109, v15
	v_or_b32_e32 v26, v12, v13
	s_waitcnt lgkmcnt(1)
	v_or_b32_e32 v12, v16, v17
	v_cndmask_b32_e32 v16, 0, v8, vcc
	v_cmp_eq_u32_e64 s[46:47], 2, v14
	s_waitcnt lgkmcnt(0)
	v_or_b32_e32 v17, v15, v18
	v_cndmask_b32_e32 v15, 0, v112, vcc
	v_cmp_eq_u32_e32 vcc, 2, v20
	v_cndmask_b32_e64 v29, 0, v120, s[46:47]
	ds_bpermute_b32 v13, v109, v12
	v_cndmask_b32_e32 v18, 0, v113, vcc
	v_or_b32_e32 v15, v18, v15
	v_cndmask_b32_e32 v18, 0, v9, vcc
	v_cmp_eq_u32_e32 vcc, 2, v21
	v_or_b32_e32 v16, v18, v16
	s_nop 0
	v_cndmask_b32_e32 v18, 0, v114, vcc
	v_cndmask_b32_e32 v27, 0, v6, vcc
	v_cmp_eq_u32_e32 vcc, 2, v61
	s_nop 1
	v_cndmask_b32_e32 v28, 0, v116, vcc
	v_or3_b32 v15, v15, v18, v28
	v_cndmask_b32_e32 v18, 0, v7, vcc
	v_cmp_eq_u32_e32 vcc, 2, v59
	v_or3_b32 v16, v16, v27, v18
	s_nop 0
	v_cndmask_b32_e32 v18, 0, v117, vcc
	v_cndmask_b32_e32 v27, 0, v22, vcc
	v_cmp_eq_u32_e32 vcc, 2, v36
	s_nop 1
	v_cndmask_b32_e32 v28, 0, v118, vcc
	v_or3_b32 v15, v15, v18, v28
	v_cndmask_b32_e32 v18, 0, v23, vcc
	v_cmp_eq_u32_e32 vcc, 2, v34
	v_or3_b32 v16, v16, v27, v18
	v_cndmask_b32_e64 v27, 0, v25, s[46:47]
	v_cndmask_b32_e32 v28, 0, v119, vcc
	v_cndmask_b32_e32 v18, 0, v24, vcc
	v_cmp_eq_u32_e32 vcc, 3, v19
	v_cmp_eq_u32_e64 s[46:47], 3, v14
	v_or3_b32 v15, v15, v28, v29
	v_cndmask_b32_e32 v19, 0, v112, vcc
	v_cndmask_b32_e32 v8, 0, v8, vcc
	v_cmp_eq_u32_e32 vcc, 3, v20
	v_cndmask_b32_e64 v14, 0, v120, s[46:47]
	ds_bpermute_b32 v28, v108, v15
	v_cndmask_b32_e32 v20, 0, v113, vcc
	v_cndmask_b32_e32 v9, 0, v9, vcc
	v_cmp_eq_u32_e32 vcc, 3, v21
	v_or_b32_e32 v8, v9, v8
	v_or_b32_e32 v19, v20, v19
	v_cndmask_b32_e32 v9, 0, v114, vcc
	v_cndmask_b32_e32 v6, 0, v6, vcc
	v_cmp_eq_u32_e32 vcc, 3, v61
	v_or3_b32 v16, v16, v18, v27
	s_waitcnt lgkmcnt(0)
	v_or_b32_e32 v15, v15, v28
	v_cndmask_b32_e32 v20, 0, v116, vcc
	v_cndmask_b32_e32 v7, 0, v7, vcc
	v_cmp_eq_u32_e32 vcc, 3, v59
	v_or3_b32 v6, v8, v6, v7
	v_or3_b32 v9, v19, v9, v20
	v_cndmask_b32_e32 v7, 0, v117, vcc
	v_cndmask_b32_e32 v8, 0, v22, vcc
	v_cmp_eq_u32_e32 vcc, 3, v36
	ds_bpermute_b32 v18, v108, v16
	ds_bpermute_b32 v27, v109, v15
	v_cndmask_b32_e32 v19, 0, v118, vcc
	v_or3_b32 v7, v9, v7, v19
	v_cndmask_b32_e32 v9, 0, v23, vcc
	v_cmp_eq_u32_e32 vcc, 3, v34
	v_or3_b32 v6, v6, v8, v9
	v_cndmask_b32_e64 v9, 0, v25, s[46:47]
	v_cndmask_b32_e32 v19, 0, v119, vcc
	v_or3_b32 v7, v7, v19, v14
	ds_bpermute_b32 v14, v108, v7
	v_cndmask_b32_e32 v8, 0, v24, vcc
	v_or3_b32 v6, v6, v8, v9
	ds_bpermute_b32 v8, v108, v6
	s_waitcnt lgkmcnt(3)
	v_or_b32_e32 v9, v16, v18
	s_waitcnt lgkmcnt(1)
	v_or_b32_e32 v7, v7, v14
	ds_bpermute_b32 v19, v109, v7
	v_or_b32_e32 v18, v15, v27
	s_waitcnt lgkmcnt(1)
	v_or_b32_e32 v15, v6, v8
	ds_bpermute_b32 v14, v109, v9
	ds_bpermute_b32 v16, v109, v15
	s_waitcnt lgkmcnt(2)
	v_or_b32_e32 v6, v7, v19
	v_cndmask_b32_e64 v6, v6, v18, s[44:45]
	v_cndmask_b32_e64 v6, v6, v17, s[42:43]
	v_cndmask_b32_e64 v8, v6, v26, s[40:41]
	v_lshl_add_u32 v7, v8, 2, 0
	ds_add_rtn_u32 v6, v7, v195 offset:252
	s_waitcnt lgkmcnt(0)
	s_barrier
	s_and_saveexec_b64 s[14:15], s[38:39]
	s_cbranch_execz .LBB0_1240
	ds_read_b32 v18, v49 offset:256
	v_mov_b32_e32 v17, 0
	s_waitcnt lgkmcnt(0)
	v_cmp_ne_u32_e32 vcc, 0, v18
	s_and_saveexec_b64 s[24:25], vcc
	s_cbranch_execz .LBB0_1239
	global_atomic_add v17, v[44:45], v18, off sc0

.LBB0_1240:
	s_or_b64 exec, exec, s[14:15]
	v_or_b32_e32 v11, v10, v11
	v_or_b32_e32 v10, v12, v13
	v_or_b32_e32 v12, v9, v14
	v_sub_f32_e32 v9, v10, v11
	v_or_b32_e32 v13, v15, v16
	v_mul_f32_e32 v9, 0x3fb8aa3b, v9
	v_sub_f32_e32 v10, v12, v11
	v_exp_f32_e32 v9, v9
	v_mul_f32_e32 v10, 0x3fb8aa3b, v10
	v_sub_f32_e32 v11, v13, v11
	v_exp_f32_e32 v10, v10
	v_mul_f32_e32 v11, 0x3fb8aa3b, v11
	v_exp_f32_e32 v11, v11
	v_add_f32_e32 v12, 1.0, v9
	v_add_f32_e32 v12, v10, v12
	s_waitcnt lgkmcnt(0)
	v_add_f32_e32 v12, v11, v12
	v_div_scale_f32 v13, s[14:15], v12, v12, 1.0
	v_rcp_f32_e32 v14, v13
	v_div_scale_f32 v15, vcc, 1.0, v12, 1.0
	s_barrier
	v_fma_f32 v16, -v13, v14, 1.0
	v_fmac_f32_e32 v14, v16, v14
	v_mul_f32_e32 v16, v15, v14
	v_fma_f32 v17, -v13, v16, v15
	v_fmac_f32_e32 v16, v17, v14
	ds_read_b32 v7, v7 offset:380
	v_fma_f32 v13, -v13, v16, v15
	v_cndmask_b32_e64 v10, v11, v10, s[44:45]
	v_div_fmas_f32 v13, v13, v14, v16
	v_cndmask_b32_e64 v9, v10, v9, s[42:43]
	v_div_fixup_f32 v12, v13, v12, 1.0
	v_add_u32_e32 v8, -1, v8
	v_cndmask_b32_e64 v9, v9, 1.0, s[40:41]
	v_mul_f32_e32 v12, v9, v12
	v_ashrrev_i32_e32 v9, 31, v8
	s_waitcnt lgkmcnt(0)
	v_add_u32_e32 v186, v7, v6
	v_lshlrev_b64 v[6:7], 17, v[8:9]
	v_or_b32_e32 v10, s52, v63
	v_lshl_add_u64 v[6:7], s[0:1], 0, v[6:7]
	v_ashrrev_i32_e32 v11, 31, v10
	v_lshl_add_u64 v[6:7], v[186:187], 2, v[6:7]
	global_store_dword v[6:7], v10, off
	v_lshl_add_u64 v[6:7], v[10:11], 2, v[38:39]
	v_lshlrev_b64 v[6:7], 2, v[6:7]
	v_lshl_add_u64 v[10:11], s[54:55], 0, v[6:7]
	global_store_dword v[10:11], v8, off
	v_lshl_add_u64 v[8:9], s[56:57], 0, v[6:7]
	v_lshl_add_u64 v[6:7], s[58:59], 0, v[6:7]
	global_store_dword v[8:9], v186, off
	global_store_dword v[6:7], v12, off
	s_waitcnt lgkmcnt(0)
	s_barrier
	s_and_saveexec_b64 s[14:15], s[38:39]
	s_cbranch_execz .LBB0_1228
	ds_write_b32 v49, v187 offset:256
	s_branch .LBB0_1228

.LBB0_1328:
	s_nop 0
	v_cndmask_b32_e64 v2, 0, 1, s[40:41]
	v_cmp_ne_u32_e64 s[38:39], 1, v2
	s_andn2_b64 vcc, exec, s[40:41]
	v_mov_b32_e32 v169, v64
	v_mov_b32_e32 v168, v58
	v_mov_b32_e32 v170, v60
	v_mov_b32_e32 v171, v62
	s_cbranch_vccnz .LBB0_1338
	v_cmp_lt_i32_e32 vcc, v146, v167
	v_mov_b32_e32 v3, 0
	v_mov_b32_e32 v2, 0
	s_and_saveexec_b64 s[14:15], vcc
	s_cbranch_execz .LBB0_1331
	s_ashr_i32 s55, s54, 31
	s_lshl_b64 s[34:35], s[54:55], 17
	s_add_u32 s1, s13, s34
	s_addc_u32 s2, s16, s35
	s_lshl_b32 s34, s44, 8
	s_ashr_i32 s35, s34, 31
	s_lshl_b64 s[34:35], s[34:35], 2
	s_add_u32 s34, s1, s34
	s_addc_u32 s35, s2, s35
	v_lshl_add_u64 v[4:5], v[146:147], 2, s[34:35]
	global_load_dword v2, v[4:5], off
.LBB0_1331:
	s_or_b64 exec, exec, s[14:15]
	v_cmp_lt_i32_e32 vcc, v1, v167
	s_and_saveexec_b64 s[14:15], vcc
	s_cbranch_execz .LBB0_1333
	s_ashr_i32 s55, s54, 31
	s_lshl_b64 s[34:35], s[54:55], 17
	s_add_u32 s1, s13, s34
	s_addc_u32 s2, s16, s35
	s_lshl_b32 s34, s44, 8
	s_ashr_i32 s35, s34, 31
	s_lshl_b64 s[34:35], s[34:35], 2
	s_add_u32 s34, s1, s34
	s_addc_u32 s35, s2, s35
	v_lshl_add_u64 v[4:5], v[146:147], 2, s[34:35]
	global_load_dword v3, v[4:5], off offset:256
.LBB0_1333:
	s_or_b64 exec, exec, s[14:15]
	v_cmp_lt_i32_e32 vcc, v162, v167
	v_mov_b32_e32 v4, 0
	v_mov_b32_e32 v5, 0
	s_and_saveexec_b64 s[14:15], vcc
	s_cbranch_execz .LBB0_1335
	s_ashr_i32 s55, s54, 31
	s_lshl_b64 s[34:35], s[54:55], 17
	s_add_u32 s1, s13, s34
	s_addc_u32 s2, s16, s35
	s_lshl_b32 s34, s44, 8
	s_ashr_i32 s35, s34, 31
	s_lshl_b64 s[34:35], s[34:35], 2
	s_add_u32 s34, s1, s34
	s_addc_u32 s35, s2, s35
	v_lshl_add_u64 v[6:7], v[146:147], 2, s[34:35]
	global_load_dword v5, v[6:7], off offset:512
.LBB0_1335:
	s_or_b64 exec, exec, s[14:15]
	v_cmp_lt_i32_e32 vcc, v163, v167
	s_and_saveexec_b64 s[14:15], vcc
	s_cbranch_execz .LBB0_1337
	s_ashr_i32 s55, s54, 31
	s_lshl_b64 s[34:35], s[54:55], 17
	s_add_u32 s1, s13, s34
	s_addc_u32 s2, s16, s35
	s_lshl_b32 s34, s44, 8
	s_ashr_i32 s35, s34, 31
	s_lshl_b64 s[34:35], s[34:35], 2
	s_add_u32 s34, s1, s34
	s_addc_u32 s35, s2, s35
	v_lshl_add_u64 v[6:7], v[146:147], 2, s[34:35]
	global_load_dword v4, v[6:7], off offset:768
.LBB0_1337:
	s_or_b64 exec, exec, s[14:15]
	s_waitcnt vmcnt(0)
	v_lshlrev_b32_e32 v2, 10, v2
	v_lshlrev_b32_e32 v3, 10, v3
	v_lshlrev_b32_e32 v5, 10, v5
	v_lshlrev_b32_e32 v4, 10, v4
	v_add_lshl_u32 v168, v5, v164, 1
	v_add_lshl_u32 v170, v3, v164, 1
	v_add_lshl_u32 v171, v2, v164, 1
	v_add_lshl_u32 v169, v4, v164, 1
.LBB0_1338:
	s_add_u32 s1, s72, 0x100
	s_addc_u32 s2, s73, 0
	s_add_u32 s14, s70, 0x80
	v_mov_b32_e32 v59, v187
	v_mov_b32_e32 v65, v187
	s_addc_u32 s15, s71, 0
	v_mov_b32_e32 v2, 0
	v_lshl_add_u64 v[74:75], s[14:15], 0, v[64:65]
	v_lshl_add_u64 v[76:77], s[14:15], 0, v[58:59]
	s_mov_b32 s34, -2
	s_mov_b64 s[40:41], 0
	v_mov_b32_e32 v3, 0
	v_mov_b64_e32 v[4:5], 0
	v_mov_b64_e32 v[10:11], 0
	v_mov_b64_e32 v[12:13], 0
	v_mov_b64_e32 v[18:19], 0
	v_mov_b64_e32 v[20:21], 0
	v_mov_b64_e32 v[26:27], 0
	v_mov_b64_e32 v[28:29], 0
	v_mov_b64_e32 v[34:35], 0
	v_mov_b64_e32 v[36:37], 0
	v_mov_b64_e32 v[42:43], 0
	v_mov_b64_e32 v[44:45], 0
	v_mov_b64_e32 v[50:51], 0
	v_mov_b64_e32 v[52:53], 0
	v_mov_b64_e32 v[66:67], 0
	v_mov_b64_e32 v[68:69], 0
	v_mov_b64_e32 v[6:7], 0
	v_mov_b64_e32 v[8:9], 0
	v_mov_b64_e32 v[14:15], 0
	v_mov_b64_e32 v[16:17], 0
	v_mov_b64_e32 v[22:23], 0
	v_mov_b64_e32 v[24:25], 0
	v_mov_b64_e32 v[30:31], 0
	v_mov_b64_e32 v[32:33], 0
	v_mov_b64_e32 v[38:39], 0
	v_mov_b64_e32 v[40:41], 0
	v_mov_b64_e32 v[46:47], 0
	v_mov_b64_e32 v[48:49], 0
	v_mov_b64_e32 v[54:55], 0
	v_mov_b64_e32 v[56:57], 0
	v_mov_b64_e32 v[70:71], 0
	v_mov_b64_e32 v[72:73], 0
	v_mov_b64_e32 v[82:83], 0
	v_mov_b64_e32 v[84:85], 0
	v_mov_b64_e32 v[90:91], 0
	v_mov_b64_e32 v[92:93], 0
	v_mov_b64_e32 v[98:99], 0
	v_mov_b64_e32 v[100:101], 0
	v_mov_b64_e32 v[106:107], 0
	v_mov_b64_e32 v[108:109], 0
	v_mov_b64_e32 v[114:115], 0
	v_mov_b64_e32 v[116:117], 0
	v_mov_b64_e32 v[122:123], 0
	v_mov_b64_e32 v[124:125], 0
	v_mov_b64_e32 v[130:131], 0
	v_mov_b64_e32 v[132:133], 0
	v_mov_b64_e32 v[138:139], 0
	v_mov_b64_e32 v[140:141], 0
	v_mov_b64_e32 v[86:87], 0
	v_mov_b64_e32 v[88:89], 0
	v_mov_b64_e32 v[94:95], 0
	v_mov_b64_e32 v[96:97], 0
	v_mov_b64_e32 v[102:103], 0
	v_mov_b64_e32 v[104:105], 0
	v_mov_b64_e32 v[110:111], 0
	v_mov_b64_e32 v[112:113], 0
	v_mov_b64_e32 v[118:119], 0
	v_mov_b64_e32 v[120:121], 0
	v_mov_b64_e32 v[126:127], 0
	v_mov_b64_e32 v[128:129], 0
	v_mov_b64_e32 v[134:135], 0
	v_mov_b64_e32 v[136:137], 0
	v_mov_b64_e32 v[142:143], 0
	v_mov_b64_e32 v[144:145], 0

.LBB0_1342:
	s_waitcnt vmcnt(0)
	v_mov_b32_e32 v154, v79
	v_mov_b32_e32 v155, v81
	v_pk_add_f32 v[160:161], v[154:155], 1.0 op_sel_hi:[1,0]
	v_mov_b32_e32 v154, v75
	v_mov_b32_e32 v155, v77
	v_pk_add_f32 v[158:159], v[154:155], 1.0 op_sel_hi:[1,0]
	v_mov_b32_e32 v154, v63
	v_mov_b32_e32 v63, v64
	v_mov_b32_e32 v155, v65
	v_mov_b32_e32 v79, v80
	v_pk_add_f32 v[64:65], v[134:135], v[62:63]
	v_pk_add_f32 v[80:81], v[142:143], v[78:79]
	s_mov_b32 s34, 0xc01d265f
	v_min_f32_e32 v65, 0x40e00000, v65
	v_min_f32_e32 v64, 0x40e00000, v64
	v_min_f32_e32 v81, 0x40e00000, v81
	v_min_f32_e32 v80, 0x40e00000, v80
	v_pk_mul_f32 v[134:135], v[64:65], s[34:35] op_sel_hi:[1,0]
	v_pk_mul_f32 v[142:143], v[80:81], s[34:35] op_sel_hi:[1,0]
	v_exp_f32_e32 v134, v134
	v_exp_f32_e32 v135, v135
	v_exp_f32_e32 v142, v142
	v_exp_f32_e32 v143, v143
	v_pk_add_f32 v[156:157], v[154:155], 1.0 op_sel_hi:[1,0]
	v_pk_add_f32 v[134:135], v[134:135], 1.0 op_sel_hi:[1,0]
	v_mov_b32_e32 v154, v59
	v_pk_add_f32 v[142:143], v[142:143], 1.0 op_sel_hi:[1,0]
	v_rcp_f32_e32 v134, v134
	v_rcp_f32_e32 v135, v135
	v_rcp_f32_e32 v142, v142
	v_rcp_f32_e32 v143, v143
	v_mov_b32_e32 v59, v60
	v_mov_b32_e32 v155, v61
	v_mov_b32_e32 v75, v76
	v_pk_add_f32 v[130:131], v[130:131], v[156:157]
	v_pk_add_f32 v[60:61], v[136:137], v[58:59]
	v_pk_add_f32 v[154:155], v[154:155], 1.0 op_sel_hi:[1,0]
	v_pk_add_f32 v[138:139], v[138:139], v[160:161]
	v_pk_add_f32 v[76:77], v[144:145], v[74:75]
	v_med3_f32 v130, v130, s89, v238
	v_med3_f32 v131, v131, s89, v238
	v_pk_mul_f32 v[64:65], v[64:65], v[134:135]
	v_min_f32_e32 v61, 0x40e00000, v61
	v_min_f32_e32 v60, 0x40e00000, v60
	v_med3_f32 v138, v138, s89, v238
	v_med3_f32 v139, v139, s89, v238
	v_pk_mul_f32 v[80:81], v[80:81], v[142:143]
	v_min_f32_e32 v77, 0x40e00000, v77
	v_min_f32_e32 v76, 0x40e00000, v76
	v_pk_mul_f32 v[64:65], v[130:131], v[64:65]
	v_pk_add_f32 v[130:131], v[132:133], v[154:155]
	v_pk_mul_f32 v[132:133], v[60:61], s[34:35] op_sel_hi:[1,0]
	v_pk_mul_f32 v[80:81], v[138:139], v[80:81]
	v_pk_add_f32 v[138:139], v[140:141], v[158:159]
	v_pk_mul_f32 v[140:141], v[76:77], s[34:35] op_sel_hi:[1,0]
	v_exp_f32_e32 v132, v132
	v_exp_f32_e32 v133, v133
	v_exp_f32_e32 v140, v140
	v_exp_f32_e32 v141, v141
	s_lshl_b32 s1, s60, 7
	s_or_b32 s40, s1, s77
	s_lshl_b32 s1, s45, 8
	v_pk_add_f32 v[132:133], v[132:133], 1.0 op_sel_hi:[1,0]
	s_add_i32 s60, s1, s76
	v_pk_add_f32 v[140:141], v[140:141], 1.0 op_sel_hi:[1,0]
	v_rcp_f32_e32 v132, v132
	v_rcp_f32_e32 v133, v133
	s_ashr_i32 s61, s60, 31
	s_ashr_i32 s41, s40, 31
	v_rcp_f32_e32 v140, v140
	v_rcp_f32_e32 v141, v141
	s_lshl_b64 s[14:15], s[60:61], 11
	s_add_u32 s2, s78, s14
	s_addc_u32 s15, s79, s15
	s_lshl_b64 s[40:41], s[40:41], 1
	v_med3_f32 v130, v130, s89, v238
	v_med3_f32 v131, v131, s89, v238
	v_pk_mul_f32 v[60:61], v[60:61], v[132:133]
	s_add_u32 s14, s2, s40
	v_med3_f32 v138, v138, s89, v238
	v_med3_f32 v139, v139, s89, v238
	v_pk_mul_f32 v[76:77], v[76:77], v[140:141]
	v_pk_mul_f32 v[60:61], v[130:131], v[60:61]
	s_addc_u32 s15, s15, s41
	v_pk_mul_f32 v[76:77], v[138:139], v[76:77]
	v_cvt_pk_bf16_f32 v130, v80, v81
	v_pk_add_f32 v[54:55], v[54:55], v[62:63]
	v_cvt_pk_bf16_f32 v131, v76, v77
	v_cvt_pk_bf16_f32 v132, v64, v65
	v_cvt_pk_bf16_f32 v133, v60, v61
	v_lshl_add_u64 v[60:61], s[14:15], 0, v[152:153]
	global_store_dwordx4 v[60:61], v[130:133], off
	v_pk_add_f32 v[60:61], v[126:127], v[78:79]
	v_pk_add_f32 v[64:65], v[122:123], v[160:161]
	v_min_f32_e32 v61, 0x40e00000, v61
	v_min_f32_e32 v60, 0x40e00000, v60
	v_pk_mul_f32 v[76:77], v[60:61], s[34:35] op_sel_hi:[1,0]
	v_med3_f32 v64, v64, s89, v238
	v_exp_f32_e32 v76, v76
	v_exp_f32_e32 v77, v77
	v_med3_f32 v65, v65, s89, v238
	s_add_i32 s14, s85, s1
	s_ashr_i32 s15, s14, 31
	v_pk_add_f32 v[76:77], v[76:77], 1.0 op_sel_hi:[1,0]
	s_lshl_b64 s[14:15], s[14:15], 11
	v_rcp_f32_e32 v76, v76
	v_rcp_f32_e32 v77, v77
	s_add_u32 s2, s78, s14
	s_addc_u32 s15, s79, s15
	s_add_u32 s14, s2, s40
	v_pk_mul_f32 v[60:61], v[60:61], v[76:77]
	v_pk_add_f32 v[76:77], v[124:125], v[158:159]
	v_pk_mul_f32 v[60:61], v[64:65], v[60:61]
	v_pk_add_f32 v[64:65], v[128:129], v[74:75]
	v_med3_f32 v76, v76, s89, v238
	v_min_f32_e32 v65, 0x40e00000, v65
	v_min_f32_e32 v64, 0x40e00000, v64
	v_pk_mul_f32 v[80:81], v[64:65], s[34:35] op_sel_hi:[1,0]
	v_med3_f32 v77, v77, s89, v238
	v_exp_f32_e32 v80, v80
	v_exp_f32_e32 v81, v81
	s_addc_u32 s15, s15, s41
	v_min_f32_e32 v55, 0x40e00000, v55
	v_min_f32_e32 v54, 0x40e00000, v54
	v_pk_add_f32 v[80:81], v[80:81], 1.0 op_sel_hi:[1,0]
	v_pk_add_f32 v[50:51], v[50:51], v[156:157]
	v_rcp_f32_e32 v80, v80
	v_rcp_f32_e32 v81, v81
	v_med3_f32 v50, v50, s89, v238
	v_med3_f32 v51, v51, s89, v238
	v_pk_add_f32 v[52:53], v[52:53], v[154:155]
	v_pk_mul_f32 v[64:65], v[64:65], v[80:81]
	v_pk_add_f32 v[80:81], v[114:115], v[156:157]
	v_pk_mul_f32 v[64:65], v[76:77], v[64:65]
	v_pk_add_f32 v[76:77], v[118:119], v[62:63]
	v_med3_f32 v80, v80, s89, v238
	v_min_f32_e32 v77, 0x40e00000, v77
	v_min_f32_e32 v76, 0x40e00000, v76
	v_pk_mul_f32 v[114:115], v[76:77], s[34:35] op_sel_hi:[1,0]
	v_med3_f32 v81, v81, s89, v238
	v_exp_f32_e32 v114, v114
	v_exp_f32_e32 v115, v115
	v_med3_f32 v52, v52, s89, v238
	v_med3_f32 v53, v53, s89, v238
	v_pk_add_f32 v[46:47], v[46:47], v[78:79]
	v_pk_add_f32 v[114:115], v[114:115], 1.0 op_sel_hi:[1,0]
	v_min_f32_e32 v47, 0x40e00000, v47
	v_rcp_f32_e32 v114, v114
	v_rcp_f32_e32 v115, v115
	v_min_f32_e32 v46, 0x40e00000, v46
	v_pk_add_f32 v[42:43], v[42:43], v[160:161]
	v_pk_add_f32 v[44:45], v[44:45], v[158:159]
	v_pk_mul_f32 v[76:77], v[76:77], v[114:115]
	v_pk_add_f32 v[114:115], v[116:117], v[154:155]
	v_pk_mul_f32 v[76:77], v[80:81], v[76:77]
	v_pk_add_f32 v[80:81], v[120:121], v[58:59]
	v_med3_f32 v114, v114, s89, v238
	v_min_f32_e32 v81, 0x40e00000, v81
	v_min_f32_e32 v80, 0x40e00000, v80
	v_pk_mul_f32 v[116:117], v[80:81], s[34:35] op_sel_hi:[1,0]
	v_med3_f32 v115, v115, s89, v238
	v_exp_f32_e32 v116, v116
	v_exp_f32_e32 v117, v117
	v_med3_f32 v42, v42, s89, v238
	v_med3_f32 v43, v43, s89, v238
	v_pk_add_f32 v[38:39], v[38:39], v[62:63]
	v_pk_add_f32 v[116:117], v[116:117], 1.0 op_sel_hi:[1,0]
	v_med3_f32 v44, v44, s89, v238
	v_rcp_f32_e32 v116, v116
	v_rcp_f32_e32 v117, v117
	v_med3_f32 v45, v45, s89, v238
	v_min_f32_e32 v39, 0x40e00000, v39
	v_min_f32_e32 v38, 0x40e00000, v38
	v_pk_mul_f32 v[80:81], v[80:81], v[116:117]
	v_pk_add_f32 v[34:35], v[34:35], v[156:157]
	v_pk_mul_f32 v[80:81], v[114:115], v[80:81]
	v_cvt_pk_bf16_f32 v114, v60, v61
	v_lshl_add_u64 v[60:61], s[14:15], 0, v[152:153]
	v_cvt_pk_bf16_f32 v115, v64, v65
	v_cvt_pk_bf16_f32 v116, v76, v77
	v_cvt_pk_bf16_f32 v117, v80, v81
	global_store_dwordx4 v[60:61], v[114:117], off
	v_pk_add_f32 v[60:61], v[110:111], v[78:79]
	v_pk_add_f32 v[64:65], v[106:107], v[160:161]
	v_min_f32_e32 v61, 0x40e00000, v61
	v_min_f32_e32 v60, 0x40e00000, v60
	v_pk_mul_f32 v[76:77], v[60:61], s[34:35] op_sel_hi:[1,0]
	v_med3_f32 v64, v64, s89, v238
	v_exp_f32_e32 v76, v76
	v_exp_f32_e32 v77, v77
	v_med3_f32 v65, v65, s89, v238
	s_add_i32 s14, s90, s1
	s_ashr_i32 s15, s14, 31
	v_pk_add_f32 v[76:77], v[76:77], 1.0 op_sel_hi:[1,0]
	s_lshl_b64 s[14:15], s[14:15], 11
	v_rcp_f32_e32 v76, v76
	v_rcp_f32_e32 v77, v77
	s_add_u32 s2, s78, s14
	s_addc_u32 s15, s79, s15
	s_add_u32 s14, s2, s40
	v_pk_mul_f32 v[60:61], v[60:61], v[76:77]
	v_pk_add_f32 v[76:77], v[108:109], v[158:159]
	v_pk_mul_f32 v[60:61], v[64:65], v[60:61]
	v_pk_add_f32 v[64:65], v[112:113], v[74:75]
	v_med3_f32 v76, v76, s89, v238
	v_min_f32_e32 v65, 0x40e00000, v65
	v_min_f32_e32 v64, 0x40e00000, v64
	v_pk_mul_f32 v[80:81], v[64:65], s[34:35] op_sel_hi:[1,0]
	v_med3_f32 v77, v77, s89, v238
	v_exp_f32_e32 v80, v80
	v_exp_f32_e32 v81, v81
	s_addc_u32 s15, s15, s41
	v_med3_f32 v34, v34, s89, v238
	v_med3_f32 v35, v35, s89, v238
	v_pk_add_f32 v[80:81], v[80:81], 1.0 op_sel_hi:[1,0]
	v_pk_add_f32 v[36:37], v[36:37], v[154:155]
	v_rcp_f32_e32 v80, v80
	v_rcp_f32_e32 v81, v81
	v_med3_f32 v36, v36, s89, v238
	v_med3_f32 v37, v37, s89, v238
	v_pk_add_f32 v[30:31], v[30:31], v[78:79]
	v_pk_mul_f32 v[64:65], v[64:65], v[80:81]
	v_pk_add_f32 v[80:81], v[98:99], v[156:157]
	v_pk_mul_f32 v[64:65], v[76:77], v[64:65]
	v_pk_add_f32 v[76:77], v[102:103], v[62:63]
	v_med3_f32 v80, v80, s89, v238
	v_min_f32_e32 v77, 0x40e00000, v77
	v_min_f32_e32 v76, 0x40e00000, v76
	v_pk_mul_f32 v[98:99], v[76:77], s[34:35] op_sel_hi:[1,0]
	v_med3_f32 v81, v81, s89, v238
	v_exp_f32_e32 v98, v98
	v_exp_f32_e32 v99, v99
	v_min_f32_e32 v31, 0x40e00000, v31
	v_min_f32_e32 v30, 0x40e00000, v30
	v_pk_add_f32 v[26:27], v[26:27], v[160:161]
	v_pk_add_f32 v[98:99], v[98:99], 1.0 op_sel_hi:[1,0]
	v_med3_f32 v26, v26, s89, v238
	v_rcp_f32_e32 v98, v98
	v_rcp_f32_e32 v99, v99
	v_med3_f32 v27, v27, s89, v238
	v_pk_add_f32 v[28:29], v[28:29], v[158:159]
	v_pk_add_f32 v[22:23], v[22:23], v[62:63]
	v_pk_mul_f32 v[76:77], v[76:77], v[98:99]
	v_pk_add_f32 v[98:99], v[100:101], v[154:155]
	v_pk_mul_f32 v[76:77], v[80:81], v[76:77]
	v_pk_add_f32 v[80:81], v[104:105], v[58:59]
	v_med3_f32 v98, v98, s89, v238
	v_min_f32_e32 v81, 0x40e00000, v81
	v_min_f32_e32 v80, 0x40e00000, v80
	v_pk_mul_f32 v[100:101], v[80:81], s[34:35] op_sel_hi:[1,0]
	v_med3_f32 v99, v99, s89, v238
	v_exp_f32_e32 v100, v100
	v_exp_f32_e32 v101, v101
	v_med3_f32 v28, v28, s89, v238
	v_med3_f32 v29, v29, s89, v238
	v_min_f32_e32 v23, 0x40e00000, v23
	v_pk_add_f32 v[100:101], v[100:101], 1.0 op_sel_hi:[1,0]
	v_min_f32_e32 v22, 0x40e00000, v22
	v_rcp_f32_e32 v100, v100
	v_rcp_f32_e32 v101, v101
	v_pk_add_f32 v[18:19], v[18:19], v[156:157]
	v_pk_add_f32 v[20:21], v[20:21], v[154:155]
	v_med3_f32 v18, v18, s89, v238
	v_pk_mul_f32 v[80:81], v[80:81], v[100:101]
	v_med3_f32 v19, v19, s89, v238
	v_pk_mul_f32 v[80:81], v[98:99], v[80:81]
	v_cvt_pk_bf16_f32 v98, v60, v61
	v_lshl_add_u64 v[60:61], s[14:15], 0, v[152:153]
	v_cvt_pk_bf16_f32 v99, v64, v65
	v_cvt_pk_bf16_f32 v100, v76, v77
	v_cvt_pk_bf16_f32 v101, v80, v81
	global_store_dwordx4 v[60:61], v[98:101], off
	v_pk_add_f32 v[60:61], v[94:95], v[78:79]
	v_pk_add_f32 v[64:65], v[90:91], v[160:161]
	v_min_f32_e32 v61, 0x40e00000, v61
	v_min_f32_e32 v60, 0x40e00000, v60
	v_pk_mul_f32 v[76:77], v[60:61], s[34:35] op_sel_hi:[1,0]
	v_med3_f32 v64, v64, s89, v238
	v_exp_f32_e32 v76, v76
	v_exp_f32_e32 v77, v77
	v_med3_f32 v65, v65, s89, v238
	s_add_i32 s14, s91, s1
	s_ashr_i32 s15, s14, 31
	v_pk_add_f32 v[76:77], v[76:77], 1.0 op_sel_hi:[1,0]
	s_lshl_b64 s[14:15], s[14:15], 11
	v_rcp_f32_e32 v76, v76
	v_rcp_f32_e32 v77, v77
	s_add_u32 s1, s78, s14
	s_addc_u32 s2, s79, s15
	s_add_u32 s14, s1, s40
	v_pk_mul_f32 v[60:61], v[60:61], v[76:77]
	v_pk_add_f32 v[76:77], v[92:93], v[158:159]
	v_pk_mul_f32 v[60:61], v[64:65], v[60:61]
	v_pk_add_f32 v[64:65], v[96:97], v[74:75]
	v_med3_f32 v76, v76, s89, v238
	v_min_f32_e32 v65, 0x40e00000, v65
	v_min_f32_e32 v64, 0x40e00000, v64
	v_pk_mul_f32 v[80:81], v[64:65], s[34:35] op_sel_hi:[1,0]
	v_med3_f32 v77, v77, s89, v238
	v_exp_f32_e32 v80, v80
	v_exp_f32_e32 v81, v81
	s_addc_u32 s15, s2, s41
	v_med3_f32 v20, v20, s89, v238
	v_med3_f32 v21, v21, s89, v238
	v_pk_add_f32 v[80:81], v[80:81], 1.0 op_sel_hi:[1,0]
	v_pk_add_f32 v[14:15], v[14:15], v[78:79]
	v_rcp_f32_e32 v80, v80
	v_rcp_f32_e32 v81, v81
	v_min_f32_e32 v15, 0x40e00000, v15
	v_min_f32_e32 v14, 0x40e00000, v14
	v_pk_add_f32 v[10:11], v[10:11], v[160:161]
	v_pk_mul_f32 v[64:65], v[64:65], v[80:81]
	v_pk_add_f32 v[80:81], v[82:83], v[156:157]
	v_pk_mul_f32 v[64:65], v[76:77], v[64:65]
	v_pk_add_f32 v[76:77], v[86:87], v[62:63]
	v_med3_f32 v80, v80, s89, v238
	v_min_f32_e32 v77, 0x40e00000, v77
	v_min_f32_e32 v76, 0x40e00000, v76
	v_pk_mul_f32 v[82:83], v[76:77], s[34:35] op_sel_hi:[1,0]
	v_med3_f32 v81, v81, s89, v238
	v_exp_f32_e32 v82, v82
	v_exp_f32_e32 v83, v83
	v_med3_f32 v10, v10, s89, v238
	v_med3_f32 v11, v11, s89, v238
	v_pk_add_f32 v[12:13], v[12:13], v[158:159]
	v_pk_add_f32 v[82:83], v[82:83], 1.0 op_sel_hi:[1,0]
	v_pk_add_f32 v[6:7], v[6:7], v[62:63]
	v_rcp_f32_e32 v82, v82
	v_rcp_f32_e32 v83, v83
	v_med3_f32 v12, v12, s89, v238
	v_med3_f32 v13, v13, s89, v238
	v_min_f32_e32 v7, 0x40e00000, v7
	v_pk_mul_f32 v[76:77], v[76:77], v[82:83]
	v_pk_add_f32 v[82:83], v[84:85], v[154:155]
	v_pk_mul_f32 v[76:77], v[80:81], v[76:77]
	v_pk_add_f32 v[80:81], v[88:89], v[58:59]
	v_med3_f32 v82, v82, s89, v238
	v_min_f32_e32 v81, 0x40e00000, v81
	v_min_f32_e32 v80, 0x40e00000, v80
	v_pk_mul_f32 v[84:85], v[80:81], s[34:35] op_sel_hi:[1,0]
	v_med3_f32 v83, v83, s89, v238
	v_exp_f32_e32 v84, v84
	v_exp_f32_e32 v85, v85
	v_min_f32_e32 v6, 0x40e00000, v6
	v_pk_add_f32 v[2:3], v[2:3], v[156:157]
	v_pk_add_f32 v[4:5], v[4:5], v[154:155]
	v_pk_add_f32 v[84:85], v[84:85], 1.0 op_sel_hi:[1,0]
	v_med3_f32 v2, v2, s89, v238
	v_rcp_f32_e32 v84, v84
	v_rcp_f32_e32 v85, v85
	v_med3_f32 v3, v3, s89, v238
	v_med3_f32 v4, v4, s89, v238
	v_med3_f32 v5, v5, s89, v238
	v_pk_mul_f32 v[80:81], v[80:81], v[84:85]
	s_nop 0
	v_pk_mul_f32 v[84:85], v[82:83], v[80:81]
	v_cvt_pk_bf16_f32 v80, v60, v61
	v_lshl_add_u64 v[60:61], s[14:15], 0, v[152:153]
	v_cvt_pk_bf16_f32 v81, v64, v65
	v_cvt_pk_bf16_f32 v82, v76, v77
	v_cvt_pk_bf16_f32 v83, v84, v85
	global_store_dwordx4 v[60:61], v[80:83], off
	v_pk_add_f32 v[60:61], v[70:71], v[78:79]
	v_pk_add_f32 v[64:65], v[66:67], v[160:161]
	v_min_f32_e32 v61, 0x40e00000, v61
	v_min_f32_e32 v60, 0x40e00000, v60
	v_pk_mul_f32 v[66:67], v[60:61], s[34:35] op_sel_hi:[1,0]
	v_med3_f32 v64, v64, s89, v238
	v_exp_f32_e32 v66, v66
	v_exp_f32_e32 v67, v67
	v_med3_f32 v65, v65, s89, v238
	s_add_i32 s14, s60, 0x80
	s_ashr_i32 s15, s14, 31
	v_pk_add_f32 v[66:67], v[66:67], 1.0 op_sel_hi:[1,0]
	s_lshl_b64 s[14:15], s[14:15], 11
	v_rcp_f32_e32 v66, v66
	v_rcp_f32_e32 v67, v67
	s_add_u32 s1, s78, s14
	s_addc_u32 s2, s79, s15
	s_add_u32 s14, s1, s40
	v_pk_mul_f32 v[60:61], v[60:61], v[66:67]
	v_pk_add_f32 v[66:67], v[68:69], v[158:159]
	v_pk_mul_f32 v[60:61], v[64:65], v[60:61]
	v_pk_add_f32 v[64:65], v[72:73], v[74:75]
	v_med3_f32 v66, v66, s89, v238
	v_min_f32_e32 v65, 0x40e00000, v65
	v_min_f32_e32 v64, 0x40e00000, v64
	v_pk_mul_f32 v[68:69], v[64:65], s[34:35] op_sel_hi:[1,0]
	v_med3_f32 v67, v67, s89, v238
	v_exp_f32_e32 v68, v68
	v_exp_f32_e32 v69, v69
	s_addc_u32 s15, s2, s41
	v_pk_add_f32 v[68:69], v[68:69], 1.0 op_sel_hi:[1,0]
	s_nop 0
	v_rcp_f32_e32 v68, v68
	v_rcp_f32_e32 v69, v69
	s_nop 0
	v_pk_mul_f32 v[64:65], v[64:65], v[68:69]
	s_nop 0
	v_pk_mul_f32 v[64:65], v[66:67], v[64:65]
	v_pk_mul_f32 v[66:67], v[54:55], s[34:35] op_sel_hi:[1,0]
	s_nop 0
	v_exp_f32_e32 v66, v66
	v_exp_f32_e32 v67, v67
	s_nop 0
	v_pk_add_f32 v[66:67], v[66:67], 1.0 op_sel_hi:[1,0]
	s_nop 0
	v_rcp_f32_e32 v66, v66
	v_rcp_f32_e32 v67, v67
	s_nop 0
	v_pk_mul_f32 v[54:55], v[54:55], v[66:67]
	s_nop 0
	v_pk_mul_f32 v[54:55], v[50:51], v[54:55]
	v_pk_add_f32 v[50:51], v[56:57], v[58:59]
	s_nop 0
	v_min_f32_e32 v51, 0x40e00000, v51
	v_min_f32_e32 v50, 0x40e00000, v50
	v_pk_mul_f32 v[56:57], v[50:51], s[34:35] op_sel_hi:[1,0]
	s_nop 0
	v_exp_f32_e32 v56, v56
	v_exp_f32_e32 v57, v57
	s_nop 0
	v_pk_add_f32 v[56:57], v[56:57], 1.0 op_sel_hi:[1,0]
	s_nop 0
	v_rcp_f32_e32 v56, v56
	v_rcp_f32_e32 v57, v57
	s_nop 0
	v_pk_mul_f32 v[50:51], v[50:51], v[56:57]
	s_nop 0
	v_pk_mul_f32 v[56:57], v[52:53], v[50:51]
	v_cvt_pk_bf16_f32 v50, v60, v61
	v_cvt_pk_bf16_f32 v51, v64, v65
	v_cvt_pk_bf16_f32 v52, v54, v55
	v_lshl_add_u64 v[54:55], s[14:15], 0, v[152:153]
	v_cvt_pk_bf16_f32 v53, v56, v57
	global_store_dwordx4 v[54:55], v[50:53], off
	s_add_i32 s14, s60, 0x90
	s_ashr_i32 s15, s14, 31
	v_pk_mul_f32 v[50:51], v[46:47], s[34:35] op_sel_hi:[1,0]
	s_lshl_b64 s[14:15], s[14:15], 11
	v_exp_f32_e32 v50, v50
	v_exp_f32_e32 v51, v51
	s_add_u32 s1, s78, s14
	s_addc_u32 s2, s79, s15
	s_add_u32 s14, s1, s40
	v_pk_add_f32 v[50:51], v[50:51], 1.0 op_sel_hi:[1,0]
	s_addc_u32 s15, s2, s41
	v_rcp_f32_e32 v50, v50
	v_rcp_f32_e32 v51, v51
	s_nop 0
	v_pk_mul_f32 v[46:47], v[46:47], v[50:51]
	s_nop 0
	v_pk_mul_f32 v[42:43], v[42:43], v[46:47]
	v_pk_add_f32 v[46:47], v[48:49], v[74:75]
	s_nop 0
	v_min_f32_e32 v47, 0x40e00000, v47
	v_min_f32_e32 v46, 0x40e00000, v46
	v_pk_mul_f32 v[48:49], v[46:47], s[34:35] op_sel_hi:[1,0]
	s_nop 0
	v_exp_f32_e32 v48, v48
	v_exp_f32_e32 v49, v49
	s_nop 0
	v_pk_add_f32 v[48:49], v[48:49], 1.0 op_sel_hi:[1,0]
	s_nop 0
	v_rcp_f32_e32 v48, v48
	v_rcp_f32_e32 v49, v49
	s_nop 0
	v_pk_mul_f32 v[46:47], v[46:47], v[48:49]
	s_nop 0
	v_pk_mul_f32 v[44:45], v[44:45], v[46:47]
	v_pk_mul_f32 v[46:47], v[38:39], s[34:35] op_sel_hi:[1,0]
	s_nop 0
	v_exp_f32_e32 v46, v46
	v_exp_f32_e32 v47, v47
	s_nop 0
	v_pk_add_f32 v[46:47], v[46:47], 1.0 op_sel_hi:[1,0]
	s_nop 0
	v_rcp_f32_e32 v46, v46
	v_rcp_f32_e32 v47, v47
	s_nop 0
	v_pk_mul_f32 v[38:39], v[38:39], v[46:47]
	s_nop 0
	v_pk_mul_f32 v[38:39], v[34:35], v[38:39]
	v_pk_add_f32 v[34:35], v[40:41], v[58:59]
	s_nop 0
	v_min_f32_e32 v35, 0x40e00000, v35
	v_min_f32_e32 v34, 0x40e00000, v34
	v_pk_mul_f32 v[40:41], v[34:35], s[34:35] op_sel_hi:[1,0]
	s_nop 0
	v_exp_f32_e32 v40, v40
	v_exp_f32_e32 v41, v41
	s_nop 0
	v_pk_add_f32 v[40:41], v[40:41], 1.0 op_sel_hi:[1,0]
	s_nop 0
	v_rcp_f32_e32 v40, v40
	v_rcp_f32_e32 v41, v41
	s_nop 0
	v_pk_mul_f32 v[34:35], v[34:35], v[40:41]
	s_nop 0
	v_pk_mul_f32 v[40:41], v[36:37], v[34:35]
	v_cvt_pk_bf16_f32 v34, v42, v43
	v_cvt_pk_bf16_f32 v35, v44, v45
	v_cvt_pk_bf16_f32 v36, v38, v39
	v_lshl_add_u64 v[38:39], s[14:15], 0, v[152:153]
	v_cvt_pk_bf16_f32 v37, v40, v41
	global_store_dwordx4 v[38:39], v[34:37], off
	s_add_i32 s14, s60, 0xa0
	s_ashr_i32 s15, s14, 31
	v_pk_mul_f32 v[34:35], v[30:31], s[34:35] op_sel_hi:[1,0]
	s_lshl_b64 s[14:15], s[14:15], 11
	v_exp_f32_e32 v34, v34
	v_exp_f32_e32 v35, v35
	s_add_u32 s1, s78, s14
	s_addc_u32 s2, s79, s15
	s_add_u32 s14, s1, s40
	v_pk_add_f32 v[34:35], v[34:35], 1.0 op_sel_hi:[1,0]
	s_addc_u32 s15, s2, s41
	v_rcp_f32_e32 v34, v34
	v_rcp_f32_e32 v35, v35
	s_nop 0
	v_pk_mul_f32 v[30:31], v[30:31], v[34:35]
	s_nop 0
	v_pk_mul_f32 v[26:27], v[26:27], v[30:31]
	v_pk_add_f32 v[30:31], v[32:33], v[74:75]
	s_nop 0
	v_min_f32_e32 v31, 0x40e00000, v31
	v_min_f32_e32 v30, 0x40e00000, v30
	v_pk_mul_f32 v[32:33], v[30:31], s[34:35] op_sel_hi:[1,0]
	s_nop 0
	v_exp_f32_e32 v32, v32
	v_exp_f32_e32 v33, v33
	s_nop 0
	v_pk_add_f32 v[32:33], v[32:33], 1.0 op_sel_hi:[1,0]
	s_nop 0
	v_rcp_f32_e32 v32, v32
	v_rcp_f32_e32 v33, v33
	s_nop 0
	v_pk_mul_f32 v[30:31], v[30:31], v[32:33]
	s_nop 0
	v_pk_mul_f32 v[28:29], v[28:29], v[30:31]
	v_pk_mul_f32 v[30:31], v[22:23], s[34:35] op_sel_hi:[1,0]
	s_nop 0
	v_exp_f32_e32 v30, v30
	v_exp_f32_e32 v31, v31
	s_nop 0
	v_pk_add_f32 v[30:31], v[30:31], 1.0 op_sel_hi:[1,0]
	s_nop 0
	v_rcp_f32_e32 v30, v30
	v_rcp_f32_e32 v31, v31
	s_nop 0
	v_pk_mul_f32 v[22:23], v[22:23], v[30:31]
	s_nop 0
	v_pk_mul_f32 v[22:23], v[18:19], v[22:23]
	v_pk_add_f32 v[18:19], v[24:25], v[58:59]
	s_nop 0
	v_min_f32_e32 v19, 0x40e00000, v19
	v_min_f32_e32 v18, 0x40e00000, v18
	v_pk_mul_f32 v[24:25], v[18:19], s[34:35] op_sel_hi:[1,0]
	s_nop 0
	v_exp_f32_e32 v24, v24
	v_exp_f32_e32 v25, v25
	s_nop 0
	v_pk_add_f32 v[24:25], v[24:25], 1.0 op_sel_hi:[1,0]
	s_nop 0
	v_rcp_f32_e32 v24, v24
	v_rcp_f32_e32 v25, v25
	s_nop 0
	v_pk_mul_f32 v[18:19], v[18:19], v[24:25]
	s_nop 0
	v_pk_mul_f32 v[24:25], v[20:21], v[18:19]
	v_cvt_pk_bf16_f32 v18, v26, v27
	v_cvt_pk_bf16_f32 v19, v28, v29
	v_cvt_pk_bf16_f32 v20, v22, v23
	v_lshl_add_u64 v[22:23], s[14:15], 0, v[152:153]
	v_cvt_pk_bf16_f32 v21, v24, v25
	global_store_dwordx4 v[22:23], v[18:21], off
	s_add_i32 s14, s60, 0xb0
	s_ashr_i32 s15, s14, 31
	v_pk_mul_f32 v[18:19], v[14:15], s[34:35] op_sel_hi:[1,0]
	s_lshl_b64 s[14:15], s[14:15], 11
	v_exp_f32_e32 v18, v18
	v_exp_f32_e32 v19, v19
	s_add_u32 s1, s78, s14
	s_addc_u32 s2, s79, s15
	s_add_u32 s14, s1, s40
	v_pk_add_f32 v[18:19], v[18:19], 1.0 op_sel_hi:[1,0]
	s_addc_u32 s15, s2, s41
	v_rcp_f32_e32 v18, v18
	v_rcp_f32_e32 v19, v19
	s_and_b64 vcc, exec, s[38:39]
	v_pk_mul_f32 v[14:15], v[14:15], v[18:19]
	s_nop 0
	v_pk_mul_f32 v[10:11], v[10:11], v[14:15]
	v_pk_add_f32 v[14:15], v[16:17], v[74:75]
	s_nop 0
	v_min_f32_e32 v15, 0x40e00000, v15
	v_min_f32_e32 v14, 0x40e00000, v14
	v_pk_mul_f32 v[16:17], v[14:15], s[34:35] op_sel_hi:[1,0]
	s_nop 0
	v_exp_f32_e32 v16, v16
	v_exp_f32_e32 v17, v17
	s_nop 0
	v_pk_add_f32 v[16:17], v[16:17], 1.0 op_sel_hi:[1,0]
	s_nop 0
	v_rcp_f32_e32 v16, v16
	v_rcp_f32_e32 v17, v17
	s_nop 0
	v_pk_mul_f32 v[14:15], v[14:15], v[16:17]
	s_nop 0
	v_pk_mul_f32 v[12:13], v[12:13], v[14:15]
	v_pk_mul_f32 v[14:15], v[6:7], s[34:35] op_sel_hi:[1,0]
	s_nop 0
	v_exp_f32_e32 v14, v14
	v_exp_f32_e32 v15, v15
	s_nop 0
	v_pk_add_f32 v[14:15], v[14:15], 1.0 op_sel_hi:[1,0]
	s_nop 0
	v_rcp_f32_e32 v14, v14
	v_rcp_f32_e32 v15, v15
	s_nop 0
	v_pk_mul_f32 v[6:7], v[6:7], v[14:15]
	s_nop 0
	v_pk_mul_f32 v[6:7], v[2:3], v[6:7]
	v_pk_add_f32 v[2:3], v[8:9], v[58:59]
	s_nop 0
	v_min_f32_e32 v3, 0x40e00000, v3
	v_min_f32_e32 v2, 0x40e00000, v2
	v_pk_mul_f32 v[8:9], v[2:3], s[34:35] op_sel_hi:[1,0]
	s_nop 0
	v_exp_f32_e32 v8, v8
	v_exp_f32_e32 v9, v9
	s_nop 0
	v_pk_add_f32 v[8:9], v[8:9], 1.0 op_sel_hi:[1,0]
	s_nop 0
	v_rcp_f32_e32 v8, v8
	v_rcp_f32_e32 v9, v9
	s_nop 0
	v_pk_mul_f32 v[2:3], v[2:3], v[8:9]
	s_nop 0
	v_pk_mul_f32 v[8:9], v[4:5], v[2:3]
	v_cvt_pk_bf16_f32 v2, v10, v11
	v_cvt_pk_bf16_f32 v3, v12, v13
	v_cvt_pk_bf16_f32 v4, v6, v7
	v_lshl_add_u64 v[6:7], s[14:15], 0, v[152:153]
	s_mov_b64 s[14:15], -1
	v_cvt_pk_bf16_f32 v5, v8, v9
	global_store_dwordx4 v[6:7], v[2:5], off
	s_cbranch_vccnz .LBB0_1325
	s_andn2_b64 vcc, exec, s[48:49]
	s_cbranch_vccnz .LBB0_1324
	s_barrier
	s_branch .LBB0_1324

.LBB0_1368:
	v_and_b32_e32 v150, 15, v24
	v_lshlrev_b32_e32 v26, 4, v1
	v_lshlrev_b32_e32 v24, 2, v24
	s_lshl_b32 s34, s35, 6
	v_lshl_or_b32 v26, v150, 6, v26
	s_lshl_b32 s35, s35, 13
	v_and_b32_e32 v24, 32, v24
	v_bitop3_b32 v28, v26, s35, v24 bitop3:0xde
	s_lshl_b32 s35, s3, 7
	v_bitop3_b32 v151, v26, s35, v24 bitop3:0xde
	v_lshl_add_u64 v[26:27], v[18:19], 0, s[92:93]
	s_add_i32 m0, s16, 0x19000
	s_waitcnt vmcnt(2)
	s_barrier
	global_load_lds_dwordx4 v[26:27], off
	v_lshl_add_u64 v[26:27], v[18:19], 0, s[4:5]
	s_add_i32 m0, s16, 0x1b000
	s_add_i32 s35, s16, 0x9000
	global_load_lds_dwordx4 v[26:27], off
	v_lshl_add_u64 v[26:27], v[20:21], 0, s[92:93]
	s_mov_b32 m0, s35
	s_add_i32 s42, s16, 0xb000
	global_load_lds_dwordx4 v[26:27], off
	v_lshl_add_u64 v[20:21], v[20:21], 0, s[4:5]
	s_mov_b32 m0, s42
	s_mov_b64 s[46:47], 0
	global_load_lds_dwordx4 v[20:21], off
	s_add_i32 m0, s16, 0x1d000
	v_lshl_add_u64 v[20:21], v[18:19], 0, s[6:7]
	global_load_lds_dwordx4 v[20:21], off
	v_lshl_add_u64 v[18:19], v[18:19], 0, s[8:9]
	s_add_i32 m0, s16, 0x1f000
	s_add_u32 s14, s14, s24
	global_load_lds_dwordx4 v[18:19], off
	v_lshlrev_b32_e32 v18, 14, v23
	v_and_b32_e32 v18, 0xffff8000, v18
	v_lshl_add_u32 v18, v22, 11, v18
	v_and_b32_e32 v19, 1, v23
	v_lshl_or_b32 v18, v19, 6, v18
	s_waitcnt vmcnt(6)
	v_lshl_add_u32 v18, v25, 1, v18
	v_mov_b32_e32 v19, v187
	s_addc_u32 s15, s15, s25
	v_lshl_add_u64 v[148:149], s[14:15], 0, v[18:19]
	v_mov_b32_e32 v18, 0
	s_mov_b32 s24, -2
	v_add_u32_e32 v152, 0, v28
	v_mov_b32_e32 v19, 0
	v_mov_b64_e32 v[20:21], 0
	v_mov_b64_e32 v[22:23], 0
	v_mov_b64_e32 v[24:25], 0
	v_mov_b64_e32 v[34:35], 0
	v_mov_b64_e32 v[36:37], 0
	v_mov_b64_e32 v[38:39], 0
	v_mov_b64_e32 v[40:41], 0
	v_mov_b64_e32 v[50:51], 0
	v_mov_b64_e32 v[52:53], 0
	v_mov_b64_e32 v[54:55], 0
	v_mov_b64_e32 v[56:57], 0
	v_mov_b64_e32 v[66:67], 0
	v_mov_b64_e32 v[68:69], 0
	v_mov_b64_e32 v[70:71], 0
	v_mov_b64_e32 v[72:73], 0
	v_mov_b64_e32 v[26:27], 0
	v_mov_b64_e32 v[28:29], 0
	v_mov_b64_e32 v[30:31], 0
	v_mov_b64_e32 v[32:33], 0
	v_mov_b64_e32 v[42:43], 0
	v_mov_b64_e32 v[44:45], 0
	v_mov_b64_e32 v[46:47], 0
	v_mov_b64_e32 v[48:49], 0
	v_mov_b64_e32 v[58:59], 0
	v_mov_b64_e32 v[60:61], 0
	v_mov_b64_e32 v[62:63], 0
	v_mov_b64_e32 v[64:65], 0
	v_mov_b64_e32 v[74:75], 0
	v_mov_b64_e32 v[76:77], 0
	v_mov_b64_e32 v[78:79], 0
	v_mov_b64_e32 v[80:81], 0
	v_mov_b64_e32 v[82:83], 0
	v_mov_b64_e32 v[84:85], 0
	v_mov_b64_e32 v[86:87], 0
	v_mov_b64_e32 v[88:89], 0
	v_mov_b64_e32 v[98:99], 0
	v_mov_b64_e32 v[100:101], 0
	v_mov_b64_e32 v[102:103], 0
	v_mov_b64_e32 v[104:105], 0
	v_mov_b64_e32 v[114:115], 0
	v_mov_b64_e32 v[116:117], 0
	v_mov_b64_e32 v[118:119], 0
	v_mov_b64_e32 v[120:121], 0
	v_mov_b64_e32 v[130:131], 0
	v_mov_b64_e32 v[132:133], 0
	v_mov_b64_e32 v[134:135], 0
	v_mov_b64_e32 v[136:137], 0
	v_mov_b64_e32 v[90:91], 0
	v_mov_b64_e32 v[92:93], 0
	v_mov_b64_e32 v[94:95], 0
	v_mov_b64_e32 v[96:97], 0
	v_mov_b64_e32 v[106:107], 0
	v_mov_b64_e32 v[108:109], 0
	v_mov_b64_e32 v[110:111], 0
	v_mov_b64_e32 v[112:113], 0
	v_mov_b64_e32 v[122:123], 0
	v_mov_b64_e32 v[124:125], 0
	v_mov_b64_e32 v[126:127], 0
	v_mov_b64_e32 v[128:129], 0
	v_mov_b64_e32 v[138:139], 0
	v_mov_b64_e32 v[140:141], 0
	v_mov_b64_e32 v[142:143], 0
	v_mov_b64_e32 v[144:145], 0
	s_barrier

.LBB0_1372:
	s_add_u32 s2, s38, 0x7f000000
	s_addc_u32 s13, s39, 0
	s_lshl_b32 s0, s96, 8
	s_add_i32 s0, s34, s0
	s_ashr_i32 s1, s0, 31
	s_lshl_b64 s[14:15], s[0:1], 10
	s_add_u32 s1, s2, s14
	s_addc_u32 s14, s13, s15
	s_add_u32 s1, s1, s12
	s_addc_u32 s15, s14, 0
	v_lshlrev_b32_e32 v146, 10, v150
	s_add_u32 s14, s1, s3
	v_lshl_or_b32 v186, v1, 3, v146
	s_waitcnt vmcnt(0)
	v_pk_add_f32 v[138:139], v[10:11], v[138:139]
	v_mov_b32_e32 v147, v187
	s_addc_u32 s15, s15, 0
	v_cvt_pk_fp8_f32 v147, v138, v139
	v_lshl_add_u64 v[138:139], s[14:15], 0, v[186:187]
	s_add_i32 s14, s0, 16
	s_ashr_i32 s15, s14, 31
	s_lshl_b64 s[14:15], s[14:15], 10
	s_add_u32 s1, s2, s14
	s_addc_u32 s14, s13, s15
	s_add_u32 s1, s1, s12
	v_pk_add_f32 v[140:141], v[12:13], v[140:141]
	s_addc_u32 s15, s14, 0
	v_cvt_pk_fp8_f32 v147, v140, v141 op_sel:[0,0,1]
	v_pk_add_f32 v[130:131], v[2:3], v[130:131]
	v_mov_b32_e32 v141, v187
	s_add_u32 s14, s1, s3
	v_cvt_pk_fp8_f32 v141, v130, v131
	v_pk_add_f32 v[122:123], v[10:11], v[122:123]
	v_mov_b32_e32 v131, v187
	s_addc_u32 s15, s15, 0
	v_cvt_pk_fp8_f32 v131, v122, v123
	v_lshl_add_u64 v[122:123], s[14:15], 0, v[186:187]
	s_add_i32 s14, s0, 32
	s_ashr_i32 s15, s14, 31
	s_lshl_b64 s[14:15], s[14:15], 10
	s_add_u32 s1, s2, s14
	s_addc_u32 s14, s13, s15
	s_add_u32 s1, s1, s12
	v_pk_add_f32 v[124:125], v[12:13], v[124:125]
	s_addc_u32 s15, s14, 0
	v_cvt_pk_fp8_f32 v131, v124, v125 op_sel:[0,0,1]
	v_pk_add_f32 v[114:115], v[2:3], v[114:115]
	v_mov_b32_e32 v125, v187
	s_add_u32 s14, s1, s3
	v_cvt_pk_fp8_f32 v125, v114, v115
	v_pk_add_f32 v[106:107], v[10:11], v[106:107]
	v_mov_b32_e32 v115, v187
	s_addc_u32 s15, s15, 0
	v_cvt_pk_fp8_f32 v115, v106, v107
	v_lshl_add_u64 v[106:107], s[14:15], 0, v[186:187]
	s_add_i32 s14, s0, 48
	s_ashr_i32 s15, s14, 31
	s_lshl_b64 s[14:15], s[14:15], 10
	s_add_u32 s1, s2, s14
	s_addc_u32 s14, s13, s15
	s_add_u32 s1, s1, s12
	v_pk_add_f32 v[108:109], v[12:13], v[108:109]
	s_addc_u32 s15, s14, 0
	v_cvt_pk_fp8_f32 v115, v108, v109 op_sel:[0,0,1]
	v_pk_add_f32 v[98:99], v[2:3], v[98:99]
	v_mov_b32_e32 v109, v187
	s_add_u32 s14, s1, s3
	v_cvt_pk_fp8_f32 v109, v98, v99
	v_pk_add_f32 v[90:91], v[10:11], v[90:91]
	v_mov_b32_e32 v99, v187
	s_addc_u32 s15, s15, 0
	v_cvt_pk_fp8_f32 v99, v90, v91
	v_lshl_add_u64 v[90:91], s[14:15], 0, v[186:187]
	s_add_i32 s14, s0, 0x80
	s_ashr_i32 s15, s14, 31
	s_lshl_b64 s[14:15], s[14:15], 10
	s_add_u32 s1, s2, s14
	s_addc_u32 s14, s13, s15
	s_add_u32 s1, s1, s12
	v_pk_add_f32 v[92:93], v[12:13], v[92:93]
	s_addc_u32 s15, s14, 0
	v_cvt_pk_fp8_f32 v99, v92, v93 op_sel:[0,0,1]
	v_pk_add_f32 v[82:83], v[2:3], v[82:83]
	v_mov_b32_e32 v93, v187
	s_add_u32 s14, s1, s3
	v_cvt_pk_fp8_f32 v93, v82, v83
	v_pk_add_f32 v[74:75], v[10:11], v[74:75]
	v_mov_b32_e32 v83, v187
	s_addc_u32 s15, s15, 0
	v_cvt_pk_fp8_f32 v83, v74, v75
	v_lshl_add_u64 v[74:75], s[14:15], 0, v[186:187]
	s_add_i32 s14, s0, 0x90
	s_ashr_i32 s15, s14, 31
	s_lshl_b64 s[14:15], s[14:15], 10
	s_add_u32 s1, s2, s14
	s_addc_u32 s14, s13, s15
	v_pk_add_f32 v[76:77], v[12:13], v[76:77]
	s_add_u32 s1, s1, s12
	v_cvt_pk_fp8_f32 v83, v76, v77 op_sel:[0,0,1]
	v_pk_add_f32 v[66:67], v[2:3], v[66:67]
	v_mov_b32_e32 v77, v187
	s_addc_u32 s15, s14, 0
	v_cvt_pk_fp8_f32 v77, v66, v67
	v_pk_add_f32 v[58:59], v[10:11], v[58:59]
	v_mov_b32_e32 v67, v187
	s_add_u32 s14, s1, s3
	v_cvt_pk_fp8_f32 v67, v58, v59
	s_addc_u32 s15, s15, 0
	v_lshl_add_u64 v[58:59], s[14:15], 0, v[186:187]
	s_add_i32 s14, s0, 0xa0
	s_ashr_i32 s15, s14, 31
	v_pk_add_f32 v[60:61], v[12:13], v[60:61]
	s_lshl_b64 s[14:15], s[14:15], 10
	v_cvt_pk_fp8_f32 v67, v60, v61 op_sel:[0,0,1]
	v_pk_add_f32 v[50:51], v[2:3], v[50:51]
	v_mov_b32_e32 v61, v187
	s_add_u32 s1, s2, s14
	v_cvt_pk_fp8_f32 v61, v50, v51
	v_pk_add_f32 v[42:43], v[10:11], v[42:43]
	v_mov_b32_e32 v51, v187
	s_addc_u32 s14, s13, s15
	v_pk_add_f32 v[10:11], v[10:11], v[26:27]
	v_mov_b32_e32 v27, v187
	v_cvt_pk_fp8_f32 v51, v42, v43
	s_add_u32 s1, s1, s12
	v_cvt_pk_fp8_f32 v27, v10, v11
	s_addc_u32 s15, s14, 0
	s_add_u32 s14, s1, s3
	v_pk_add_f32 v[44:45], v[12:13], v[44:45]
	s_addc_u32 s15, s15, 0
	s_addk_i32 s0, 0xb0
	v_pk_add_f32 v[12:13], v[12:13], v[28:29]
	v_pk_add_f32 v[142:143], v[14:15], v[142:143]
	v_mov_b32_e32 v146, v187
	v_pk_add_f32 v[134:135], v[6:7], v[134:135]
	v_mov_b32_e32 v140, v187
	v_pk_add_f32 v[126:127], v[14:15], v[126:127]
	v_mov_b32_e32 v130, v187
	v_pk_add_f32 v[118:119], v[6:7], v[118:119]
	v_mov_b32_e32 v124, v187
	v_pk_add_f32 v[110:111], v[14:15], v[110:111]
	v_mov_b32_e32 v114, v187
	v_pk_add_f32 v[102:103], v[6:7], v[102:103]
	v_mov_b32_e32 v108, v187
	v_pk_add_f32 v[94:95], v[14:15], v[94:95]
	v_mov_b32_e32 v98, v187
	v_pk_add_f32 v[86:87], v[6:7], v[86:87]
	v_mov_b32_e32 v92, v187
	v_pk_add_f32 v[78:79], v[14:15], v[78:79]
	v_mov_b32_e32 v82, v187
	v_pk_add_f32 v[70:71], v[6:7], v[70:71]
	v_mov_b32_e32 v76, v187
	v_pk_add_f32 v[62:63], v[14:15], v[62:63]
	v_mov_b32_e32 v66, v187
	v_pk_add_f32 v[54:55], v[6:7], v[54:55]
	v_mov_b32_e32 v60, v187
	v_pk_add_f32 v[46:47], v[14:15], v[46:47]
	v_mov_b32_e32 v50, v187
	v_cvt_pk_fp8_f32 v51, v44, v45 op_sel:[0,0,1]
	v_pk_add_f32 v[38:39], v[6:7], v[38:39]
	v_pk_add_f32 v[34:35], v[2:3], v[34:35]
	v_mov_b32_e32 v44, v187
	v_mov_b32_e32 v45, v187
	s_ashr_i32 s1, s0, 31
	v_pk_add_f32 v[14:15], v[14:15], v[30:31]
	v_mov_b32_e32 v26, v187
	v_cvt_pk_fp8_f32 v27, v12, v13 op_sel:[0,0,1]
	v_pk_add_f32 v[6:7], v[6:7], v[22:23]
	v_pk_add_f32 v[2:3], v[2:3], v[18:19]
	v_mov_b32_e32 v12, v187
	v_mov_b32_e32 v13, v187
	v_cvt_pk_fp8_f32 v146, v142, v143
	v_cvt_pk_fp8_f32 v140, v134, v135
	v_cvt_pk_fp8_f32 v130, v126, v127
	v_cvt_pk_fp8_f32 v124, v118, v119
	v_cvt_pk_fp8_f32 v114, v110, v111
	v_cvt_pk_fp8_f32 v108, v102, v103
	v_cvt_pk_fp8_f32 v98, v94, v95
	v_cvt_pk_fp8_f32 v92, v86, v87
	v_cvt_pk_fp8_f32 v82, v78, v79
	v_cvt_pk_fp8_f32 v76, v70, v71
	v_cvt_pk_fp8_f32 v66, v62, v63
	v_cvt_pk_fp8_f32 v60, v54, v55
	v_cvt_pk_fp8_f32 v50, v46, v47
	v_cvt_pk_fp8_f32 v44, v38, v39
	v_cvt_pk_fp8_f32 v45, v34, v35
	s_lshl_b64 s[0:1], s[0:1], 10
	v_cvt_pk_fp8_f32 v26, v14, v15
	v_cvt_pk_fp8_f32 v12, v6, v7
	v_cvt_pk_fp8_f32 v13, v2, v3
	s_add_u32 s0, s2, s0
	s_addc_u32 s1, s13, s1
	v_pk_add_f32 v[144:145], v[16:17], v[144:145]
	v_pk_add_f32 v[136:137], v[8:9], v[136:137]
	v_pk_add_f32 v[132:133], v[4:5], v[132:133]
	v_pk_add_f32 v[128:129], v[16:17], v[128:129]
	v_pk_add_f32 v[120:121], v[8:9], v[120:121]
	v_pk_add_f32 v[116:117], v[4:5], v[116:117]
	v_pk_add_f32 v[112:113], v[16:17], v[112:113]
	v_pk_add_f32 v[104:105], v[8:9], v[104:105]
	v_pk_add_f32 v[100:101], v[4:5], v[100:101]
	v_pk_add_f32 v[96:97], v[16:17], v[96:97]
	v_pk_add_f32 v[88:89], v[8:9], v[88:89]
	v_pk_add_f32 v[84:85], v[4:5], v[84:85]
	v_pk_add_f32 v[80:81], v[16:17], v[80:81]
	v_pk_add_f32 v[72:73], v[8:9], v[72:73]
	v_pk_add_f32 v[68:69], v[4:5], v[68:69]
	v_pk_add_f32 v[64:65], v[16:17], v[64:65]
	v_pk_add_f32 v[56:57], v[8:9], v[56:57]
	v_pk_add_f32 v[52:53], v[4:5], v[52:53]
	v_pk_add_f32 v[48:49], v[16:17], v[48:49]
	v_pk_add_f32 v[40:41], v[8:9], v[40:41]
	v_pk_add_f32 v[36:37], v[4:5], v[36:37]
	v_pk_add_f32 v[16:17], v[16:17], v[32:33]
	s_add_u32 s0, s0, s12
	v_pk_add_f32 v[8:9], v[8:9], v[24:25]
	v_pk_add_f32 v[4:5], v[4:5], v[20:21]
	v_cvt_pk_fp8_f32 v146, v144, v145 op_sel:[0,0,1]
	v_cvt_pk_fp8_f32 v140, v136, v137 op_sel:[0,0,1]
	v_cvt_pk_fp8_f32 v141, v132, v133 op_sel:[0,0,1]
	v_cvt_pk_fp8_f32 v130, v128, v129 op_sel:[0,0,1]
	v_cvt_pk_fp8_f32 v124, v120, v121 op_sel:[0,0,1]
	v_cvt_pk_fp8_f32 v125, v116, v117 op_sel:[0,0,1]
	v_cvt_pk_fp8_f32 v114, v112, v113 op_sel:[0,0,1]
	v_cvt_pk_fp8_f32 v108, v104, v105 op_sel:[0,0,1]
	v_cvt_pk_fp8_f32 v109, v100, v101 op_sel:[0,0,1]
	v_cvt_pk_fp8_f32 v98, v96, v97 op_sel:[0,0,1]
	v_cvt_pk_fp8_f32 v92, v88, v89 op_sel:[0,0,1]
	v_cvt_pk_fp8_f32 v93, v84, v85 op_sel:[0,0,1]
	v_cvt_pk_fp8_f32 v82, v80, v81 op_sel:[0,0,1]
	v_cvt_pk_fp8_f32 v76, v72, v73 op_sel:[0,0,1]
	v_cvt_pk_fp8_f32 v77, v68, v69 op_sel:[0,0,1]
	v_cvt_pk_fp8_f32 v66, v64, v65 op_sel:[0,0,1]
	v_cvt_pk_fp8_f32 v60, v56, v57 op_sel:[0,0,1]
	v_cvt_pk_fp8_f32 v61, v52, v53 op_sel:[0,0,1]
	v_cvt_pk_fp8_f32 v50, v48, v49 op_sel:[0,0,1]
	v_cvt_pk_fp8_f32 v44, v40, v41 op_sel:[0,0,1]
	v_cvt_pk_fp8_f32 v45, v36, v37 op_sel:[0,0,1]
	v_cvt_pk_fp8_f32 v26, v16, v17 op_sel:[0,0,1]
	s_addc_u32 s1, s1, 0
	v_cvt_pk_fp8_f32 v12, v8, v9 op_sel:[0,0,1]
	v_cvt_pk_fp8_f32 v13, v4, v5 op_sel:[0,0,1]
	s_add_u32 s0, s0, s3
	s_addc_u32 s1, s1, 0
	v_lshl_add_u64 v[42:43], s[14:15], 0, v[186:187]
	v_lshl_add_u64 v[10:11], s[0:1], 0, v[186:187]
	global_store_dwordx2 v[138:139], v[146:147], off
	global_store_dwordx2 v[138:139], v[140:141], off offset:128
	global_store_dwordx2 v[122:123], v[130:131], off
	global_store_dwordx2 v[122:123], v[124:125], off offset:128
	global_store_dwordx2 v[106:107], v[114:115], off
	global_store_dwordx2 v[106:107], v[108:109], off offset:128
	global_store_dwordx2 v[90:91], v[98:99], off
	global_store_dwordx2 v[90:91], v[92:93], off offset:128
	global_store_dwordx2 v[74:75], v[82:83], off
	global_store_dwordx2 v[74:75], v[76:77], off offset:128
	global_store_dwordx2 v[58:59], v[66:67], off
	global_store_dwordx2 v[58:59], v[60:61], off offset:128
	global_store_dwordx2 v[42:43], v[50:51], off
	global_store_dwordx2 v[42:43], v[44:45], off offset:128
	global_store_dwordx2 v[10:11], v[26:27], off
	global_store_dwordx2 v[10:11], v[12:13], off offset:128
	s_waitcnt vmcnt(0)
	s_barrier

.LBB0_1462:
	s_add_u32 s2, s56, 0x100
	s_addc_u32 s24, s57, 0
	s_add_u32 s56, s58, 0x40080
	s_waitcnt lgkmcnt(0)
	v_mov_b32_e32 v18, 0
	s_addc_u32 s57, s59, 0
	s_mov_b32 s25, -2
	v_mov_b32_e32 v19, 0
	v_mov_b64_e32 v[20:21], 0
	v_mov_b64_e32 v[22:23], 0
	v_mov_b64_e32 v[24:25], 0
	v_mov_b64_e32 v[34:35], 0
	v_mov_b64_e32 v[36:37], 0
	v_mov_b64_e32 v[38:39], 0
	v_mov_b64_e32 v[40:41], 0
	v_mov_b64_e32 v[50:51], 0
	v_mov_b64_e32 v[52:53], 0
	v_mov_b64_e32 v[54:55], 0
	v_mov_b64_e32 v[56:57], 0
	v_mov_b64_e32 v[66:67], 0
	v_mov_b64_e32 v[68:69], 0
	v_mov_b64_e32 v[70:71], 0
	v_mov_b64_e32 v[72:73], 0
	v_mov_b64_e32 v[26:27], 0
	v_mov_b64_e32 v[28:29], 0
	v_mov_b64_e32 v[30:31], 0
	v_mov_b64_e32 v[32:33], 0
	v_mov_b64_e32 v[42:43], 0
	v_mov_b64_e32 v[44:45], 0
	v_mov_b64_e32 v[46:47], 0
	v_mov_b64_e32 v[48:49], 0
	v_mov_b64_e32 v[58:59], 0
	v_mov_b64_e32 v[60:61], 0
	v_mov_b64_e32 v[62:63], 0
	v_mov_b64_e32 v[64:65], 0
	v_mov_b64_e32 v[74:75], 0
	v_mov_b64_e32 v[76:77], 0
	v_mov_b64_e32 v[78:79], 0
	v_mov_b64_e32 v[80:81], 0
	v_mov_b64_e32 v[82:83], 0
	v_mov_b64_e32 v[84:85], 0
	v_mov_b64_e32 v[86:87], 0
	v_mov_b64_e32 v[88:89], 0
	v_mov_b64_e32 v[98:99], 0
	v_mov_b64_e32 v[100:101], 0
	v_mov_b64_e32 v[102:103], 0
	v_mov_b64_e32 v[104:105], 0
	v_mov_b64_e32 v[114:115], 0
	v_mov_b64_e32 v[116:117], 0
	v_mov_b64_e32 v[118:119], 0
	v_mov_b64_e32 v[120:121], 0
	v_mov_b64_e32 v[130:131], 0
	v_mov_b64_e32 v[132:133], 0
	v_mov_b64_e32 v[134:135], 0
	v_mov_b64_e32 v[136:137], 0
	v_mov_b64_e32 v[90:91], 0
	v_mov_b64_e32 v[92:93], 0
	v_mov_b64_e32 v[94:95], 0
	v_mov_b64_e32 v[96:97], 0
	v_mov_b64_e32 v[106:107], 0
	v_mov_b64_e32 v[108:109], 0
	v_mov_b64_e32 v[110:111], 0
	v_mov_b64_e32 v[112:113], 0
	v_mov_b64_e32 v[122:123], 0
	v_mov_b64_e32 v[124:125], 0
	v_mov_b64_e32 v[126:127], 0
	v_mov_b64_e32 v[128:129], 0
	v_mov_b64_e32 v[138:139], 0
	v_mov_b64_e32 v[140:141], 0
	v_mov_b64_e32 v[142:143], 0
	v_mov_b64_e32 v[144:145], 0

.LBB0_1466:
	s_lshl_b32 s15, s54, 8
	s_add_i32 s54, s15, s72
	s_ashr_i32 s55, s54, 31
	s_lshl_b64 s[24:25], s[54:55], 10
	s_add_u32 s24, s73, s24
	s_addc_u32 s25, s74, s25
	s_lshl_b32 s2, s42, 8
	s_ashr_i32 s14, s2, 31
	s_add_u32 s24, s24, s2
	s_addc_u32 s25, s25, s14
	s_add_u32 s24, s24, s29
	s_waitcnt vmcnt(0)
	v_pk_add_f32 v[138:139], v[10:11], v[138:139]
	v_mov_b32_e32 v157, v187
	s_addc_u32 s25, s25, 0
	v_cvt_pk_fp8_f32 v157, v138, v139
	v_lshl_add_u64 v[138:139], s[24:25], 0, v[150:151]
	s_add_i32 s24, s77, s15
	s_ashr_i32 s25, s24, 31
	s_lshl_b64 s[24:25], s[24:25], 10
	s_add_u32 s24, s73, s24
	s_addc_u32 s25, s74, s25
	s_add_u32 s24, s24, s2
	v_pk_add_f32 v[140:141], v[12:13], v[140:141]
	s_addc_u32 s25, s25, s14
	v_cvt_pk_fp8_f32 v157, v140, v141 op_sel:[0,0,1]
	v_pk_add_f32 v[130:131], v[2:3], v[130:131]
	v_mov_b32_e32 v141, v187
	s_add_u32 s24, s24, s29
	v_cvt_pk_fp8_f32 v141, v130, v131
	v_pk_add_f32 v[122:123], v[10:11], v[122:123]
	v_mov_b32_e32 v131, v187
	s_addc_u32 s25, s25, 0
	v_cvt_pk_fp8_f32 v131, v122, v123
	v_lshl_add_u64 v[122:123], s[24:25], 0, v[150:151]
	s_add_i32 s24, s78, s15
	s_ashr_i32 s25, s24, 31
	s_lshl_b64 s[24:25], s[24:25], 10
	s_add_u32 s24, s73, s24
	s_addc_u32 s25, s74, s25
	s_add_u32 s24, s24, s2
	v_pk_add_f32 v[124:125], v[12:13], v[124:125]
	s_addc_u32 s25, s25, s14
	v_cvt_pk_fp8_f32 v131, v124, v125 op_sel:[0,0,1]
	v_pk_add_f32 v[114:115], v[2:3], v[114:115]
	v_mov_b32_e32 v125, v187
	s_add_u32 s24, s24, s29
	v_cvt_pk_fp8_f32 v125, v114, v115
	v_pk_add_f32 v[106:107], v[10:11], v[106:107]
	v_mov_b32_e32 v115, v187
	s_addc_u32 s25, s25, 0
	v_cvt_pk_fp8_f32 v115, v106, v107
	v_lshl_add_u64 v[106:107], s[24:25], 0, v[150:151]
	s_add_i32 s24, s79, s15
	s_ashr_i32 s25, s24, 31
	s_lshl_b64 s[24:25], s[24:25], 10
	s_add_u32 s15, s73, s24
	s_addc_u32 s24, s74, s25
	s_add_u32 s15, s15, s2
	v_pk_add_f32 v[108:109], v[12:13], v[108:109]
	s_addc_u32 s25, s24, s14
	v_cvt_pk_fp8_f32 v115, v108, v109 op_sel:[0,0,1]
	v_pk_add_f32 v[98:99], v[2:3], v[98:99]
	v_mov_b32_e32 v109, v187
	s_add_u32 s24, s15, s29
	v_cvt_pk_fp8_f32 v109, v98, v99
	v_pk_add_f32 v[90:91], v[10:11], v[90:91]
	v_mov_b32_e32 v99, v187
	s_addc_u32 s25, s25, 0
	v_cvt_pk_fp8_f32 v99, v90, v91
	v_lshl_add_u64 v[90:91], s[24:25], 0, v[150:151]
	s_add_i32 s24, s54, 0x80
	s_ashr_i32 s25, s24, 31
	s_lshl_b64 s[24:25], s[24:25], 10
	s_add_u32 s15, s73, s24
	s_addc_u32 s24, s74, s25
	s_add_u32 s15, s15, s2
	v_pk_add_f32 v[92:93], v[12:13], v[92:93]
	s_addc_u32 s25, s24, s14
	v_cvt_pk_fp8_f32 v99, v92, v93 op_sel:[0,0,1]
	v_pk_add_f32 v[82:83], v[2:3], v[82:83]
	v_mov_b32_e32 v93, v187
	s_add_u32 s24, s15, s29
	v_cvt_pk_fp8_f32 v93, v82, v83
	v_pk_add_f32 v[74:75], v[10:11], v[74:75]
	v_mov_b32_e32 v83, v187
	s_addc_u32 s25, s25, 0
	v_cvt_pk_fp8_f32 v83, v74, v75
	v_lshl_add_u64 v[74:75], s[24:25], 0, v[150:151]
	s_add_i32 s24, s54, 0x90
	s_ashr_i32 s25, s24, 31
	s_lshl_b64 s[24:25], s[24:25], 10
	s_add_u32 s15, s73, s24
	s_addc_u32 s24, s74, s25
	s_add_u32 s15, s15, s2
	v_pk_add_f32 v[76:77], v[12:13], v[76:77]
	s_addc_u32 s25, s24, s14
	v_cvt_pk_fp8_f32 v83, v76, v77 op_sel:[0,0,1]
	v_pk_add_f32 v[66:67], v[2:3], v[66:67]
	v_mov_b32_e32 v77, v187
	s_add_u32 s24, s15, s29
	v_cvt_pk_fp8_f32 v77, v66, v67
	v_pk_add_f32 v[58:59], v[10:11], v[58:59]
	v_mov_b32_e32 v67, v187
	s_addc_u32 s25, s25, 0
	v_cvt_pk_fp8_f32 v67, v58, v59
	v_lshl_add_u64 v[58:59], s[24:25], 0, v[150:151]
	s_add_i32 s24, s54, 0xa0
	s_ashr_i32 s25, s24, 31
	s_lshl_b64 s[24:25], s[24:25], 10
	v_pk_add_f32 v[60:61], v[12:13], v[60:61]
	s_add_u32 s15, s73, s24
	v_cvt_pk_fp8_f32 v67, v60, v61 op_sel:[0,0,1]
	v_pk_add_f32 v[50:51], v[2:3], v[50:51]
	v_mov_b32_e32 v61, v187
	s_addc_u32 s24, s74, s25
	v_cvt_pk_fp8_f32 v61, v50, v51
	v_pk_add_f32 v[42:43], v[10:11], v[42:43]
	v_mov_b32_e32 v51, v187
	s_add_u32 s15, s15, s2
	v_pk_add_f32 v[10:11], v[10:11], v[26:27]
	v_mov_b32_e32 v27, v187
	v_cvt_pk_fp8_f32 v51, v42, v43
	s_addc_u32 s25, s24, s14
	v_cvt_pk_fp8_f32 v27, v10, v11
	s_add_u32 s24, s15, s29
	s_addc_u32 s25, s25, 0
	v_pk_add_f32 v[44:45], v[12:13], v[44:45]
	v_lshl_add_u64 v[42:43], s[24:25], 0, v[150:151]
	s_add_i32 s24, s54, 0xb0
	v_pk_add_f32 v[12:13], v[12:13], v[28:29]
	v_pk_add_f32 v[142:143], v[14:15], v[142:143]
	v_mov_b32_e32 v156, v187
	v_pk_add_f32 v[134:135], v[6:7], v[134:135]
	v_mov_b32_e32 v140, v187
	v_pk_add_f32 v[126:127], v[14:15], v[126:127]
	v_mov_b32_e32 v130, v187
	v_pk_add_f32 v[118:119], v[6:7], v[118:119]
	v_mov_b32_e32 v124, v187
	v_pk_add_f32 v[110:111], v[14:15], v[110:111]
	v_mov_b32_e32 v114, v187
	v_pk_add_f32 v[102:103], v[6:7], v[102:103]
	v_mov_b32_e32 v108, v187
	v_pk_add_f32 v[94:95], v[14:15], v[94:95]
	v_mov_b32_e32 v98, v187
	v_pk_add_f32 v[86:87], v[6:7], v[86:87]
	v_mov_b32_e32 v92, v187
	v_pk_add_f32 v[78:79], v[14:15], v[78:79]
	v_mov_b32_e32 v82, v187
	v_pk_add_f32 v[70:71], v[6:7], v[70:71]
	v_mov_b32_e32 v76, v187
	v_pk_add_f32 v[62:63], v[14:15], v[62:63]
	v_mov_b32_e32 v66, v187
	v_pk_add_f32 v[54:55], v[6:7], v[54:55]
	v_mov_b32_e32 v60, v187
	v_pk_add_f32 v[46:47], v[14:15], v[46:47]
	v_mov_b32_e32 v50, v187
	v_cvt_pk_fp8_f32 v51, v44, v45 op_sel:[0,0,1]
	v_pk_add_f32 v[38:39], v[6:7], v[38:39]
	v_pk_add_f32 v[34:35], v[2:3], v[34:35]
	v_mov_b32_e32 v44, v187
	v_mov_b32_e32 v45, v187
	s_ashr_i32 s25, s24, 31
	v_pk_add_f32 v[14:15], v[14:15], v[30:31]
	v_mov_b32_e32 v26, v187
	v_cvt_pk_fp8_f32 v27, v12, v13 op_sel:[0,0,1]
	v_pk_add_f32 v[6:7], v[6:7], v[22:23]
	v_pk_add_f32 v[2:3], v[2:3], v[18:19]
	v_mov_b32_e32 v12, v187
	v_mov_b32_e32 v13, v187
	v_cvt_pk_fp8_f32 v156, v142, v143
	v_cvt_pk_fp8_f32 v140, v134, v135
	v_cvt_pk_fp8_f32 v130, v126, v127
	v_cvt_pk_fp8_f32 v124, v118, v119
	v_cvt_pk_fp8_f32 v114, v110, v111
	v_cvt_pk_fp8_f32 v108, v102, v103
	v_cvt_pk_fp8_f32 v98, v94, v95
	v_cvt_pk_fp8_f32 v92, v86, v87
	v_cvt_pk_fp8_f32 v82, v78, v79
	v_cvt_pk_fp8_f32 v76, v70, v71
	v_cvt_pk_fp8_f32 v66, v62, v63
	v_cvt_pk_fp8_f32 v60, v54, v55
	v_cvt_pk_fp8_f32 v50, v46, v47
	v_cvt_pk_fp8_f32 v44, v38, v39
	v_cvt_pk_fp8_f32 v45, v34, v35
	s_lshl_b64 s[24:25], s[24:25], 10
	v_cvt_pk_fp8_f32 v26, v14, v15
	v_cvt_pk_fp8_f32 v12, v6, v7
	v_cvt_pk_fp8_f32 v13, v2, v3
	s_add_u32 s15, s73, s24
	s_addc_u32 s24, s74, s25
	v_pk_add_f32 v[144:145], v[16:17], v[144:145]
	v_pk_add_f32 v[136:137], v[8:9], v[136:137]
	v_pk_add_f32 v[132:133], v[4:5], v[132:133]
	v_pk_add_f32 v[128:129], v[16:17], v[128:129]
	v_pk_add_f32 v[120:121], v[8:9], v[120:121]
	v_pk_add_f32 v[116:117], v[4:5], v[116:117]
	v_pk_add_f32 v[112:113], v[16:17], v[112:113]
	v_pk_add_f32 v[104:105], v[8:9], v[104:105]
	v_pk_add_f32 v[100:101], v[4:5], v[100:101]
	v_pk_add_f32 v[96:97], v[16:17], v[96:97]
	v_pk_add_f32 v[88:89], v[8:9], v[88:89]
	v_pk_add_f32 v[84:85], v[4:5], v[84:85]
	v_pk_add_f32 v[80:81], v[16:17], v[80:81]
	v_pk_add_f32 v[72:73], v[8:9], v[72:73]
	v_pk_add_f32 v[68:69], v[4:5], v[68:69]
	v_pk_add_f32 v[64:65], v[16:17], v[64:65]
	v_pk_add_f32 v[56:57], v[8:9], v[56:57]
	v_pk_add_f32 v[52:53], v[4:5], v[52:53]
	v_pk_add_f32 v[48:49], v[16:17], v[48:49]
	v_pk_add_f32 v[40:41], v[8:9], v[40:41]
	v_pk_add_f32 v[36:37], v[4:5], v[36:37]
	v_pk_add_f32 v[16:17], v[16:17], v[32:33]
	s_add_u32 s2, s15, s2
	v_pk_add_f32 v[8:9], v[8:9], v[24:25]
	v_pk_add_f32 v[4:5], v[4:5], v[20:21]
	v_cvt_pk_fp8_f32 v156, v144, v145 op_sel:[0,0,1]
	v_cvt_pk_fp8_f32 v140, v136, v137 op_sel:[0,0,1]
	v_cvt_pk_fp8_f32 v141, v132, v133 op_sel:[0,0,1]
	v_cvt_pk_fp8_f32 v130, v128, v129 op_sel:[0,0,1]
	v_cvt_pk_fp8_f32 v124, v120, v121 op_sel:[0,0,1]
	v_cvt_pk_fp8_f32 v125, v116, v117 op_sel:[0,0,1]
	v_cvt_pk_fp8_f32 v114, v112, v113 op_sel:[0,0,1]
	v_cvt_pk_fp8_f32 v108, v104, v105 op_sel:[0,0,1]
	v_cvt_pk_fp8_f32 v109, v100, v101 op_sel:[0,0,1]
	v_cvt_pk_fp8_f32 v98, v96, v97 op_sel:[0,0,1]
	v_cvt_pk_fp8_f32 v92, v88, v89 op_sel:[0,0,1]
	v_cvt_pk_fp8_f32 v93, v84, v85 op_sel:[0,0,1]
	v_cvt_pk_fp8_f32 v82, v80, v81 op_sel:[0,0,1]
	v_cvt_pk_fp8_f32 v76, v72, v73 op_sel:[0,0,1]
	v_cvt_pk_fp8_f32 v77, v68, v69 op_sel:[0,0,1]
	v_cvt_pk_fp8_f32 v66, v64, v65 op_sel:[0,0,1]
	v_cvt_pk_fp8_f32 v60, v56, v57 op_sel:[0,0,1]
	v_cvt_pk_fp8_f32 v61, v52, v53 op_sel:[0,0,1]
	v_cvt_pk_fp8_f32 v50, v48, v49 op_sel:[0,0,1]
	v_cvt_pk_fp8_f32 v44, v40, v41 op_sel:[0,0,1]
	v_cvt_pk_fp8_f32 v45, v36, v37 op_sel:[0,0,1]
	v_cvt_pk_fp8_f32 v26, v16, v17 op_sel:[0,0,1]
	s_addc_u32 s15, s24, s14
	v_cvt_pk_fp8_f32 v12, v8, v9 op_sel:[0,0,1]
	v_cvt_pk_fp8_f32 v13, v4, v5 op_sel:[0,0,1]
	s_add_u32 s14, s2, s29
	s_addc_u32 s15, s15, 0
	v_lshl_add_u64 v[10:11], s[14:15], 0, v[150:151]
	s_mov_b64 s[14:15], -1
	s_andn2_b64 vcc, exec, s[38:39]
	global_store_dwordx2 v[138:139], v[156:157], off
	global_store_dwordx2 v[138:139], v[140:141], off offset:128
	global_store_dwordx2 v[122:123], v[130:131], off
	global_store_dwordx2 v[122:123], v[124:125], off offset:128
	global_store_dwordx2 v[106:107], v[114:115], off
	global_store_dwordx2 v[106:107], v[108:109], off offset:128
	global_store_dwordx2 v[90:91], v[98:99], off
	global_store_dwordx2 v[90:91], v[92:93], off offset:128
	global_store_dwordx2 v[74:75], v[82:83], off
	global_store_dwordx2 v[74:75], v[76:77], off offset:128
	global_store_dwordx2 v[58:59], v[66:67], off
	global_store_dwordx2 v[58:59], v[60:61], off offset:128
	global_store_dwordx2 v[42:43], v[50:51], off
	global_store_dwordx2 v[42:43], v[44:45], off offset:128
	global_store_dwordx2 v[10:11], v[26:27], off
	global_store_dwordx2 v[10:11], v[12:13], off offset:128
	s_cbranch_vccnz .LBB0_1453
	s_ashr_i32 s49, s48, 31
	s_lshl_b64 s[14:15], s[48:49], 12
	s_add_u32 s2, s16, s14
	s_addc_u32 s24, s17, s15
	s_lshl_b32 s14, s42, 8
	s_ashr_i32 s15, s14, 31
	s_lshl_b64 s[14:15], s[14:15], 2
	s_add_u32 s2, s2, s14
	s_addc_u32 s15, s24, s15
	s_add_u32 s14, s2, s43
	s_addc_u32 s15, s15, 0
	v_lshl_add_u64 v[6:7], s[14:15], 0, v[148:149]
	global_load_dwordx4 v[10:13], v[6:7], off offset:16
	global_load_dwordx4 v[14:17], v[6:7], off
	global_load_dwordx4 v[2:5], v[6:7], off offset:528
	s_nop 0
	global_load_dwordx4 v[6:9], v[6:7], off offset:512
	s_andn2_b64 vcc, exec, s[44:45]
	s_cbranch_vccnz .LBB0_1452
	s_barrier
	s_branch .LBB0_1452
